# GEMM K-loops (all 20 phases): s_setprio immediates swapped so the LDS-read / LDS-DMA issue segments run at raised priority instead of the MFMA blocks (section 6.3 / 7.4 priority lever)
# baseline (speedup 1.0000x reference)
.LBB0_236:
	ds_read_b128 v[20:23], v188
	ds_read_b128 v[24:27], v189
	ds_read_b128 v[16:19], v183
	ds_read_b128 v[0:3], v184
	ds_read_b128 v[28:31], v190
	ds_read_b128 v[4:7], v191
	ds_read_b128 v[8:11], v192
	ds_read_b128 v[12:15], v193
	s_add_u32 s42, s40, 0xfffe0080
	s_addc_u32 s43, s41, -1
	s_cmp_eq_u32 s58, 4
	s_cselect_b32 s45, s15, s43
	s_cselect_b32 s44, s54, s42
	s_cselect_b32 s43, s13, s57
	s_cselect_b32 s42, s55, s56
	v_lshl_add_u64 v[232:233], s[40:41], 0, v[168:169]
	s_add_i32 m0, s20, 0xc000
	ds_read_b128 v[174:177], v200
	ds_read_b128 v[178:181], v200 offset:1024
	ds_read_b128 v[208:211], v200 offset:2048
	ds_read_b128 v[212:215], v200 offset:3072
	ds_read_b128 v[216:219], v200 offset:4096
	ds_read_b128 v[220:223], v200 offset:5120
	ds_read_b128 v[224:227], v200 offset:6144
	ds_read_b128 v[228:231], v200 offset:7168
	global_load_lds_dwordx4 v[232:233], off
	v_lshl_add_u64 v[232:233], s[40:41], 0, v[170:171]
	s_add_i32 m0, s20, 0xe000
	s_nop 0
	global_load_lds_dwordx4 v[232:233], off
	s_waitcnt vmcnt(8)
	s_waitcnt lgkmcnt(0)
	s_barrier
	s_setprio 0
	s_waitcnt lgkmcnt(0)
	v_mfma_f32_16x16x128_f8f6f4 v[156:159], v[16:23], v[174:181], v[156:159]
	v_mfma_f32_16x16x128_f8f6f4 v[124:127], v[24:31], v[174:181], v[124:127]
	v_mfma_f32_16x16x128_f8f6f4 v[144:147], v[16:23], v[208:215], v[144:147]
	v_mfma_f32_16x16x128_f8f6f4 v[112:115], v[24:31], v[208:215], v[112:115]
	v_mfma_f32_16x16x128_f8f6f4 v[140:143], v[16:23], v[216:223], v[140:143]
	v_mfma_f32_16x16x128_f8f6f4 v[108:111], v[24:31], v[216:223], v[108:111]
	v_mfma_f32_16x16x128_f8f6f4 v[136:139], v[16:23], v[224:231], v[136:139]
	v_mfma_f32_16x16x128_f8f6f4 v[96:99], v[24:31], v[224:231], v[96:99]
	s_setprio 1
	s_setprio 0
	v_mfma_f32_16x16x128_f8f6f4 v[72:75], v[0:7], v[174:181], v[72:75]
	v_mfma_f32_16x16x128_f8f6f4 v[44:47], v[8:15], v[174:181], v[44:47]
	v_mfma_f32_16x16x128_f8f6f4 v[56:59], v[0:7], v[208:215], v[56:59]
	v_mfma_f32_16x16x128_f8f6f4 v[40:43], v[8:15], v[208:215], v[40:43]
	v_mfma_f32_16x16x128_f8f6f4 v[52:55], v[0:7], v[216:223], v[52:55]
	v_mfma_f32_16x16x128_f8f6f4 v[36:39], v[8:15], v[216:223], v[36:39]
	v_mfma_f32_16x16x128_f8f6f4 v[48:51], v[0:7], v[224:231], v[48:51]
	v_mfma_f32_16x16x128_f8f6f4 v[32:35], v[8:15], v[224:231], v[32:35]
	s_setprio 1
	s_barrier
	s_mov_b32 m0, s21
	v_lshl_add_u64 v[174:175], s[42:43], 0, v[162:163]
	s_add_u32 s60, s42, 0x20000
	ds_read_b128 v[208:211], v200 offset:16384
	ds_read_b128 v[212:215], v200 offset:17408
	ds_read_b128 v[216:219], v200 offset:18432
	ds_read_b128 v[220:223], v200 offset:19456
	ds_read_b128 v[224:227], v200 offset:20480
	ds_read_b128 v[228:231], v200 offset:21504
	ds_read_b128 v[232:235], v200 offset:22528
	ds_read_b128 v[236:239], v200 offset:23552
	global_load_lds_dwordx4 v[174:175], off
	v_lshl_add_u64 v[176:177], s[42:43], 0, v[160:161]
	s_mov_b32 m0, s22
	s_addc_u32 s61, s43, 0
	global_load_lds_dwordx4 v[176:177], off
	v_lshl_add_u64 v[178:179], s[60:61], 0, v[162:163]
	s_mov_b32 m0, s23
	v_lshl_add_u64 v[180:181], s[44:45], 0, v[166:167]
	global_load_lds_dwordx4 v[178:179], off
	v_lshl_add_u64 v[178:179], s[60:61], 0, v[160:161]
	s_mov_b32 m0, s24
	s_nop 0
	global_load_lds_dwordx4 v[178:179], off
	v_lshl_add_u64 v[178:179], s[44:45], 0, v[164:165]
	s_mov_b32 m0, s20
	s_nop 0
	global_load_lds_dwordx4 v[178:179], off
	s_mov_b32 m0, s25
	s_nop 0
	global_load_lds_dwordx4 v[180:181], off
	s_waitcnt vmcnt(8)
	s_waitcnt lgkmcnt(0)
	s_barrier
	s_setprio 0
	s_waitcnt lgkmcnt(0)
	v_mfma_f32_16x16x128_f8f6f4 v[128:131], v[16:23], v[208:215], v[128:131]
	v_mfma_f32_16x16x128_f8f6f4 v[84:87], v[24:31], v[208:215], v[84:87]
	v_mfma_f32_16x16x128_f8f6f4 v[116:119], v[16:23], v[216:223], v[116:119]
	v_mfma_f32_16x16x128_f8f6f4 v[64:67], v[24:31], v[216:223], v[64:67]
	v_mfma_f32_16x16x128_f8f6f4 v[148:151], v[16:23], v[224:231], v[148:151]
	v_mfma_f32_16x16x128_f8f6f4 v[120:123], v[24:31], v[224:231], v[120:123]
	v_mfma_f32_16x16x128_f8f6f4 v[152:155], v[16:23], v[232:239], v[152:155]
	v_mfma_f32_16x16x128_f8f6f4 v[132:135], v[24:31], v[232:239], v[132:135]
	s_setprio 1
	s_setprio 0
	v_mfma_f32_16x16x128_f8f6f4 v[88:91], v[0:7], v[208:215], v[88:91]
	v_mfma_f32_16x16x128_f8f6f4 v[60:63], v[8:15], v[208:215], v[60:63]
	v_mfma_f32_16x16x128_f8f6f4 v[92:95], v[0:7], v[216:223], v[92:95]
	v_mfma_f32_16x16x128_f8f6f4 v[68:71], v[8:15], v[216:223], v[68:71]
	v_mfma_f32_16x16x128_f8f6f4 v[100:103], v[0:7], v[224:231], v[100:103]
	v_mfma_f32_16x16x128_f8f6f4 v[76:79], v[8:15], v[224:231], v[76:79]
	v_mfma_f32_16x16x128_f8f6f4 v[104:107], v[0:7], v[232:239], v[104:107]
	v_mfma_f32_16x16x128_f8f6f4 v[80:83], v[8:15], v[232:239], v[80:83]
	s_setprio 1
	s_barrier
	ds_read_b128 v[4:7], v194
	ds_read_b128 v[8:11], v195
	ds_read_b128 v[0:3], v185
	ds_read_b128 v[16:19], v186
	ds_read_b128 v[12:15], v196
	ds_read_b128 v[20:23], v197
	ds_read_b128 v[24:27], v198
	ds_read_b128 v[28:31], v199
	s_add_u32 s44, s44, 0x20000
	s_addc_u32 s45, s45, 0
	s_mov_b32 m0, s26
	v_lshl_add_u64 v[240:241], s[44:45], 0, v[164:165]
	ds_read_b128 v[208:211], v200 offset:32768
	ds_read_b128 v[212:215], v200 offset:33792
	ds_read_b128 v[216:219], v200 offset:34816
	ds_read_b128 v[220:223], v200 offset:35840
	ds_read_b128 v[224:227], v200 offset:36864
	ds_read_b128 v[228:231], v200 offset:37888
	ds_read_b128 v[232:235], v200 offset:38912
	ds_read_b128 v[236:239], v200 offset:39936
	global_load_lds_dwordx4 v[240:241], off
	v_lshl_add_u64 v[240:241], s[44:45], 0, v[166:167]
	s_mov_b32 m0, s27
	s_nop 0
	global_load_lds_dwordx4 v[240:241], off
	s_waitcnt vmcnt(8)
	s_waitcnt lgkmcnt(0)
	s_barrier
	s_setprio 0
	s_waitcnt lgkmcnt(0)
	v_mfma_f32_16x16x128_f8f6f4 v[156:159], v[0:7], v[208:215], v[156:159]
	v_mfma_f32_16x16x128_f8f6f4 v[124:127], v[8:15], v[208:215], v[124:127]
	v_mfma_f32_16x16x128_f8f6f4 v[144:147], v[0:7], v[216:223], v[144:147]
	v_mfma_f32_16x16x128_f8f6f4 v[112:115], v[8:15], v[216:223], v[112:115]
	v_mfma_f32_16x16x128_f8f6f4 v[140:143], v[0:7], v[224:231], v[140:143]
	v_mfma_f32_16x16x128_f8f6f4 v[108:111], v[8:15], v[224:231], v[108:111]
	v_mfma_f32_16x16x128_f8f6f4 v[136:139], v[0:7], v[232:239], v[136:139]
	v_mfma_f32_16x16x128_f8f6f4 v[96:99], v[8:15], v[232:239], v[96:99]
	s_setprio 1
	s_setprio 0
	v_mfma_f32_16x16x128_f8f6f4 v[72:75], v[16:23], v[208:215], v[72:75]
	v_mfma_f32_16x16x128_f8f6f4 v[44:47], v[24:31], v[208:215], v[44:47]
	v_mfma_f32_16x16x128_f8f6f4 v[56:59], v[16:23], v[216:223], v[56:59]
	v_mfma_f32_16x16x128_f8f6f4 v[40:43], v[24:31], v[216:223], v[40:43]
	v_mfma_f32_16x16x128_f8f6f4 v[52:55], v[16:23], v[224:231], v[52:55]
	v_mfma_f32_16x16x128_f8f6f4 v[36:39], v[24:31], v[224:231], v[36:39]
	v_mfma_f32_16x16x128_f8f6f4 v[48:51], v[16:23], v[232:239], v[48:51]
	v_mfma_f32_16x16x128_f8f6f4 v[32:35], v[24:31], v[232:239], v[32:35]
	s_setprio 1
	s_barrier
	s_mov_b32 m0, s29
	v_lshl_add_u64 v[174:175], v[174:175], 0, s[8:9]
	s_add_u32 s42, s42, 0x20080
	ds_read_b128 v[208:211], v200 offset:49152
	ds_read_b128 v[212:215], v200 offset:50176
	ds_read_b128 v[216:219], v200 offset:51200
	ds_read_b128 v[220:223], v200 offset:52224
	ds_read_b128 v[224:227], v200 offset:53248
	ds_read_b128 v[228:231], v200 offset:54272
	ds_read_b128 v[232:235], v200 offset:55296
	ds_read_b128 v[236:239], v200 offset:56320
	global_load_lds_dwordx4 v[174:175], off
	v_lshl_add_u64 v[174:175], v[176:177], 0, s[8:9]
	s_mov_b32 m0, s30
	s_addc_u32 s43, s43, 0
	global_load_lds_dwordx4 v[174:175], off
	v_lshl_add_u64 v[174:175], s[42:43], 0, v[162:163]
	s_mov_b32 m0, s46
	s_nop 0
	global_load_lds_dwordx4 v[174:175], off
	v_lshl_add_u64 v[174:175], s[42:43], 0, v[160:161]
	s_mov_b32 m0, s47
	s_nop 0
	global_load_lds_dwordx4 v[174:175], off
	v_lshl_add_u64 v[174:175], v[178:179], 0, s[8:9]
	s_mov_b32 m0, s31
	s_nop 0
	global_load_lds_dwordx4 v[174:175], off
	v_lshl_add_u64 v[174:175], v[180:181], 0, s[8:9]
	s_mov_b32 m0, s33
	s_nop 0
	global_load_lds_dwordx4 v[174:175], off
	s_waitcnt vmcnt(8)
	s_waitcnt lgkmcnt(0)
	s_barrier
	s_setprio 0
	s_waitcnt lgkmcnt(0)
	v_mfma_f32_16x16x128_f8f6f4 v[128:131], v[0:7], v[208:215], v[128:131]
	v_mfma_f32_16x16x128_f8f6f4 v[84:87], v[8:15], v[208:215], v[84:87]
	v_mfma_f32_16x16x128_f8f6f4 v[116:119], v[0:7], v[216:223], v[116:119]
	v_mfma_f32_16x16x128_f8f6f4 v[64:67], v[8:15], v[216:223], v[64:67]
	v_mfma_f32_16x16x128_f8f6f4 v[148:151], v[0:7], v[224:231], v[148:151]
	v_mfma_f32_16x16x128_f8f6f4 v[120:123], v[8:15], v[224:231], v[120:123]
	v_mfma_f32_16x16x128_f8f6f4 v[152:155], v[0:7], v[232:239], v[152:155]
	v_mfma_f32_16x16x128_f8f6f4 v[132:135], v[8:15], v[232:239], v[132:135]
	s_setprio 1
	s_setprio 0
	v_mfma_f32_16x16x128_f8f6f4 v[88:91], v[16:23], v[208:215], v[88:91]
	v_mfma_f32_16x16x128_f8f6f4 v[60:63], v[24:31], v[208:215], v[60:63]
	v_mfma_f32_16x16x128_f8f6f4 v[92:95], v[16:23], v[216:223], v[92:95]
	v_mfma_f32_16x16x128_f8f6f4 v[68:71], v[24:31], v[216:223], v[68:71]
	v_mfma_f32_16x16x128_f8f6f4 v[100:103], v[16:23], v[224:231], v[100:103]
	v_mfma_f32_16x16x128_f8f6f4 v[76:79], v[24:31], v[224:231], v[76:79]
	v_mfma_f32_16x16x128_f8f6f4 v[104:107], v[16:23], v[232:239], v[104:107]
	v_mfma_f32_16x16x128_f8f6f4 v[80:83], v[24:31], v[232:239], v[80:83]
	s_setprio 1
	s_barrier
	s_add_i32 s58, s58, 2
	s_add_u32 s40, s40, 0x100
	s_addc_u32 s41, s41, 0
	s_add_u32 s56, s56, 0x100
	s_addc_u32 s57, s57, 0
	s_cmp_gt_u32 s58, 5
	s_cbranch_scc0 .LBB0_236
	s_nop 15
	s_nop 7
	s_and_b64 vcc, exec, s[10:11]
	s_cbranch_vccz .LBB0_239
	s_barrier

.LBB0_577:
	ds_read_b128 v[20:23], v184
	ds_read_b128 v[24:27], v185
	ds_read_b128 v[16:19], v180
	ds_read_b128 v[0:3], v181
	ds_read_b128 v[28:31], v186
	ds_read_b128 v[4:7], v187
	ds_read_b128 v[8:11], v188
	ds_read_b128 v[12:15], v189
	s_add_u32 s34, s90, s48
	s_addc_u32 s35, s91, s49
	s_add_u32 s55, s90, s50
	s_addc_u32 s56, s91, s51
	s_cmp_eq_u32 s52, 4
	s_cselect_b32 s37, s15, s35
	s_cselect_b32 s36, s14, s34
	s_cselect_b32 s35, s7, s56
	s_cselect_b32 s34, s6, s55
	s_mov_b32 m0, s53
	v_lshl_add_u64 v[222:223], s[90:91], 0, v[168:169]
	ds_read_b128 v[172:175], v196
	ds_read_b128 v[176:179], v196 offset:1024
	ds_read_b128 v[198:201], v196 offset:2048
	ds_read_b128 v[202:205], v196 offset:3072
	ds_read_b128 v[206:209], v196 offset:4096
	ds_read_b128 v[210:213], v196 offset:5120
	ds_read_b128 v[214:217], v196 offset:6144
	ds_read_b128 v[218:221], v196 offset:7168
	global_load_lds_dwordx4 v[222:223], off
	v_lshl_add_u64 v[222:223], s[90:91], 0, v[170:171]
	s_mov_b32 m0, s54
	s_nop 0
	global_load_lds_dwordx4 v[222:223], off
	s_waitcnt vmcnt(8)
	s_waitcnt lgkmcnt(0)
	s_barrier
	s_setprio 0
	s_waitcnt lgkmcnt(0)
	v_mfma_f32_16x16x128_f8f6f4 v[116:119], v[16:23], v[172:179], v[116:119]
	v_mfma_f32_16x16x128_f8f6f4 v[112:115], v[24:31], v[172:179], v[112:115]
	v_mfma_f32_16x16x128_f8f6f4 v[100:103], v[16:23], v[198:205], v[100:103]
	v_mfma_f32_16x16x128_f8f6f4 v[96:99], v[24:31], v[198:205], v[96:99]
	v_mfma_f32_16x16x128_f8f6f4 v[84:87], v[16:23], v[206:213], v[84:87]
	v_mfma_f32_16x16x128_f8f6f4 v[80:83], v[24:31], v[206:213], v[80:83]
	v_mfma_f32_16x16x128_f8f6f4 v[68:71], v[16:23], v[214:221], v[68:71]
	v_mfma_f32_16x16x128_f8f6f4 v[64:67], v[24:31], v[214:221], v[64:67]
	s_setprio 1
	s_setprio 0
	v_mfma_f32_16x16x128_f8f6f4 v[108:111], v[0:7], v[172:179], v[108:111]
	v_mfma_f32_16x16x128_f8f6f4 v[104:107], v[8:15], v[172:179], v[104:107]
	v_mfma_f32_16x16x128_f8f6f4 v[92:95], v[0:7], v[198:205], v[92:95]
	v_mfma_f32_16x16x128_f8f6f4 v[88:91], v[8:15], v[198:205], v[88:91]
	v_mfma_f32_16x16x128_f8f6f4 v[76:79], v[0:7], v[206:213], v[76:79]
	v_mfma_f32_16x16x128_f8f6f4 v[72:75], v[8:15], v[206:213], v[72:75]
	v_mfma_f32_16x16x128_f8f6f4 v[60:63], v[0:7], v[214:221], v[60:63]
	v_mfma_f32_16x16x128_f8f6f4 v[56:59], v[8:15], v[214:221], v[56:59]
	s_setprio 1
	s_barrier
	s_mov_b32 m0, s28
	v_lshl_add_u64 v[172:173], s[34:35], 0, v[122:123]
	s_add_u32 s56, s34, 0x20000
	ds_read_b128 v[198:201], v196 offset:16384
	ds_read_b128 v[202:205], v196 offset:17408
	ds_read_b128 v[206:209], v196 offset:18432
	ds_read_b128 v[210:213], v196 offset:19456
	ds_read_b128 v[214:217], v196 offset:20480
	ds_read_b128 v[218:221], v196 offset:21504
	ds_read_b128 v[222:225], v196 offset:22528
	ds_read_b128 v[226:229], v196 offset:23552
	global_load_lds_dwordx4 v[172:173], off
	v_lshl_add_u64 v[174:175], s[34:35], 0, v[120:121]
	s_mov_b32 m0, s29
	s_addc_u32 s57, s35, 0
	global_load_lds_dwordx4 v[174:175], off
	v_lshl_add_u64 v[176:177], s[56:57], 0, v[122:123]
	s_mov_b32 m0, s30
	v_lshl_add_u64 v[178:179], s[36:37], 0, v[126:127]
	global_load_lds_dwordx4 v[176:177], off
	v_lshl_add_u64 v[176:177], s[56:57], 0, v[120:121]
	s_mov_b32 m0, s31
	s_nop 0
	global_load_lds_dwordx4 v[176:177], off
	v_lshl_add_u64 v[176:177], s[36:37], 0, v[124:125]
	s_mov_b32 m0, s3
	s_nop 0
	global_load_lds_dwordx4 v[176:177], off
	s_mov_b32 m0, s33
	s_nop 0
	global_load_lds_dwordx4 v[178:179], off
	s_waitcnt vmcnt(8)
	s_waitcnt lgkmcnt(0)
	s_barrier
	s_setprio 0
	s_waitcnt lgkmcnt(0)
	v_mfma_f32_16x16x128_f8f6f4 v[48:51], v[16:23], v[198:205], v[48:51]
	v_mfma_f32_16x16x128_f8f6f4 v[40:43], v[24:31], v[198:205], v[40:43]
	v_mfma_f32_16x16x128_f8f6f4 v[44:47], v[16:23], v[206:213], v[44:47]
	v_mfma_f32_16x16x128_f8f6f4 v[32:35], v[24:31], v[206:213], v[32:35]
	v_mfma_f32_16x16x128_f8f6f4 v[36:39], v[16:23], v[214:221], v[36:39]
	v_mfma_f32_16x16x128_f8f6f4 v[144:147], v[24:31], v[214:221], v[144:147]
	v_mfma_f32_16x16x128_f8f6f4 v[128:131], v[16:23], v[222:229], v[128:131]
	v_mfma_f32_16x16x128_f8f6f4 v[132:135], v[24:31], v[222:229], v[132:135]
	s_setprio 1
	s_setprio 0
	v_mfma_f32_16x16x128_f8f6f4 v[52:55], v[0:7], v[198:205], v[52:55]
	v_mfma_f32_16x16x128_f8f6f4 v[164:167], v[8:15], v[198:205], v[164:167]
	v_mfma_f32_16x16x128_f8f6f4 v[156:159], v[0:7], v[206:213], v[156:159]
	v_mfma_f32_16x16x128_f8f6f4 v[160:163], v[8:15], v[206:213], v[160:163]
	v_mfma_f32_16x16x128_f8f6f4 v[148:151], v[0:7], v[214:221], v[148:151]
	v_mfma_f32_16x16x128_f8f6f4 v[152:155], v[8:15], v[214:221], v[152:155]
	v_mfma_f32_16x16x128_f8f6f4 v[140:143], v[0:7], v[222:229], v[140:143]
	v_mfma_f32_16x16x128_f8f6f4 v[136:139], v[8:15], v[222:229], v[136:139]
	s_setprio 1
	s_barrier
	ds_read_b128 v[4:7], v190
	ds_read_b128 v[8:11], v191
	ds_read_b128 v[0:3], v182
	ds_read_b128 v[16:19], v183
	ds_read_b128 v[12:15], v192
	ds_read_b128 v[20:23], v193
	ds_read_b128 v[24:27], v194
	ds_read_b128 v[28:31], v195
	s_add_u32 s36, s36, 0x20000
	s_addc_u32 s37, s37, 0
	s_mov_b32 m0, s40
	v_lshl_add_u64 v[230:231], s[36:37], 0, v[124:125]
	ds_read_b128 v[198:201], v196 offset:32768
	ds_read_b128 v[202:205], v196 offset:33792
	ds_read_b128 v[206:209], v196 offset:34816
	ds_read_b128 v[210:213], v196 offset:35840
	ds_read_b128 v[214:217], v196 offset:36864
	ds_read_b128 v[218:221], v196 offset:37888
	ds_read_b128 v[222:225], v196 offset:38912
	ds_read_b128 v[226:229], v196 offset:39936
	global_load_lds_dwordx4 v[230:231], off
	v_lshl_add_u64 v[230:231], s[36:37], 0, v[126:127]
	s_mov_b32 m0, s41
	s_nop 0
	global_load_lds_dwordx4 v[230:231], off
	s_waitcnt vmcnt(8)
	s_waitcnt lgkmcnt(0)
	s_barrier
	s_setprio 0
	s_waitcnt lgkmcnt(0)
	v_mfma_f32_16x16x128_f8f6f4 v[116:119], v[0:7], v[198:205], v[116:119]
	v_mfma_f32_16x16x128_f8f6f4 v[112:115], v[8:15], v[198:205], v[112:115]
	v_mfma_f32_16x16x128_f8f6f4 v[100:103], v[0:7], v[206:213], v[100:103]
	v_mfma_f32_16x16x128_f8f6f4 v[96:99], v[8:15], v[206:213], v[96:99]
	v_mfma_f32_16x16x128_f8f6f4 v[84:87], v[0:7], v[214:221], v[84:87]
	v_mfma_f32_16x16x128_f8f6f4 v[80:83], v[8:15], v[214:221], v[80:83]
	v_mfma_f32_16x16x128_f8f6f4 v[68:71], v[0:7], v[222:229], v[68:71]
	v_mfma_f32_16x16x128_f8f6f4 v[64:67], v[8:15], v[222:229], v[64:67]
	s_setprio 1
	s_setprio 0
	v_mfma_f32_16x16x128_f8f6f4 v[108:111], v[16:23], v[198:205], v[108:111]
	v_mfma_f32_16x16x128_f8f6f4 v[104:107], v[24:31], v[198:205], v[104:107]
	v_mfma_f32_16x16x128_f8f6f4 v[92:95], v[16:23], v[206:213], v[92:95]
	v_mfma_f32_16x16x128_f8f6f4 v[88:91], v[24:31], v[206:213], v[88:91]
	v_mfma_f32_16x16x128_f8f6f4 v[76:79], v[16:23], v[214:221], v[76:79]
	v_mfma_f32_16x16x128_f8f6f4 v[72:75], v[24:31], v[214:221], v[72:75]
	v_mfma_f32_16x16x128_f8f6f4 v[60:63], v[16:23], v[222:229], v[60:63]
	v_mfma_f32_16x16x128_f8f6f4 v[56:59], v[24:31], v[222:229], v[56:59]
	s_setprio 1
	s_barrier
	s_mov_b32 m0, s42
	v_lshl_add_u64 v[172:173], v[172:173], 0, s[24:25]
	s_add_u32 s34, s34, 0x20080
	ds_read_b128 v[198:201], v196 offset:49152
	ds_read_b128 v[202:205], v196 offset:50176
	ds_read_b128 v[206:209], v196 offset:51200
	ds_read_b128 v[210:213], v196 offset:52224
	ds_read_b128 v[214:217], v196 offset:53248
	ds_read_b128 v[218:221], v196 offset:54272
	ds_read_b128 v[222:225], v196 offset:55296
	ds_read_b128 v[226:229], v196 offset:56320
	global_load_lds_dwordx4 v[172:173], off
	v_lshl_add_u64 v[172:173], v[174:175], 0, s[24:25]
	s_mov_b32 m0, s43
	s_addc_u32 s35, s35, 0
	global_load_lds_dwordx4 v[172:173], off
	v_lshl_add_u64 v[172:173], s[34:35], 0, v[122:123]
	s_mov_b32 m0, s46
	s_nop 0
	global_load_lds_dwordx4 v[172:173], off
	v_lshl_add_u64 v[172:173], s[34:35], 0, v[120:121]
	s_mov_b32 m0, s47
	s_nop 0
	global_load_lds_dwordx4 v[172:173], off
	v_lshl_add_u64 v[172:173], v[176:177], 0, s[24:25]
	s_mov_b32 m0, s44
	s_nop 0
	global_load_lds_dwordx4 v[172:173], off
	v_lshl_add_u64 v[172:173], v[178:179], 0, s[24:25]
	s_mov_b32 m0, s45
	s_nop 0
	global_load_lds_dwordx4 v[172:173], off
	s_waitcnt vmcnt(8)
	s_waitcnt lgkmcnt(0)
	s_barrier
	s_setprio 0
	s_waitcnt lgkmcnt(0)
	v_mfma_f32_16x16x128_f8f6f4 v[48:51], v[0:7], v[198:205], v[48:51]
	v_mfma_f32_16x16x128_f8f6f4 v[40:43], v[8:15], v[198:205], v[40:43]
	v_mfma_f32_16x16x128_f8f6f4 v[44:47], v[0:7], v[206:213], v[44:47]
	v_mfma_f32_16x16x128_f8f6f4 v[32:35], v[8:15], v[206:213], v[32:35]
	v_mfma_f32_16x16x128_f8f6f4 v[36:39], v[0:7], v[214:221], v[36:39]
	v_mfma_f32_16x16x128_f8f6f4 v[144:147], v[8:15], v[214:221], v[144:147]
	v_mfma_f32_16x16x128_f8f6f4 v[128:131], v[0:7], v[222:229], v[128:131]
	v_mfma_f32_16x16x128_f8f6f4 v[132:135], v[8:15], v[222:229], v[132:135]
	s_setprio 1
	s_setprio 0
	v_mfma_f32_16x16x128_f8f6f4 v[52:55], v[16:23], v[198:205], v[52:55]
	v_mfma_f32_16x16x128_f8f6f4 v[164:167], v[24:31], v[198:205], v[164:167]
	v_mfma_f32_16x16x128_f8f6f4 v[156:159], v[16:23], v[206:213], v[156:159]
	v_mfma_f32_16x16x128_f8f6f4 v[160:163], v[24:31], v[206:213], v[160:163]
	v_mfma_f32_16x16x128_f8f6f4 v[148:151], v[16:23], v[214:221], v[148:151]
	v_mfma_f32_16x16x128_f8f6f4 v[152:155], v[24:31], v[214:221], v[152:155]
	v_mfma_f32_16x16x128_f8f6f4 v[140:143], v[16:23], v[222:229], v[140:143]
	v_mfma_f32_16x16x128_f8f6f4 v[136:139], v[24:31], v[222:229], v[136:139]
	s_setprio 1
	s_barrier
	s_add_i32 s52, s52, 2
	s_add_u32 s48, s48, 0x100
	s_addc_u32 s49, s49, 0
	s_add_u32 s50, s50, 0x100
	s_addc_u32 s51, s51, 0
	v_lshl_add_u64 v[168:169], v[168:169], 0, s[26:27]
	s_cmp_gt_u32 s52, 5
	v_lshl_add_u64 v[170:171], v[170:171], 0, s[26:27]
	s_cbranch_scc0 .LBB0_577
	s_nop 15
	s_nop 7
	s_waitcnt vmcnt(0)
	s_cmpk_lt_u32 s21, 0x100
	s_cbranch_scc0 .LBB0_580
	s_barrier

.LBB0_626:
	ds_read_b128 v[20:23], v184
	ds_read_b128 v[24:27], v185
	ds_read_b128 v[16:19], v180
	ds_read_b128 v[0:3], v181
	ds_read_b128 v[28:31], v186
	ds_read_b128 v[4:7], v187
	ds_read_b128 v[8:11], v188
	ds_read_b128 v[12:15], v189
	s_add_u32 s34, s90, s44
	s_addc_u32 s35, s91, s45
	s_add_u32 s51, s90, s46
	s_addc_u32 s52, s91, s47
	s_cmp_eq_u32 s48, 4
	s_cselect_b32 s37, s15, s35
	s_cselect_b32 s36, s14, s34
	s_cselect_b32 s35, s7, s52
	s_cselect_b32 s34, s6, s51
	s_mov_b32 m0, s49
	v_lshl_add_u64 v[222:223], s[90:91], 0, v[168:169]
	ds_read_b128 v[172:175], v196
	ds_read_b128 v[176:179], v196 offset:1024
	ds_read_b128 v[198:201], v196 offset:2048
	ds_read_b128 v[202:205], v196 offset:3072
	ds_read_b128 v[206:209], v196 offset:4096
	ds_read_b128 v[210:213], v196 offset:5120
	ds_read_b128 v[214:217], v196 offset:6144
	ds_read_b128 v[218:221], v196 offset:7168
	global_load_lds_dwordx4 v[222:223], off
	v_lshl_add_u64 v[222:223], s[90:91], 0, v[170:171]
	s_mov_b32 m0, s50
	s_nop 0
	global_load_lds_dwordx4 v[222:223], off
	s_waitcnt vmcnt(8)
	s_waitcnt lgkmcnt(0)
	s_barrier
	s_setprio 0
	s_waitcnt lgkmcnt(0)
	v_mfma_f32_16x16x128_f8f6f4 v[116:119], v[16:23], v[172:179], v[116:119]
	v_mfma_f32_16x16x128_f8f6f4 v[112:115], v[24:31], v[172:179], v[112:115]
	v_mfma_f32_16x16x128_f8f6f4 v[100:103], v[16:23], v[198:205], v[100:103]
	v_mfma_f32_16x16x128_f8f6f4 v[96:99], v[24:31], v[198:205], v[96:99]
	v_mfma_f32_16x16x128_f8f6f4 v[84:87], v[16:23], v[206:213], v[84:87]
	v_mfma_f32_16x16x128_f8f6f4 v[80:83], v[24:31], v[206:213], v[80:83]
	v_mfma_f32_16x16x128_f8f6f4 v[68:71], v[16:23], v[214:221], v[68:71]
	v_mfma_f32_16x16x128_f8f6f4 v[64:67], v[24:31], v[214:221], v[64:67]
	s_setprio 1
	s_setprio 0
	v_mfma_f32_16x16x128_f8f6f4 v[108:111], v[0:7], v[172:179], v[108:111]
	v_mfma_f32_16x16x128_f8f6f4 v[104:107], v[8:15], v[172:179], v[104:107]
	v_mfma_f32_16x16x128_f8f6f4 v[92:95], v[0:7], v[198:205], v[92:95]
	v_mfma_f32_16x16x128_f8f6f4 v[88:91], v[8:15], v[198:205], v[88:91]
	v_mfma_f32_16x16x128_f8f6f4 v[76:79], v[0:7], v[206:213], v[76:79]
	v_mfma_f32_16x16x128_f8f6f4 v[72:75], v[8:15], v[206:213], v[72:75]
	v_mfma_f32_16x16x128_f8f6f4 v[60:63], v[0:7], v[214:221], v[60:63]
	v_mfma_f32_16x16x128_f8f6f4 v[56:59], v[8:15], v[214:221], v[56:59]
	s_setprio 1
	s_barrier
	s_mov_b32 m0, s16
	v_lshl_add_u64 v[172:173], s[34:35], 0, v[122:123]
	s_add_u32 s52, s34, 0x20000
	ds_read_b128 v[198:201], v196 offset:16384
	ds_read_b128 v[202:205], v196 offset:17408
	ds_read_b128 v[206:209], v196 offset:18432
	ds_read_b128 v[210:213], v196 offset:19456
	ds_read_b128 v[214:217], v196 offset:20480
	ds_read_b128 v[218:221], v196 offset:21504
	ds_read_b128 v[222:225], v196 offset:22528
	ds_read_b128 v[226:229], v196 offset:23552
	global_load_lds_dwordx4 v[172:173], off
	v_lshl_add_u64 v[174:175], s[34:35], 0, v[120:121]
	s_mov_b32 m0, s17
	s_addc_u32 s53, s35, 0
	global_load_lds_dwordx4 v[174:175], off
	v_lshl_add_u64 v[176:177], s[52:53], 0, v[122:123]
	s_mov_b32 m0, s22
	v_lshl_add_u64 v[178:179], s[36:37], 0, v[126:127]
	global_load_lds_dwordx4 v[176:177], off
	v_lshl_add_u64 v[176:177], s[52:53], 0, v[120:121]
	s_mov_b32 m0, s23
	s_nop 0
	global_load_lds_dwordx4 v[176:177], off
	v_lshl_add_u64 v[176:177], s[36:37], 0, v[124:125]
	s_mov_b32 m0, s3
	s_nop 0
	global_load_lds_dwordx4 v[176:177], off
	s_mov_b32 m0, s28
	s_nop 0
	global_load_lds_dwordx4 v[178:179], off
	s_waitcnt vmcnt(8)
	s_waitcnt lgkmcnt(0)
	s_barrier
	s_setprio 0
	s_waitcnt lgkmcnt(0)
	v_mfma_f32_16x16x128_f8f6f4 v[48:51], v[16:23], v[198:205], v[48:51]
	v_mfma_f32_16x16x128_f8f6f4 v[40:43], v[24:31], v[198:205], v[40:43]
	v_mfma_f32_16x16x128_f8f6f4 v[44:47], v[16:23], v[206:213], v[44:47]
	v_mfma_f32_16x16x128_f8f6f4 v[32:35], v[24:31], v[206:213], v[32:35]
	v_mfma_f32_16x16x128_f8f6f4 v[36:39], v[16:23], v[214:221], v[36:39]
	v_mfma_f32_16x16x128_f8f6f4 v[144:147], v[24:31], v[214:221], v[144:147]
	v_mfma_f32_16x16x128_f8f6f4 v[128:131], v[16:23], v[222:229], v[128:131]
	v_mfma_f32_16x16x128_f8f6f4 v[132:135], v[24:31], v[222:229], v[132:135]
	s_setprio 1
	s_setprio 0
	v_mfma_f32_16x16x128_f8f6f4 v[52:55], v[0:7], v[198:205], v[52:55]
	v_mfma_f32_16x16x128_f8f6f4 v[164:167], v[8:15], v[198:205], v[164:167]
	v_mfma_f32_16x16x128_f8f6f4 v[156:159], v[0:7], v[206:213], v[156:159]
	v_mfma_f32_16x16x128_f8f6f4 v[160:163], v[8:15], v[206:213], v[160:163]
	v_mfma_f32_16x16x128_f8f6f4 v[148:151], v[0:7], v[214:221], v[148:151]
	v_mfma_f32_16x16x128_f8f6f4 v[152:155], v[8:15], v[214:221], v[152:155]
	v_mfma_f32_16x16x128_f8f6f4 v[140:143], v[0:7], v[222:229], v[140:143]
	v_mfma_f32_16x16x128_f8f6f4 v[136:139], v[8:15], v[222:229], v[136:139]
	s_setprio 1
	s_barrier
	ds_read_b128 v[4:7], v190
	ds_read_b128 v[8:11], v191
	ds_read_b128 v[0:3], v182
	ds_read_b128 v[16:19], v183
	ds_read_b128 v[12:15], v192
	ds_read_b128 v[20:23], v193
	ds_read_b128 v[24:27], v194
	ds_read_b128 v[28:31], v195
	s_add_u32 s36, s36, 0x20000
	s_addc_u32 s37, s37, 0
	s_mov_b32 m0, s29
	v_lshl_add_u64 v[230:231], s[36:37], 0, v[124:125]
	ds_read_b128 v[198:201], v196 offset:32768
	ds_read_b128 v[202:205], v196 offset:33792
	ds_read_b128 v[206:209], v196 offset:34816
	ds_read_b128 v[210:213], v196 offset:35840
	ds_read_b128 v[214:217], v196 offset:36864
	ds_read_b128 v[218:221], v196 offset:37888
	ds_read_b128 v[222:225], v196 offset:38912
	ds_read_b128 v[226:229], v196 offset:39936
	global_load_lds_dwordx4 v[230:231], off
	v_lshl_add_u64 v[230:231], s[36:37], 0, v[126:127]
	s_mov_b32 m0, s30
	s_nop 0
	global_load_lds_dwordx4 v[230:231], off
	s_waitcnt vmcnt(8)
	s_waitcnt lgkmcnt(0)
	s_barrier
	s_setprio 0
	s_waitcnt lgkmcnt(0)
	v_mfma_f32_16x16x128_f8f6f4 v[116:119], v[0:7], v[198:205], v[116:119]
	v_mfma_f32_16x16x128_f8f6f4 v[112:115], v[8:15], v[198:205], v[112:115]
	v_mfma_f32_16x16x128_f8f6f4 v[100:103], v[0:7], v[206:213], v[100:103]
	v_mfma_f32_16x16x128_f8f6f4 v[96:99], v[8:15], v[206:213], v[96:99]
	v_mfma_f32_16x16x128_f8f6f4 v[84:87], v[0:7], v[214:221], v[84:87]
	v_mfma_f32_16x16x128_f8f6f4 v[80:83], v[8:15], v[214:221], v[80:83]
	v_mfma_f32_16x16x128_f8f6f4 v[68:71], v[0:7], v[222:229], v[68:71]
	v_mfma_f32_16x16x128_f8f6f4 v[64:67], v[8:15], v[222:229], v[64:67]
	s_setprio 1
	s_setprio 0
	v_mfma_f32_16x16x128_f8f6f4 v[108:111], v[16:23], v[198:205], v[108:111]
	v_mfma_f32_16x16x128_f8f6f4 v[104:107], v[24:31], v[198:205], v[104:107]
	v_mfma_f32_16x16x128_f8f6f4 v[92:95], v[16:23], v[206:213], v[92:95]
	v_mfma_f32_16x16x128_f8f6f4 v[88:91], v[24:31], v[206:213], v[88:91]
	v_mfma_f32_16x16x128_f8f6f4 v[76:79], v[16:23], v[214:221], v[76:79]
	v_mfma_f32_16x16x128_f8f6f4 v[72:75], v[24:31], v[214:221], v[72:75]
	v_mfma_f32_16x16x128_f8f6f4 v[60:63], v[16:23], v[222:229], v[60:63]
	v_mfma_f32_16x16x128_f8f6f4 v[56:59], v[24:31], v[222:229], v[56:59]
	s_setprio 1
	s_barrier
	s_mov_b32 m0, s31
	v_lshl_add_u64 v[172:173], v[172:173], 0, s[24:25]
	s_add_u32 s34, s34, 0x20080
	ds_read_b128 v[198:201], v196 offset:49152
	ds_read_b128 v[202:205], v196 offset:50176
	ds_read_b128 v[206:209], v196 offset:51200
	ds_read_b128 v[210:213], v196 offset:52224
	ds_read_b128 v[214:217], v196 offset:53248
	ds_read_b128 v[218:221], v196 offset:54272
	ds_read_b128 v[222:225], v196 offset:55296
	ds_read_b128 v[226:229], v196 offset:56320
	global_load_lds_dwordx4 v[172:173], off
	v_lshl_add_u64 v[172:173], v[174:175], 0, s[24:25]
	s_mov_b32 m0, s33
	s_addc_u32 s35, s35, 0
	global_load_lds_dwordx4 v[172:173], off
	v_lshl_add_u64 v[172:173], s[34:35], 0, v[122:123]
	s_mov_b32 m0, s42
	s_nop 0
	global_load_lds_dwordx4 v[172:173], off
	v_lshl_add_u64 v[172:173], s[34:35], 0, v[120:121]
	s_mov_b32 m0, s43
	s_nop 0
	global_load_lds_dwordx4 v[172:173], off
	v_lshl_add_u64 v[172:173], v[176:177], 0, s[24:25]
	s_mov_b32 m0, s40
	s_nop 0
	global_load_lds_dwordx4 v[172:173], off
	v_lshl_add_u64 v[172:173], v[178:179], 0, s[24:25]
	s_mov_b32 m0, s41
	s_nop 0
	global_load_lds_dwordx4 v[172:173], off
	s_waitcnt vmcnt(8)
	s_waitcnt lgkmcnt(0)
	s_barrier
	s_setprio 0
	s_waitcnt lgkmcnt(0)
	v_mfma_f32_16x16x128_f8f6f4 v[48:51], v[0:7], v[198:205], v[48:51]
	v_mfma_f32_16x16x128_f8f6f4 v[40:43], v[8:15], v[198:205], v[40:43]
	v_mfma_f32_16x16x128_f8f6f4 v[44:47], v[0:7], v[206:213], v[44:47]
	v_mfma_f32_16x16x128_f8f6f4 v[32:35], v[8:15], v[206:213], v[32:35]
	v_mfma_f32_16x16x128_f8f6f4 v[36:39], v[0:7], v[214:221], v[36:39]
	v_mfma_f32_16x16x128_f8f6f4 v[144:147], v[8:15], v[214:221], v[144:147]
	v_mfma_f32_16x16x128_f8f6f4 v[128:131], v[0:7], v[222:229], v[128:131]
	v_mfma_f32_16x16x128_f8f6f4 v[132:135], v[8:15], v[222:229], v[132:135]
	s_setprio 1
	s_setprio 0
	v_mfma_f32_16x16x128_f8f6f4 v[52:55], v[16:23], v[198:205], v[52:55]
	v_mfma_f32_16x16x128_f8f6f4 v[164:167], v[24:31], v[198:205], v[164:167]
	v_mfma_f32_16x16x128_f8f6f4 v[156:159], v[16:23], v[206:213], v[156:159]
	v_mfma_f32_16x16x128_f8f6f4 v[160:163], v[24:31], v[206:213], v[160:163]
	v_mfma_f32_16x16x128_f8f6f4 v[148:151], v[16:23], v[214:221], v[148:151]
	v_mfma_f32_16x16x128_f8f6f4 v[152:155], v[24:31], v[214:221], v[152:155]
	v_mfma_f32_16x16x128_f8f6f4 v[140:143], v[16:23], v[222:229], v[140:143]
	v_mfma_f32_16x16x128_f8f6f4 v[136:139], v[24:31], v[222:229], v[136:139]
	s_setprio 1
	s_barrier
	s_add_i32 s48, s48, 2
	s_add_u32 s44, s44, 0x100
	s_addc_u32 s45, s45, 0
	s_add_u32 s46, s46, 0x100
	s_addc_u32 s47, s47, 0
	v_lshl_add_u64 v[168:169], v[168:169], 0, s[26:27]
	s_cmp_gt_u32 s48, 5
	v_lshl_add_u64 v[170:171], v[170:171], 0, s[26:27]
	s_cbranch_scc0 .LBB0_626
	s_nop 15
	s_nop 7
	s_waitcnt vmcnt(0)
	s_cmpk_lt_u32 s19, 0x100
	s_cbranch_scc0 .LBB0_629
	s_barrier

.LBB0_815:
	s_add_u32 s44, s90, s4
	s_addc_u32 s45, s91, s5
	s_add_u32 s71, s44, 0x21c00100
	s_addc_u32 s72, s45, 0
	s_cmpk_eq_i32 s4, 0x300
	v_lshl_add_u64 v[0:1], v[180:181], 0, s[4:5]
	s_cselect_b64 vcc, -1, 0
	v_cndmask_b32_e32 v183, v1, v167, vcc
	v_cndmask_b32_e32 v182, v0, v220, vcc
	ds_read_b128 v[8:11], v194
	ds_read_b128 v[12:15], v198
	ds_read_b128 v[24:27], v199
	ds_read_b128 v[28:31], v200
	ds_read_b128 v[0:3], v195
	ds_read_b128 v[4:7], v201
	ds_read_b128 v[16:19], v202
	ds_read_b128 v[20:23], v203
	s_and_b64 s[44:45], vcc, exec
	s_cselect_b32 s45, s13, s72
	s_cselect_b32 s44, s12, s71
	v_cndmask_b32_e32 v160, v219, v215, vcc
	v_cndmask_b32_e32 v184, v170, v216, vcc
	v_cndmask_b32_e32 v175, v172, v217, vcc
	v_cndmask_b32_e32 v173, v174, v218, vcc
	v_lshl_add_u64 v[186:187], v[178:179], 0, s[4:5]
	s_add_i32 m0, s0, 0xc000
	ds_read_b128 v[222:225], v212
	ds_read_b128 v[226:229], v212 offset:1024
	ds_read_b128 v[230:233], v212 offset:2048
	ds_read_b128 v[234:237], v212 offset:3072
	ds_read_b128 v[238:241], v212 offset:4096
	ds_read_b128 v[242:245], v212 offset:5120
	ds_read_b128 v[246:249], v212 offset:6144
	ds_read_b128 v[250:253], v212 offset:7168
	global_load_lds_dwordx4 v[186:187], off
	v_lshl_add_u64 v[186:187], v[176:177], 0, s[4:5]
	s_add_i32 m0, s0, 0xe000
	s_nop 0
	global_load_lds_dwordx4 v[186:187], off
	s_waitcnt vmcnt(8)
	s_waitcnt lgkmcnt(0)
	s_barrier
	s_setprio 0
	s_waitcnt lgkmcnt(0)
	v_mfma_f32_16x16x128_f8f6f4 v[156:159], v[8:15], v[222:229], v[156:159]
	v_mfma_f32_16x16x128_f8f6f4 v[152:155], v[24:31], v[222:229], v[152:155]
	v_mfma_f32_16x16x128_f8f6f4 v[140:143], v[8:15], v[230:237], v[140:143]
	v_mfma_f32_16x16x128_f8f6f4 v[136:139], v[24:31], v[230:237], v[136:139]
	v_mfma_f32_16x16x128_f8f6f4 v[124:127], v[8:15], v[238:245], v[124:127]
	v_mfma_f32_16x16x128_f8f6f4 v[120:123], v[24:31], v[238:245], v[120:123]
	v_mfma_f32_16x16x128_f8f6f4 v[108:111], v[8:15], v[246:253], v[108:111]
	v_mfma_f32_16x16x128_f8f6f4 v[104:107], v[24:31], v[246:253], v[104:107]
	s_setprio 1
	s_setprio 0
	v_mfma_f32_16x16x128_f8f6f4 v[148:151], v[0:7], v[222:229], v[148:151]
	v_mfma_f32_16x16x128_f8f6f4 v[144:147], v[16:23], v[222:229], v[144:147]
	v_mfma_f32_16x16x128_f8f6f4 v[132:135], v[0:7], v[230:237], v[132:135]
	v_mfma_f32_16x16x128_f8f6f4 v[128:131], v[16:23], v[230:237], v[128:131]
	v_mfma_f32_16x16x128_f8f6f4 v[116:119], v[0:7], v[238:245], v[116:119]
	v_mfma_f32_16x16x128_f8f6f4 v[112:115], v[16:23], v[238:245], v[112:115]
	v_mfma_f32_16x16x128_f8f6f4 v[100:103], v[0:7], v[246:253], v[100:103]
	v_mfma_f32_16x16x128_f8f6f4 v[96:99], v[16:23], v[246:253], v[96:99]
	s_setprio 1
	s_barrier
	s_mov_b32 m0, s21
	v_lshl_add_u64 v[186:187], v[182:183], 0, v[164:165]
	ds_read_b128 v[222:225], v212 offset:16384
	ds_read_b128 v[226:229], v212 offset:17408
	ds_read_b128 v[230:233], v212 offset:18432
	ds_read_b128 v[234:237], v212 offset:19456
	ds_read_b128 v[238:241], v212 offset:20480
	ds_read_b128 v[242:245], v212 offset:21504
	ds_read_b128 v[246:249], v212 offset:22528
	ds_read_b128 v[250:253], v212 offset:23552
	global_load_lds_dwordx4 v[186:187], off
	v_lshl_add_u64 v[188:189], v[182:183], 0, v[162:163]
	s_mov_b32 m0, s22
	v_lshl_add_u64 v[190:191], v[182:183], 0, s[16:17]
	global_load_lds_dwordx4 v[188:189], off
	v_lshl_add_u64 v[192:193], v[190:191], 0, v[164:165]
	s_mov_b32 m0, s23
	v_lshl_add_u64 v[190:191], v[190:191], 0, v[162:163]
	global_load_lds_dwordx4 v[192:193], off
	s_mov_b32 m0, s28
	v_mov_b32_e32 v185, v161
	global_load_lds_dwordx4 v[190:191], off
	s_mov_b32 m0, s0
	v_lshl_add_u64 v[190:191], s[44:45], 0, v[160:161]
	global_load_lds_dwordx4 v160, s[44:45]
	s_mov_b32 m0, s29
	s_nop 0
	global_load_lds_dwordx4 v184, s[44:45]
	s_waitcnt vmcnt(8)
	s_waitcnt lgkmcnt(0)
	v_lshl_add_u64 v[184:185], s[44:45], 0, v[184:185]
	s_barrier
	s_setprio 0
	s_waitcnt lgkmcnt(0)
	v_mfma_f32_16x16x128_f8f6f4 v[84:87], v[8:15], v[222:229], v[84:87]
	v_mfma_f32_16x16x128_f8f6f4 v[80:83], v[24:31], v[222:229], v[80:83]
	v_mfma_f32_16x16x128_f8f6f4 v[68:71], v[8:15], v[230:237], v[68:71]
	v_mfma_f32_16x16x128_f8f6f4 v[64:67], v[24:31], v[230:237], v[64:67]
	v_mfma_f32_16x16x128_f8f6f4 v[52:55], v[8:15], v[238:245], v[52:55]
	v_mfma_f32_16x16x128_f8f6f4 v[48:51], v[24:31], v[238:245], v[48:51]
	v_mfma_f32_16x16x128_f8f6f4 v[36:39], v[8:15], v[246:253], v[36:39]
	v_mfma_f32_16x16x128_f8f6f4 v[32:35], v[24:31], v[246:253], v[32:35]
	s_setprio 1
	s_setprio 0
	v_mfma_f32_16x16x128_f8f6f4 v[92:95], v[0:7], v[222:229], v[92:95]
	v_mfma_f32_16x16x128_f8f6f4 v[88:91], v[16:23], v[222:229], v[88:91]
	v_mfma_f32_16x16x128_f8f6f4 v[76:79], v[0:7], v[230:237], v[76:79]
	v_mfma_f32_16x16x128_f8f6f4 v[72:75], v[16:23], v[230:237], v[72:75]
	v_mfma_f32_16x16x128_f8f6f4 v[60:63], v[0:7], v[238:245], v[60:63]
	v_mfma_f32_16x16x128_f8f6f4 v[56:59], v[16:23], v[238:245], v[56:59]
	v_mfma_f32_16x16x128_f8f6f4 v[44:47], v[0:7], v[246:253], v[44:47]
	v_mfma_f32_16x16x128_f8f6f4 v[40:43], v[16:23], v[246:253], v[40:43]
	s_setprio 1
	s_barrier
	ds_read_b128 v[4:7], v204
	ds_read_b128 v[8:11], v205
	ds_read_b128 v[0:3], v196
	ds_read_b128 v[16:19], v197
	ds_read_b128 v[12:15], v206
	ds_read_b128 v[20:23], v207
	ds_read_b128 v[24:27], v208
	ds_read_b128 v[28:31], v209
	s_mov_b32 m0, s30
	ds_read_b128 v[222:225], v212 offset:32768
	ds_read_b128 v[226:229], v212 offset:33792
	ds_read_b128 v[230:233], v212 offset:34816
	ds_read_b128 v[234:237], v212 offset:35840
	ds_read_b128 v[238:241], v212 offset:36864
	ds_read_b128 v[242:245], v212 offset:37888
	ds_read_b128 v[246:249], v212 offset:38912
	ds_read_b128 v[250:253], v212 offset:39936
	global_load_lds_dwordx4 v175, s[44:45]
	s_mov_b32 m0, s31
	s_nop 0
	global_load_lds_dwordx4 v173, s[44:45]
	s_waitcnt vmcnt(8)
	s_waitcnt lgkmcnt(0)
	s_barrier
	s_setprio 0
	s_waitcnt lgkmcnt(0)
	v_mfma_f32_16x16x128_f8f6f4 v[156:159], v[0:7], v[222:229], v[156:159]
	v_mfma_f32_16x16x128_f8f6f4 v[152:155], v[8:15], v[222:229], v[152:155]
	v_mfma_f32_16x16x128_f8f6f4 v[140:143], v[0:7], v[230:237], v[140:143]
	v_mfma_f32_16x16x128_f8f6f4 v[136:139], v[8:15], v[230:237], v[136:139]
	v_mfma_f32_16x16x128_f8f6f4 v[124:127], v[0:7], v[238:245], v[124:127]
	v_mfma_f32_16x16x128_f8f6f4 v[120:123], v[8:15], v[238:245], v[120:123]
	v_mfma_f32_16x16x128_f8f6f4 v[108:111], v[0:7], v[246:253], v[108:111]
	v_mfma_f32_16x16x128_f8f6f4 v[104:107], v[8:15], v[246:253], v[104:107]
	s_setprio 1
	s_setprio 0
	v_mfma_f32_16x16x128_f8f6f4 v[148:151], v[16:23], v[222:229], v[148:151]
	v_mfma_f32_16x16x128_f8f6f4 v[144:147], v[24:31], v[222:229], v[144:147]
	v_mfma_f32_16x16x128_f8f6f4 v[132:135], v[16:23], v[230:237], v[132:135]
	v_mfma_f32_16x16x128_f8f6f4 v[128:131], v[24:31], v[230:237], v[128:131]
	v_mfma_f32_16x16x128_f8f6f4 v[116:119], v[16:23], v[238:245], v[116:119]
	v_mfma_f32_16x16x128_f8f6f4 v[112:115], v[24:31], v[238:245], v[112:115]
	v_mfma_f32_16x16x128_f8f6f4 v[100:103], v[16:23], v[246:253], v[100:103]
	v_mfma_f32_16x16x128_f8f6f4 v[96:99], v[24:31], v[246:253], v[96:99]
	s_setprio 1
	s_barrier
	s_mov_b32 m0, s33
	v_lshl_add_u64 v[186:187], v[186:187], 0, s[26:27]
	ds_read_b128 v[222:225], v212 offset:49152
	ds_read_b128 v[226:229], v212 offset:50176
	ds_read_b128 v[230:233], v212 offset:51200
	ds_read_b128 v[234:237], v212 offset:52224
	ds_read_b128 v[238:241], v212 offset:53248
	ds_read_b128 v[242:245], v212 offset:54272
	ds_read_b128 v[246:249], v212 offset:55296
	ds_read_b128 v[250:253], v212 offset:56320
	global_load_lds_dwordx4 v[186:187], off
	v_lshl_add_u64 v[186:187], v[188:189], 0, s[26:27]
	s_mov_b32 m0, s46
	v_lshl_add_u64 v[182:183], v[182:183], 0, s[36:37]
	global_load_lds_dwordx4 v[186:187], off
	v_lshl_add_u64 v[186:187], v[182:183], 0, v[164:165]
	s_mov_b32 m0, s49
	v_lshl_add_u64 v[182:183], v[182:183], 0, v[162:163]
	global_load_lds_dwordx4 v[186:187], off
	s_mov_b32 m0, s50
	s_nop 0
	global_load_lds_dwordx4 v[182:183], off
	v_lshl_add_u64 v[182:183], v[190:191], 0, s[26:27]
	s_mov_b32 m0, s47
	s_nop 0
	global_load_lds_dwordx4 v[182:183], off
	v_lshl_add_u64 v[182:183], v[184:185], 0, s[26:27]
	s_mov_b32 m0, s48
	s_nop 0
	global_load_lds_dwordx4 v[182:183], off
	s_waitcnt vmcnt(8)
	s_waitcnt lgkmcnt(0)
	s_barrier
	s_setprio 0
	s_waitcnt lgkmcnt(0)
	v_mfma_f32_16x16x128_f8f6f4 v[84:87], v[0:7], v[222:229], v[84:87]
	v_mfma_f32_16x16x128_f8f6f4 v[80:83], v[8:15], v[222:229], v[80:83]
	v_mfma_f32_16x16x128_f8f6f4 v[68:71], v[0:7], v[230:237], v[68:71]
	v_mfma_f32_16x16x128_f8f6f4 v[64:67], v[8:15], v[230:237], v[64:67]
	v_mfma_f32_16x16x128_f8f6f4 v[52:55], v[0:7], v[238:245], v[52:55]
	v_mfma_f32_16x16x128_f8f6f4 v[48:51], v[8:15], v[238:245], v[48:51]
	v_mfma_f32_16x16x128_f8f6f4 v[36:39], v[0:7], v[246:253], v[36:39]
	v_mfma_f32_16x16x128_f8f6f4 v[32:35], v[8:15], v[246:253], v[32:35]
	s_setprio 1
	s_setprio 0
	v_mfma_f32_16x16x128_f8f6f4 v[92:95], v[16:23], v[222:229], v[92:95]
	v_mfma_f32_16x16x128_f8f6f4 v[88:91], v[24:31], v[222:229], v[88:91]
	v_mfma_f32_16x16x128_f8f6f4 v[76:79], v[16:23], v[230:237], v[76:79]
	v_mfma_f32_16x16x128_f8f6f4 v[72:75], v[24:31], v[230:237], v[72:75]
	v_mfma_f32_16x16x128_f8f6f4 v[60:63], v[16:23], v[238:245], v[60:63]
	v_mfma_f32_16x16x128_f8f6f4 v[56:59], v[24:31], v[238:245], v[56:59]
	v_mfma_f32_16x16x128_f8f6f4 v[44:47], v[16:23], v[246:253], v[44:47]
	v_mfma_f32_16x16x128_f8f6f4 v[40:43], v[24:31], v[246:253], v[40:43]
	s_setprio 1
	s_barrier
	s_add_i32 s43, s43, 2
	s_add_u32 s4, s4, 0x100
	s_addc_u32 s5, s5, 0
	s_cmp_gt_u32 s43, 5
	s_cbranch_scc0 .LBB0_815
	s_nop 15
	s_nop 7
	s_and_b64 vcc, exec, s[38:39]
	s_cbranch_vccz .LBB0_818
	s_barrier

.LBB0_832:
	s_add_u32 s50, s38, s44
	s_addc_u32 s51, s39, s45
	s_add_u32 s48, s50, 0x100
	s_addc_u32 s49, s51, 0
	s_and_b64 s[46:47], s[42:43], exec
	s_cselect_b32 s47, s17, s49
	s_cselect_b32 s46, s59, s48
	s_add_u32 s44, s36, s44
	s_addc_u32 s45, s37, s45
	s_add_u32 s44, s44, 0x100
	s_addc_u32 s45, s45, 0
	s_and_b64 s[42:43], s[42:43], exec
	s_cselect_b32 s49, s25, s45
	s_cselect_b32 s48, s60, s44
	s_add_u32 s52, s50, 0x10080
	ds_read_b128 v[146:149], v143
	ds_read_b128 v[150:153], v143 offset:1024
	ds_read_b128 v[154:157], v143 offset:2048
	ds_read_b128 v[158:161], v143 offset:3072
	ds_read_b128 v[162:165], v144
	ds_read_b128 v[166:169], v144 offset:1024
	ds_read_b128 v[170:173], v144 offset:2048
	ds_read_b128 v[174:177], v144 offset:3072
	s_addc_u32 s53, s51, 0
	s_add_i32 s70, s0, s28
	s_add_i32 m0, s29, 0xc000
	s_add_i32 s71, s29, 0xe000
	s_add_i32 s67, s70, 0x2000
	s_add_u32 s50, s48, 0x10000
	s_addc_u32 s51, s49, 0
	s_add_i32 s69, s56, s28
	s_add_i32 s68, s69, 0x2000
	s_add_i32 s66, 0, 0x18000
	s_add_i32 s65, 0, 0x1c000
	s_add_u32 s44, s46, 0x10000
	s_addc_u32 s45, s47, 0
	s_add_i32 s64, s66, s28
	s_add_i32 s62, s64, 0x2000
	s_add_u32 s42, s48, 0x10080
	s_addc_u32 s43, s49, 0
	s_add_i32 s63, s65, s28
	s_add_i32 s61, s63, 0x2000
	v_lshl_add_u64 v[138:139], s[52:53], 0, v[132:133]
	ds_read_b128 v[178:181], v145
	ds_read_b128 v[182:185], v145 offset:1024
	ds_read_b128 v[186:189], v145 offset:2048
	ds_read_b128 v[190:193], v145 offset:3072
	ds_read_b128 v[194:197], v145 offset:4096
	ds_read_b128 v[198:201], v145 offset:5120
	ds_read_b128 v[202:205], v145 offset:6144
	ds_read_b128 v[206:209], v145 offset:7168
	global_load_lds_dwordx4 v[138:139], off
	v_lshl_add_u64 v[138:139], s[52:53], 0, v[134:135]
	s_mov_b32 m0, s71
	s_nop 0
	global_load_lds_dwordx4 v[138:139], off
	s_waitcnt vmcnt(8)
	s_waitcnt lgkmcnt(0)
	s_barrier
	s_setprio 0
	s_waitcnt lgkmcnt(0)
	v_mfma_f32_16x16x32_bf16 v[124:127], v[146:149], v[178:181], v[124:127]
	v_mfma_f32_16x16x32_bf16 v[120:123], v[154:157], v[178:181], v[120:123]
	v_mfma_f32_16x16x32_bf16 v[116:119], v[146:149], v[186:189], v[116:119]
	v_mfma_f32_16x16x32_bf16 v[108:111], v[154:157], v[186:189], v[108:111]
	v_mfma_f32_16x16x32_bf16 v[100:103], v[146:149], v[194:197], v[100:103]
	v_mfma_f32_16x16x32_bf16 v[92:95], v[154:157], v[194:197], v[92:95]
	v_mfma_f32_16x16x32_bf16 v[84:87], v[146:149], v[202:205], v[84:87]
	v_mfma_f32_16x16x32_bf16 v[76:79], v[154:157], v[202:205], v[76:79]
	v_mfma_f32_16x16x32_bf16 v[124:127], v[150:153], v[182:185], v[124:127]
	v_mfma_f32_16x16x32_bf16 v[120:123], v[158:161], v[182:185], v[120:123]
	v_mfma_f32_16x16x32_bf16 v[116:119], v[150:153], v[190:193], v[116:119]
	v_mfma_f32_16x16x32_bf16 v[108:111], v[158:161], v[190:193], v[108:111]
	v_mfma_f32_16x16x32_bf16 v[100:103], v[150:153], v[198:201], v[100:103]
	v_mfma_f32_16x16x32_bf16 v[92:95], v[158:161], v[198:201], v[92:95]
	v_mfma_f32_16x16x32_bf16 v[84:87], v[150:153], v[206:209], v[84:87]
	v_mfma_f32_16x16x32_bf16 v[76:79], v[158:161], v[206:209], v[76:79]
	s_setprio 1
	s_setprio 0
	v_mfma_f32_16x16x32_bf16 v[112:115], v[162:165], v[178:181], v[112:115]
	v_mfma_f32_16x16x32_bf16 v[104:107], v[170:173], v[178:181], v[104:107]
	v_mfma_f32_16x16x32_bf16 v[96:99], v[162:165], v[186:189], v[96:99]
	v_mfma_f32_16x16x32_bf16 v[88:91], v[170:173], v[186:189], v[88:91]
	v_mfma_f32_16x16x32_bf16 v[80:83], v[162:165], v[194:197], v[80:83]
	v_mfma_f32_16x16x32_bf16 v[72:75], v[170:173], v[194:197], v[72:75]
	v_mfma_f32_16x16x32_bf16 v[52:55], v[162:165], v[202:205], v[52:55]
	v_mfma_f32_16x16x32_bf16 v[48:51], v[170:173], v[202:205], v[48:51]
	v_mfma_f32_16x16x32_bf16 v[112:115], v[166:169], v[182:185], v[112:115]
	v_mfma_f32_16x16x32_bf16 v[104:107], v[174:177], v[182:185], v[104:107]
	v_mfma_f32_16x16x32_bf16 v[96:99], v[166:169], v[190:193], v[96:99]
	v_mfma_f32_16x16x32_bf16 v[88:91], v[174:177], v[190:193], v[88:91]
	v_mfma_f32_16x16x32_bf16 v[80:83], v[166:169], v[198:201], v[80:83]
	v_mfma_f32_16x16x32_bf16 v[72:75], v[174:177], v[198:201], v[72:75]
	v_mfma_f32_16x16x32_bf16 v[52:55], v[166:169], v[206:209], v[52:55]
	v_mfma_f32_16x16x32_bf16 v[48:51], v[174:177], v[206:209], v[48:51]
	s_setprio 1
	s_barrier
	s_mov_b32 m0, s70
	v_lshl_add_u64 v[138:139], s[48:49], 0, v[130:131]
	ds_read_b128 v[178:181], v145 offset:16384
	ds_read_b128 v[182:185], v145 offset:17408
	ds_read_b128 v[186:189], v145 offset:18432
	ds_read_b128 v[190:193], v145 offset:19456
	ds_read_b128 v[194:197], v145 offset:20480
	ds_read_b128 v[198:201], v145 offset:21504
	ds_read_b128 v[202:205], v145 offset:22528
	ds_read_b128 v[206:209], v145 offset:23552
	global_load_lds_dwordx4 v[138:139], off
	v_lshl_add_u64 v[210:211], s[48:49], 0, v[128:129]
	s_mov_b32 m0, s67
	v_lshl_add_u64 v[212:213], s[50:51], 0, v[130:131]
	global_load_lds_dwordx4 v[210:211], off
	s_mov_b32 m0, s69
	v_lshl_add_u64 v[214:215], s[46:47], 0, v[134:135]
	global_load_lds_dwordx4 v[212:213], off
	v_lshl_add_u64 v[212:213], s[50:51], 0, v[128:129]
	s_mov_b32 m0, s68
	s_nop 0
	global_load_lds_dwordx4 v[212:213], off
	v_lshl_add_u64 v[212:213], s[46:47], 0, v[132:133]
	s_mov_b32 m0, s29
	s_nop 0
	global_load_lds_dwordx4 v[212:213], off
	s_mov_b32 m0, s30
	s_nop 0
	global_load_lds_dwordx4 v[214:215], off
	s_waitcnt vmcnt(8)
	s_waitcnt lgkmcnt(0)
	s_barrier
	s_setprio 0
	s_waitcnt lgkmcnt(0)
	v_mfma_f32_16x16x32_bf16 v[44:47], v[146:149], v[178:181], v[44:47]
	v_mfma_f32_16x16x32_bf16 v[32:35], v[154:157], v[178:181], v[32:35]
	v_mfma_f32_16x16x32_bf16 v[4:7], v[146:149], v[186:189], v[4:7]
	v_mfma_f32_16x16x32_bf16 v[0:3], v[154:157], v[186:189], v[0:3]
	v_mfma_f32_16x16x32_bf16 v[28:31], v[146:149], v[194:197], v[28:31]
	v_mfma_f32_16x16x32_bf16 v[24:27], v[154:157], v[194:197], v[24:27]
	v_mfma_f32_16x16x32_bf16 v[12:15], v[146:149], v[202:205], v[12:15]
	v_mfma_f32_16x16x32_bf16 v[8:11], v[154:157], v[202:205], v[8:11]
	v_mfma_f32_16x16x32_bf16 v[44:47], v[150:153], v[182:185], v[44:47]
	v_mfma_f32_16x16x32_bf16 v[32:35], v[158:161], v[182:185], v[32:35]
	v_mfma_f32_16x16x32_bf16 v[4:7], v[150:153], v[190:193], v[4:7]
	v_mfma_f32_16x16x32_bf16 v[0:3], v[158:161], v[190:193], v[0:3]
	v_mfma_f32_16x16x32_bf16 v[28:31], v[150:153], v[198:201], v[28:31]
	v_mfma_f32_16x16x32_bf16 v[24:27], v[158:161], v[198:201], v[24:27]
	v_mfma_f32_16x16x32_bf16 v[12:15], v[150:153], v[206:209], v[12:15]
	v_mfma_f32_16x16x32_bf16 v[8:11], v[158:161], v[206:209], v[8:11]
	s_setprio 1
	s_setprio 0
	v_mfma_f32_16x16x32_bf16 v[68:71], v[162:165], v[178:181], v[68:71]
	v_mfma_f32_16x16x32_bf16 v[64:67], v[170:173], v[178:181], v[64:67]
	v_mfma_f32_16x16x32_bf16 v[60:63], v[162:165], v[186:189], v[60:63]
	v_mfma_f32_16x16x32_bf16 v[56:59], v[170:173], v[186:189], v[56:59]
	v_mfma_f32_16x16x32_bf16 v[40:43], v[162:165], v[194:197], v[40:43]
	v_mfma_f32_16x16x32_bf16 v[36:39], v[170:173], v[194:197], v[36:39]
	v_mfma_f32_16x16x32_bf16 v[20:23], v[162:165], v[202:205], v[20:23]
	v_mfma_f32_16x16x32_bf16 v[16:19], v[170:173], v[202:205], v[16:19]
	v_mfma_f32_16x16x32_bf16 v[68:71], v[166:169], v[182:185], v[68:71]
	v_mfma_f32_16x16x32_bf16 v[64:67], v[174:177], v[182:185], v[64:67]
	v_mfma_f32_16x16x32_bf16 v[60:63], v[166:169], v[190:193], v[60:63]
	v_mfma_f32_16x16x32_bf16 v[56:59], v[174:177], v[190:193], v[56:59]
	v_mfma_f32_16x16x32_bf16 v[40:43], v[166:169], v[198:201], v[40:43]
	v_mfma_f32_16x16x32_bf16 v[36:39], v[174:177], v[198:201], v[36:39]
	v_mfma_f32_16x16x32_bf16 v[20:23], v[166:169], v[206:209], v[20:23]
	v_mfma_f32_16x16x32_bf16 v[16:19], v[174:177], v[206:209], v[16:19]
	s_setprio 1
	s_barrier
	v_add_u32_e32 v158, s66, v141
	v_add_u32_e32 v174, s65, v141
	ds_read_b128 v[146:149], v158
	ds_read_b128 v[150:153], v158 offset:1024
	ds_read_b128 v[154:157], v158 offset:2048
	ds_read_b128 v[158:161], v158 offset:3072
	ds_read_b128 v[162:165], v174
	ds_read_b128 v[166:169], v174 offset:1024
	ds_read_b128 v[170:173], v174 offset:2048
	ds_read_b128 v[174:177], v174 offset:3072
	s_mov_b32 m0, s31
	v_lshl_add_u64 v[216:217], s[44:45], 0, v[132:133]
	ds_read_b128 v[178:181], v145 offset:32768
	ds_read_b128 v[182:185], v145 offset:33792
	ds_read_b128 v[186:189], v145 offset:34816
	ds_read_b128 v[190:193], v145 offset:35840
	ds_read_b128 v[194:197], v145 offset:36864
	ds_read_b128 v[198:201], v145 offset:37888
	ds_read_b128 v[202:205], v145 offset:38912
	ds_read_b128 v[206:209], v145 offset:39936
	global_load_lds_dwordx4 v[216:217], off
	v_lshl_add_u64 v[216:217], s[44:45], 0, v[134:135]
	s_mov_b32 m0, s33
	s_nop 0
	global_load_lds_dwordx4 v[216:217], off
	s_waitcnt vmcnt(8)
	s_waitcnt lgkmcnt(0)
	s_barrier
	s_setprio 0
	s_waitcnt lgkmcnt(0)
	v_mfma_f32_16x16x32_bf16 v[124:127], v[146:149], v[178:181], v[124:127]
	v_mfma_f32_16x16x32_bf16 v[120:123], v[154:157], v[178:181], v[120:123]
	v_mfma_f32_16x16x32_bf16 v[116:119], v[146:149], v[186:189], v[116:119]
	v_mfma_f32_16x16x32_bf16 v[108:111], v[154:157], v[186:189], v[108:111]
	v_mfma_f32_16x16x32_bf16 v[100:103], v[146:149], v[194:197], v[100:103]
	v_mfma_f32_16x16x32_bf16 v[92:95], v[154:157], v[194:197], v[92:95]
	v_mfma_f32_16x16x32_bf16 v[84:87], v[146:149], v[202:205], v[84:87]
	v_mfma_f32_16x16x32_bf16 v[76:79], v[154:157], v[202:205], v[76:79]
	v_mfma_f32_16x16x32_bf16 v[124:127], v[150:153], v[182:185], v[124:127]
	v_mfma_f32_16x16x32_bf16 v[120:123], v[158:161], v[182:185], v[120:123]
	v_mfma_f32_16x16x32_bf16 v[116:119], v[150:153], v[190:193], v[116:119]
	v_mfma_f32_16x16x32_bf16 v[108:111], v[158:161], v[190:193], v[108:111]
	v_mfma_f32_16x16x32_bf16 v[100:103], v[150:153], v[198:201], v[100:103]
	v_mfma_f32_16x16x32_bf16 v[92:95], v[158:161], v[198:201], v[92:95]
	v_mfma_f32_16x16x32_bf16 v[84:87], v[150:153], v[206:209], v[84:87]
	v_mfma_f32_16x16x32_bf16 v[76:79], v[158:161], v[206:209], v[76:79]
	s_setprio 1
	s_setprio 0
	v_mfma_f32_16x16x32_bf16 v[112:115], v[162:165], v[178:181], v[112:115]
	v_mfma_f32_16x16x32_bf16 v[104:107], v[170:173], v[178:181], v[104:107]
	v_mfma_f32_16x16x32_bf16 v[96:99], v[162:165], v[186:189], v[96:99]
	v_mfma_f32_16x16x32_bf16 v[88:91], v[170:173], v[186:189], v[88:91]
	v_mfma_f32_16x16x32_bf16 v[80:83], v[162:165], v[194:197], v[80:83]
	v_mfma_f32_16x16x32_bf16 v[72:75], v[170:173], v[194:197], v[72:75]
	v_mfma_f32_16x16x32_bf16 v[52:55], v[162:165], v[202:205], v[52:55]
	v_mfma_f32_16x16x32_bf16 v[48:51], v[170:173], v[202:205], v[48:51]
	v_mfma_f32_16x16x32_bf16 v[112:115], v[166:169], v[182:185], v[112:115]
	v_mfma_f32_16x16x32_bf16 v[104:107], v[174:177], v[182:185], v[104:107]
	v_mfma_f32_16x16x32_bf16 v[96:99], v[166:169], v[190:193], v[96:99]
	v_mfma_f32_16x16x32_bf16 v[88:91], v[174:177], v[190:193], v[88:91]
	v_mfma_f32_16x16x32_bf16 v[80:83], v[166:169], v[198:201], v[80:83]
	v_mfma_f32_16x16x32_bf16 v[72:75], v[174:177], v[198:201], v[72:75]
	v_mfma_f32_16x16x32_bf16 v[52:55], v[166:169], v[206:209], v[52:55]
	v_mfma_f32_16x16x32_bf16 v[48:51], v[174:177], v[206:209], v[48:51]
	s_setprio 1
	s_barrier
	s_mov_b32 m0, s64
	v_lshl_add_u64 v[138:139], v[138:139], 0, s[12:13]
	ds_read_b128 v[178:181], v145 offset:49152
	ds_read_b128 v[182:185], v145 offset:50176
	ds_read_b128 v[186:189], v145 offset:51200
	ds_read_b128 v[190:193], v145 offset:52224
	ds_read_b128 v[194:197], v145 offset:53248
	ds_read_b128 v[198:201], v145 offset:54272
	ds_read_b128 v[202:205], v145 offset:55296
	ds_read_b128 v[206:209], v145 offset:56320
	global_load_lds_dwordx4 v[138:139], off
	v_lshl_add_u64 v[138:139], v[210:211], 0, s[12:13]
	s_mov_b32 m0, s62
	s_nop 0
	global_load_lds_dwordx4 v[138:139], off
	v_lshl_add_u64 v[138:139], s[42:43], 0, v[130:131]
	s_mov_b32 m0, s63
	s_nop 0
	global_load_lds_dwordx4 v[138:139], off
	v_lshl_add_u64 v[138:139], s[42:43], 0, v[128:129]
	s_mov_b32 m0, s61
	s_nop 0
	global_load_lds_dwordx4 v[138:139], off
	v_lshl_add_u64 v[138:139], v[212:213], 0, s[12:13]
	s_mov_b32 m0, s54
	s_nop 0
	global_load_lds_dwordx4 v[138:139], off
	v_lshl_add_u64 v[138:139], v[214:215], 0, s[12:13]
	s_mov_b32 m0, s55
	s_nop 0
	global_load_lds_dwordx4 v[138:139], off
	s_waitcnt vmcnt(8)
	s_waitcnt lgkmcnt(0)
	s_barrier
	s_setprio 0
	s_waitcnt lgkmcnt(0)
	v_mfma_f32_16x16x32_bf16 v[44:47], v[146:149], v[178:181], v[44:47]
	v_mfma_f32_16x16x32_bf16 v[32:35], v[154:157], v[178:181], v[32:35]
	v_mfma_f32_16x16x32_bf16 v[4:7], v[146:149], v[186:189], v[4:7]
	v_mfma_f32_16x16x32_bf16 v[0:3], v[154:157], v[186:189], v[0:3]
	v_mfma_f32_16x16x32_bf16 v[28:31], v[146:149], v[194:197], v[28:31]
	v_mfma_f32_16x16x32_bf16 v[24:27], v[154:157], v[194:197], v[24:27]
	v_mfma_f32_16x16x32_bf16 v[12:15], v[146:149], v[202:205], v[12:15]
	v_mfma_f32_16x16x32_bf16 v[8:11], v[154:157], v[202:205], v[8:11]
	v_mfma_f32_16x16x32_bf16 v[44:47], v[150:153], v[182:185], v[44:47]
	v_mfma_f32_16x16x32_bf16 v[32:35], v[158:161], v[182:185], v[32:35]
	v_mfma_f32_16x16x32_bf16 v[4:7], v[150:153], v[190:193], v[4:7]
	v_mfma_f32_16x16x32_bf16 v[0:3], v[158:161], v[190:193], v[0:3]
	v_mfma_f32_16x16x32_bf16 v[28:31], v[150:153], v[198:201], v[28:31]
	v_mfma_f32_16x16x32_bf16 v[24:27], v[158:161], v[198:201], v[24:27]
	v_mfma_f32_16x16x32_bf16 v[12:15], v[150:153], v[206:209], v[12:15]
	v_mfma_f32_16x16x32_bf16 v[8:11], v[158:161], v[206:209], v[8:11]
	s_setprio 1
	s_setprio 0
	v_mfma_f32_16x16x32_bf16 v[68:71], v[162:165], v[178:181], v[68:71]
	v_mfma_f32_16x16x32_bf16 v[64:67], v[170:173], v[178:181], v[64:67]
	v_mfma_f32_16x16x32_bf16 v[60:63], v[162:165], v[186:189], v[60:63]
	v_mfma_f32_16x16x32_bf16 v[56:59], v[170:173], v[186:189], v[56:59]
	v_mfma_f32_16x16x32_bf16 v[40:43], v[162:165], v[194:197], v[40:43]
	v_mfma_f32_16x16x32_bf16 v[36:39], v[170:173], v[194:197], v[36:39]
	v_mfma_f32_16x16x32_bf16 v[20:23], v[162:165], v[202:205], v[20:23]
	v_mfma_f32_16x16x32_bf16 v[16:19], v[170:173], v[202:205], v[16:19]
	v_mfma_f32_16x16x32_bf16 v[68:71], v[166:169], v[182:185], v[68:71]
	v_mfma_f32_16x16x32_bf16 v[64:67], v[174:177], v[182:185], v[64:67]
	v_mfma_f32_16x16x32_bf16 v[60:63], v[166:169], v[190:193], v[60:63]
	v_mfma_f32_16x16x32_bf16 v[56:59], v[174:177], v[190:193], v[56:59]
	v_mfma_f32_16x16x32_bf16 v[40:43], v[166:169], v[198:201], v[40:43]
	v_mfma_f32_16x16x32_bf16 v[36:39], v[174:177], v[198:201], v[36:39]
	v_mfma_f32_16x16x32_bf16 v[20:23], v[166:169], v[206:209], v[20:23]
	v_mfma_f32_16x16x32_bf16 v[16:19], v[174:177], v[206:209], v[16:19]
	s_setprio 1
	s_barrier
	s_andn2_b64 vcc, exec, s[40:41]
	s_mov_b64 s[42:43], -1
	s_mov_b64 s[40:41], 0
	s_mov_b64 s[44:45], 0x100
	s_cbranch_vccz .LBB0_832
	s_and_b64 vcc, exec, s[14:15]
	s_cbranch_vccz .LBB0_835
	s_barrier

.LBB0_913:
	v_lshl_add_u64 v[0:1], v[168:169], 0, s[44:45]
	v_lshl_add_u64 v[0:1], v[0:1], 0, s[92:93]
	v_cndmask_b32_e64 v179, v1, v171, s[42:43]
	v_cndmask_b32_e64 v178, v0, v205, s[42:43]
	ds_read_b128 v[8:11], v185
	ds_read_b128 v[12:15], v189
	ds_read_b128 v[24:27], v190
	ds_read_b128 v[28:31], v191
	ds_read_b128 v[0:3], v186
	ds_read_b128 v[4:7], v192
	ds_read_b128 v[16:19], v193
	ds_read_b128 v[20:23], v194
	s_add_u32 s25, s34, s44
	s_addc_u32 s75, s35, s45
	s_add_u32 s94, s25, 0x100
	s_addc_u32 s95, s75, 0
	s_and_b64 s[46:47], s[42:43], exec
	s_cselect_b32 s47, s37, s95
	s_cselect_b32 s46, s74, s94
	s_add_u32 s44, s25, 0x10080
	s_addc_u32 s45, s75, 0
	s_add_i32 m0, s23, 0xc000
	s_add_i32 s25, s23, 0xe000
	s_add_u32 s42, s46, 0x10000
	s_addc_u32 s43, s47, 0
	v_lshl_add_u64 v[180:181], v[178:179], 0, s[0:1]
	v_lshl_add_u64 v[174:175], v[178:179], 0, s[14:15]
	v_lshl_add_u64 v[176:177], s[44:45], 0, v[164:165]
	ds_read_b128 v[206:209], v203
	ds_read_b128 v[210:213], v203 offset:1024
	ds_read_b128 v[214:217], v203 offset:2048
	ds_read_b128 v[218:221], v203 offset:3072
	ds_read_b128 v[222:225], v203 offset:4096
	ds_read_b128 v[226:229], v203 offset:5120
	ds_read_b128 v[230:233], v203 offset:6144
	ds_read_b128 v[234:237], v203 offset:7168
	global_load_lds_dwordx4 v[176:177], off
	v_lshl_add_u64 v[176:177], s[44:45], 0, v[166:167]
	s_mov_b32 m0, s25
	s_nop 0
	global_load_lds_dwordx4 v[176:177], off
	s_waitcnt vmcnt(8)
	s_waitcnt lgkmcnt(0)
	s_barrier
	s_setprio 0
	s_waitcnt lgkmcnt(0)
	v_mfma_f32_16x16x128_f8f6f4 v[156:159], v[8:15], v[206:213], v[156:159]
	v_mfma_f32_16x16x128_f8f6f4 v[152:155], v[24:31], v[206:213], v[152:155]
	v_mfma_f32_16x16x128_f8f6f4 v[140:143], v[8:15], v[214:221], v[140:143]
	v_mfma_f32_16x16x128_f8f6f4 v[136:139], v[24:31], v[214:221], v[136:139]
	v_mfma_f32_16x16x128_f8f6f4 v[124:127], v[8:15], v[222:229], v[124:127]
	v_mfma_f32_16x16x128_f8f6f4 v[120:123], v[24:31], v[222:229], v[120:123]
	v_mfma_f32_16x16x128_f8f6f4 v[108:111], v[8:15], v[230:237], v[108:111]
	v_mfma_f32_16x16x128_f8f6f4 v[104:107], v[24:31], v[230:237], v[104:107]
	s_setprio 1
	s_setprio 0
	v_mfma_f32_16x16x128_f8f6f4 v[148:151], v[0:7], v[206:213], v[148:151]
	v_mfma_f32_16x16x128_f8f6f4 v[144:147], v[16:23], v[206:213], v[144:147]
	v_mfma_f32_16x16x128_f8f6f4 v[132:135], v[0:7], v[214:221], v[132:135]
	v_mfma_f32_16x16x128_f8f6f4 v[128:131], v[16:23], v[214:221], v[128:131]
	v_mfma_f32_16x16x128_f8f6f4 v[116:119], v[0:7], v[222:229], v[116:119]
	v_mfma_f32_16x16x128_f8f6f4 v[112:115], v[16:23], v[222:229], v[112:115]
	v_mfma_f32_16x16x128_f8f6f4 v[96:99], v[0:7], v[230:237], v[96:99]
	v_mfma_f32_16x16x128_f8f6f4 v[88:91], v[16:23], v[230:237], v[88:91]
	s_setprio 1
	s_barrier
	s_mov_b32 m0, s27
	v_lshl_add_u64 v[176:177], v[178:179], 0, v[162:163]
	ds_read_b128 v[206:209], v203 offset:16384
	ds_read_b128 v[210:213], v203 offset:17408
	ds_read_b128 v[214:217], v203 offset:18432
	ds_read_b128 v[218:221], v203 offset:19456
	ds_read_b128 v[222:225], v203 offset:20480
	ds_read_b128 v[226:229], v203 offset:21504
	ds_read_b128 v[230:233], v203 offset:22528
	ds_read_b128 v[234:237], v203 offset:23552
	global_load_lds_dwordx4 v[176:177], off
	v_lshl_add_u64 v[178:179], v[178:179], 0, v[160:161]
	s_mov_b32 m0, s28
	v_lshl_add_u64 v[182:183], v[180:181], 0, v[162:163]
	global_load_lds_dwordx4 v[178:179], off
	s_mov_b32 m0, s29
	v_lshl_add_u64 v[180:181], v[180:181], 0, v[160:161]
	global_load_lds_dwordx4 v[182:183], off
	s_mov_b32 m0, s30
	v_lshl_add_u64 v[182:183], s[46:47], 0, v[166:167]
	global_load_lds_dwordx4 v[180:181], off
	v_lshl_add_u64 v[180:181], s[46:47], 0, v[164:165]
	s_mov_b32 m0, s23
	s_nop 0
	global_load_lds_dwordx4 v[180:181], off
	s_mov_b32 m0, s31
	s_nop 0
	global_load_lds_dwordx4 v[182:183], off
	s_waitcnt vmcnt(8)
	s_waitcnt lgkmcnt(0)
	s_barrier
	s_setprio 0
	s_waitcnt lgkmcnt(0)
	v_mfma_f32_16x16x128_f8f6f4 v[84:87], v[8:15], v[206:213], v[84:87]
	v_mfma_f32_16x16x128_f8f6f4 v[76:79], v[24:31], v[206:213], v[76:79]
	v_mfma_f32_16x16x128_f8f6f4 v[60:63], v[8:15], v[214:221], v[60:63]
	v_mfma_f32_16x16x128_f8f6f4 v[48:51], v[24:31], v[214:221], v[48:51]
	v_mfma_f32_16x16x128_f8f6f4 v[68:71], v[8:15], v[222:229], v[68:71]
	v_mfma_f32_16x16x128_f8f6f4 v[56:59], v[24:31], v[222:229], v[56:59]
	v_mfma_f32_16x16x128_f8f6f4 v[44:47], v[8:15], v[230:237], v[44:47]
	v_mfma_f32_16x16x128_f8f6f4 v[36:39], v[24:31], v[230:237], v[36:39]
	s_setprio 1
	s_setprio 0
	v_mfma_f32_16x16x128_f8f6f4 v[100:103], v[0:7], v[206:213], v[100:103]
	v_mfma_f32_16x16x128_f8f6f4 v[92:95], v[16:23], v[206:213], v[92:95]
	v_mfma_f32_16x16x128_f8f6f4 v[80:83], v[0:7], v[214:221], v[80:83]
	v_mfma_f32_16x16x128_f8f6f4 v[72:75], v[16:23], v[214:221], v[72:75]
	v_mfma_f32_16x16x128_f8f6f4 v[64:67], v[0:7], v[222:229], v[64:67]
	v_mfma_f32_16x16x128_f8f6f4 v[52:55], v[16:23], v[222:229], v[52:55]
	v_mfma_f32_16x16x128_f8f6f4 v[40:43], v[0:7], v[230:237], v[40:43]
	v_mfma_f32_16x16x128_f8f6f4 v[32:35], v[16:23], v[230:237], v[32:35]
	s_setprio 1
	s_barrier
	ds_read_b128 v[4:7], v195
	ds_read_b128 v[8:11], v196
	ds_read_b128 v[0:3], v187
	ds_read_b128 v[16:19], v188
	ds_read_b128 v[12:15], v197
	ds_read_b128 v[20:23], v198
	ds_read_b128 v[24:27], v199
	ds_read_b128 v[28:31], v200
	s_mov_b32 m0, s33
	v_lshl_add_u64 v[238:239], s[42:43], 0, v[164:165]
	ds_read_b128 v[206:209], v203 offset:32768
	ds_read_b128 v[210:213], v203 offset:33792
	ds_read_b128 v[214:217], v203 offset:34816
	ds_read_b128 v[218:221], v203 offset:35840
	ds_read_b128 v[222:225], v203 offset:36864
	ds_read_b128 v[226:229], v203 offset:37888
	ds_read_b128 v[230:233], v203 offset:38912
	ds_read_b128 v[234:237], v203 offset:39936
	global_load_lds_dwordx4 v[238:239], off
	v_lshl_add_u64 v[238:239], s[42:43], 0, v[166:167]
	s_mov_b32 m0, s48
	s_nop 0
	global_load_lds_dwordx4 v[238:239], off
	s_waitcnt vmcnt(8)
	s_waitcnt lgkmcnt(0)
	s_barrier
	s_setprio 0
	s_waitcnt lgkmcnt(0)
	v_mfma_f32_16x16x128_f8f6f4 v[156:159], v[0:7], v[206:213], v[156:159]
	v_mfma_f32_16x16x128_f8f6f4 v[152:155], v[8:15], v[206:213], v[152:155]
	v_mfma_f32_16x16x128_f8f6f4 v[140:143], v[0:7], v[214:221], v[140:143]
	v_mfma_f32_16x16x128_f8f6f4 v[136:139], v[8:15], v[214:221], v[136:139]
	v_mfma_f32_16x16x128_f8f6f4 v[124:127], v[0:7], v[222:229], v[124:127]
	v_mfma_f32_16x16x128_f8f6f4 v[120:123], v[8:15], v[222:229], v[120:123]
	v_mfma_f32_16x16x128_f8f6f4 v[108:111], v[0:7], v[230:237], v[108:111]
	v_mfma_f32_16x16x128_f8f6f4 v[104:107], v[8:15], v[230:237], v[104:107]
	s_setprio 1
	s_setprio 0
	v_mfma_f32_16x16x128_f8f6f4 v[148:151], v[16:23], v[206:213], v[148:151]
	v_mfma_f32_16x16x128_f8f6f4 v[144:147], v[24:31], v[206:213], v[144:147]
	v_mfma_f32_16x16x128_f8f6f4 v[132:135], v[16:23], v[214:221], v[132:135]
	v_mfma_f32_16x16x128_f8f6f4 v[128:131], v[24:31], v[214:221], v[128:131]
	v_mfma_f32_16x16x128_f8f6f4 v[116:119], v[16:23], v[222:229], v[116:119]
	v_mfma_f32_16x16x128_f8f6f4 v[112:115], v[24:31], v[222:229], v[112:115]
	v_mfma_f32_16x16x128_f8f6f4 v[96:99], v[16:23], v[230:237], v[96:99]
	v_mfma_f32_16x16x128_f8f6f4 v[88:91], v[24:31], v[230:237], v[88:91]
	s_setprio 1
	s_barrier
	s_mov_b32 m0, s50
	v_lshl_add_u64 v[176:177], v[176:177], 0, s[12:13]
	ds_read_b128 v[206:209], v203 offset:49152
	ds_read_b128 v[210:213], v203 offset:50176
	ds_read_b128 v[214:217], v203 offset:51200
	ds_read_b128 v[218:221], v203 offset:52224
	ds_read_b128 v[222:225], v203 offset:53248
	ds_read_b128 v[226:229], v203 offset:54272
	ds_read_b128 v[230:233], v203 offset:55296
	ds_read_b128 v[234:237], v203 offset:56320
	global_load_lds_dwordx4 v[176:177], off
	v_lshl_add_u64 v[176:177], v[178:179], 0, s[12:13]
	s_mov_b32 m0, s51
	s_nop 0
	global_load_lds_dwordx4 v[176:177], off
	v_lshl_add_u64 v[176:177], v[174:175], 0, v[162:163]
	s_mov_b32 m0, s54
	v_lshl_add_u64 v[174:175], v[174:175], 0, v[160:161]
	global_load_lds_dwordx4 v[176:177], off
	s_mov_b32 m0, s55
	s_nop 0
	global_load_lds_dwordx4 v[174:175], off
	v_lshl_add_u64 v[174:175], v[180:181], 0, s[12:13]
	s_mov_b32 m0, s52
	s_nop 0
	global_load_lds_dwordx4 v[174:175], off
	v_lshl_add_u64 v[174:175], v[182:183], 0, s[12:13]
	s_mov_b32 m0, s53
	s_nop 0
	global_load_lds_dwordx4 v[174:175], off
	s_waitcnt vmcnt(8)
	s_waitcnt lgkmcnt(0)
	s_barrier
	s_setprio 0
	s_waitcnt lgkmcnt(0)
	v_mfma_f32_16x16x128_f8f6f4 v[84:87], v[0:7], v[206:213], v[84:87]
	v_mfma_f32_16x16x128_f8f6f4 v[76:79], v[8:15], v[206:213], v[76:79]
	v_mfma_f32_16x16x128_f8f6f4 v[60:63], v[0:7], v[214:221], v[60:63]
	v_mfma_f32_16x16x128_f8f6f4 v[48:51], v[8:15], v[214:221], v[48:51]
	v_mfma_f32_16x16x128_f8f6f4 v[68:71], v[0:7], v[222:229], v[68:71]
	v_mfma_f32_16x16x128_f8f6f4 v[56:59], v[8:15], v[222:229], v[56:59]
	v_mfma_f32_16x16x128_f8f6f4 v[44:47], v[0:7], v[230:237], v[44:47]
	v_mfma_f32_16x16x128_f8f6f4 v[36:39], v[8:15], v[230:237], v[36:39]
	s_setprio 1
	s_setprio 0
	v_mfma_f32_16x16x128_f8f6f4 v[100:103], v[16:23], v[206:213], v[100:103]
	v_mfma_f32_16x16x128_f8f6f4 v[92:95], v[24:31], v[206:213], v[92:95]
	v_mfma_f32_16x16x128_f8f6f4 v[80:83], v[16:23], v[214:221], v[80:83]
	v_mfma_f32_16x16x128_f8f6f4 v[72:75], v[24:31], v[214:221], v[72:75]
	v_mfma_f32_16x16x128_f8f6f4 v[64:67], v[16:23], v[222:229], v[64:67]
	v_mfma_f32_16x16x128_f8f6f4 v[52:55], v[24:31], v[222:229], v[52:55]
	v_mfma_f32_16x16x128_f8f6f4 v[40:43], v[16:23], v[230:237], v[40:43]
	v_mfma_f32_16x16x128_f8f6f4 v[32:35], v[24:31], v[230:237], v[32:35]
	s_setprio 1
	s_barrier
	s_andn2_b64 vcc, exec, s[40:41]
	s_mov_b64 s[42:43], -1
	s_mov_b64 s[40:41], 0
	s_mov_b64 s[44:45], 0x100
	s_cbranch_vccz .LBB0_913
	s_nop 15
	s_nop 7
	s_and_b64 vcc, exec, s[16:17]
	s_cbranch_vccz .LBB0_916
	s_barrier

.LBB0_925:
	s_add_u32 s34, s4, s16
	s_addc_u32 s35, s5, s17
	s_add_u32 s26, s34, 0x100
	s_addc_u32 s27, s35, 0
	s_and_b64 s[24:25], s[14:15], exec
	s_cselect_b32 s25, s5, s27
	s_cselect_b32 s24, s4, s26
	s_add_u32 s16, s0, s16
	s_addc_u32 s17, s1, s17
	s_add_u32 s16, s16, 0x100
	ds_read_b128 v[144:147], v138
	ds_read_b128 v[148:151], v138 offset:1024
	ds_read_b128 v[152:155], v138 offset:2048
	ds_read_b128 v[156:159], v138 offset:3072
	ds_read_b128 v[160:163], v139
	ds_read_b128 v[164:167], v139 offset:1024
	ds_read_b128 v[168:171], v139 offset:2048
	ds_read_b128 v[172:175], v139 offset:3072
	s_addc_u32 s17, s17, 0
	s_and_b64 s[14:15], s[14:15], exec
	s_cselect_b32 s27, s1, s17
	s_cselect_b32 s26, s0, s16
	s_add_u32 s36, s34, 0x10080
	s_addc_u32 s37, s35, 0
	s_add_u32 s34, s26, 0x10000
	s_addc_u32 s35, s27, 0
	s_add_u32 s16, s24, 0x10000
	s_addc_u32 s17, s25, 0
	s_add_u32 s14, s26, 0x10080
	s_addc_u32 s15, s27, 0
	s_mov_b32 m0, s33
	v_lshl_add_u64 v[208:209], s[36:37], 0, v[132:133]
	ds_read_b128 v[176:179], v140
	ds_read_b128 v[180:183], v140 offset:1024
	ds_read_b128 v[184:187], v140 offset:2048
	ds_read_b128 v[188:191], v140 offset:3072
	ds_read_b128 v[192:195], v140 offset:4096
	ds_read_b128 v[196:199], v140 offset:5120
	ds_read_b128 v[200:203], v140 offset:6144
	ds_read_b128 v[204:207], v140 offset:7168
	global_load_lds_dwordx4 v[208:209], off
	v_lshl_add_u64 v[208:209], s[36:37], 0, v[134:135]
	s_mov_b32 m0, s38
	s_nop 0
	global_load_lds_dwordx4 v[208:209], off
	s_waitcnt vmcnt(8)
	s_waitcnt lgkmcnt(0)
	s_barrier
	s_setprio 0
	s_waitcnt lgkmcnt(0)
	v_mfma_f32_16x16x32_bf16 v[124:127], v[144:147], v[176:179], v[124:127]
	v_mfma_f32_16x16x32_bf16 v[120:123], v[152:155], v[176:179], v[120:123]
	v_mfma_f32_16x16x32_bf16 v[116:119], v[144:147], v[184:187], v[116:119]
	v_mfma_f32_16x16x32_bf16 v[108:111], v[152:155], v[184:187], v[108:111]
	v_mfma_f32_16x16x32_bf16 v[100:103], v[144:147], v[192:195], v[100:103]
	v_mfma_f32_16x16x32_bf16 v[92:95], v[152:155], v[192:195], v[92:95]
	v_mfma_f32_16x16x32_bf16 v[84:87], v[144:147], v[200:203], v[84:87]
	v_mfma_f32_16x16x32_bf16 v[76:79], v[152:155], v[200:203], v[76:79]
	v_mfma_f32_16x16x32_bf16 v[124:127], v[148:151], v[180:183], v[124:127]
	v_mfma_f32_16x16x32_bf16 v[120:123], v[156:159], v[180:183], v[120:123]
	v_mfma_f32_16x16x32_bf16 v[116:119], v[148:151], v[188:191], v[116:119]
	v_mfma_f32_16x16x32_bf16 v[108:111], v[156:159], v[188:191], v[108:111]
	v_mfma_f32_16x16x32_bf16 v[100:103], v[148:151], v[196:199], v[100:103]
	v_mfma_f32_16x16x32_bf16 v[92:95], v[156:159], v[196:199], v[92:95]
	v_mfma_f32_16x16x32_bf16 v[84:87], v[148:151], v[204:207], v[84:87]
	v_mfma_f32_16x16x32_bf16 v[76:79], v[156:159], v[204:207], v[76:79]
	s_setprio 1
	s_setprio 0
	v_mfma_f32_16x16x32_bf16 v[112:115], v[160:163], v[176:179], v[112:115]
	v_mfma_f32_16x16x32_bf16 v[104:107], v[168:171], v[176:179], v[104:107]
	v_mfma_f32_16x16x32_bf16 v[96:99], v[160:163], v[184:187], v[96:99]
	v_mfma_f32_16x16x32_bf16 v[88:91], v[168:171], v[184:187], v[88:91]
	v_mfma_f32_16x16x32_bf16 v[80:83], v[160:163], v[192:195], v[80:83]
	v_mfma_f32_16x16x32_bf16 v[72:75], v[168:171], v[192:195], v[72:75]
	v_mfma_f32_16x16x32_bf16 v[52:55], v[160:163], v[200:203], v[52:55]
	v_mfma_f32_16x16x32_bf16 v[48:51], v[168:171], v[200:203], v[48:51]
	v_mfma_f32_16x16x32_bf16 v[112:115], v[164:167], v[180:183], v[112:115]
	v_mfma_f32_16x16x32_bf16 v[104:107], v[172:175], v[180:183], v[104:107]
	v_mfma_f32_16x16x32_bf16 v[96:99], v[164:167], v[188:191], v[96:99]
	v_mfma_f32_16x16x32_bf16 v[88:91], v[172:175], v[188:191], v[88:91]
	v_mfma_f32_16x16x32_bf16 v[80:83], v[164:167], v[196:199], v[80:83]
	v_mfma_f32_16x16x32_bf16 v[72:75], v[172:175], v[196:199], v[72:75]
	v_mfma_f32_16x16x32_bf16 v[52:55], v[164:167], v[204:207], v[52:55]
	v_mfma_f32_16x16x32_bf16 v[48:51], v[172:175], v[204:207], v[48:51]
	s_setprio 1
	s_barrier
	s_mov_b32 m0, s39
	v_lshl_add_u64 v[208:209], s[26:27], 0, v[130:131]
	ds_read_b128 v[176:179], v140 offset:16384
	ds_read_b128 v[180:183], v140 offset:17408
	ds_read_b128 v[184:187], v140 offset:18432
	ds_read_b128 v[188:191], v140 offset:19456
	ds_read_b128 v[192:195], v140 offset:20480
	ds_read_b128 v[196:199], v140 offset:21504
	ds_read_b128 v[200:203], v140 offset:22528
	ds_read_b128 v[204:207], v140 offset:23552
	global_load_lds_dwordx4 v[208:209], off
	v_lshl_add_u64 v[210:211], s[26:27], 0, v[128:129]
	s_mov_b32 m0, s40
	v_lshl_add_u64 v[212:213], s[34:35], 0, v[130:131]
	global_load_lds_dwordx4 v[210:211], off
	s_mov_b32 m0, s41
	v_lshl_add_u64 v[214:215], s[24:25], 0, v[134:135]
	global_load_lds_dwordx4 v[212:213], off
	v_lshl_add_u64 v[212:213], s[34:35], 0, v[128:129]
	s_mov_b32 m0, s42
	s_nop 0
	global_load_lds_dwordx4 v[212:213], off
	v_lshl_add_u64 v[212:213], s[24:25], 0, v[132:133]
	s_mov_b32 m0, s21
	s_nop 0
	global_load_lds_dwordx4 v[212:213], off
	s_mov_b32 m0, s22
	s_nop 0
	global_load_lds_dwordx4 v[214:215], off
	s_waitcnt vmcnt(8)
	s_waitcnt lgkmcnt(0)
	s_barrier
	s_setprio 0
	s_waitcnt lgkmcnt(0)
	v_mfma_f32_16x16x32_bf16 v[44:47], v[144:147], v[176:179], v[44:47]
	v_mfma_f32_16x16x32_bf16 v[32:35], v[152:155], v[176:179], v[32:35]
	v_mfma_f32_16x16x32_bf16 v[4:7], v[144:147], v[184:187], v[4:7]
	v_mfma_f32_16x16x32_bf16 v[0:3], v[152:155], v[184:187], v[0:3]
	v_mfma_f32_16x16x32_bf16 v[28:31], v[144:147], v[192:195], v[28:31]
	v_mfma_f32_16x16x32_bf16 v[24:27], v[152:155], v[192:195], v[24:27]
	v_mfma_f32_16x16x32_bf16 v[12:15], v[144:147], v[200:203], v[12:15]
	v_mfma_f32_16x16x32_bf16 v[8:11], v[152:155], v[200:203], v[8:11]
	v_mfma_f32_16x16x32_bf16 v[44:47], v[148:151], v[180:183], v[44:47]
	v_mfma_f32_16x16x32_bf16 v[32:35], v[156:159], v[180:183], v[32:35]
	v_mfma_f32_16x16x32_bf16 v[4:7], v[148:151], v[188:191], v[4:7]
	v_mfma_f32_16x16x32_bf16 v[0:3], v[156:159], v[188:191], v[0:3]
	v_mfma_f32_16x16x32_bf16 v[28:31], v[148:151], v[196:199], v[28:31]
	v_mfma_f32_16x16x32_bf16 v[24:27], v[156:159], v[196:199], v[24:27]
	v_mfma_f32_16x16x32_bf16 v[12:15], v[148:151], v[204:207], v[12:15]
	v_mfma_f32_16x16x32_bf16 v[8:11], v[156:159], v[204:207], v[8:11]
	s_setprio 1
	s_setprio 0
	v_mfma_f32_16x16x32_bf16 v[68:71], v[160:163], v[176:179], v[68:71]
	v_mfma_f32_16x16x32_bf16 v[64:67], v[168:171], v[176:179], v[64:67]
	v_mfma_f32_16x16x32_bf16 v[60:63], v[160:163], v[184:187], v[60:63]
	v_mfma_f32_16x16x32_bf16 v[56:59], v[168:171], v[184:187], v[56:59]
	v_mfma_f32_16x16x32_bf16 v[40:43], v[160:163], v[192:195], v[40:43]
	v_mfma_f32_16x16x32_bf16 v[36:39], v[168:171], v[192:195], v[36:39]
	v_mfma_f32_16x16x32_bf16 v[20:23], v[160:163], v[200:203], v[20:23]
	v_mfma_f32_16x16x32_bf16 v[16:19], v[168:171], v[200:203], v[16:19]
	v_mfma_f32_16x16x32_bf16 v[68:71], v[164:167], v[180:183], v[68:71]
	v_mfma_f32_16x16x32_bf16 v[64:67], v[172:175], v[180:183], v[64:67]
	v_mfma_f32_16x16x32_bf16 v[60:63], v[164:167], v[188:191], v[60:63]
	v_mfma_f32_16x16x32_bf16 v[56:59], v[172:175], v[188:191], v[56:59]
	v_mfma_f32_16x16x32_bf16 v[40:43], v[164:167], v[196:199], v[40:43]
	v_mfma_f32_16x16x32_bf16 v[36:39], v[172:175], v[196:199], v[36:39]
	v_mfma_f32_16x16x32_bf16 v[20:23], v[164:167], v[204:207], v[20:23]
	v_mfma_f32_16x16x32_bf16 v[16:19], v[172:175], v[204:207], v[16:19]
	s_setprio 1
	s_barrier
	ds_read_b128 v[144:147], v141
	ds_read_b128 v[148:151], v141 offset:1024
	ds_read_b128 v[152:155], v141 offset:2048
	ds_read_b128 v[156:159], v141 offset:3072
	ds_read_b128 v[160:163], v142
	ds_read_b128 v[164:167], v142 offset:1024
	ds_read_b128 v[168:171], v142 offset:2048
	ds_read_b128 v[172:175], v142 offset:3072
	s_mov_b32 m0, s23
	v_lshl_add_u64 v[216:217], s[16:17], 0, v[132:133]
	ds_read_b128 v[176:179], v140 offset:32768
	ds_read_b128 v[180:183], v140 offset:33792
	ds_read_b128 v[184:187], v140 offset:34816
	ds_read_b128 v[188:191], v140 offset:35840
	ds_read_b128 v[192:195], v140 offset:36864
	ds_read_b128 v[196:199], v140 offset:37888
	ds_read_b128 v[200:203], v140 offset:38912
	ds_read_b128 v[204:207], v140 offset:39936
	global_load_lds_dwordx4 v[216:217], off
	v_lshl_add_u64 v[216:217], s[16:17], 0, v[134:135]
	s_mov_b32 m0, s28
	s_nop 0
	global_load_lds_dwordx4 v[216:217], off
	s_waitcnt vmcnt(8)
	s_waitcnt lgkmcnt(0)
	s_barrier
	s_setprio 0
	s_waitcnt lgkmcnt(0)
	v_mfma_f32_16x16x32_bf16 v[124:127], v[144:147], v[176:179], v[124:127]
	v_mfma_f32_16x16x32_bf16 v[120:123], v[152:155], v[176:179], v[120:123]
	v_mfma_f32_16x16x32_bf16 v[116:119], v[144:147], v[184:187], v[116:119]
	v_mfma_f32_16x16x32_bf16 v[108:111], v[152:155], v[184:187], v[108:111]
	v_mfma_f32_16x16x32_bf16 v[100:103], v[144:147], v[192:195], v[100:103]
	v_mfma_f32_16x16x32_bf16 v[92:95], v[152:155], v[192:195], v[92:95]
	v_mfma_f32_16x16x32_bf16 v[84:87], v[144:147], v[200:203], v[84:87]
	v_mfma_f32_16x16x32_bf16 v[76:79], v[152:155], v[200:203], v[76:79]
	v_mfma_f32_16x16x32_bf16 v[124:127], v[148:151], v[180:183], v[124:127]
	v_mfma_f32_16x16x32_bf16 v[120:123], v[156:159], v[180:183], v[120:123]
	v_mfma_f32_16x16x32_bf16 v[116:119], v[148:151], v[188:191], v[116:119]
	v_mfma_f32_16x16x32_bf16 v[108:111], v[156:159], v[188:191], v[108:111]
	v_mfma_f32_16x16x32_bf16 v[100:103], v[148:151], v[196:199], v[100:103]
	v_mfma_f32_16x16x32_bf16 v[92:95], v[156:159], v[196:199], v[92:95]
	v_mfma_f32_16x16x32_bf16 v[84:87], v[148:151], v[204:207], v[84:87]
	v_mfma_f32_16x16x32_bf16 v[76:79], v[156:159], v[204:207], v[76:79]
	s_setprio 1
	s_setprio 0
	v_mfma_f32_16x16x32_bf16 v[112:115], v[160:163], v[176:179], v[112:115]
	v_mfma_f32_16x16x32_bf16 v[104:107], v[168:171], v[176:179], v[104:107]
	v_mfma_f32_16x16x32_bf16 v[96:99], v[160:163], v[184:187], v[96:99]
	v_mfma_f32_16x16x32_bf16 v[88:91], v[168:171], v[184:187], v[88:91]
	v_mfma_f32_16x16x32_bf16 v[80:83], v[160:163], v[192:195], v[80:83]
	v_mfma_f32_16x16x32_bf16 v[72:75], v[168:171], v[192:195], v[72:75]
	v_mfma_f32_16x16x32_bf16 v[52:55], v[160:163], v[200:203], v[52:55]
	v_mfma_f32_16x16x32_bf16 v[48:51], v[168:171], v[200:203], v[48:51]
	v_mfma_f32_16x16x32_bf16 v[112:115], v[164:167], v[180:183], v[112:115]
	v_mfma_f32_16x16x32_bf16 v[104:107], v[172:175], v[180:183], v[104:107]
	v_mfma_f32_16x16x32_bf16 v[96:99], v[164:167], v[188:191], v[96:99]
	v_mfma_f32_16x16x32_bf16 v[88:91], v[172:175], v[188:191], v[88:91]
	v_mfma_f32_16x16x32_bf16 v[80:83], v[164:167], v[196:199], v[80:83]
	v_mfma_f32_16x16x32_bf16 v[72:75], v[172:175], v[196:199], v[72:75]
	v_mfma_f32_16x16x32_bf16 v[52:55], v[164:167], v[204:207], v[52:55]
	v_mfma_f32_16x16x32_bf16 v[48:51], v[172:175], v[204:207], v[48:51]
	s_setprio 1
	s_barrier
	s_mov_b32 m0, s43
	v_lshl_add_u64 v[208:209], v[208:209], 0, s[6:7]
	ds_read_b128 v[176:179], v140 offset:49152
	ds_read_b128 v[180:183], v140 offset:50176
	ds_read_b128 v[184:187], v140 offset:51200
	ds_read_b128 v[188:191], v140 offset:52224
	ds_read_b128 v[192:195], v140 offset:53248
	ds_read_b128 v[196:199], v140 offset:54272
	ds_read_b128 v[200:203], v140 offset:55296
	ds_read_b128 v[204:207], v140 offset:56320
	global_load_lds_dwordx4 v[208:209], off
	v_lshl_add_u64 v[208:209], v[210:211], 0, s[6:7]
	s_mov_b32 m0, s44
	s_nop 0
	global_load_lds_dwordx4 v[208:209], off
	v_lshl_add_u64 v[208:209], s[14:15], 0, v[130:131]
	s_mov_b32 m0, s45
	s_nop 0
	global_load_lds_dwordx4 v[208:209], off
	v_lshl_add_u64 v[208:209], s[14:15], 0, v[128:129]
	s_mov_b32 m0, s46
	s_nop 0
	global_load_lds_dwordx4 v[208:209], off
	v_lshl_add_u64 v[208:209], v[212:213], 0, s[6:7]
	s_mov_b32 m0, s30
	s_nop 0
	global_load_lds_dwordx4 v[208:209], off
	v_lshl_add_u64 v[208:209], v[214:215], 0, s[6:7]
	s_mov_b32 m0, s31
	s_nop 0
	global_load_lds_dwordx4 v[208:209], off
	s_waitcnt vmcnt(8)
	s_waitcnt lgkmcnt(0)
	s_barrier
	s_setprio 0
	s_waitcnt lgkmcnt(0)
	v_mfma_f32_16x16x32_bf16 v[44:47], v[144:147], v[176:179], v[44:47]
	v_mfma_f32_16x16x32_bf16 v[32:35], v[152:155], v[176:179], v[32:35]
	v_mfma_f32_16x16x32_bf16 v[4:7], v[144:147], v[184:187], v[4:7]
	v_mfma_f32_16x16x32_bf16 v[0:3], v[152:155], v[184:187], v[0:3]
	v_mfma_f32_16x16x32_bf16 v[28:31], v[144:147], v[192:195], v[28:31]
	v_mfma_f32_16x16x32_bf16 v[24:27], v[152:155], v[192:195], v[24:27]
	v_mfma_f32_16x16x32_bf16 v[12:15], v[144:147], v[200:203], v[12:15]
	v_mfma_f32_16x16x32_bf16 v[8:11], v[152:155], v[200:203], v[8:11]
	v_mfma_f32_16x16x32_bf16 v[44:47], v[148:151], v[180:183], v[44:47]
	v_mfma_f32_16x16x32_bf16 v[32:35], v[156:159], v[180:183], v[32:35]
	v_mfma_f32_16x16x32_bf16 v[4:7], v[148:151], v[188:191], v[4:7]
	v_mfma_f32_16x16x32_bf16 v[0:3], v[156:159], v[188:191], v[0:3]
	v_mfma_f32_16x16x32_bf16 v[28:31], v[148:151], v[196:199], v[28:31]
	v_mfma_f32_16x16x32_bf16 v[24:27], v[156:159], v[196:199], v[24:27]
	v_mfma_f32_16x16x32_bf16 v[12:15], v[148:151], v[204:207], v[12:15]
	v_mfma_f32_16x16x32_bf16 v[8:11], v[156:159], v[204:207], v[8:11]
	s_setprio 1
	s_setprio 0
	v_mfma_f32_16x16x32_bf16 v[68:71], v[160:163], v[176:179], v[68:71]
	v_mfma_f32_16x16x32_bf16 v[64:67], v[168:171], v[176:179], v[64:67]
	v_mfma_f32_16x16x32_bf16 v[60:63], v[160:163], v[184:187], v[60:63]
	v_mfma_f32_16x16x32_bf16 v[56:59], v[168:171], v[184:187], v[56:59]
	v_mfma_f32_16x16x32_bf16 v[40:43], v[160:163], v[192:195], v[40:43]
	v_mfma_f32_16x16x32_bf16 v[36:39], v[168:171], v[192:195], v[36:39]
	v_mfma_f32_16x16x32_bf16 v[20:23], v[160:163], v[200:203], v[20:23]
	v_mfma_f32_16x16x32_bf16 v[16:19], v[168:171], v[200:203], v[16:19]
	v_mfma_f32_16x16x32_bf16 v[68:71], v[164:167], v[180:183], v[68:71]
	v_mfma_f32_16x16x32_bf16 v[64:67], v[172:175], v[180:183], v[64:67]
	v_mfma_f32_16x16x32_bf16 v[60:63], v[164:167], v[188:191], v[60:63]
	v_mfma_f32_16x16x32_bf16 v[56:59], v[172:175], v[188:191], v[56:59]
	v_mfma_f32_16x16x32_bf16 v[40:43], v[164:167], v[196:199], v[40:43]
	v_mfma_f32_16x16x32_bf16 v[36:39], v[172:175], v[196:199], v[36:39]
	v_mfma_f32_16x16x32_bf16 v[20:23], v[164:167], v[204:207], v[20:23]
	v_mfma_f32_16x16x32_bf16 v[16:19], v[172:175], v[204:207], v[16:19]
	s_setprio 1
	s_barrier
	s_andn2_b64 vcc, exec, s[12:13]
	s_mov_b64 s[14:15], -1
	s_mov_b64 s[12:13], 0
	s_mov_b64 s[16:17], 0x100
	s_cbranch_vccz .LBB0_925
	s_cmpk_lt_u32 s18, 0x100
	s_cbranch_scc0 .LBB0_928
	s_barrier

.LBB0_1081:
	s_add_u32 s46, s34, s40
	s_addc_u32 s47, s35, s41
	s_add_u32 s44, s46, 0x100
	s_addc_u32 s45, s47, 0
	s_and_b64 s[42:43], s[38:39], exec
	s_cselect_b32 s43, s13, s45
	s_cselect_b32 s42, s57, s44
	s_add_u32 s40, s26, s40
	s_addc_u32 s41, s27, s41
	s_add_u32 s40, s40, 0x100
	s_addc_u32 s41, s41, 0
	s_and_b64 s[38:39], s[38:39], exec
	s_cselect_b32 s45, s11, s41
	s_cselect_b32 s44, s58, s40
	s_add_u32 s48, s46, 0x10080
	ds_read_b128 v[148:151], v145
	ds_read_b128 v[152:155], v145 offset:1024
	ds_read_b128 v[156:159], v145 offset:2048
	ds_read_b128 v[160:163], v145 offset:3072
	ds_read_b128 v[164:167], v146
	ds_read_b128 v[168:171], v146 offset:1024
	ds_read_b128 v[172:175], v146 offset:2048
	ds_read_b128 v[176:179], v146 offset:3072
	s_addc_u32 s49, s47, 0
	s_add_i32 s68, s54, s21
	s_add_i32 m0, s15, 0xc000
	s_add_i32 s69, s15, 0xe000
	s_add_i32 s65, s68, 0x2000
	s_add_u32 s46, s44, 0x10000
	s_addc_u32 s47, s45, 0
	s_add_i32 s67, s55, s21
	s_add_i32 s66, s67, 0x2000
	s_add_i32 s64, 0, 0x18000
	s_add_i32 s63, 0, 0x1c000
	s_add_u32 s40, s42, 0x10000
	s_addc_u32 s41, s43, 0
	s_add_i32 s62, s64, s21
	s_add_i32 s60, s62, 0x2000
	s_add_u32 s38, s44, 0x10080
	s_addc_u32 s39, s45, 0
	s_add_i32 s61, s63, s21
	s_add_i32 s59, s61, 0x2000
	v_lshl_add_u64 v[140:141], s[48:49], 0, v[132:133]
	ds_read_b128 v[180:183], v147
	ds_read_b128 v[184:187], v147 offset:1024
	ds_read_b128 v[188:191], v147 offset:2048
	ds_read_b128 v[192:195], v147 offset:3072
	ds_read_b128 v[196:199], v147 offset:4096
	ds_read_b128 v[200:203], v147 offset:5120
	ds_read_b128 v[204:207], v147 offset:6144
	ds_read_b128 v[208:211], v147 offset:7168
	global_load_lds_dwordx4 v[140:141], off
	v_lshl_add_u64 v[140:141], s[48:49], 0, v[134:135]
	s_mov_b32 m0, s69
	s_nop 0
	global_load_lds_dwordx4 v[140:141], off
	s_waitcnt vmcnt(8)
	s_waitcnt lgkmcnt(0)
	s_barrier
	s_setprio 0
	s_waitcnt lgkmcnt(0)
	v_mfma_f32_16x16x32_bf16 v[124:127], v[148:151], v[180:183], v[124:127]
	v_mfma_f32_16x16x32_bf16 v[120:123], v[156:159], v[180:183], v[120:123]
	v_mfma_f32_16x16x32_bf16 v[116:119], v[148:151], v[188:191], v[116:119]
	v_mfma_f32_16x16x32_bf16 v[108:111], v[156:159], v[188:191], v[108:111]
	v_mfma_f32_16x16x32_bf16 v[100:103], v[148:151], v[196:199], v[100:103]
	v_mfma_f32_16x16x32_bf16 v[92:95], v[156:159], v[196:199], v[92:95]
	v_mfma_f32_16x16x32_bf16 v[84:87], v[148:151], v[204:207], v[84:87]
	v_mfma_f32_16x16x32_bf16 v[76:79], v[156:159], v[204:207], v[76:79]
	v_mfma_f32_16x16x32_bf16 v[124:127], v[152:155], v[184:187], v[124:127]
	v_mfma_f32_16x16x32_bf16 v[120:123], v[160:163], v[184:187], v[120:123]
	v_mfma_f32_16x16x32_bf16 v[116:119], v[152:155], v[192:195], v[116:119]
	v_mfma_f32_16x16x32_bf16 v[108:111], v[160:163], v[192:195], v[108:111]
	v_mfma_f32_16x16x32_bf16 v[100:103], v[152:155], v[200:203], v[100:103]
	v_mfma_f32_16x16x32_bf16 v[92:95], v[160:163], v[200:203], v[92:95]
	v_mfma_f32_16x16x32_bf16 v[84:87], v[152:155], v[208:211], v[84:87]
	v_mfma_f32_16x16x32_bf16 v[76:79], v[160:163], v[208:211], v[76:79]
	s_setprio 1
	s_setprio 0
	v_mfma_f32_16x16x32_bf16 v[112:115], v[164:167], v[180:183], v[112:115]
	v_mfma_f32_16x16x32_bf16 v[104:107], v[172:175], v[180:183], v[104:107]
	v_mfma_f32_16x16x32_bf16 v[96:99], v[164:167], v[188:191], v[96:99]
	v_mfma_f32_16x16x32_bf16 v[88:91], v[172:175], v[188:191], v[88:91]
	v_mfma_f32_16x16x32_bf16 v[80:83], v[164:167], v[196:199], v[80:83]
	v_mfma_f32_16x16x32_bf16 v[72:75], v[172:175], v[196:199], v[72:75]
	v_mfma_f32_16x16x32_bf16 v[52:55], v[164:167], v[204:207], v[52:55]
	v_mfma_f32_16x16x32_bf16 v[48:51], v[172:175], v[204:207], v[48:51]
	v_mfma_f32_16x16x32_bf16 v[112:115], v[168:171], v[184:187], v[112:115]
	v_mfma_f32_16x16x32_bf16 v[104:107], v[176:179], v[184:187], v[104:107]
	v_mfma_f32_16x16x32_bf16 v[96:99], v[168:171], v[192:195], v[96:99]
	v_mfma_f32_16x16x32_bf16 v[88:91], v[176:179], v[192:195], v[88:91]
	v_mfma_f32_16x16x32_bf16 v[80:83], v[168:171], v[200:203], v[80:83]
	v_mfma_f32_16x16x32_bf16 v[72:75], v[176:179], v[200:203], v[72:75]
	v_mfma_f32_16x16x32_bf16 v[52:55], v[168:171], v[208:211], v[52:55]
	v_mfma_f32_16x16x32_bf16 v[48:51], v[176:179], v[208:211], v[48:51]
	s_setprio 1
	s_barrier
	s_mov_b32 m0, s68
	v_lshl_add_u64 v[140:141], s[44:45], 0, v[128:129]
	ds_read_b128 v[180:183], v147 offset:16384
	ds_read_b128 v[184:187], v147 offset:17408
	ds_read_b128 v[188:191], v147 offset:18432
	ds_read_b128 v[192:195], v147 offset:19456
	ds_read_b128 v[196:199], v147 offset:20480
	ds_read_b128 v[200:203], v147 offset:21504
	ds_read_b128 v[204:207], v147 offset:22528
	ds_read_b128 v[208:211], v147 offset:23552
	global_load_lds_dwordx4 v[140:141], off
	v_lshl_add_u64 v[212:213], s[44:45], 0, v[130:131]
	s_mov_b32 m0, s65
	v_lshl_add_u64 v[214:215], s[46:47], 0, v[128:129]
	global_load_lds_dwordx4 v[212:213], off
	s_mov_b32 m0, s67
	v_lshl_add_u64 v[216:217], s[42:43], 0, v[134:135]
	global_load_lds_dwordx4 v[214:215], off
	v_lshl_add_u64 v[214:215], s[46:47], 0, v[130:131]
	s_mov_b32 m0, s66
	s_nop 0
	global_load_lds_dwordx4 v[214:215], off
	v_lshl_add_u64 v[214:215], s[42:43], 0, v[132:133]
	s_mov_b32 m0, s15
	s_nop 0
	global_load_lds_dwordx4 v[214:215], off
	s_mov_b32 m0, s30
	s_nop 0
	global_load_lds_dwordx4 v[216:217], off
	s_waitcnt vmcnt(8)
	s_waitcnt lgkmcnt(0)
	s_barrier
	s_setprio 0
	s_waitcnt lgkmcnt(0)
	v_mfma_f32_16x16x32_bf16 v[44:47], v[148:151], v[180:183], v[44:47]
	v_mfma_f32_16x16x32_bf16 v[32:35], v[156:159], v[180:183], v[32:35]
	v_mfma_f32_16x16x32_bf16 v[4:7], v[148:151], v[188:191], v[4:7]
	v_mfma_f32_16x16x32_bf16 v[0:3], v[156:159], v[188:191], v[0:3]
	v_mfma_f32_16x16x32_bf16 v[28:31], v[148:151], v[196:199], v[28:31]
	v_mfma_f32_16x16x32_bf16 v[24:27], v[156:159], v[196:199], v[24:27]
	v_mfma_f32_16x16x32_bf16 v[12:15], v[148:151], v[204:207], v[12:15]
	v_mfma_f32_16x16x32_bf16 v[8:11], v[156:159], v[204:207], v[8:11]
	v_mfma_f32_16x16x32_bf16 v[44:47], v[152:155], v[184:187], v[44:47]
	v_mfma_f32_16x16x32_bf16 v[32:35], v[160:163], v[184:187], v[32:35]
	v_mfma_f32_16x16x32_bf16 v[4:7], v[152:155], v[192:195], v[4:7]
	v_mfma_f32_16x16x32_bf16 v[0:3], v[160:163], v[192:195], v[0:3]
	v_mfma_f32_16x16x32_bf16 v[28:31], v[152:155], v[200:203], v[28:31]
	v_mfma_f32_16x16x32_bf16 v[24:27], v[160:163], v[200:203], v[24:27]
	v_mfma_f32_16x16x32_bf16 v[12:15], v[152:155], v[208:211], v[12:15]
	v_mfma_f32_16x16x32_bf16 v[8:11], v[160:163], v[208:211], v[8:11]
	s_setprio 1
	s_setprio 0
	v_mfma_f32_16x16x32_bf16 v[68:71], v[164:167], v[180:183], v[68:71]
	v_mfma_f32_16x16x32_bf16 v[64:67], v[172:175], v[180:183], v[64:67]
	v_mfma_f32_16x16x32_bf16 v[60:63], v[164:167], v[188:191], v[60:63]
	v_mfma_f32_16x16x32_bf16 v[56:59], v[172:175], v[188:191], v[56:59]
	v_mfma_f32_16x16x32_bf16 v[40:43], v[164:167], v[196:199], v[40:43]
	v_mfma_f32_16x16x32_bf16 v[36:39], v[172:175], v[196:199], v[36:39]
	v_mfma_f32_16x16x32_bf16 v[20:23], v[164:167], v[204:207], v[20:23]
	v_mfma_f32_16x16x32_bf16 v[16:19], v[172:175], v[204:207], v[16:19]
	v_mfma_f32_16x16x32_bf16 v[68:71], v[168:171], v[184:187], v[68:71]
	v_mfma_f32_16x16x32_bf16 v[64:67], v[176:179], v[184:187], v[64:67]
	v_mfma_f32_16x16x32_bf16 v[60:63], v[168:171], v[192:195], v[60:63]
	v_mfma_f32_16x16x32_bf16 v[56:59], v[176:179], v[192:195], v[56:59]
	v_mfma_f32_16x16x32_bf16 v[40:43], v[168:171], v[200:203], v[40:43]
	v_mfma_f32_16x16x32_bf16 v[36:39], v[176:179], v[200:203], v[36:39]
	v_mfma_f32_16x16x32_bf16 v[20:23], v[168:171], v[208:211], v[20:23]
	v_mfma_f32_16x16x32_bf16 v[16:19], v[176:179], v[208:211], v[16:19]
	s_setprio 1
	s_barrier
	v_add_u32_e32 v160, s64, v143
	v_add_u32_e32 v176, s63, v143
	ds_read_b128 v[148:151], v160
	ds_read_b128 v[152:155], v160 offset:1024
	ds_read_b128 v[156:159], v160 offset:2048
	ds_read_b128 v[160:163], v160 offset:3072
	ds_read_b128 v[164:167], v176
	ds_read_b128 v[168:171], v176 offset:1024
	ds_read_b128 v[172:175], v176 offset:2048
	ds_read_b128 v[176:179], v176 offset:3072
	s_mov_b32 m0, s31
	v_lshl_add_u64 v[218:219], s[40:41], 0, v[132:133]
	ds_read_b128 v[180:183], v147 offset:32768
	ds_read_b128 v[184:187], v147 offset:33792
	ds_read_b128 v[188:191], v147 offset:34816
	ds_read_b128 v[192:195], v147 offset:35840
	ds_read_b128 v[196:199], v147 offset:36864
	ds_read_b128 v[200:203], v147 offset:37888
	ds_read_b128 v[204:207], v147 offset:38912
	ds_read_b128 v[208:211], v147 offset:39936
	global_load_lds_dwordx4 v[218:219], off
	v_lshl_add_u64 v[218:219], s[40:41], 0, v[134:135]
	s_mov_b32 m0, s33
	s_nop 0
	global_load_lds_dwordx4 v[218:219], off
	s_waitcnt vmcnt(8)
	s_waitcnt lgkmcnt(0)
	s_barrier
	s_setprio 0
	s_waitcnt lgkmcnt(0)
	v_mfma_f32_16x16x32_bf16 v[124:127], v[148:151], v[180:183], v[124:127]
	v_mfma_f32_16x16x32_bf16 v[120:123], v[156:159], v[180:183], v[120:123]
	v_mfma_f32_16x16x32_bf16 v[116:119], v[148:151], v[188:191], v[116:119]
	v_mfma_f32_16x16x32_bf16 v[108:111], v[156:159], v[188:191], v[108:111]
	v_mfma_f32_16x16x32_bf16 v[100:103], v[148:151], v[196:199], v[100:103]
	v_mfma_f32_16x16x32_bf16 v[92:95], v[156:159], v[196:199], v[92:95]
	v_mfma_f32_16x16x32_bf16 v[84:87], v[148:151], v[204:207], v[84:87]
	v_mfma_f32_16x16x32_bf16 v[76:79], v[156:159], v[204:207], v[76:79]
	v_mfma_f32_16x16x32_bf16 v[124:127], v[152:155], v[184:187], v[124:127]
	v_mfma_f32_16x16x32_bf16 v[120:123], v[160:163], v[184:187], v[120:123]
	v_mfma_f32_16x16x32_bf16 v[116:119], v[152:155], v[192:195], v[116:119]
	v_mfma_f32_16x16x32_bf16 v[108:111], v[160:163], v[192:195], v[108:111]
	v_mfma_f32_16x16x32_bf16 v[100:103], v[152:155], v[200:203], v[100:103]
	v_mfma_f32_16x16x32_bf16 v[92:95], v[160:163], v[200:203], v[92:95]
	v_mfma_f32_16x16x32_bf16 v[84:87], v[152:155], v[208:211], v[84:87]
	v_mfma_f32_16x16x32_bf16 v[76:79], v[160:163], v[208:211], v[76:79]
	s_setprio 1
	s_setprio 0
	v_mfma_f32_16x16x32_bf16 v[112:115], v[164:167], v[180:183], v[112:115]
	v_mfma_f32_16x16x32_bf16 v[104:107], v[172:175], v[180:183], v[104:107]
	v_mfma_f32_16x16x32_bf16 v[96:99], v[164:167], v[188:191], v[96:99]
	v_mfma_f32_16x16x32_bf16 v[88:91], v[172:175], v[188:191], v[88:91]
	v_mfma_f32_16x16x32_bf16 v[80:83], v[164:167], v[196:199], v[80:83]
	v_mfma_f32_16x16x32_bf16 v[72:75], v[172:175], v[196:199], v[72:75]
	v_mfma_f32_16x16x32_bf16 v[52:55], v[164:167], v[204:207], v[52:55]
	v_mfma_f32_16x16x32_bf16 v[48:51], v[172:175], v[204:207], v[48:51]
	v_mfma_f32_16x16x32_bf16 v[112:115], v[168:171], v[184:187], v[112:115]
	v_mfma_f32_16x16x32_bf16 v[104:107], v[176:179], v[184:187], v[104:107]
	v_mfma_f32_16x16x32_bf16 v[96:99], v[168:171], v[192:195], v[96:99]
	v_mfma_f32_16x16x32_bf16 v[88:91], v[176:179], v[192:195], v[88:91]
	v_mfma_f32_16x16x32_bf16 v[80:83], v[168:171], v[200:203], v[80:83]
	v_mfma_f32_16x16x32_bf16 v[72:75], v[176:179], v[200:203], v[72:75]
	v_mfma_f32_16x16x32_bf16 v[52:55], v[168:171], v[208:211], v[52:55]
	v_mfma_f32_16x16x32_bf16 v[48:51], v[176:179], v[208:211], v[48:51]
	s_setprio 1
	s_barrier
	s_mov_b32 m0, s62
	v_lshl_add_u64 v[140:141], v[140:141], 0, s[4:5]
	ds_read_b128 v[180:183], v147 offset:49152
	ds_read_b128 v[184:187], v147 offset:50176
	ds_read_b128 v[188:191], v147 offset:51200
	ds_read_b128 v[192:195], v147 offset:52224
	ds_read_b128 v[196:199], v147 offset:53248
	ds_read_b128 v[200:203], v147 offset:54272
	ds_read_b128 v[204:207], v147 offset:55296
	ds_read_b128 v[208:211], v147 offset:56320
	global_load_lds_dwordx4 v[140:141], off
	v_lshl_add_u64 v[140:141], v[212:213], 0, s[4:5]
	s_mov_b32 m0, s60
	s_nop 0
	global_load_lds_dwordx4 v[140:141], off
	v_lshl_add_u64 v[140:141], s[38:39], 0, v[128:129]
	s_mov_b32 m0, s61
	s_nop 0
	global_load_lds_dwordx4 v[140:141], off
	v_lshl_add_u64 v[140:141], s[38:39], 0, v[130:131]
	s_mov_b32 m0, s59
	s_nop 0
	global_load_lds_dwordx4 v[140:141], off
	v_lshl_add_u64 v[140:141], v[214:215], 0, s[4:5]
	s_mov_b32 m0, s51
	s_nop 0
	global_load_lds_dwordx4 v[140:141], off
	v_lshl_add_u64 v[140:141], v[216:217], 0, s[4:5]
	s_mov_b32 m0, s52
	s_nop 0
	global_load_lds_dwordx4 v[140:141], off
	s_waitcnt vmcnt(8)
	s_waitcnt lgkmcnt(0)
	s_barrier
	s_setprio 0
	s_waitcnt lgkmcnt(0)
	v_mfma_f32_16x16x32_bf16 v[44:47], v[148:151], v[180:183], v[44:47]
	v_mfma_f32_16x16x32_bf16 v[32:35], v[156:159], v[180:183], v[32:35]
	v_mfma_f32_16x16x32_bf16 v[4:7], v[148:151], v[188:191], v[4:7]
	v_mfma_f32_16x16x32_bf16 v[0:3], v[156:159], v[188:191], v[0:3]
	v_mfma_f32_16x16x32_bf16 v[28:31], v[148:151], v[196:199], v[28:31]
	v_mfma_f32_16x16x32_bf16 v[24:27], v[156:159], v[196:199], v[24:27]
	v_mfma_f32_16x16x32_bf16 v[12:15], v[148:151], v[204:207], v[12:15]
	v_mfma_f32_16x16x32_bf16 v[8:11], v[156:159], v[204:207], v[8:11]
	v_mfma_f32_16x16x32_bf16 v[44:47], v[152:155], v[184:187], v[44:47]
	v_mfma_f32_16x16x32_bf16 v[32:35], v[160:163], v[184:187], v[32:35]
	v_mfma_f32_16x16x32_bf16 v[4:7], v[152:155], v[192:195], v[4:7]
	v_mfma_f32_16x16x32_bf16 v[0:3], v[160:163], v[192:195], v[0:3]
	v_mfma_f32_16x16x32_bf16 v[28:31], v[152:155], v[200:203], v[28:31]
	v_mfma_f32_16x16x32_bf16 v[24:27], v[160:163], v[200:203], v[24:27]
	v_mfma_f32_16x16x32_bf16 v[12:15], v[152:155], v[208:211], v[12:15]
	v_mfma_f32_16x16x32_bf16 v[8:11], v[160:163], v[208:211], v[8:11]
	s_setprio 1
	s_setprio 0
	v_mfma_f32_16x16x32_bf16 v[68:71], v[164:167], v[180:183], v[68:71]
	v_mfma_f32_16x16x32_bf16 v[64:67], v[172:175], v[180:183], v[64:67]
	v_mfma_f32_16x16x32_bf16 v[60:63], v[164:167], v[188:191], v[60:63]
	v_mfma_f32_16x16x32_bf16 v[56:59], v[172:175], v[188:191], v[56:59]
	v_mfma_f32_16x16x32_bf16 v[40:43], v[164:167], v[196:199], v[40:43]
	v_mfma_f32_16x16x32_bf16 v[36:39], v[172:175], v[196:199], v[36:39]
	v_mfma_f32_16x16x32_bf16 v[20:23], v[164:167], v[204:207], v[20:23]
	v_mfma_f32_16x16x32_bf16 v[16:19], v[172:175], v[204:207], v[16:19]
	v_mfma_f32_16x16x32_bf16 v[68:71], v[168:171], v[184:187], v[68:71]
	v_mfma_f32_16x16x32_bf16 v[64:67], v[176:179], v[184:187], v[64:67]
	v_mfma_f32_16x16x32_bf16 v[60:63], v[168:171], v[192:195], v[60:63]
	v_mfma_f32_16x16x32_bf16 v[56:59], v[176:179], v[192:195], v[56:59]
	v_mfma_f32_16x16x32_bf16 v[40:43], v[168:171], v[200:203], v[40:43]
	v_mfma_f32_16x16x32_bf16 v[36:39], v[176:179], v[200:203], v[36:39]
	v_mfma_f32_16x16x32_bf16 v[20:23], v[168:171], v[208:211], v[20:23]
	v_mfma_f32_16x16x32_bf16 v[16:19], v[176:179], v[208:211], v[16:19]
	s_setprio 1
	s_barrier
	s_andn2_b64 vcc, exec, s[36:37]
	s_mov_b64 s[38:39], -1
	s_mov_b64 s[36:37], 0
	s_mov_b64 s[40:41], 0x100
	s_cbranch_vccz .LBB0_1081
	s_and_b64 vcc, exec, s[6:7]
	s_cbranch_vccz .LBB0_1084
	s_barrier

.LBB0_1102:
	ds_read_b128 v[124:127], v221
	ds_read_b128 v[132:135], v221 offset:1024
	ds_read_b128 v[136:139], v221 offset:2048
	ds_read_b128 v[140:143], v221 offset:3072
	ds_read_b128 v[144:147], v222
	ds_read_b128 v[148:151], v222 offset:1024
	ds_read_b128 v[152:155], v222 offset:2048
	ds_read_b128 v[156:159], v222 offset:3072
	s_add_u32 s36, s34, 0xfffc0080
	s_addc_u32 s37, s35, -1
	s_cmp_eq_u32 s48, 12
	s_cselect_b32 s39, s13, s37
	s_cselect_b32 s38, s44, s36
	s_cselect_b32 s37, s11, s47
	s_cselect_b32 s36, s45, s46
	v_lshl_add_u64 v[206:207], s[34:35], 0, v[180:181]
	s_add_i32 m0, s22, 0xc000
	ds_read_b128 v[160:163], v223
	ds_read_b128 v[164:167], v223 offset:1024
	ds_read_b128 v[168:171], v223 offset:2048
	ds_read_b128 v[186:189], v223 offset:3072
	ds_read_b128 v[190:193], v223 offset:4096
	ds_read_b128 v[194:197], v223 offset:5120
	ds_read_b128 v[198:201], v223 offset:6144
	ds_read_b128 v[202:205], v223 offset:7168
	global_load_lds_dwordx4 v[206:207], off
	v_lshl_add_u64 v[206:207], s[34:35], 0, v[182:183]
	s_add_i32 m0, s22, 0xe000
	s_nop 0
	global_load_lds_dwordx4 v[206:207], off
	s_waitcnt vmcnt(8)
	s_waitcnt lgkmcnt(0)
	s_barrier
	s_setprio 0
	s_waitcnt lgkmcnt(0)
	v_mfma_f32_16x16x32_bf16 v[120:123], v[124:127], v[160:163], v[120:123]
	v_mfma_f32_16x16x32_bf16 v[128:131], v[136:139], v[160:163], v[128:131]
	v_mfma_f32_16x16x32_bf16 v[108:111], v[124:127], v[168:171], v[108:111]
	v_mfma_f32_16x16x32_bf16 v[104:107], v[136:139], v[168:171], v[104:107]
	v_mfma_f32_16x16x32_bf16 v[92:95], v[124:127], v[190:193], v[92:95]
	v_mfma_f32_16x16x32_bf16 v[88:91], v[136:139], v[190:193], v[88:91]
	v_mfma_f32_16x16x32_bf16 v[76:79], v[124:127], v[198:201], v[76:79]
	v_mfma_f32_16x16x32_bf16 v[72:75], v[136:139], v[198:201], v[72:75]
	v_mfma_f32_16x16x32_bf16 v[120:123], v[132:135], v[164:167], v[120:123]
	v_mfma_f32_16x16x32_bf16 v[128:131], v[140:143], v[164:167], v[128:131]
	v_mfma_f32_16x16x32_bf16 v[108:111], v[132:135], v[186:189], v[108:111]
	v_mfma_f32_16x16x32_bf16 v[104:107], v[140:143], v[186:189], v[104:107]
	v_mfma_f32_16x16x32_bf16 v[92:95], v[132:135], v[194:197], v[92:95]
	v_mfma_f32_16x16x32_bf16 v[88:91], v[140:143], v[194:197], v[88:91]
	v_mfma_f32_16x16x32_bf16 v[76:79], v[132:135], v[202:205], v[76:79]
	v_mfma_f32_16x16x32_bf16 v[72:75], v[140:143], v[202:205], v[72:75]
	s_setprio 1
	s_setprio 0
	v_mfma_f32_16x16x32_bf16 v[116:119], v[144:147], v[160:163], v[116:119]
	v_mfma_f32_16x16x32_bf16 v[112:115], v[152:155], v[160:163], v[112:115]
	v_mfma_f32_16x16x32_bf16 v[100:103], v[144:147], v[168:171], v[100:103]
	v_mfma_f32_16x16x32_bf16 v[96:99], v[152:155], v[168:171], v[96:99]
	v_mfma_f32_16x16x32_bf16 v[84:87], v[144:147], v[190:193], v[84:87]
	v_mfma_f32_16x16x32_bf16 v[80:83], v[152:155], v[190:193], v[80:83]
	v_mfma_f32_16x16x32_bf16 v[68:71], v[144:147], v[198:201], v[68:71]
	v_mfma_f32_16x16x32_bf16 v[64:67], v[152:155], v[198:201], v[64:67]
	v_mfma_f32_16x16x32_bf16 v[116:119], v[148:151], v[164:167], v[116:119]
	v_mfma_f32_16x16x32_bf16 v[112:115], v[156:159], v[164:167], v[112:115]
	v_mfma_f32_16x16x32_bf16 v[100:103], v[148:151], v[186:189], v[100:103]
	v_mfma_f32_16x16x32_bf16 v[96:99], v[156:159], v[186:189], v[96:99]
	v_mfma_f32_16x16x32_bf16 v[84:87], v[148:151], v[194:197], v[84:87]
	v_mfma_f32_16x16x32_bf16 v[80:83], v[156:159], v[194:197], v[80:83]
	v_mfma_f32_16x16x32_bf16 v[68:71], v[148:151], v[202:205], v[68:71]
	v_mfma_f32_16x16x32_bf16 v[64:67], v[156:159], v[202:205], v[64:67]
	s_setprio 1
	s_barrier
	s_add_i32 s49, s40, s20
	v_lshl_add_u64 v[206:207], s[36:37], 0, v[174:175]
	s_mov_b32 m0, s49
	ds_read_b128 v[160:163], v223 offset:16384
	ds_read_b128 v[164:167], v223 offset:17408
	ds_read_b128 v[168:171], v223 offset:18432
	ds_read_b128 v[186:189], v223 offset:19456
	ds_read_b128 v[190:193], v223 offset:20480
	ds_read_b128 v[194:197], v223 offset:21504
	ds_read_b128 v[198:201], v223 offset:22528
	ds_read_b128 v[202:205], v223 offset:23552
	global_load_lds_dwordx4 v[206:207], off
	s_add_i32 m0, s49, 0x2000
	s_add_u32 s50, s36, 0x40000
	v_lshl_add_u64 v[208:209], s[36:37], 0, v[172:173]
	s_addc_u32 s51, s37, 0
	s_add_i32 s49, s41, s20
	global_load_lds_dwordx4 v[208:209], off
	v_lshl_add_u64 v[210:211], s[50:51], 0, v[174:175]
	s_mov_b32 m0, s49
	v_lshl_add_u64 v[212:213], s[38:39], 0, v[178:179]
	global_load_lds_dwordx4 v[210:211], off
	v_lshl_add_u64 v[210:211], s[50:51], 0, v[172:173]
	s_add_i32 m0, s49, 0x2000
	s_nop 0
	global_load_lds_dwordx4 v[210:211], off
	v_lshl_add_u64 v[210:211], s[38:39], 0, v[176:177]
	s_mov_b32 m0, s22
	s_nop 0
	global_load_lds_dwordx4 v[210:211], off
	s_mov_b32 m0, s23
	s_nop 0
	global_load_lds_dwordx4 v[212:213], off
	s_waitcnt vmcnt(8)
	s_waitcnt lgkmcnt(0)
	s_barrier
	s_setprio 0
	s_waitcnt lgkmcnt(0)
	v_mfma_f32_16x16x32_bf16 v[60:63], v[124:127], v[160:163], v[60:63]
	v_mfma_f32_16x16x32_bf16 v[52:55], v[136:139], v[160:163], v[52:55]
	v_mfma_f32_16x16x32_bf16 v[44:47], v[124:127], v[168:171], v[44:47]
	v_mfma_f32_16x16x32_bf16 v[36:39], v[136:139], v[168:171], v[36:39]
	v_mfma_f32_16x16x32_bf16 v[28:31], v[124:127], v[190:193], v[28:31]
	v_mfma_f32_16x16x32_bf16 v[24:27], v[136:139], v[190:193], v[24:27]
	v_mfma_f32_16x16x32_bf16 v[12:15], v[124:127], v[198:201], v[12:15]
	v_mfma_f32_16x16x32_bf16 v[8:11], v[136:139], v[198:201], v[8:11]
	v_mfma_f32_16x16x32_bf16 v[60:63], v[132:135], v[164:167], v[60:63]
	v_mfma_f32_16x16x32_bf16 v[52:55], v[140:143], v[164:167], v[52:55]
	v_mfma_f32_16x16x32_bf16 v[44:47], v[132:135], v[186:189], v[44:47]
	v_mfma_f32_16x16x32_bf16 v[36:39], v[140:143], v[186:189], v[36:39]
	v_mfma_f32_16x16x32_bf16 v[28:31], v[132:135], v[194:197], v[28:31]
	v_mfma_f32_16x16x32_bf16 v[24:27], v[140:143], v[194:197], v[24:27]
	v_mfma_f32_16x16x32_bf16 v[12:15], v[132:135], v[202:205], v[12:15]
	v_mfma_f32_16x16x32_bf16 v[8:11], v[140:143], v[202:205], v[8:11]
	s_setprio 1
	s_setprio 0
	v_mfma_f32_16x16x32_bf16 v[56:59], v[144:147], v[160:163], v[56:59]
	v_mfma_f32_16x16x32_bf16 v[48:51], v[152:155], v[160:163], v[48:51]
	v_mfma_f32_16x16x32_bf16 v[40:43], v[144:147], v[168:171], v[40:43]
	v_mfma_f32_16x16x32_bf16 v[32:35], v[152:155], v[168:171], v[32:35]
	v_mfma_f32_16x16x32_bf16 v[20:23], v[144:147], v[190:193], v[20:23]
	v_mfma_f32_16x16x32_bf16 v[16:19], v[152:155], v[190:193], v[16:19]
	v_mfma_f32_16x16x32_bf16 v[4:7], v[144:147], v[198:201], v[4:7]
	v_mfma_f32_16x16x32_bf16 v[0:3], v[152:155], v[198:201], v[0:3]
	v_mfma_f32_16x16x32_bf16 v[56:59], v[148:151], v[164:167], v[56:59]
	v_mfma_f32_16x16x32_bf16 v[48:51], v[156:159], v[164:167], v[48:51]
	v_mfma_f32_16x16x32_bf16 v[40:43], v[148:151], v[186:189], v[40:43]
	v_mfma_f32_16x16x32_bf16 v[32:35], v[156:159], v[186:189], v[32:35]
	v_mfma_f32_16x16x32_bf16 v[20:23], v[148:151], v[194:197], v[20:23]
	v_mfma_f32_16x16x32_bf16 v[16:19], v[156:159], v[194:197], v[16:19]
	v_mfma_f32_16x16x32_bf16 v[4:7], v[148:151], v[202:205], v[4:7]
	v_mfma_f32_16x16x32_bf16 v[0:3], v[156:159], v[202:205], v[0:3]
	s_setprio 1
	s_barrier
	s_add_i32 s49, 0, 0x18000
	s_add_i32 s50, 0, 0x1c000
	v_add_u32_e32 v140, s49, v219
	v_add_u32_e32 v156, s50, v219
	ds_read_b128 v[124:127], v140
	ds_read_b128 v[132:135], v140 offset:1024
	ds_read_b128 v[136:139], v140 offset:2048
	ds_read_b128 v[140:143], v140 offset:3072
	ds_read_b128 v[144:147], v156
	ds_read_b128 v[148:151], v156 offset:1024
	ds_read_b128 v[152:155], v156 offset:2048
	ds_read_b128 v[156:159], v156 offset:3072
	s_add_u32 s38, s38, 0x40000
	s_addc_u32 s39, s39, 0
	s_mov_b32 m0, s27
	v_lshl_add_u64 v[214:215], s[38:39], 0, v[176:177]
	ds_read_b128 v[160:163], v223 offset:32768
	ds_read_b128 v[164:167], v223 offset:33792
	ds_read_b128 v[168:171], v223 offset:34816
	ds_read_b128 v[186:189], v223 offset:35840
	ds_read_b128 v[190:193], v223 offset:36864
	ds_read_b128 v[194:197], v223 offset:37888
	ds_read_b128 v[198:201], v223 offset:38912
	ds_read_b128 v[202:205], v223 offset:39936
	global_load_lds_dwordx4 v[214:215], off
	v_lshl_add_u64 v[214:215], s[38:39], 0, v[178:179]
	s_mov_b32 m0, s28
	s_nop 0
	global_load_lds_dwordx4 v[214:215], off
	s_waitcnt vmcnt(8)
	s_waitcnt lgkmcnt(0)
	s_barrier
	s_setprio 0
	s_waitcnt lgkmcnt(0)
	v_mfma_f32_16x16x32_bf16 v[120:123], v[124:127], v[160:163], v[120:123]
	v_mfma_f32_16x16x32_bf16 v[128:131], v[136:139], v[160:163], v[128:131]
	v_mfma_f32_16x16x32_bf16 v[108:111], v[124:127], v[168:171], v[108:111]
	v_mfma_f32_16x16x32_bf16 v[104:107], v[136:139], v[168:171], v[104:107]
	v_mfma_f32_16x16x32_bf16 v[92:95], v[124:127], v[190:193], v[92:95]
	v_mfma_f32_16x16x32_bf16 v[88:91], v[136:139], v[190:193], v[88:91]
	v_mfma_f32_16x16x32_bf16 v[76:79], v[124:127], v[198:201], v[76:79]
	v_mfma_f32_16x16x32_bf16 v[72:75], v[136:139], v[198:201], v[72:75]
	v_mfma_f32_16x16x32_bf16 v[120:123], v[132:135], v[164:167], v[120:123]
	v_mfma_f32_16x16x32_bf16 v[128:131], v[140:143], v[164:167], v[128:131]
	v_mfma_f32_16x16x32_bf16 v[108:111], v[132:135], v[186:189], v[108:111]
	v_mfma_f32_16x16x32_bf16 v[104:107], v[140:143], v[186:189], v[104:107]
	v_mfma_f32_16x16x32_bf16 v[92:95], v[132:135], v[194:197], v[92:95]
	v_mfma_f32_16x16x32_bf16 v[88:91], v[140:143], v[194:197], v[88:91]
	v_mfma_f32_16x16x32_bf16 v[76:79], v[132:135], v[202:205], v[76:79]
	v_mfma_f32_16x16x32_bf16 v[72:75], v[140:143], v[202:205], v[72:75]
	s_setprio 1
	s_setprio 0
	v_mfma_f32_16x16x32_bf16 v[116:119], v[144:147], v[160:163], v[116:119]
	v_mfma_f32_16x16x32_bf16 v[112:115], v[152:155], v[160:163], v[112:115]
	v_mfma_f32_16x16x32_bf16 v[100:103], v[144:147], v[168:171], v[100:103]
	v_mfma_f32_16x16x32_bf16 v[96:99], v[152:155], v[168:171], v[96:99]
	v_mfma_f32_16x16x32_bf16 v[84:87], v[144:147], v[190:193], v[84:87]
	v_mfma_f32_16x16x32_bf16 v[80:83], v[152:155], v[190:193], v[80:83]
	v_mfma_f32_16x16x32_bf16 v[68:71], v[144:147], v[198:201], v[68:71]
	v_mfma_f32_16x16x32_bf16 v[64:67], v[152:155], v[198:201], v[64:67]
	v_mfma_f32_16x16x32_bf16 v[116:119], v[148:151], v[164:167], v[116:119]
	v_mfma_f32_16x16x32_bf16 v[112:115], v[156:159], v[164:167], v[112:115]
	v_mfma_f32_16x16x32_bf16 v[100:103], v[148:151], v[186:189], v[100:103]
	v_mfma_f32_16x16x32_bf16 v[96:99], v[156:159], v[186:189], v[96:99]
	v_mfma_f32_16x16x32_bf16 v[84:87], v[148:151], v[194:197], v[84:87]
	v_mfma_f32_16x16x32_bf16 v[80:83], v[156:159], v[194:197], v[80:83]
	v_mfma_f32_16x16x32_bf16 v[68:71], v[148:151], v[202:205], v[68:71]
	v_mfma_f32_16x16x32_bf16 v[64:67], v[156:159], v[202:205], v[64:67]
	s_setprio 1
	s_barrier
	s_add_i32 s38, s49, s20
	v_lshl_add_u64 v[206:207], v[206:207], 0, s[4:5]
	s_mov_b32 m0, s38
	ds_read_b128 v[160:163], v223 offset:49152
	ds_read_b128 v[164:167], v223 offset:50176
	ds_read_b128 v[168:171], v223 offset:51200
	ds_read_b128 v[186:189], v223 offset:52224
	ds_read_b128 v[190:193], v223 offset:53248
	ds_read_b128 v[194:197], v223 offset:54272
	ds_read_b128 v[198:201], v223 offset:55296
	ds_read_b128 v[202:205], v223 offset:56320
	global_load_lds_dwordx4 v[206:207], off
	s_add_i32 m0, s38, 0x2000
	s_add_u32 s36, s36, 0x40080
	v_lshl_add_u64 v[206:207], v[208:209], 0, s[4:5]
	s_addc_u32 s37, s37, 0
	s_add_i32 s38, s50, s20
	global_load_lds_dwordx4 v[206:207], off
	v_lshl_add_u64 v[206:207], s[36:37], 0, v[174:175]
	s_mov_b32 m0, s38
	s_nop 0
	global_load_lds_dwordx4 v[206:207], off
	v_lshl_add_u64 v[206:207], s[36:37], 0, v[172:173]
	s_add_i32 m0, s38, 0x2000
	s_nop 0
	global_load_lds_dwordx4 v[206:207], off
	v_lshl_add_u64 v[206:207], v[210:211], 0, s[4:5]
	s_mov_b32 m0, s31
	s_nop 0
	global_load_lds_dwordx4 v[206:207], off
	v_lshl_add_u64 v[206:207], v[212:213], 0, s[4:5]
	s_mov_b32 m0, s33
	s_nop 0
	global_load_lds_dwordx4 v[206:207], off
	s_waitcnt vmcnt(8)
	s_waitcnt lgkmcnt(0)
	s_barrier
	s_setprio 0
	s_waitcnt lgkmcnt(0)
	v_mfma_f32_16x16x32_bf16 v[60:63], v[124:127], v[160:163], v[60:63]
	v_mfma_f32_16x16x32_bf16 v[52:55], v[136:139], v[160:163], v[52:55]
	v_mfma_f32_16x16x32_bf16 v[44:47], v[124:127], v[168:171], v[44:47]
	v_mfma_f32_16x16x32_bf16 v[36:39], v[136:139], v[168:171], v[36:39]
	v_mfma_f32_16x16x32_bf16 v[28:31], v[124:127], v[190:193], v[28:31]
	v_mfma_f32_16x16x32_bf16 v[24:27], v[136:139], v[190:193], v[24:27]
	v_mfma_f32_16x16x32_bf16 v[12:15], v[124:127], v[198:201], v[12:15]
	v_mfma_f32_16x16x32_bf16 v[8:11], v[136:139], v[198:201], v[8:11]
	v_mfma_f32_16x16x32_bf16 v[60:63], v[132:135], v[164:167], v[60:63]
	v_mfma_f32_16x16x32_bf16 v[52:55], v[140:143], v[164:167], v[52:55]
	v_mfma_f32_16x16x32_bf16 v[44:47], v[132:135], v[186:189], v[44:47]
	v_mfma_f32_16x16x32_bf16 v[36:39], v[140:143], v[186:189], v[36:39]
	v_mfma_f32_16x16x32_bf16 v[28:31], v[132:135], v[194:197], v[28:31]
	v_mfma_f32_16x16x32_bf16 v[24:27], v[140:143], v[194:197], v[24:27]
	v_mfma_f32_16x16x32_bf16 v[12:15], v[132:135], v[202:205], v[12:15]
	v_mfma_f32_16x16x32_bf16 v[8:11], v[140:143], v[202:205], v[8:11]
	s_setprio 1
	s_setprio 0
	v_mfma_f32_16x16x32_bf16 v[56:59], v[144:147], v[160:163], v[56:59]
	v_mfma_f32_16x16x32_bf16 v[48:51], v[152:155], v[160:163], v[48:51]
	v_mfma_f32_16x16x32_bf16 v[40:43], v[144:147], v[168:171], v[40:43]
	v_mfma_f32_16x16x32_bf16 v[32:35], v[152:155], v[168:171], v[32:35]
	v_mfma_f32_16x16x32_bf16 v[20:23], v[144:147], v[190:193], v[20:23]
	v_mfma_f32_16x16x32_bf16 v[16:19], v[152:155], v[190:193], v[16:19]
	v_mfma_f32_16x16x32_bf16 v[4:7], v[144:147], v[198:201], v[4:7]
	v_mfma_f32_16x16x32_bf16 v[0:3], v[152:155], v[198:201], v[0:3]
	v_mfma_f32_16x16x32_bf16 v[56:59], v[148:151], v[164:167], v[56:59]
	v_mfma_f32_16x16x32_bf16 v[48:51], v[156:159], v[164:167], v[48:51]
	v_mfma_f32_16x16x32_bf16 v[40:43], v[148:151], v[186:189], v[40:43]
	v_mfma_f32_16x16x32_bf16 v[32:35], v[156:159], v[186:189], v[32:35]
	v_mfma_f32_16x16x32_bf16 v[20:23], v[148:151], v[194:197], v[20:23]
	v_mfma_f32_16x16x32_bf16 v[16:19], v[156:159], v[194:197], v[16:19]
	v_mfma_f32_16x16x32_bf16 v[4:7], v[148:151], v[202:205], v[4:7]
	v_mfma_f32_16x16x32_bf16 v[0:3], v[156:159], v[202:205], v[0:3]
	s_setprio 1
	s_barrier
	s_add_i32 s48, s48, 2
	s_add_u32 s34, s34, 0x100
	s_addc_u32 s35, s35, 0
	s_add_u32 s46, s46, 0x100
	s_addc_u32 s47, s47, 0
	s_cmp_gt_u32 s48, 13
	s_cbranch_scc0 .LBB0_1102
	s_and_b64 vcc, exec, s[6:7]
	s_cbranch_vccz .LBB0_1105
	s_barrier

.LBB0_1175:
	ds_read_b128 v[20:23], v188
	ds_read_b128 v[24:27], v189
	ds_read_b128 v[16:19], v183
	ds_read_b128 v[0:3], v184
	ds_read_b128 v[28:31], v190
	ds_read_b128 v[4:7], v191
	ds_read_b128 v[8:11], v192
	ds_read_b128 v[12:15], v193
	s_add_u32 s26, s24, 0xfffe0080
	s_addc_u32 s27, s25, -1
	s_cmp_eq_u32 s50, 4
	s_cselect_b32 s35, s9, s27
	s_cselect_b32 s34, s46, s26
	s_cselect_b32 s27, s7, s49
	s_cselect_b32 s26, s47, s48
	v_lshl_add_u64 v[228:229], s[24:25], 0, v[168:169]
	s_add_i32 m0, s17, 0xc000
	ds_read_b128 v[174:177], v200
	ds_read_b128 v[178:181], v200 offset:1024
	ds_read_b128 v[204:207], v200 offset:2048
	ds_read_b128 v[208:211], v200 offset:3072
	ds_read_b128 v[212:215], v200 offset:4096
	ds_read_b128 v[216:219], v200 offset:5120
	ds_read_b128 v[220:223], v200 offset:6144
	ds_read_b128 v[224:227], v200 offset:7168
	global_load_lds_dwordx4 v[228:229], off
	v_lshl_add_u64 v[228:229], s[24:25], 0, v[170:171]
	s_add_i32 m0, s17, 0xe000
	s_nop 0
	global_load_lds_dwordx4 v[228:229], off
	s_waitcnt vmcnt(8)
	s_waitcnt lgkmcnt(0)
	s_barrier
	s_setprio 0
	s_waitcnt lgkmcnt(0)
	v_mfma_f32_16x16x128_f8f6f4 v[156:159], v[16:23], v[174:181], v[156:159]
	v_mfma_f32_16x16x128_f8f6f4 v[152:155], v[24:31], v[174:181], v[152:155]
	v_mfma_f32_16x16x128_f8f6f4 v[144:147], v[16:23], v[204:211], v[144:147]
	v_mfma_f32_16x16x128_f8f6f4 v[136:139], v[24:31], v[204:211], v[136:139]
	v_mfma_f32_16x16x128_f8f6f4 v[128:131], v[16:23], v[212:219], v[128:131]
	v_mfma_f32_16x16x128_f8f6f4 v[120:123], v[24:31], v[212:219], v[120:123]
	v_mfma_f32_16x16x128_f8f6f4 v[112:115], v[16:23], v[220:227], v[112:115]
	v_mfma_f32_16x16x128_f8f6f4 v[104:107], v[24:31], v[220:227], v[104:107]
	s_setprio 1
	s_setprio 0
	v_mfma_f32_16x16x128_f8f6f4 v[148:151], v[0:7], v[174:181], v[148:151]
	v_mfma_f32_16x16x128_f8f6f4 v[140:143], v[8:15], v[174:181], v[140:143]
	v_mfma_f32_16x16x128_f8f6f4 v[132:135], v[0:7], v[204:211], v[132:135]
	v_mfma_f32_16x16x128_f8f6f4 v[124:127], v[8:15], v[204:211], v[124:127]
	v_mfma_f32_16x16x128_f8f6f4 v[116:119], v[0:7], v[212:219], v[116:119]
	v_mfma_f32_16x16x128_f8f6f4 v[108:111], v[8:15], v[212:219], v[108:111]
	v_mfma_f32_16x16x128_f8f6f4 v[92:95], v[0:7], v[220:227], v[92:95]
	v_mfma_f32_16x16x128_f8f6f4 v[88:91], v[8:15], v[220:227], v[88:91]
	s_setprio 1
	s_barrier
	s_mov_b32 m0, s22
	v_lshl_add_u64 v[174:175], s[26:27], 0, v[162:163]
	s_add_u32 s52, s26, 0x20000
	ds_read_b128 v[204:207], v200 offset:16384
	ds_read_b128 v[208:211], v200 offset:17408
	ds_read_b128 v[212:215], v200 offset:18432
	ds_read_b128 v[216:219], v200 offset:19456
	ds_read_b128 v[220:223], v200 offset:20480
	ds_read_b128 v[224:227], v200 offset:21504
	ds_read_b128 v[228:231], v200 offset:22528
	ds_read_b128 v[232:235], v200 offset:23552
	global_load_lds_dwordx4 v[174:175], off
	v_lshl_add_u64 v[176:177], s[26:27], 0, v[160:161]
	s_mov_b32 m0, s23
	s_addc_u32 s53, s27, 0
	global_load_lds_dwordx4 v[176:177], off
	v_lshl_add_u64 v[178:179], s[52:53], 0, v[162:163]
	s_mov_b32 m0, s28
	v_lshl_add_u64 v[180:181], s[34:35], 0, v[166:167]
	global_load_lds_dwordx4 v[178:179], off
	v_lshl_add_u64 v[178:179], s[52:53], 0, v[160:161]
	s_mov_b32 m0, s29
	s_nop 0
	global_load_lds_dwordx4 v[178:179], off
	v_lshl_add_u64 v[178:179], s[34:35], 0, v[164:165]
	s_mov_b32 m0, s17
	s_nop 0
	global_load_lds_dwordx4 v[178:179], off
	s_mov_b32 m0, s30
	s_nop 0
	global_load_lds_dwordx4 v[180:181], off
	s_waitcnt vmcnt(8)
	s_waitcnt lgkmcnt(0)
	s_barrier
	s_setprio 0
	s_waitcnt lgkmcnt(0)
	v_mfma_f32_16x16x128_f8f6f4 v[76:79], v[16:23], v[204:211], v[76:79]
	v_mfma_f32_16x16x128_f8f6f4 v[72:75], v[24:31], v[204:211], v[72:75]
	v_mfma_f32_16x16x128_f8f6f4 v[52:55], v[16:23], v[212:219], v[52:55]
	v_mfma_f32_16x16x128_f8f6f4 v[48:51], v[24:31], v[212:219], v[48:51]
	v_mfma_f32_16x16x128_f8f6f4 v[60:63], v[16:23], v[220:227], v[60:63]
	v_mfma_f32_16x16x128_f8f6f4 v[56:59], v[24:31], v[220:227], v[56:59]
	v_mfma_f32_16x16x128_f8f6f4 v[36:39], v[16:23], v[228:235], v[36:39]
	v_mfma_f32_16x16x128_f8f6f4 v[32:35], v[24:31], v[228:235], v[32:35]
	s_setprio 1
	s_setprio 0
	v_mfma_f32_16x16x128_f8f6f4 v[100:103], v[0:7], v[204:211], v[100:103]
	v_mfma_f32_16x16x128_f8f6f4 v[96:99], v[8:15], v[204:211], v[96:99]
	v_mfma_f32_16x16x128_f8f6f4 v[84:87], v[0:7], v[212:219], v[84:87]
	v_mfma_f32_16x16x128_f8f6f4 v[80:83], v[8:15], v[212:219], v[80:83]
	v_mfma_f32_16x16x128_f8f6f4 v[68:71], v[0:7], v[220:227], v[68:71]
	v_mfma_f32_16x16x128_f8f6f4 v[64:67], v[8:15], v[220:227], v[64:67]
	v_mfma_f32_16x16x128_f8f6f4 v[44:47], v[0:7], v[228:235], v[44:47]
	v_mfma_f32_16x16x128_f8f6f4 v[40:43], v[8:15], v[228:235], v[40:43]
	s_setprio 1
	s_barrier
	ds_read_b128 v[4:7], v194
	ds_read_b128 v[8:11], v195
	ds_read_b128 v[0:3], v185
	ds_read_b128 v[16:19], v186
	ds_read_b128 v[12:15], v196
	ds_read_b128 v[20:23], v197
	ds_read_b128 v[24:27], v198
	ds_read_b128 v[28:31], v199
	s_add_u32 s34, s34, 0x20000
	s_addc_u32 s35, s35, 0
	s_mov_b32 m0, s31
	v_lshl_add_u64 v[236:237], s[34:35], 0, v[164:165]
	ds_read_b128 v[204:207], v200 offset:32768
	ds_read_b128 v[208:211], v200 offset:33792
	ds_read_b128 v[212:215], v200 offset:34816
	ds_read_b128 v[216:219], v200 offset:35840
	ds_read_b128 v[220:223], v200 offset:36864
	ds_read_b128 v[224:227], v200 offset:37888
	ds_read_b128 v[228:231], v200 offset:38912
	ds_read_b128 v[232:235], v200 offset:39936
	global_load_lds_dwordx4 v[236:237], off
	v_lshl_add_u64 v[236:237], s[34:35], 0, v[166:167]
	s_mov_b32 m0, s33
	s_nop 0
	global_load_lds_dwordx4 v[236:237], off
	s_waitcnt vmcnt(8)
	s_waitcnt lgkmcnt(0)
	s_barrier
	s_setprio 0
	s_waitcnt lgkmcnt(0)
	v_mfma_f32_16x16x128_f8f6f4 v[156:159], v[0:7], v[204:211], v[156:159]
	v_mfma_f32_16x16x128_f8f6f4 v[152:155], v[8:15], v[204:211], v[152:155]
	v_mfma_f32_16x16x128_f8f6f4 v[144:147], v[0:7], v[212:219], v[144:147]
	v_mfma_f32_16x16x128_f8f6f4 v[136:139], v[8:15], v[212:219], v[136:139]
	v_mfma_f32_16x16x128_f8f6f4 v[128:131], v[0:7], v[220:227], v[128:131]
	v_mfma_f32_16x16x128_f8f6f4 v[120:123], v[8:15], v[220:227], v[120:123]
	v_mfma_f32_16x16x128_f8f6f4 v[112:115], v[0:7], v[228:235], v[112:115]
	v_mfma_f32_16x16x128_f8f6f4 v[104:107], v[8:15], v[228:235], v[104:107]
	s_setprio 1
	s_setprio 0
	v_mfma_f32_16x16x128_f8f6f4 v[148:151], v[16:23], v[204:211], v[148:151]
	v_mfma_f32_16x16x128_f8f6f4 v[140:143], v[24:31], v[204:211], v[140:143]
	v_mfma_f32_16x16x128_f8f6f4 v[132:135], v[16:23], v[212:219], v[132:135]
	v_mfma_f32_16x16x128_f8f6f4 v[124:127], v[24:31], v[212:219], v[124:127]
	v_mfma_f32_16x16x128_f8f6f4 v[116:119], v[16:23], v[220:227], v[116:119]
	v_mfma_f32_16x16x128_f8f6f4 v[108:111], v[24:31], v[220:227], v[108:111]
	v_mfma_f32_16x16x128_f8f6f4 v[92:95], v[16:23], v[228:235], v[92:95]
	v_mfma_f32_16x16x128_f8f6f4 v[88:91], v[24:31], v[228:235], v[88:91]
	s_setprio 1
	s_barrier
	s_mov_b32 m0, s37
	v_lshl_add_u64 v[174:175], v[174:175], 0, s[2:3]
	s_add_u32 s26, s26, 0x20080
	ds_read_b128 v[204:207], v200 offset:49152
	ds_read_b128 v[208:211], v200 offset:50176
	ds_read_b128 v[212:215], v200 offset:51200
	ds_read_b128 v[216:219], v200 offset:52224
	ds_read_b128 v[220:223], v200 offset:53248
	ds_read_b128 v[224:227], v200 offset:54272
	ds_read_b128 v[228:231], v200 offset:55296
	ds_read_b128 v[232:235], v200 offset:56320
	global_load_lds_dwordx4 v[174:175], off
	v_lshl_add_u64 v[174:175], v[176:177], 0, s[2:3]
	s_mov_b32 m0, s38
	s_addc_u32 s27, s27, 0
	global_load_lds_dwordx4 v[174:175], off
	v_lshl_add_u64 v[174:175], s[26:27], 0, v[162:163]
	s_mov_b32 m0, s41
	s_nop 0
	global_load_lds_dwordx4 v[174:175], off
	v_lshl_add_u64 v[174:175], s[26:27], 0, v[160:161]
	s_mov_b32 m0, s42
	s_nop 0
	global_load_lds_dwordx4 v[174:175], off
	v_lshl_add_u64 v[174:175], v[178:179], 0, s[2:3]
	s_mov_b32 m0, s39
	s_nop 0
	global_load_lds_dwordx4 v[174:175], off
	v_lshl_add_u64 v[174:175], v[180:181], 0, s[2:3]
	s_mov_b32 m0, s40
	s_nop 0
	global_load_lds_dwordx4 v[174:175], off
	s_waitcnt vmcnt(8)
	s_waitcnt lgkmcnt(0)
	s_barrier
	s_setprio 0
	s_waitcnt lgkmcnt(0)
	v_mfma_f32_16x16x128_f8f6f4 v[76:79], v[0:7], v[204:211], v[76:79]
	v_mfma_f32_16x16x128_f8f6f4 v[72:75], v[8:15], v[204:211], v[72:75]
	v_mfma_f32_16x16x128_f8f6f4 v[52:55], v[0:7], v[212:219], v[52:55]
	v_mfma_f32_16x16x128_f8f6f4 v[48:51], v[8:15], v[212:219], v[48:51]
	v_mfma_f32_16x16x128_f8f6f4 v[60:63], v[0:7], v[220:227], v[60:63]
	v_mfma_f32_16x16x128_f8f6f4 v[56:59], v[8:15], v[220:227], v[56:59]
	v_mfma_f32_16x16x128_f8f6f4 v[36:39], v[0:7], v[228:235], v[36:39]
	v_mfma_f32_16x16x128_f8f6f4 v[32:35], v[8:15], v[228:235], v[32:35]
	s_setprio 1
	s_setprio 0
	v_mfma_f32_16x16x128_f8f6f4 v[100:103], v[16:23], v[204:211], v[100:103]
	v_mfma_f32_16x16x128_f8f6f4 v[96:99], v[24:31], v[204:211], v[96:99]
	v_mfma_f32_16x16x128_f8f6f4 v[84:87], v[16:23], v[212:219], v[84:87]
	v_mfma_f32_16x16x128_f8f6f4 v[80:83], v[24:31], v[212:219], v[80:83]
	v_mfma_f32_16x16x128_f8f6f4 v[68:71], v[16:23], v[220:227], v[68:71]
	v_mfma_f32_16x16x128_f8f6f4 v[64:67], v[24:31], v[220:227], v[64:67]
	v_mfma_f32_16x16x128_f8f6f4 v[44:47], v[16:23], v[228:235], v[44:47]
	v_mfma_f32_16x16x128_f8f6f4 v[40:43], v[24:31], v[228:235], v[40:43]
	s_setprio 1
	s_barrier
	s_add_i32 s50, s50, 2
	s_add_u32 s24, s24, 0x100
	s_addc_u32 s25, s25, 0
	s_add_u32 s48, s48, 0x100
	s_addc_u32 s49, s49, 0
	s_cmp_gt_u32 s50, 5
	s_cbranch_scc0 .LBB0_1175
	s_nop 15
	s_nop 7
	s_and_b64 vcc, exec, s[4:5]
	s_cbranch_vccz .LBB0_1178
	s_barrier

.LBB0_1501:
	ds_read_b128 v[20:23], v217
	ds_read_b128 v[24:27], v218
	ds_read_b128 v[16:19], v213
	ds_read_b128 v[0:3], v214
	ds_read_b128 v[28:31], v219
	ds_read_b128 v[4:7], v220
	ds_read_b128 v[8:11], v221
	ds_read_b128 v[12:15], v222
	s_add_u32 s6, s2, 0xfffe0080
	s_addc_u32 s7, s3, -1
	s_cmp_eq_u32 s55, 4
	s_cselect_b32 s53, s1, s7
	s_cselect_b32 s52, s5, s6
	s_cselect_b32 s7, s33, s54
	s_cselect_b32 s6, s43, s45
	v_lshl_add_u64 v[210:211], s[2:3], 0, v[194:195]
	s_add_i32 m0, s61, 0xc000
	ds_read_b128 v[160:163], v229
	ds_read_b128 v[164:167], v229 offset:1024
	ds_read_b128 v[168:171], v229 offset:2048
	ds_read_b128 v[172:175], v229 offset:3072
	ds_read_b128 v[176:179], v229 offset:4096
	ds_read_b128 v[180:183], v229 offset:5120
	ds_read_b128 v[202:205], v229 offset:6144
	ds_read_b128 v[206:209], v229 offset:7168
	global_load_lds_dwordx4 v[210:211], off
	v_lshl_add_u64 v[210:211], s[2:3], 0, v[196:197]
	s_add_i32 m0, s61, 0xe000
	s_nop 0
	global_load_lds_dwordx4 v[210:211], off
	s_waitcnt vmcnt(8)
	s_waitcnt lgkmcnt(0)
	s_barrier
	s_setprio 0
	s_waitcnt lgkmcnt(0)
	v_mfma_f32_16x16x128_f8f6f4 v[156:159], v[16:23], v[160:167], v[156:159]
	v_mfma_f32_16x16x128_f8f6f4 v[152:155], v[24:31], v[160:167], v[152:155]
	v_mfma_f32_16x16x128_f8f6f4 v[140:143], v[16:23], v[168:175], v[140:143]
	v_mfma_f32_16x16x128_f8f6f4 v[136:139], v[24:31], v[168:175], v[136:139]
	v_mfma_f32_16x16x128_f8f6f4 v[124:127], v[16:23], v[176:183], v[124:127]
	v_mfma_f32_16x16x128_f8f6f4 v[120:123], v[24:31], v[176:183], v[120:123]
	v_mfma_f32_16x16x128_f8f6f4 v[108:111], v[16:23], v[202:209], v[108:111]
	v_mfma_f32_16x16x128_f8f6f4 v[104:107], v[24:31], v[202:209], v[104:107]
	s_setprio 1
	s_setprio 0
	v_mfma_f32_16x16x128_f8f6f4 v[148:151], v[0:7], v[160:167], v[148:151]
	v_mfma_f32_16x16x128_f8f6f4 v[144:147], v[8:15], v[160:167], v[144:147]
	v_mfma_f32_16x16x128_f8f6f4 v[132:135], v[0:7], v[168:175], v[132:135]
	v_mfma_f32_16x16x128_f8f6f4 v[128:131], v[8:15], v[168:175], v[128:131]
	v_mfma_f32_16x16x128_f8f6f4 v[116:119], v[0:7], v[176:183], v[116:119]
	v_mfma_f32_16x16x128_f8f6f4 v[112:115], v[8:15], v[176:183], v[112:115]
	v_mfma_f32_16x16x128_f8f6f4 v[100:103], v[0:7], v[202:209], v[100:103]
	v_mfma_f32_16x16x128_f8f6f4 v[96:99], v[8:15], v[202:209], v[96:99]
	s_setprio 1
	s_barrier
	s_mov_b32 m0, s62
	v_lshl_add_u64 v[160:161], s[6:7], 0, v[184:185]
	s_add_u32 s56, s6, 0x20000
	ds_read_b128 v[168:171], v229 offset:16384
	ds_read_b128 v[172:175], v229 offset:17408
	ds_read_b128 v[176:179], v229 offset:18432
	ds_read_b128 v[180:183], v229 offset:19456
	ds_read_b128 v[202:205], v229 offset:20480
	ds_read_b128 v[206:209], v229 offset:21504
	ds_read_b128 v[236:239], v229 offset:22528
	ds_read_b128 v[240:243], v229 offset:23552
	global_load_lds_dwordx4 v[160:161], off
	v_lshl_add_u64 v[162:163], s[6:7], 0, v[186:187]
	s_mov_b32 m0, s63
	s_addc_u32 s57, s7, 0
	global_load_lds_dwordx4 v[162:163], off
	v_lshl_add_u64 v[164:165], s[56:57], 0, v[184:185]
	s_mov_b32 m0, s64
	v_lshl_add_u64 v[166:167], s[52:53], 0, v[190:191]
	global_load_lds_dwordx4 v[164:165], off
	v_lshl_add_u64 v[164:165], s[56:57], 0, v[186:187]
	s_mov_b32 m0, s65
	s_nop 0
	global_load_lds_dwordx4 v[164:165], off
	v_lshl_add_u64 v[164:165], s[52:53], 0, v[188:189]
	s_mov_b32 m0, s61
	s_nop 0
	global_load_lds_dwordx4 v[164:165], off
	s_mov_b32 m0, s66
	s_nop 0
	global_load_lds_dwordx4 v[166:167], off
	s_waitcnt vmcnt(8)
	s_waitcnt lgkmcnt(0)
	s_barrier
	s_setprio 0
	s_waitcnt lgkmcnt(0)
	v_mfma_f32_16x16x128_f8f6f4 v[84:87], v[16:23], v[168:175], v[84:87]
	v_mfma_f32_16x16x128_f8f6f4 v[80:83], v[24:31], v[168:175], v[80:83]
	v_mfma_f32_16x16x128_f8f6f4 v[68:71], v[16:23], v[176:183], v[68:71]
	v_mfma_f32_16x16x128_f8f6f4 v[64:67], v[24:31], v[176:183], v[64:67]
	v_mfma_f32_16x16x128_f8f6f4 v[56:59], v[16:23], v[202:209], v[56:59]
	v_mfma_f32_16x16x128_f8f6f4 v[48:51], v[24:31], v[202:209], v[48:51]
	v_mfma_f32_16x16x128_f8f6f4 v[40:43], v[16:23], v[236:243], v[40:43]
	v_mfma_f32_16x16x128_f8f6f4 v[32:35], v[24:31], v[236:243], v[32:35]
	s_setprio 1
	s_setprio 0
	v_mfma_f32_16x16x128_f8f6f4 v[92:95], v[0:7], v[168:175], v[92:95]
	v_mfma_f32_16x16x128_f8f6f4 v[88:91], v[8:15], v[168:175], v[88:91]
	v_mfma_f32_16x16x128_f8f6f4 v[76:79], v[0:7], v[176:183], v[76:79]
	v_mfma_f32_16x16x128_f8f6f4 v[72:75], v[8:15], v[176:183], v[72:75]
	v_mfma_f32_16x16x128_f8f6f4 v[60:63], v[0:7], v[202:209], v[60:63]
	v_mfma_f32_16x16x128_f8f6f4 v[52:55], v[8:15], v[202:209], v[52:55]
	v_mfma_f32_16x16x128_f8f6f4 v[44:47], v[0:7], v[236:243], v[44:47]
	v_mfma_f32_16x16x128_f8f6f4 v[36:39], v[8:15], v[236:243], v[36:39]
	s_setprio 1
	s_barrier
	ds_read_b128 v[4:7], v223
	ds_read_b128 v[8:11], v224
	ds_read_b128 v[0:3], v215
	ds_read_b128 v[16:19], v216
	ds_read_b128 v[12:15], v225
	ds_read_b128 v[20:23], v226
	ds_read_b128 v[24:27], v227
	ds_read_b128 v[28:31], v228
	s_add_u32 s52, s52, 0x20000
	s_addc_u32 s53, s53, 0
	s_mov_b32 m0, s67
	v_lshl_add_u64 v[210:211], s[52:53], 0, v[188:189]
	ds_read_b128 v[168:171], v229 offset:32768
	ds_read_b128 v[172:175], v229 offset:33792
	ds_read_b128 v[176:179], v229 offset:34816
	ds_read_b128 v[180:183], v229 offset:35840
	ds_read_b128 v[202:205], v229 offset:36864
	ds_read_b128 v[206:209], v229 offset:37888
	ds_read_b128 v[236:239], v229 offset:38912
	ds_read_b128 v[240:243], v229 offset:39936
	global_load_lds_dwordx4 v[210:211], off
	v_lshl_add_u64 v[210:211], s[52:53], 0, v[190:191]
	s_mov_b32 m0, s68
	s_nop 0
	global_load_lds_dwordx4 v[210:211], off
	s_waitcnt vmcnt(8)
	s_waitcnt lgkmcnt(0)
	s_barrier
	s_setprio 0
	s_waitcnt lgkmcnt(0)
	v_mfma_f32_16x16x128_f8f6f4 v[156:159], v[0:7], v[168:175], v[156:159]
	v_mfma_f32_16x16x128_f8f6f4 v[152:155], v[8:15], v[168:175], v[152:155]
	v_mfma_f32_16x16x128_f8f6f4 v[140:143], v[0:7], v[176:183], v[140:143]
	v_mfma_f32_16x16x128_f8f6f4 v[136:139], v[8:15], v[176:183], v[136:139]
	v_mfma_f32_16x16x128_f8f6f4 v[124:127], v[0:7], v[202:209], v[124:127]
	v_mfma_f32_16x16x128_f8f6f4 v[120:123], v[8:15], v[202:209], v[120:123]
	v_mfma_f32_16x16x128_f8f6f4 v[108:111], v[0:7], v[236:243], v[108:111]
	v_mfma_f32_16x16x128_f8f6f4 v[104:107], v[8:15], v[236:243], v[104:107]
	s_setprio 1
	s_setprio 0
	v_mfma_f32_16x16x128_f8f6f4 v[148:151], v[16:23], v[168:175], v[148:151]
	v_mfma_f32_16x16x128_f8f6f4 v[144:147], v[24:31], v[168:175], v[144:147]
	v_mfma_f32_16x16x128_f8f6f4 v[132:135], v[16:23], v[176:183], v[132:135]
	v_mfma_f32_16x16x128_f8f6f4 v[128:131], v[24:31], v[176:183], v[128:131]
	v_mfma_f32_16x16x128_f8f6f4 v[116:119], v[16:23], v[202:209], v[116:119]
	v_mfma_f32_16x16x128_f8f6f4 v[112:115], v[24:31], v[202:209], v[112:115]
	v_mfma_f32_16x16x128_f8f6f4 v[100:103], v[16:23], v[236:243], v[100:103]
	v_mfma_f32_16x16x128_f8f6f4 v[96:99], v[24:31], v[236:243], v[96:99]
	s_setprio 1
	s_barrier
	s_mov_b32 m0, s11
	v_lshl_add_u64 v[160:161], v[160:161], 0, s[30:31]
	s_add_u32 s6, s6, 0x20080
	ds_read_b128 v[168:171], v229 offset:49152
	ds_read_b128 v[172:175], v229 offset:50176
	ds_read_b128 v[176:179], v229 offset:51200
	ds_read_b128 v[180:183], v229 offset:52224
	ds_read_b128 v[202:205], v229 offset:53248
	ds_read_b128 v[206:209], v229 offset:54272
	ds_read_b128 v[236:239], v229 offset:55296
	ds_read_b128 v[240:243], v229 offset:56320
	global_load_lds_dwordx4 v[160:161], off
	v_lshl_add_u64 v[160:161], v[162:163], 0, s[30:31]
	s_mov_b32 m0, s39
	s_addc_u32 s7, s7, 0
	global_load_lds_dwordx4 v[160:161], off
	v_lshl_add_u64 v[160:161], s[6:7], 0, v[184:185]
	s_mov_b32 m0, s20
	s_nop 0
	global_load_lds_dwordx4 v[160:161], off
	v_lshl_add_u64 v[160:161], s[6:7], 0, v[186:187]
	s_mov_b32 m0, s21
	s_nop 0
	global_load_lds_dwordx4 v[160:161], off
	v_lshl_add_u64 v[160:161], v[164:165], 0, s[30:31]
	s_mov_b32 m0, s18
	s_nop 0
	global_load_lds_dwordx4 v[160:161], off
	v_lshl_add_u64 v[160:161], v[166:167], 0, s[30:31]
	s_mov_b32 m0, s19
	s_nop 0
	global_load_lds_dwordx4 v[160:161], off
	s_waitcnt vmcnt(8)
	s_waitcnt lgkmcnt(0)
	s_barrier
	s_setprio 0
	s_waitcnt lgkmcnt(0)
	v_mfma_f32_16x16x128_f8f6f4 v[84:87], v[0:7], v[168:175], v[84:87]
	v_mfma_f32_16x16x128_f8f6f4 v[80:83], v[8:15], v[168:175], v[80:83]
	v_mfma_f32_16x16x128_f8f6f4 v[68:71], v[0:7], v[176:183], v[68:71]
	v_mfma_f32_16x16x128_f8f6f4 v[64:67], v[8:15], v[176:183], v[64:67]
	v_mfma_f32_16x16x128_f8f6f4 v[56:59], v[0:7], v[202:209], v[56:59]
	v_mfma_f32_16x16x128_f8f6f4 v[48:51], v[8:15], v[202:209], v[48:51]
	v_mfma_f32_16x16x128_f8f6f4 v[40:43], v[0:7], v[236:243], v[40:43]
	v_mfma_f32_16x16x128_f8f6f4 v[32:35], v[8:15], v[236:243], v[32:35]
	s_setprio 1
	s_setprio 0
	v_mfma_f32_16x16x128_f8f6f4 v[92:95], v[16:23], v[168:175], v[92:95]
	v_mfma_f32_16x16x128_f8f6f4 v[88:91], v[24:31], v[168:175], v[88:91]
	v_mfma_f32_16x16x128_f8f6f4 v[76:79], v[16:23], v[176:183], v[76:79]
	v_mfma_f32_16x16x128_f8f6f4 v[72:75], v[24:31], v[176:183], v[72:75]
	v_mfma_f32_16x16x128_f8f6f4 v[60:63], v[16:23], v[202:209], v[60:63]
	v_mfma_f32_16x16x128_f8f6f4 v[52:55], v[24:31], v[202:209], v[52:55]
	v_mfma_f32_16x16x128_f8f6f4 v[44:47], v[16:23], v[236:243], v[44:47]
	v_mfma_f32_16x16x128_f8f6f4 v[36:39], v[24:31], v[236:243], v[36:39]
	s_setprio 1
	s_barrier
	s_add_i32 s55, s55, 2
	s_add_u32 s2, s2, 0x100
	s_addc_u32 s3, s3, 0
	s_add_u32 s45, s45, 0x100
	s_addc_u32 s54, s54, 0
	s_cmp_gt_u32 s55, 5
	s_cbranch_scc0 .LBB0_1501
	s_nop 15
	s_nop 7
	s_and_b64 vcc, exec, s[34:35]
	s_cbranch_vccz .LBB0_1504
	s_barrier

.LBB0_1692:
	s_add_u32 s42, s90, s4
	s_addc_u32 s43, s91, s5
	s_add_u32 s73, s42, 0x21c00100
	s_addc_u32 s74, s43, 0
	s_cmpk_eq_i32 s4, 0x300
	v_lshl_add_u64 v[0:1], v[180:181], 0, s[4:5]
	s_cselect_b64 vcc, -1, 0
	v_cndmask_b32_e32 v183, v1, v167, vcc
	v_cndmask_b32_e32 v182, v0, v220, vcc
	ds_read_b128 v[8:11], v194
	ds_read_b128 v[12:15], v198
	ds_read_b128 v[24:27], v199
	ds_read_b128 v[28:31], v200
	ds_read_b128 v[0:3], v195
	ds_read_b128 v[4:7], v201
	ds_read_b128 v[16:19], v202
	ds_read_b128 v[20:23], v203
	s_and_b64 s[42:43], vcc, exec
	s_cselect_b32 s43, s9, s74
	s_cselect_b32 s42, s8, s73
	v_cndmask_b32_e32 v160, v219, v215, vcc
	v_cndmask_b32_e32 v184, v170, v216, vcc
	v_cndmask_b32_e32 v175, v172, v217, vcc
	v_cndmask_b32_e32 v173, v174, v218, vcc
	v_lshl_add_u64 v[186:187], v[178:179], 0, s[4:5]
	s_add_i32 m0, s0, 0xc000
	ds_read_b128 v[222:225], v212
	ds_read_b128 v[226:229], v212 offset:1024
	ds_read_b128 v[230:233], v212 offset:2048
	ds_read_b128 v[234:237], v212 offset:3072
	ds_read_b128 v[238:241], v212 offset:4096
	ds_read_b128 v[242:245], v212 offset:5120
	ds_read_b128 v[246:249], v212 offset:6144
	ds_read_b128 v[250:253], v212 offset:7168
	global_load_lds_dwordx4 v[186:187], off
	v_lshl_add_u64 v[186:187], v[176:177], 0, s[4:5]
	s_add_i32 m0, s0, 0xe000
	s_nop 0
	global_load_lds_dwordx4 v[186:187], off
	s_waitcnt vmcnt(8)
	s_waitcnt lgkmcnt(0)
	s_barrier
	s_setprio 0
	s_waitcnt lgkmcnt(0)
	v_mfma_f32_16x16x128_f8f6f4 v[156:159], v[8:15], v[222:229], v[156:159]
	v_mfma_f32_16x16x128_f8f6f4 v[152:155], v[24:31], v[222:229], v[152:155]
	v_mfma_f32_16x16x128_f8f6f4 v[140:143], v[8:15], v[230:237], v[140:143]
	v_mfma_f32_16x16x128_f8f6f4 v[136:139], v[24:31], v[230:237], v[136:139]
	v_mfma_f32_16x16x128_f8f6f4 v[124:127], v[8:15], v[238:245], v[124:127]
	v_mfma_f32_16x16x128_f8f6f4 v[120:123], v[24:31], v[238:245], v[120:123]
	v_mfma_f32_16x16x128_f8f6f4 v[108:111], v[8:15], v[246:253], v[108:111]
	v_mfma_f32_16x16x128_f8f6f4 v[104:107], v[24:31], v[246:253], v[104:107]
	s_setprio 1
	s_setprio 0
	v_mfma_f32_16x16x128_f8f6f4 v[148:151], v[0:7], v[222:229], v[148:151]
	v_mfma_f32_16x16x128_f8f6f4 v[144:147], v[16:23], v[222:229], v[144:147]
	v_mfma_f32_16x16x128_f8f6f4 v[132:135], v[0:7], v[230:237], v[132:135]
	v_mfma_f32_16x16x128_f8f6f4 v[128:131], v[16:23], v[230:237], v[128:131]
	v_mfma_f32_16x16x128_f8f6f4 v[116:119], v[0:7], v[238:245], v[116:119]
	v_mfma_f32_16x16x128_f8f6f4 v[112:115], v[16:23], v[238:245], v[112:115]
	v_mfma_f32_16x16x128_f8f6f4 v[100:103], v[0:7], v[246:253], v[100:103]
	v_mfma_f32_16x16x128_f8f6f4 v[96:99], v[16:23], v[246:253], v[96:99]
	s_setprio 1
	s_barrier
	s_mov_b32 m0, s21
	v_lshl_add_u64 v[186:187], v[182:183], 0, v[164:165]
	ds_read_b128 v[222:225], v212 offset:16384
	ds_read_b128 v[226:229], v212 offset:17408
	ds_read_b128 v[230:233], v212 offset:18432
	ds_read_b128 v[234:237], v212 offset:19456
	ds_read_b128 v[238:241], v212 offset:20480
	ds_read_b128 v[242:245], v212 offset:21504
	ds_read_b128 v[246:249], v212 offset:22528
	ds_read_b128 v[250:253], v212 offset:23552
	global_load_lds_dwordx4 v[186:187], off
	v_lshl_add_u64 v[188:189], v[182:183], 0, v[162:163]
	s_mov_b32 m0, s22
	v_lshl_add_u64 v[190:191], v[182:183], 0, s[12:13]
	global_load_lds_dwordx4 v[188:189], off
	v_lshl_add_u64 v[192:193], v[190:191], 0, v[164:165]
	s_mov_b32 m0, s23
	v_lshl_add_u64 v[190:191], v[190:191], 0, v[162:163]
	global_load_lds_dwordx4 v[192:193], off
	s_mov_b32 m0, s33
	v_mov_b32_e32 v185, v161
	global_load_lds_dwordx4 v[190:191], off
	s_mov_b32 m0, s0
	v_lshl_add_u64 v[190:191], s[42:43], 0, v[160:161]
	global_load_lds_dwordx4 v160, s[42:43]
	s_mov_b32 m0, s44
	s_nop 0
	global_load_lds_dwordx4 v184, s[42:43]
	s_waitcnt vmcnt(8)
	s_waitcnt lgkmcnt(0)
	v_lshl_add_u64 v[184:185], s[42:43], 0, v[184:185]
	s_barrier
	s_setprio 0
	s_waitcnt lgkmcnt(0)
	v_mfma_f32_16x16x128_f8f6f4 v[84:87], v[8:15], v[222:229], v[84:87]
	v_mfma_f32_16x16x128_f8f6f4 v[80:83], v[24:31], v[222:229], v[80:83]
	v_mfma_f32_16x16x128_f8f6f4 v[68:71], v[8:15], v[230:237], v[68:71]
	v_mfma_f32_16x16x128_f8f6f4 v[64:67], v[24:31], v[230:237], v[64:67]
	v_mfma_f32_16x16x128_f8f6f4 v[52:55], v[8:15], v[238:245], v[52:55]
	v_mfma_f32_16x16x128_f8f6f4 v[48:51], v[24:31], v[238:245], v[48:51]
	v_mfma_f32_16x16x128_f8f6f4 v[36:39], v[8:15], v[246:253], v[36:39]
	v_mfma_f32_16x16x128_f8f6f4 v[32:35], v[24:31], v[246:253], v[32:35]
	s_setprio 1
	s_setprio 0
	v_mfma_f32_16x16x128_f8f6f4 v[92:95], v[0:7], v[222:229], v[92:95]
	v_mfma_f32_16x16x128_f8f6f4 v[88:91], v[16:23], v[222:229], v[88:91]
	v_mfma_f32_16x16x128_f8f6f4 v[76:79], v[0:7], v[230:237], v[76:79]
	v_mfma_f32_16x16x128_f8f6f4 v[72:75], v[16:23], v[230:237], v[72:75]
	v_mfma_f32_16x16x128_f8f6f4 v[60:63], v[0:7], v[238:245], v[60:63]
	v_mfma_f32_16x16x128_f8f6f4 v[56:59], v[16:23], v[238:245], v[56:59]
	v_mfma_f32_16x16x128_f8f6f4 v[44:47], v[0:7], v[246:253], v[44:47]
	v_mfma_f32_16x16x128_f8f6f4 v[40:43], v[16:23], v[246:253], v[40:43]
	s_setprio 1
	s_barrier
	ds_read_b128 v[4:7], v204
	ds_read_b128 v[8:11], v205
	ds_read_b128 v[0:3], v196
	ds_read_b128 v[16:19], v197
	ds_read_b128 v[12:15], v206
	ds_read_b128 v[20:23], v207
	ds_read_b128 v[24:27], v208
	ds_read_b128 v[28:31], v209
	s_mov_b32 m0, s45
	ds_read_b128 v[222:225], v212 offset:32768
	ds_read_b128 v[226:229], v212 offset:33792
	ds_read_b128 v[230:233], v212 offset:34816
	ds_read_b128 v[234:237], v212 offset:35840
	ds_read_b128 v[238:241], v212 offset:36864
	ds_read_b128 v[242:245], v212 offset:37888
	ds_read_b128 v[246:249], v212 offset:38912
	ds_read_b128 v[250:253], v212 offset:39936
	global_load_lds_dwordx4 v175, s[42:43]
	s_mov_b32 m0, s46
	s_nop 0
	global_load_lds_dwordx4 v173, s[42:43]
	s_waitcnt vmcnt(8)
	s_waitcnt lgkmcnt(0)
	s_barrier
	s_setprio 0
	s_waitcnt lgkmcnt(0)
	v_mfma_f32_16x16x128_f8f6f4 v[156:159], v[0:7], v[222:229], v[156:159]
	v_mfma_f32_16x16x128_f8f6f4 v[152:155], v[8:15], v[222:229], v[152:155]
	v_mfma_f32_16x16x128_f8f6f4 v[140:143], v[0:7], v[230:237], v[140:143]
	v_mfma_f32_16x16x128_f8f6f4 v[136:139], v[8:15], v[230:237], v[136:139]
	v_mfma_f32_16x16x128_f8f6f4 v[124:127], v[0:7], v[238:245], v[124:127]
	v_mfma_f32_16x16x128_f8f6f4 v[120:123], v[8:15], v[238:245], v[120:123]
	v_mfma_f32_16x16x128_f8f6f4 v[108:111], v[0:7], v[246:253], v[108:111]
	v_mfma_f32_16x16x128_f8f6f4 v[104:107], v[8:15], v[246:253], v[104:107]
	s_setprio 1
	s_setprio 0
	v_mfma_f32_16x16x128_f8f6f4 v[148:151], v[16:23], v[222:229], v[148:151]
	v_mfma_f32_16x16x128_f8f6f4 v[144:147], v[24:31], v[222:229], v[144:147]
	v_mfma_f32_16x16x128_f8f6f4 v[132:135], v[16:23], v[230:237], v[132:135]
	v_mfma_f32_16x16x128_f8f6f4 v[128:131], v[24:31], v[230:237], v[128:131]
	v_mfma_f32_16x16x128_f8f6f4 v[116:119], v[16:23], v[238:245], v[116:119]
	v_mfma_f32_16x16x128_f8f6f4 v[112:115], v[24:31], v[238:245], v[112:115]
	v_mfma_f32_16x16x128_f8f6f4 v[100:103], v[16:23], v[246:253], v[100:103]
	v_mfma_f32_16x16x128_f8f6f4 v[96:99], v[24:31], v[246:253], v[96:99]
	s_setprio 1
	s_barrier
	s_mov_b32 m0, s47
	v_lshl_add_u64 v[186:187], v[186:187], 0, s[16:17]
	ds_read_b128 v[222:225], v212 offset:49152
	ds_read_b128 v[226:229], v212 offset:50176
	ds_read_b128 v[230:233], v212 offset:51200
	ds_read_b128 v[234:237], v212 offset:52224
	ds_read_b128 v[238:241], v212 offset:53248
	ds_read_b128 v[242:245], v212 offset:54272
	ds_read_b128 v[246:249], v212 offset:55296
	ds_read_b128 v[250:253], v212 offset:56320
	global_load_lds_dwordx4 v[186:187], off
	v_lshl_add_u64 v[186:187], v[188:189], 0, s[16:17]
	s_mov_b32 m0, s48
	v_lshl_add_u64 v[182:183], v[182:183], 0, s[34:35]
	global_load_lds_dwordx4 v[186:187], off
	v_lshl_add_u64 v[186:187], v[182:183], 0, v[164:165]
	s_mov_b32 m0, s51
	v_lshl_add_u64 v[182:183], v[182:183], 0, v[162:163]
	global_load_lds_dwordx4 v[186:187], off
	s_mov_b32 m0, s52
	s_nop 0
	global_load_lds_dwordx4 v[182:183], off
	v_lshl_add_u64 v[182:183], v[190:191], 0, s[16:17]
	s_mov_b32 m0, s49
	s_nop 0
	global_load_lds_dwordx4 v[182:183], off
	v_lshl_add_u64 v[182:183], v[184:185], 0, s[16:17]
	s_mov_b32 m0, s50
	s_nop 0
	global_load_lds_dwordx4 v[182:183], off
	s_waitcnt vmcnt(8)
	s_waitcnt lgkmcnt(0)
	s_barrier
	s_setprio 0
	s_waitcnt lgkmcnt(0)
	v_mfma_f32_16x16x128_f8f6f4 v[84:87], v[0:7], v[222:229], v[84:87]
	v_mfma_f32_16x16x128_f8f6f4 v[80:83], v[8:15], v[222:229], v[80:83]
	v_mfma_f32_16x16x128_f8f6f4 v[68:71], v[0:7], v[230:237], v[68:71]
	v_mfma_f32_16x16x128_f8f6f4 v[64:67], v[8:15], v[230:237], v[64:67]
	v_mfma_f32_16x16x128_f8f6f4 v[52:55], v[0:7], v[238:245], v[52:55]
	v_mfma_f32_16x16x128_f8f6f4 v[48:51], v[8:15], v[238:245], v[48:51]
	v_mfma_f32_16x16x128_f8f6f4 v[36:39], v[0:7], v[246:253], v[36:39]
	v_mfma_f32_16x16x128_f8f6f4 v[32:35], v[8:15], v[246:253], v[32:35]
	s_setprio 1
	s_setprio 0
	v_mfma_f32_16x16x128_f8f6f4 v[92:95], v[16:23], v[222:229], v[92:95]
	v_mfma_f32_16x16x128_f8f6f4 v[88:91], v[24:31], v[222:229], v[88:91]
	v_mfma_f32_16x16x128_f8f6f4 v[76:79], v[16:23], v[230:237], v[76:79]
	v_mfma_f32_16x16x128_f8f6f4 v[72:75], v[24:31], v[230:237], v[72:75]
	v_mfma_f32_16x16x128_f8f6f4 v[60:63], v[16:23], v[238:245], v[60:63]
	v_mfma_f32_16x16x128_f8f6f4 v[56:59], v[24:31], v[238:245], v[56:59]
	v_mfma_f32_16x16x128_f8f6f4 v[44:47], v[16:23], v[246:253], v[44:47]
	v_mfma_f32_16x16x128_f8f6f4 v[40:43], v[24:31], v[246:253], v[40:43]
	s_setprio 1
	s_barrier
	s_add_i32 s41, s41, 2
	s_add_u32 s4, s4, 0x100
	s_addc_u32 s5, s5, 0
	s_cmp_gt_u32 s41, 5
	s_cbranch_scc0 .LBB0_1692
	s_nop 15
	s_nop 7
	s_and_b64 vcc, exec, s[36:37]
	s_cbranch_vccz .LBB0_1695
	s_barrier

.LBB0_1709:
	s_add_u32 s48, s36, s42
	s_addc_u32 s49, s37, s43
	s_add_u32 s46, s48, 0x100
	s_addc_u32 s47, s49, 0
	s_and_b64 s[44:45], s[40:41], exec
	s_cselect_b32 s45, s13, s47
	s_cselect_b32 s44, s61, s46
	s_add_u32 s42, s34, s42
	s_addc_u32 s43, s35, s43
	s_add_u32 s42, s42, 0x100
	s_addc_u32 s43, s43, 0
	s_and_b64 s[40:41], s[40:41], exec
	s_cselect_b32 s47, s15, s43
	s_cselect_b32 s46, s62, s42
	s_add_u32 s50, s48, 0x10080
	ds_read_b128 v[146:149], v143
	ds_read_b128 v[150:153], v143 offset:1024
	ds_read_b128 v[154:157], v143 offset:2048
	ds_read_b128 v[158:161], v143 offset:3072
	ds_read_b128 v[162:165], v144
	ds_read_b128 v[166:169], v144 offset:1024
	ds_read_b128 v[170:173], v144 offset:2048
	ds_read_b128 v[174:177], v144 offset:3072
	s_addc_u32 s51, s49, 0
	s_add_i32 s72, s0, s33
	s_add_i32 m0, s52, 0xc000
	s_add_i32 s73, s52, 0xe000
	s_add_i32 s69, s72, 0x2000
	s_add_u32 s48, s46, 0x10000
	s_addc_u32 s49, s47, 0
	s_add_i32 s71, s58, s33
	s_add_i32 s70, s71, 0x2000
	s_add_i32 s68, 0, 0x18000
	s_add_i32 s67, 0, 0x1c000
	s_add_u32 s42, s44, 0x10000
	s_addc_u32 s43, s45, 0
	s_add_i32 s66, s68, s33
	s_add_i32 s64, s66, 0x2000
	s_add_u32 s40, s46, 0x10080
	s_addc_u32 s41, s47, 0
	s_add_i32 s65, s67, s33
	s_add_i32 s63, s65, 0x2000
	v_lshl_add_u64 v[138:139], s[50:51], 0, v[132:133]
	ds_read_b128 v[178:181], v145
	ds_read_b128 v[182:185], v145 offset:1024
	ds_read_b128 v[186:189], v145 offset:2048
	ds_read_b128 v[190:193], v145 offset:3072
	ds_read_b128 v[194:197], v145 offset:4096
	ds_read_b128 v[198:201], v145 offset:5120
	ds_read_b128 v[202:205], v145 offset:6144
	ds_read_b128 v[206:209], v145 offset:7168
	global_load_lds_dwordx4 v[138:139], off
	v_lshl_add_u64 v[138:139], s[50:51], 0, v[134:135]
	s_mov_b32 m0, s73
	s_nop 0
	global_load_lds_dwordx4 v[138:139], off
	s_waitcnt vmcnt(8)
	s_waitcnt lgkmcnt(0)
	s_barrier
	s_setprio 0
	s_waitcnt lgkmcnt(0)
	v_mfma_f32_16x16x32_bf16 v[124:127], v[146:149], v[178:181], v[124:127]
	v_mfma_f32_16x16x32_bf16 v[120:123], v[154:157], v[178:181], v[120:123]
	v_mfma_f32_16x16x32_bf16 v[116:119], v[146:149], v[186:189], v[116:119]
	v_mfma_f32_16x16x32_bf16 v[108:111], v[154:157], v[186:189], v[108:111]
	v_mfma_f32_16x16x32_bf16 v[100:103], v[146:149], v[194:197], v[100:103]
	v_mfma_f32_16x16x32_bf16 v[92:95], v[154:157], v[194:197], v[92:95]
	v_mfma_f32_16x16x32_bf16 v[84:87], v[146:149], v[202:205], v[84:87]
	v_mfma_f32_16x16x32_bf16 v[76:79], v[154:157], v[202:205], v[76:79]
	v_mfma_f32_16x16x32_bf16 v[124:127], v[150:153], v[182:185], v[124:127]
	v_mfma_f32_16x16x32_bf16 v[120:123], v[158:161], v[182:185], v[120:123]
	v_mfma_f32_16x16x32_bf16 v[116:119], v[150:153], v[190:193], v[116:119]
	v_mfma_f32_16x16x32_bf16 v[108:111], v[158:161], v[190:193], v[108:111]
	v_mfma_f32_16x16x32_bf16 v[100:103], v[150:153], v[198:201], v[100:103]
	v_mfma_f32_16x16x32_bf16 v[92:95], v[158:161], v[198:201], v[92:95]
	v_mfma_f32_16x16x32_bf16 v[84:87], v[150:153], v[206:209], v[84:87]
	v_mfma_f32_16x16x32_bf16 v[76:79], v[158:161], v[206:209], v[76:79]
	s_setprio 1
	s_setprio 0
	v_mfma_f32_16x16x32_bf16 v[112:115], v[162:165], v[178:181], v[112:115]
	v_mfma_f32_16x16x32_bf16 v[104:107], v[170:173], v[178:181], v[104:107]
	v_mfma_f32_16x16x32_bf16 v[96:99], v[162:165], v[186:189], v[96:99]
	v_mfma_f32_16x16x32_bf16 v[88:91], v[170:173], v[186:189], v[88:91]
	v_mfma_f32_16x16x32_bf16 v[80:83], v[162:165], v[194:197], v[80:83]
	v_mfma_f32_16x16x32_bf16 v[72:75], v[170:173], v[194:197], v[72:75]
	v_mfma_f32_16x16x32_bf16 v[52:55], v[162:165], v[202:205], v[52:55]
	v_mfma_f32_16x16x32_bf16 v[48:51], v[170:173], v[202:205], v[48:51]
	v_mfma_f32_16x16x32_bf16 v[112:115], v[166:169], v[182:185], v[112:115]
	v_mfma_f32_16x16x32_bf16 v[104:107], v[174:177], v[182:185], v[104:107]
	v_mfma_f32_16x16x32_bf16 v[96:99], v[166:169], v[190:193], v[96:99]
	v_mfma_f32_16x16x32_bf16 v[88:91], v[174:177], v[190:193], v[88:91]
	v_mfma_f32_16x16x32_bf16 v[80:83], v[166:169], v[198:201], v[80:83]
	v_mfma_f32_16x16x32_bf16 v[72:75], v[174:177], v[198:201], v[72:75]
	v_mfma_f32_16x16x32_bf16 v[52:55], v[166:169], v[206:209], v[52:55]
	v_mfma_f32_16x16x32_bf16 v[48:51], v[174:177], v[206:209], v[48:51]
	s_setprio 1
	s_barrier
	s_mov_b32 m0, s72
	v_lshl_add_u64 v[138:139], s[46:47], 0, v[130:131]
	ds_read_b128 v[178:181], v145 offset:16384
	ds_read_b128 v[182:185], v145 offset:17408
	ds_read_b128 v[186:189], v145 offset:18432
	ds_read_b128 v[190:193], v145 offset:19456
	ds_read_b128 v[194:197], v145 offset:20480
	ds_read_b128 v[198:201], v145 offset:21504
	ds_read_b128 v[202:205], v145 offset:22528
	ds_read_b128 v[206:209], v145 offset:23552
	global_load_lds_dwordx4 v[138:139], off
	v_lshl_add_u64 v[210:211], s[46:47], 0, v[128:129]
	s_mov_b32 m0, s69
	v_lshl_add_u64 v[212:213], s[48:49], 0, v[130:131]
	global_load_lds_dwordx4 v[210:211], off
	s_mov_b32 m0, s71
	v_lshl_add_u64 v[214:215], s[44:45], 0, v[134:135]
	global_load_lds_dwordx4 v[212:213], off
	v_lshl_add_u64 v[212:213], s[48:49], 0, v[128:129]
	s_mov_b32 m0, s70
	s_nop 0
	global_load_lds_dwordx4 v[212:213], off
	v_lshl_add_u64 v[212:213], s[44:45], 0, v[132:133]
	s_mov_b32 m0, s52
	s_nop 0
	global_load_lds_dwordx4 v[212:213], off
	s_mov_b32 m0, s53
	s_nop 0
	global_load_lds_dwordx4 v[214:215], off
	s_waitcnt vmcnt(8)
	s_waitcnt lgkmcnt(0)
	s_barrier
	s_setprio 0
	s_waitcnt lgkmcnt(0)
	v_mfma_f32_16x16x32_bf16 v[44:47], v[146:149], v[178:181], v[44:47]
	v_mfma_f32_16x16x32_bf16 v[32:35], v[154:157], v[178:181], v[32:35]
	v_mfma_f32_16x16x32_bf16 v[4:7], v[146:149], v[186:189], v[4:7]
	v_mfma_f32_16x16x32_bf16 v[0:3], v[154:157], v[186:189], v[0:3]
	v_mfma_f32_16x16x32_bf16 v[28:31], v[146:149], v[194:197], v[28:31]
	v_mfma_f32_16x16x32_bf16 v[24:27], v[154:157], v[194:197], v[24:27]
	v_mfma_f32_16x16x32_bf16 v[12:15], v[146:149], v[202:205], v[12:15]
	v_mfma_f32_16x16x32_bf16 v[8:11], v[154:157], v[202:205], v[8:11]
	v_mfma_f32_16x16x32_bf16 v[44:47], v[150:153], v[182:185], v[44:47]
	v_mfma_f32_16x16x32_bf16 v[32:35], v[158:161], v[182:185], v[32:35]
	v_mfma_f32_16x16x32_bf16 v[4:7], v[150:153], v[190:193], v[4:7]
	v_mfma_f32_16x16x32_bf16 v[0:3], v[158:161], v[190:193], v[0:3]
	v_mfma_f32_16x16x32_bf16 v[28:31], v[150:153], v[198:201], v[28:31]
	v_mfma_f32_16x16x32_bf16 v[24:27], v[158:161], v[198:201], v[24:27]
	v_mfma_f32_16x16x32_bf16 v[12:15], v[150:153], v[206:209], v[12:15]
	v_mfma_f32_16x16x32_bf16 v[8:11], v[158:161], v[206:209], v[8:11]
	s_setprio 1
	s_setprio 0
	v_mfma_f32_16x16x32_bf16 v[68:71], v[162:165], v[178:181], v[68:71]
	v_mfma_f32_16x16x32_bf16 v[64:67], v[170:173], v[178:181], v[64:67]
	v_mfma_f32_16x16x32_bf16 v[60:63], v[162:165], v[186:189], v[60:63]
	v_mfma_f32_16x16x32_bf16 v[56:59], v[170:173], v[186:189], v[56:59]
	v_mfma_f32_16x16x32_bf16 v[40:43], v[162:165], v[194:197], v[40:43]
	v_mfma_f32_16x16x32_bf16 v[36:39], v[170:173], v[194:197], v[36:39]
	v_mfma_f32_16x16x32_bf16 v[20:23], v[162:165], v[202:205], v[20:23]
	v_mfma_f32_16x16x32_bf16 v[16:19], v[170:173], v[202:205], v[16:19]
	v_mfma_f32_16x16x32_bf16 v[68:71], v[166:169], v[182:185], v[68:71]
	v_mfma_f32_16x16x32_bf16 v[64:67], v[174:177], v[182:185], v[64:67]
	v_mfma_f32_16x16x32_bf16 v[60:63], v[166:169], v[190:193], v[60:63]
	v_mfma_f32_16x16x32_bf16 v[56:59], v[174:177], v[190:193], v[56:59]
	v_mfma_f32_16x16x32_bf16 v[40:43], v[166:169], v[198:201], v[40:43]
	v_mfma_f32_16x16x32_bf16 v[36:39], v[174:177], v[198:201], v[36:39]
	v_mfma_f32_16x16x32_bf16 v[20:23], v[166:169], v[206:209], v[20:23]
	v_mfma_f32_16x16x32_bf16 v[16:19], v[174:177], v[206:209], v[16:19]
	s_setprio 1
	s_barrier
	v_add_u32_e32 v158, s68, v141
	v_add_u32_e32 v174, s67, v141
	ds_read_b128 v[146:149], v158
	ds_read_b128 v[150:153], v158 offset:1024
	ds_read_b128 v[154:157], v158 offset:2048
	ds_read_b128 v[158:161], v158 offset:3072
	ds_read_b128 v[162:165], v174
	ds_read_b128 v[166:169], v174 offset:1024
	ds_read_b128 v[170:173], v174 offset:2048
	ds_read_b128 v[174:177], v174 offset:3072
	s_mov_b32 m0, s54
	v_lshl_add_u64 v[216:217], s[42:43], 0, v[132:133]
	ds_read_b128 v[178:181], v145 offset:32768
	ds_read_b128 v[182:185], v145 offset:33792
	ds_read_b128 v[186:189], v145 offset:34816
	ds_read_b128 v[190:193], v145 offset:35840
	ds_read_b128 v[194:197], v145 offset:36864
	ds_read_b128 v[198:201], v145 offset:37888
	ds_read_b128 v[202:205], v145 offset:38912
	ds_read_b128 v[206:209], v145 offset:39936
	global_load_lds_dwordx4 v[216:217], off
	v_lshl_add_u64 v[216:217], s[42:43], 0, v[134:135]
	s_mov_b32 m0, s55
	s_nop 0
	global_load_lds_dwordx4 v[216:217], off
	s_waitcnt vmcnt(8)
	s_waitcnt lgkmcnt(0)
	s_barrier
	s_setprio 0
	s_waitcnt lgkmcnt(0)
	v_mfma_f32_16x16x32_bf16 v[124:127], v[146:149], v[178:181], v[124:127]
	v_mfma_f32_16x16x32_bf16 v[120:123], v[154:157], v[178:181], v[120:123]
	v_mfma_f32_16x16x32_bf16 v[116:119], v[146:149], v[186:189], v[116:119]
	v_mfma_f32_16x16x32_bf16 v[108:111], v[154:157], v[186:189], v[108:111]
	v_mfma_f32_16x16x32_bf16 v[100:103], v[146:149], v[194:197], v[100:103]
	v_mfma_f32_16x16x32_bf16 v[92:95], v[154:157], v[194:197], v[92:95]
	v_mfma_f32_16x16x32_bf16 v[84:87], v[146:149], v[202:205], v[84:87]
	v_mfma_f32_16x16x32_bf16 v[76:79], v[154:157], v[202:205], v[76:79]
	v_mfma_f32_16x16x32_bf16 v[124:127], v[150:153], v[182:185], v[124:127]
	v_mfma_f32_16x16x32_bf16 v[120:123], v[158:161], v[182:185], v[120:123]
	v_mfma_f32_16x16x32_bf16 v[116:119], v[150:153], v[190:193], v[116:119]
	v_mfma_f32_16x16x32_bf16 v[108:111], v[158:161], v[190:193], v[108:111]
	v_mfma_f32_16x16x32_bf16 v[100:103], v[150:153], v[198:201], v[100:103]
	v_mfma_f32_16x16x32_bf16 v[92:95], v[158:161], v[198:201], v[92:95]
	v_mfma_f32_16x16x32_bf16 v[84:87], v[150:153], v[206:209], v[84:87]
	v_mfma_f32_16x16x32_bf16 v[76:79], v[158:161], v[206:209], v[76:79]
	s_setprio 1
	s_setprio 0
	v_mfma_f32_16x16x32_bf16 v[112:115], v[162:165], v[178:181], v[112:115]
	v_mfma_f32_16x16x32_bf16 v[104:107], v[170:173], v[178:181], v[104:107]
	v_mfma_f32_16x16x32_bf16 v[96:99], v[162:165], v[186:189], v[96:99]
	v_mfma_f32_16x16x32_bf16 v[88:91], v[170:173], v[186:189], v[88:91]
	v_mfma_f32_16x16x32_bf16 v[80:83], v[162:165], v[194:197], v[80:83]
	v_mfma_f32_16x16x32_bf16 v[72:75], v[170:173], v[194:197], v[72:75]
	v_mfma_f32_16x16x32_bf16 v[52:55], v[162:165], v[202:205], v[52:55]
	v_mfma_f32_16x16x32_bf16 v[48:51], v[170:173], v[202:205], v[48:51]
	v_mfma_f32_16x16x32_bf16 v[112:115], v[166:169], v[182:185], v[112:115]
	v_mfma_f32_16x16x32_bf16 v[104:107], v[174:177], v[182:185], v[104:107]
	v_mfma_f32_16x16x32_bf16 v[96:99], v[166:169], v[190:193], v[96:99]
	v_mfma_f32_16x16x32_bf16 v[88:91], v[174:177], v[190:193], v[88:91]
	v_mfma_f32_16x16x32_bf16 v[80:83], v[166:169], v[198:201], v[80:83]
	v_mfma_f32_16x16x32_bf16 v[72:75], v[174:177], v[198:201], v[72:75]
	v_mfma_f32_16x16x32_bf16 v[52:55], v[166:169], v[206:209], v[52:55]
	v_mfma_f32_16x16x32_bf16 v[48:51], v[174:177], v[206:209], v[48:51]
	s_setprio 1
	s_barrier
	s_mov_b32 m0, s66
	v_lshl_add_u64 v[138:139], v[138:139], 0, s[8:9]
	ds_read_b128 v[178:181], v145 offset:49152
	ds_read_b128 v[182:185], v145 offset:50176
	ds_read_b128 v[186:189], v145 offset:51200
	ds_read_b128 v[190:193], v145 offset:52224
	ds_read_b128 v[194:197], v145 offset:53248
	ds_read_b128 v[198:201], v145 offset:54272
	ds_read_b128 v[202:205], v145 offset:55296
	ds_read_b128 v[206:209], v145 offset:56320
	global_load_lds_dwordx4 v[138:139], off
	v_lshl_add_u64 v[138:139], v[210:211], 0, s[8:9]
	s_mov_b32 m0, s64
	s_nop 0
	global_load_lds_dwordx4 v[138:139], off
	v_lshl_add_u64 v[138:139], s[40:41], 0, v[130:131]
	s_mov_b32 m0, s65
	s_nop 0
	global_load_lds_dwordx4 v[138:139], off
	v_lshl_add_u64 v[138:139], s[40:41], 0, v[128:129]
	s_mov_b32 m0, s63
	s_nop 0
	global_load_lds_dwordx4 v[138:139], off
	v_lshl_add_u64 v[138:139], v[212:213], 0, s[8:9]
	s_mov_b32 m0, s56
	s_nop 0
	global_load_lds_dwordx4 v[138:139], off
	v_lshl_add_u64 v[138:139], v[214:215], 0, s[8:9]
	s_mov_b32 m0, s57
	s_nop 0
	global_load_lds_dwordx4 v[138:139], off
	s_waitcnt vmcnt(8)
	s_waitcnt lgkmcnt(0)
	s_barrier
	s_setprio 0
	s_waitcnt lgkmcnt(0)
	v_mfma_f32_16x16x32_bf16 v[44:47], v[146:149], v[178:181], v[44:47]
	v_mfma_f32_16x16x32_bf16 v[32:35], v[154:157], v[178:181], v[32:35]
	v_mfma_f32_16x16x32_bf16 v[4:7], v[146:149], v[186:189], v[4:7]
	v_mfma_f32_16x16x32_bf16 v[0:3], v[154:157], v[186:189], v[0:3]
	v_mfma_f32_16x16x32_bf16 v[28:31], v[146:149], v[194:197], v[28:31]
	v_mfma_f32_16x16x32_bf16 v[24:27], v[154:157], v[194:197], v[24:27]
	v_mfma_f32_16x16x32_bf16 v[12:15], v[146:149], v[202:205], v[12:15]
	v_mfma_f32_16x16x32_bf16 v[8:11], v[154:157], v[202:205], v[8:11]
	v_mfma_f32_16x16x32_bf16 v[44:47], v[150:153], v[182:185], v[44:47]
	v_mfma_f32_16x16x32_bf16 v[32:35], v[158:161], v[182:185], v[32:35]
	v_mfma_f32_16x16x32_bf16 v[4:7], v[150:153], v[190:193], v[4:7]
	v_mfma_f32_16x16x32_bf16 v[0:3], v[158:161], v[190:193], v[0:3]
	v_mfma_f32_16x16x32_bf16 v[28:31], v[150:153], v[198:201], v[28:31]
	v_mfma_f32_16x16x32_bf16 v[24:27], v[158:161], v[198:201], v[24:27]
	v_mfma_f32_16x16x32_bf16 v[12:15], v[150:153], v[206:209], v[12:15]
	v_mfma_f32_16x16x32_bf16 v[8:11], v[158:161], v[206:209], v[8:11]
	s_setprio 1
	s_setprio 0
	v_mfma_f32_16x16x32_bf16 v[68:71], v[162:165], v[178:181], v[68:71]
	v_mfma_f32_16x16x32_bf16 v[64:67], v[170:173], v[178:181], v[64:67]
	v_mfma_f32_16x16x32_bf16 v[60:63], v[162:165], v[186:189], v[60:63]
	v_mfma_f32_16x16x32_bf16 v[56:59], v[170:173], v[186:189], v[56:59]
	v_mfma_f32_16x16x32_bf16 v[40:43], v[162:165], v[194:197], v[40:43]
	v_mfma_f32_16x16x32_bf16 v[36:39], v[170:173], v[194:197], v[36:39]
	v_mfma_f32_16x16x32_bf16 v[20:23], v[162:165], v[202:205], v[20:23]
	v_mfma_f32_16x16x32_bf16 v[16:19], v[170:173], v[202:205], v[16:19]
	v_mfma_f32_16x16x32_bf16 v[68:71], v[166:169], v[182:185], v[68:71]
	v_mfma_f32_16x16x32_bf16 v[64:67], v[174:177], v[182:185], v[64:67]
	v_mfma_f32_16x16x32_bf16 v[60:63], v[166:169], v[190:193], v[60:63]
	v_mfma_f32_16x16x32_bf16 v[56:59], v[174:177], v[190:193], v[56:59]
	v_mfma_f32_16x16x32_bf16 v[40:43], v[166:169], v[198:201], v[40:43]
	v_mfma_f32_16x16x32_bf16 v[36:39], v[174:177], v[198:201], v[36:39]
	v_mfma_f32_16x16x32_bf16 v[20:23], v[166:169], v[206:209], v[20:23]
	v_mfma_f32_16x16x32_bf16 v[16:19], v[174:177], v[206:209], v[16:19]
	s_setprio 1
	s_barrier
	s_andn2_b64 vcc, exec, s[38:39]
	s_mov_b64 s[40:41], -1
	s_mov_b64 s[38:39], 0
	s_mov_b64 s[42:43], 0x100
	s_cbranch_vccz .LBB0_1709
	s_and_b64 vcc, exec, s[10:11]
	s_cbranch_vccz .LBB0_1712
	s_barrier

.LBB0_1790:
	v_lshl_add_u64 v[0:1], v[168:169], 0, s[42:43]
	v_lshl_add_u64 v[0:1], v[0:1], 0, s[94:95]
	v_cndmask_b32_e64 v179, v1, v171, s[40:41]
	v_cndmask_b32_e64 v178, v0, v205, s[40:41]
	ds_read_b128 v[8:11], v185
	ds_read_b128 v[12:15], v189
	ds_read_b128 v[24:27], v190
	ds_read_b128 v[28:31], v191
	ds_read_b128 v[0:3], v186
	ds_read_b128 v[4:7], v192
	ds_read_b128 v[16:19], v193
	ds_read_b128 v[20:23], v194
	s_add_u32 s15, s30, s42
	s_addc_u32 s93, s31, s43
	s_add_u32 vcc_lo, s15, 0x100
	s_addc_u32 vcc_hi, s93, 0
	s_and_b64 s[44:45], s[40:41], exec
	s_cselect_b32 s45, s35, vcc_hi
	s_cselect_b32 s44, s92, vcc_lo
	s_add_u32 s42, s15, 0x10080
	s_addc_u32 s43, s93, 0
	s_add_i32 m0, s22, 0xc000
	s_add_i32 s15, s22, 0xe000
	s_add_u32 s40, s44, 0x10000
	s_addc_u32 s41, s45, 0
	v_lshl_add_u64 v[180:181], v[178:179], 0, s[0:1]
	v_lshl_add_u64 v[174:175], v[178:179], 0, s[10:11]
	v_lshl_add_u64 v[176:177], s[42:43], 0, v[164:165]
	ds_read_b128 v[206:209], v203
	ds_read_b128 v[210:213], v203 offset:1024
	ds_read_b128 v[214:217], v203 offset:2048
	ds_read_b128 v[218:221], v203 offset:3072
	ds_read_b128 v[222:225], v203 offset:4096
	ds_read_b128 v[226:229], v203 offset:5120
	ds_read_b128 v[230:233], v203 offset:6144
	ds_read_b128 v[234:237], v203 offset:7168
	global_load_lds_dwordx4 v[176:177], off
	v_lshl_add_u64 v[176:177], s[42:43], 0, v[166:167]
	s_mov_b32 m0, s15
	s_nop 0
	global_load_lds_dwordx4 v[176:177], off
	s_waitcnt vmcnt(8)
	s_waitcnt lgkmcnt(0)
	s_barrier
	s_setprio 0
	s_waitcnt lgkmcnt(0)
	v_mfma_f32_16x16x128_f8f6f4 v[156:159], v[8:15], v[206:213], v[156:159]
	v_mfma_f32_16x16x128_f8f6f4 v[152:155], v[24:31], v[206:213], v[152:155]
	v_mfma_f32_16x16x128_f8f6f4 v[140:143], v[8:15], v[214:221], v[140:143]
	v_mfma_f32_16x16x128_f8f6f4 v[136:139], v[24:31], v[214:221], v[136:139]
	v_mfma_f32_16x16x128_f8f6f4 v[124:127], v[8:15], v[222:229], v[124:127]
	v_mfma_f32_16x16x128_f8f6f4 v[120:123], v[24:31], v[222:229], v[120:123]
	v_mfma_f32_16x16x128_f8f6f4 v[108:111], v[8:15], v[230:237], v[108:111]
	v_mfma_f32_16x16x128_f8f6f4 v[104:107], v[24:31], v[230:237], v[104:107]
	s_setprio 1
	s_setprio 0
	v_mfma_f32_16x16x128_f8f6f4 v[148:151], v[0:7], v[206:213], v[148:151]
	v_mfma_f32_16x16x128_f8f6f4 v[144:147], v[16:23], v[206:213], v[144:147]
	v_mfma_f32_16x16x128_f8f6f4 v[132:135], v[0:7], v[214:221], v[132:135]
	v_mfma_f32_16x16x128_f8f6f4 v[128:131], v[16:23], v[214:221], v[128:131]
	v_mfma_f32_16x16x128_f8f6f4 v[116:119], v[0:7], v[222:229], v[116:119]
	v_mfma_f32_16x16x128_f8f6f4 v[112:115], v[16:23], v[222:229], v[112:115]
	v_mfma_f32_16x16x128_f8f6f4 v[96:99], v[0:7], v[230:237], v[96:99]
	v_mfma_f32_16x16x128_f8f6f4 v[88:91], v[16:23], v[230:237], v[88:91]
	s_setprio 1
	s_barrier
	s_mov_b32 m0, s23
	v_lshl_add_u64 v[176:177], v[178:179], 0, v[162:163]
	ds_read_b128 v[206:209], v203 offset:16384
	ds_read_b128 v[210:213], v203 offset:17408
	ds_read_b128 v[214:217], v203 offset:18432
	ds_read_b128 v[218:221], v203 offset:19456
	ds_read_b128 v[222:225], v203 offset:20480
	ds_read_b128 v[226:229], v203 offset:21504
	ds_read_b128 v[230:233], v203 offset:22528
	ds_read_b128 v[234:237], v203 offset:23552
	global_load_lds_dwordx4 v[176:177], off
	v_lshl_add_u64 v[178:179], v[178:179], 0, v[160:161]
	s_mov_b32 m0, s33
	v_lshl_add_u64 v[182:183], v[180:181], 0, v[162:163]
	global_load_lds_dwordx4 v[178:179], off
	s_mov_b32 m0, s46
	v_lshl_add_u64 v[180:181], v[180:181], 0, v[160:161]
	global_load_lds_dwordx4 v[182:183], off
	s_mov_b32 m0, s47
	v_lshl_add_u64 v[182:183], s[44:45], 0, v[166:167]
	global_load_lds_dwordx4 v[180:181], off
	v_lshl_add_u64 v[180:181], s[44:45], 0, v[164:165]
	s_mov_b32 m0, s22
	s_nop 0
	global_load_lds_dwordx4 v[180:181], off
	s_mov_b32 m0, s48
	s_nop 0
	global_load_lds_dwordx4 v[182:183], off
	s_waitcnt vmcnt(8)
	s_waitcnt lgkmcnt(0)
	s_barrier
	s_setprio 0
	s_waitcnt lgkmcnt(0)
	v_mfma_f32_16x16x128_f8f6f4 v[84:87], v[8:15], v[206:213], v[84:87]
	v_mfma_f32_16x16x128_f8f6f4 v[76:79], v[24:31], v[206:213], v[76:79]
	v_mfma_f32_16x16x128_f8f6f4 v[60:63], v[8:15], v[214:221], v[60:63]
	v_mfma_f32_16x16x128_f8f6f4 v[48:51], v[24:31], v[214:221], v[48:51]
	v_mfma_f32_16x16x128_f8f6f4 v[68:71], v[8:15], v[222:229], v[68:71]
	v_mfma_f32_16x16x128_f8f6f4 v[56:59], v[24:31], v[222:229], v[56:59]
	v_mfma_f32_16x16x128_f8f6f4 v[44:47], v[8:15], v[230:237], v[44:47]
	v_mfma_f32_16x16x128_f8f6f4 v[36:39], v[24:31], v[230:237], v[36:39]
	s_setprio 1
	s_setprio 0
	v_mfma_f32_16x16x128_f8f6f4 v[100:103], v[0:7], v[206:213], v[100:103]
	v_mfma_f32_16x16x128_f8f6f4 v[92:95], v[16:23], v[206:213], v[92:95]
	v_mfma_f32_16x16x128_f8f6f4 v[80:83], v[0:7], v[214:221], v[80:83]
	v_mfma_f32_16x16x128_f8f6f4 v[72:75], v[16:23], v[214:221], v[72:75]
	v_mfma_f32_16x16x128_f8f6f4 v[64:67], v[0:7], v[222:229], v[64:67]
	v_mfma_f32_16x16x128_f8f6f4 v[52:55], v[16:23], v[222:229], v[52:55]
	v_mfma_f32_16x16x128_f8f6f4 v[40:43], v[0:7], v[230:237], v[40:43]
	v_mfma_f32_16x16x128_f8f6f4 v[32:35], v[16:23], v[230:237], v[32:35]
	s_setprio 1
	s_barrier
	ds_read_b128 v[4:7], v195
	ds_read_b128 v[8:11], v196
	ds_read_b128 v[0:3], v187
	ds_read_b128 v[16:19], v188
	ds_read_b128 v[12:15], v197
	ds_read_b128 v[20:23], v198
	ds_read_b128 v[24:27], v199
	ds_read_b128 v[28:31], v200
	s_mov_b32 m0, s49
	v_lshl_add_u64 v[238:239], s[40:41], 0, v[164:165]
	ds_read_b128 v[206:209], v203 offset:32768
	ds_read_b128 v[210:213], v203 offset:33792
	ds_read_b128 v[214:217], v203 offset:34816
	ds_read_b128 v[218:221], v203 offset:35840
	ds_read_b128 v[222:225], v203 offset:36864
	ds_read_b128 v[226:229], v203 offset:37888
	ds_read_b128 v[230:233], v203 offset:38912
	ds_read_b128 v[234:237], v203 offset:39936
	global_load_lds_dwordx4 v[238:239], off
	v_lshl_add_u64 v[238:239], s[40:41], 0, v[166:167]
	s_mov_b32 m0, s50
	s_nop 0
	global_load_lds_dwordx4 v[238:239], off
	s_waitcnt vmcnt(8)
	s_waitcnt lgkmcnt(0)
	s_barrier
	s_setprio 0
	s_waitcnt lgkmcnt(0)
	v_mfma_f32_16x16x128_f8f6f4 v[156:159], v[0:7], v[206:213], v[156:159]
	v_mfma_f32_16x16x128_f8f6f4 v[152:155], v[8:15], v[206:213], v[152:155]
	v_mfma_f32_16x16x128_f8f6f4 v[140:143], v[0:7], v[214:221], v[140:143]
	v_mfma_f32_16x16x128_f8f6f4 v[136:139], v[8:15], v[214:221], v[136:139]
	v_mfma_f32_16x16x128_f8f6f4 v[124:127], v[0:7], v[222:229], v[124:127]
	v_mfma_f32_16x16x128_f8f6f4 v[120:123], v[8:15], v[222:229], v[120:123]
	v_mfma_f32_16x16x128_f8f6f4 v[108:111], v[0:7], v[230:237], v[108:111]
	v_mfma_f32_16x16x128_f8f6f4 v[104:107], v[8:15], v[230:237], v[104:107]
	s_setprio 1
	s_setprio 0
	v_mfma_f32_16x16x128_f8f6f4 v[148:151], v[16:23], v[206:213], v[148:151]
	v_mfma_f32_16x16x128_f8f6f4 v[144:147], v[24:31], v[206:213], v[144:147]
	v_mfma_f32_16x16x128_f8f6f4 v[132:135], v[16:23], v[214:221], v[132:135]
	v_mfma_f32_16x16x128_f8f6f4 v[128:131], v[24:31], v[214:221], v[128:131]
	v_mfma_f32_16x16x128_f8f6f4 v[116:119], v[16:23], v[222:229], v[116:119]
	v_mfma_f32_16x16x128_f8f6f4 v[112:115], v[24:31], v[222:229], v[112:115]
	v_mfma_f32_16x16x128_f8f6f4 v[96:99], v[16:23], v[230:237], v[96:99]
	v_mfma_f32_16x16x128_f8f6f4 v[88:91], v[24:31], v[230:237], v[88:91]
	s_setprio 1
	s_barrier
	s_mov_b32 m0, s52
	v_lshl_add_u64 v[176:177], v[176:177], 0, s[8:9]
	ds_read_b128 v[206:209], v203 offset:49152
	ds_read_b128 v[210:213], v203 offset:50176
	ds_read_b128 v[214:217], v203 offset:51200
	ds_read_b128 v[218:221], v203 offset:52224
	ds_read_b128 v[222:225], v203 offset:53248
	ds_read_b128 v[226:229], v203 offset:54272
	ds_read_b128 v[230:233], v203 offset:55296
	ds_read_b128 v[234:237], v203 offset:56320
	global_load_lds_dwordx4 v[176:177], off
	v_lshl_add_u64 v[176:177], v[178:179], 0, s[8:9]
	s_mov_b32 m0, s53
	s_nop 0
	global_load_lds_dwordx4 v[176:177], off
	v_lshl_add_u64 v[176:177], v[174:175], 0, v[162:163]
	s_mov_b32 m0, s56
	v_lshl_add_u64 v[174:175], v[174:175], 0, v[160:161]
	global_load_lds_dwordx4 v[176:177], off
	s_mov_b32 m0, s57
	s_nop 0
	global_load_lds_dwordx4 v[174:175], off
	v_lshl_add_u64 v[174:175], v[180:181], 0, s[8:9]
	s_mov_b32 m0, s54
	s_nop 0
	global_load_lds_dwordx4 v[174:175], off
	v_lshl_add_u64 v[174:175], v[182:183], 0, s[8:9]
	s_mov_b32 m0, s55
	s_nop 0
	global_load_lds_dwordx4 v[174:175], off
	s_waitcnt vmcnt(8)
	s_waitcnt lgkmcnt(0)
	s_barrier
	s_setprio 0
	s_waitcnt lgkmcnt(0)
	v_mfma_f32_16x16x128_f8f6f4 v[84:87], v[0:7], v[206:213], v[84:87]
	v_mfma_f32_16x16x128_f8f6f4 v[76:79], v[8:15], v[206:213], v[76:79]
	v_mfma_f32_16x16x128_f8f6f4 v[60:63], v[0:7], v[214:221], v[60:63]
	v_mfma_f32_16x16x128_f8f6f4 v[48:51], v[8:15], v[214:221], v[48:51]
	v_mfma_f32_16x16x128_f8f6f4 v[68:71], v[0:7], v[222:229], v[68:71]
	v_mfma_f32_16x16x128_f8f6f4 v[56:59], v[8:15], v[222:229], v[56:59]
	v_mfma_f32_16x16x128_f8f6f4 v[44:47], v[0:7], v[230:237], v[44:47]
	v_mfma_f32_16x16x128_f8f6f4 v[36:39], v[8:15], v[230:237], v[36:39]
	s_setprio 1
	s_setprio 0
	v_mfma_f32_16x16x128_f8f6f4 v[100:103], v[16:23], v[206:213], v[100:103]
	v_mfma_f32_16x16x128_f8f6f4 v[92:95], v[24:31], v[206:213], v[92:95]
	v_mfma_f32_16x16x128_f8f6f4 v[80:83], v[16:23], v[214:221], v[80:83]
	v_mfma_f32_16x16x128_f8f6f4 v[72:75], v[24:31], v[214:221], v[72:75]
	v_mfma_f32_16x16x128_f8f6f4 v[64:67], v[16:23], v[222:229], v[64:67]
	v_mfma_f32_16x16x128_f8f6f4 v[52:55], v[24:31], v[222:229], v[52:55]
	v_mfma_f32_16x16x128_f8f6f4 v[40:43], v[16:23], v[230:237], v[40:43]
	v_mfma_f32_16x16x128_f8f6f4 v[32:35], v[24:31], v[230:237], v[32:35]
	s_setprio 1
	s_barrier
	s_andn2_b64 vcc, exec, s[38:39]
	s_mov_b64 s[40:41], -1
	s_mov_b64 s[38:39], 0
	s_mov_b64 s[42:43], 0x100
	s_cbranch_vccz .LBB0_1790
	s_nop 15
	s_nop 7
	s_and_b64 vcc, exec, s[12:13]
	s_cbranch_vccz .LBB0_1793
	s_barrier

.LBB0_1802:
	s_add_u32 s30, s4, s12
	s_addc_u32 s31, s5, s13
	s_add_u32 s16, s30, 0x100
	s_addc_u32 s17, s31, 0
	s_and_b64 s[14:15], s[10:11], exec
	s_cselect_b32 s15, s5, s17
	s_cselect_b32 s14, s4, s16
	s_add_u32 s12, s0, s12
	s_addc_u32 s13, s1, s13
	s_add_u32 s12, s12, 0x100
	ds_read_b128 v[144:147], v138
	ds_read_b128 v[148:151], v138 offset:1024
	ds_read_b128 v[152:155], v138 offset:2048
	ds_read_b128 v[156:159], v138 offset:3072
	ds_read_b128 v[160:163], v139
	ds_read_b128 v[164:167], v139 offset:1024
	ds_read_b128 v[168:171], v139 offset:2048
	ds_read_b128 v[172:175], v139 offset:3072
	s_addc_u32 s13, s13, 0
	s_and_b64 s[10:11], s[10:11], exec
	s_cselect_b32 s17, s1, s13
	s_cselect_b32 s16, s0, s12
	s_add_u32 s34, s30, 0x10080
	s_addc_u32 s35, s31, 0
	s_add_u32 s30, s16, 0x10000
	s_addc_u32 s31, s17, 0
	s_add_u32 s12, s14, 0x10000
	s_addc_u32 s13, s15, 0
	s_add_u32 s10, s16, 0x10080
	s_addc_u32 s11, s17, 0
	s_mov_b32 m0, s39
	v_lshl_add_u64 v[208:209], s[34:35], 0, v[132:133]
	ds_read_b128 v[176:179], v140
	ds_read_b128 v[180:183], v140 offset:1024
	ds_read_b128 v[184:187], v140 offset:2048
	ds_read_b128 v[188:191], v140 offset:3072
	ds_read_b128 v[192:195], v140 offset:4096
	ds_read_b128 v[196:199], v140 offset:5120
	ds_read_b128 v[200:203], v140 offset:6144
	ds_read_b128 v[204:207], v140 offset:7168
	global_load_lds_dwordx4 v[208:209], off
	v_lshl_add_u64 v[208:209], s[34:35], 0, v[134:135]
	s_mov_b32 m0, s40
	s_nop 0
	global_load_lds_dwordx4 v[208:209], off
	s_waitcnt vmcnt(8)
	s_waitcnt lgkmcnt(0)
	s_barrier
	s_setprio 0
	s_waitcnt lgkmcnt(0)
	v_mfma_f32_16x16x32_bf16 v[124:127], v[144:147], v[176:179], v[124:127]
	v_mfma_f32_16x16x32_bf16 v[120:123], v[152:155], v[176:179], v[120:123]
	v_mfma_f32_16x16x32_bf16 v[116:119], v[144:147], v[184:187], v[116:119]
	v_mfma_f32_16x16x32_bf16 v[108:111], v[152:155], v[184:187], v[108:111]
	v_mfma_f32_16x16x32_bf16 v[100:103], v[144:147], v[192:195], v[100:103]
	v_mfma_f32_16x16x32_bf16 v[92:95], v[152:155], v[192:195], v[92:95]
	v_mfma_f32_16x16x32_bf16 v[84:87], v[144:147], v[200:203], v[84:87]
	v_mfma_f32_16x16x32_bf16 v[76:79], v[152:155], v[200:203], v[76:79]
	v_mfma_f32_16x16x32_bf16 v[124:127], v[148:151], v[180:183], v[124:127]
	v_mfma_f32_16x16x32_bf16 v[120:123], v[156:159], v[180:183], v[120:123]
	v_mfma_f32_16x16x32_bf16 v[116:119], v[148:151], v[188:191], v[116:119]
	v_mfma_f32_16x16x32_bf16 v[108:111], v[156:159], v[188:191], v[108:111]
	v_mfma_f32_16x16x32_bf16 v[100:103], v[148:151], v[196:199], v[100:103]
	v_mfma_f32_16x16x32_bf16 v[92:95], v[156:159], v[196:199], v[92:95]
	v_mfma_f32_16x16x32_bf16 v[84:87], v[148:151], v[204:207], v[84:87]
	v_mfma_f32_16x16x32_bf16 v[76:79], v[156:159], v[204:207], v[76:79]
	s_setprio 1
	s_setprio 0
	v_mfma_f32_16x16x32_bf16 v[112:115], v[160:163], v[176:179], v[112:115]
	v_mfma_f32_16x16x32_bf16 v[104:107], v[168:171], v[176:179], v[104:107]
	v_mfma_f32_16x16x32_bf16 v[96:99], v[160:163], v[184:187], v[96:99]
	v_mfma_f32_16x16x32_bf16 v[88:91], v[168:171], v[184:187], v[88:91]
	v_mfma_f32_16x16x32_bf16 v[80:83], v[160:163], v[192:195], v[80:83]
	v_mfma_f32_16x16x32_bf16 v[72:75], v[168:171], v[192:195], v[72:75]
	v_mfma_f32_16x16x32_bf16 v[52:55], v[160:163], v[200:203], v[52:55]
	v_mfma_f32_16x16x32_bf16 v[48:51], v[168:171], v[200:203], v[48:51]
	v_mfma_f32_16x16x32_bf16 v[112:115], v[164:167], v[180:183], v[112:115]
	v_mfma_f32_16x16x32_bf16 v[104:107], v[172:175], v[180:183], v[104:107]
	v_mfma_f32_16x16x32_bf16 v[96:99], v[164:167], v[188:191], v[96:99]
	v_mfma_f32_16x16x32_bf16 v[88:91], v[172:175], v[188:191], v[88:91]
	v_mfma_f32_16x16x32_bf16 v[80:83], v[164:167], v[196:199], v[80:83]
	v_mfma_f32_16x16x32_bf16 v[72:75], v[172:175], v[196:199], v[72:75]
	v_mfma_f32_16x16x32_bf16 v[52:55], v[164:167], v[204:207], v[52:55]
	v_mfma_f32_16x16x32_bf16 v[48:51], v[172:175], v[204:207], v[48:51]
	s_setprio 1
	s_barrier
	s_mov_b32 m0, s41
	v_lshl_add_u64 v[208:209], s[16:17], 0, v[130:131]
	ds_read_b128 v[176:179], v140 offset:16384
	ds_read_b128 v[180:183], v140 offset:17408
	ds_read_b128 v[184:187], v140 offset:18432
	ds_read_b128 v[188:191], v140 offset:19456
	ds_read_b128 v[192:195], v140 offset:20480
	ds_read_b128 v[196:199], v140 offset:21504
	ds_read_b128 v[200:203], v140 offset:22528
	ds_read_b128 v[204:207], v140 offset:23552
	global_load_lds_dwordx4 v[208:209], off
	v_lshl_add_u64 v[210:211], s[16:17], 0, v[128:129]
	s_mov_b32 m0, s42
	v_lshl_add_u64 v[212:213], s[30:31], 0, v[130:131]
	global_load_lds_dwordx4 v[210:211], off
	s_mov_b32 m0, s43
	v_lshl_add_u64 v[214:215], s[14:15], 0, v[134:135]
	global_load_lds_dwordx4 v[212:213], off
	v_lshl_add_u64 v[212:213], s[30:31], 0, v[128:129]
	s_mov_b32 m0, s44
	s_nop 0
	global_load_lds_dwordx4 v[212:213], off
	v_lshl_add_u64 v[212:213], s[14:15], 0, v[132:133]
	s_mov_b32 m0, s21
	s_nop 0
	global_load_lds_dwordx4 v[212:213], off
	s_mov_b32 m0, s22
	s_nop 0
	global_load_lds_dwordx4 v[214:215], off
	s_waitcnt vmcnt(8)
	s_waitcnt lgkmcnt(0)
	s_barrier
	s_setprio 0
	s_waitcnt lgkmcnt(0)
	v_mfma_f32_16x16x32_bf16 v[44:47], v[144:147], v[176:179], v[44:47]
	v_mfma_f32_16x16x32_bf16 v[32:35], v[152:155], v[176:179], v[32:35]
	v_mfma_f32_16x16x32_bf16 v[4:7], v[144:147], v[184:187], v[4:7]
	v_mfma_f32_16x16x32_bf16 v[0:3], v[152:155], v[184:187], v[0:3]
	v_mfma_f32_16x16x32_bf16 v[28:31], v[144:147], v[192:195], v[28:31]
	v_mfma_f32_16x16x32_bf16 v[24:27], v[152:155], v[192:195], v[24:27]
	v_mfma_f32_16x16x32_bf16 v[12:15], v[144:147], v[200:203], v[12:15]
	v_mfma_f32_16x16x32_bf16 v[8:11], v[152:155], v[200:203], v[8:11]
	v_mfma_f32_16x16x32_bf16 v[44:47], v[148:151], v[180:183], v[44:47]
	v_mfma_f32_16x16x32_bf16 v[32:35], v[156:159], v[180:183], v[32:35]
	v_mfma_f32_16x16x32_bf16 v[4:7], v[148:151], v[188:191], v[4:7]
	v_mfma_f32_16x16x32_bf16 v[0:3], v[156:159], v[188:191], v[0:3]
	v_mfma_f32_16x16x32_bf16 v[28:31], v[148:151], v[196:199], v[28:31]
	v_mfma_f32_16x16x32_bf16 v[24:27], v[156:159], v[196:199], v[24:27]
	v_mfma_f32_16x16x32_bf16 v[12:15], v[148:151], v[204:207], v[12:15]
	v_mfma_f32_16x16x32_bf16 v[8:11], v[156:159], v[204:207], v[8:11]
	s_setprio 1
	s_setprio 0
	v_mfma_f32_16x16x32_bf16 v[68:71], v[160:163], v[176:179], v[68:71]
	v_mfma_f32_16x16x32_bf16 v[64:67], v[168:171], v[176:179], v[64:67]
	v_mfma_f32_16x16x32_bf16 v[60:63], v[160:163], v[184:187], v[60:63]
	v_mfma_f32_16x16x32_bf16 v[56:59], v[168:171], v[184:187], v[56:59]
	v_mfma_f32_16x16x32_bf16 v[40:43], v[160:163], v[192:195], v[40:43]
	v_mfma_f32_16x16x32_bf16 v[36:39], v[168:171], v[192:195], v[36:39]
	v_mfma_f32_16x16x32_bf16 v[20:23], v[160:163], v[200:203], v[20:23]
	v_mfma_f32_16x16x32_bf16 v[16:19], v[168:171], v[200:203], v[16:19]
	v_mfma_f32_16x16x32_bf16 v[68:71], v[164:167], v[180:183], v[68:71]
	v_mfma_f32_16x16x32_bf16 v[64:67], v[172:175], v[180:183], v[64:67]
	v_mfma_f32_16x16x32_bf16 v[60:63], v[164:167], v[188:191], v[60:63]
	v_mfma_f32_16x16x32_bf16 v[56:59], v[172:175], v[188:191], v[56:59]
	v_mfma_f32_16x16x32_bf16 v[40:43], v[164:167], v[196:199], v[40:43]
	v_mfma_f32_16x16x32_bf16 v[36:39], v[172:175], v[196:199], v[36:39]
	v_mfma_f32_16x16x32_bf16 v[20:23], v[164:167], v[204:207], v[20:23]
	v_mfma_f32_16x16x32_bf16 v[16:19], v[172:175], v[204:207], v[16:19]
	s_setprio 1
	s_barrier
	ds_read_b128 v[144:147], v141
	ds_read_b128 v[148:151], v141 offset:1024
	ds_read_b128 v[152:155], v141 offset:2048
	ds_read_b128 v[156:159], v141 offset:3072
	ds_read_b128 v[160:163], v142
	ds_read_b128 v[164:167], v142 offset:1024
	ds_read_b128 v[168:171], v142 offset:2048
	ds_read_b128 v[172:175], v142 offset:3072
	s_mov_b32 m0, s23
	v_lshl_add_u64 v[216:217], s[12:13], 0, v[132:133]
	ds_read_b128 v[176:179], v140 offset:32768
	ds_read_b128 v[180:183], v140 offset:33792
	ds_read_b128 v[184:187], v140 offset:34816
	ds_read_b128 v[188:191], v140 offset:35840
	ds_read_b128 v[192:195], v140 offset:36864
	ds_read_b128 v[196:199], v140 offset:37888
	ds_read_b128 v[200:203], v140 offset:38912
	ds_read_b128 v[204:207], v140 offset:39936
	global_load_lds_dwordx4 v[216:217], off
	v_lshl_add_u64 v[216:217], s[12:13], 0, v[134:135]
	s_mov_b32 m0, s33
	s_nop 0
	global_load_lds_dwordx4 v[216:217], off
	s_waitcnt vmcnt(8)
	s_waitcnt lgkmcnt(0)
	s_barrier
	s_setprio 0
	s_waitcnt lgkmcnt(0)
	v_mfma_f32_16x16x32_bf16 v[124:127], v[144:147], v[176:179], v[124:127]
	v_mfma_f32_16x16x32_bf16 v[120:123], v[152:155], v[176:179], v[120:123]
	v_mfma_f32_16x16x32_bf16 v[116:119], v[144:147], v[184:187], v[116:119]
	v_mfma_f32_16x16x32_bf16 v[108:111], v[152:155], v[184:187], v[108:111]
	v_mfma_f32_16x16x32_bf16 v[100:103], v[144:147], v[192:195], v[100:103]
	v_mfma_f32_16x16x32_bf16 v[92:95], v[152:155], v[192:195], v[92:95]
	v_mfma_f32_16x16x32_bf16 v[84:87], v[144:147], v[200:203], v[84:87]
	v_mfma_f32_16x16x32_bf16 v[76:79], v[152:155], v[200:203], v[76:79]
	v_mfma_f32_16x16x32_bf16 v[124:127], v[148:151], v[180:183], v[124:127]
	v_mfma_f32_16x16x32_bf16 v[120:123], v[156:159], v[180:183], v[120:123]
	v_mfma_f32_16x16x32_bf16 v[116:119], v[148:151], v[188:191], v[116:119]
	v_mfma_f32_16x16x32_bf16 v[108:111], v[156:159], v[188:191], v[108:111]
	v_mfma_f32_16x16x32_bf16 v[100:103], v[148:151], v[196:199], v[100:103]
	v_mfma_f32_16x16x32_bf16 v[92:95], v[156:159], v[196:199], v[92:95]
	v_mfma_f32_16x16x32_bf16 v[84:87], v[148:151], v[204:207], v[84:87]
	v_mfma_f32_16x16x32_bf16 v[76:79], v[156:159], v[204:207], v[76:79]
	s_setprio 1
	s_setprio 0
	v_mfma_f32_16x16x32_bf16 v[112:115], v[160:163], v[176:179], v[112:115]
	v_mfma_f32_16x16x32_bf16 v[104:107], v[168:171], v[176:179], v[104:107]
	v_mfma_f32_16x16x32_bf16 v[96:99], v[160:163], v[184:187], v[96:99]
	v_mfma_f32_16x16x32_bf16 v[88:91], v[168:171], v[184:187], v[88:91]
	v_mfma_f32_16x16x32_bf16 v[80:83], v[160:163], v[192:195], v[80:83]
	v_mfma_f32_16x16x32_bf16 v[72:75], v[168:171], v[192:195], v[72:75]
	v_mfma_f32_16x16x32_bf16 v[52:55], v[160:163], v[200:203], v[52:55]
	v_mfma_f32_16x16x32_bf16 v[48:51], v[168:171], v[200:203], v[48:51]
	v_mfma_f32_16x16x32_bf16 v[112:115], v[164:167], v[180:183], v[112:115]
	v_mfma_f32_16x16x32_bf16 v[104:107], v[172:175], v[180:183], v[104:107]
	v_mfma_f32_16x16x32_bf16 v[96:99], v[164:167], v[188:191], v[96:99]
	v_mfma_f32_16x16x32_bf16 v[88:91], v[172:175], v[188:191], v[88:91]
	v_mfma_f32_16x16x32_bf16 v[80:83], v[164:167], v[196:199], v[80:83]
	v_mfma_f32_16x16x32_bf16 v[72:75], v[172:175], v[196:199], v[72:75]
	v_mfma_f32_16x16x32_bf16 v[52:55], v[164:167], v[204:207], v[52:55]
	v_mfma_f32_16x16x32_bf16 v[48:51], v[172:175], v[204:207], v[48:51]
	s_setprio 1
	s_barrier
	s_mov_b32 m0, s45
	v_lshl_add_u64 v[208:209], v[208:209], 0, s[6:7]
	ds_read_b128 v[176:179], v140 offset:49152
	ds_read_b128 v[180:183], v140 offset:50176
	ds_read_b128 v[184:187], v140 offset:51200
	ds_read_b128 v[188:191], v140 offset:52224
	ds_read_b128 v[192:195], v140 offset:53248
	ds_read_b128 v[196:199], v140 offset:54272
	ds_read_b128 v[200:203], v140 offset:55296
	ds_read_b128 v[204:207], v140 offset:56320
	global_load_lds_dwordx4 v[208:209], off
	v_lshl_add_u64 v[208:209], v[210:211], 0, s[6:7]
	s_mov_b32 m0, s46
	s_nop 0
	global_load_lds_dwordx4 v[208:209], off
	v_lshl_add_u64 v[208:209], s[10:11], 0, v[130:131]
	s_mov_b32 m0, s47
	s_nop 0
	global_load_lds_dwordx4 v[208:209], off
	v_lshl_add_u64 v[208:209], s[10:11], 0, v[128:129]
	s_mov_b32 m0, s48
	s_nop 0
	global_load_lds_dwordx4 v[208:209], off
	v_lshl_add_u64 v[208:209], v[212:213], 0, s[6:7]
	s_mov_b32 m0, s37
	s_nop 0
	global_load_lds_dwordx4 v[208:209], off
	v_lshl_add_u64 v[208:209], v[214:215], 0, s[6:7]
	s_mov_b32 m0, s38
	s_nop 0
	global_load_lds_dwordx4 v[208:209], off
	s_waitcnt vmcnt(8)
	s_waitcnt lgkmcnt(0)
	s_barrier
	s_setprio 0
	s_waitcnt lgkmcnt(0)
	v_mfma_f32_16x16x32_bf16 v[44:47], v[144:147], v[176:179], v[44:47]
	v_mfma_f32_16x16x32_bf16 v[32:35], v[152:155], v[176:179], v[32:35]
	v_mfma_f32_16x16x32_bf16 v[4:7], v[144:147], v[184:187], v[4:7]
	v_mfma_f32_16x16x32_bf16 v[0:3], v[152:155], v[184:187], v[0:3]
	v_mfma_f32_16x16x32_bf16 v[28:31], v[144:147], v[192:195], v[28:31]
	v_mfma_f32_16x16x32_bf16 v[24:27], v[152:155], v[192:195], v[24:27]
	v_mfma_f32_16x16x32_bf16 v[12:15], v[144:147], v[200:203], v[12:15]
	v_mfma_f32_16x16x32_bf16 v[8:11], v[152:155], v[200:203], v[8:11]
	v_mfma_f32_16x16x32_bf16 v[44:47], v[148:151], v[180:183], v[44:47]
	v_mfma_f32_16x16x32_bf16 v[32:35], v[156:159], v[180:183], v[32:35]
	v_mfma_f32_16x16x32_bf16 v[4:7], v[148:151], v[188:191], v[4:7]
	v_mfma_f32_16x16x32_bf16 v[0:3], v[156:159], v[188:191], v[0:3]
	v_mfma_f32_16x16x32_bf16 v[28:31], v[148:151], v[196:199], v[28:31]
	v_mfma_f32_16x16x32_bf16 v[24:27], v[156:159], v[196:199], v[24:27]
	v_mfma_f32_16x16x32_bf16 v[12:15], v[148:151], v[204:207], v[12:15]
	v_mfma_f32_16x16x32_bf16 v[8:11], v[156:159], v[204:207], v[8:11]
	s_setprio 1
	s_setprio 0
	v_mfma_f32_16x16x32_bf16 v[68:71], v[160:163], v[176:179], v[68:71]
	v_mfma_f32_16x16x32_bf16 v[64:67], v[168:171], v[176:179], v[64:67]
	v_mfma_f32_16x16x32_bf16 v[60:63], v[160:163], v[184:187], v[60:63]
	v_mfma_f32_16x16x32_bf16 v[56:59], v[168:171], v[184:187], v[56:59]
	v_mfma_f32_16x16x32_bf16 v[40:43], v[160:163], v[192:195], v[40:43]
	v_mfma_f32_16x16x32_bf16 v[36:39], v[168:171], v[192:195], v[36:39]
	v_mfma_f32_16x16x32_bf16 v[20:23], v[160:163], v[200:203], v[20:23]
	v_mfma_f32_16x16x32_bf16 v[16:19], v[168:171], v[200:203], v[16:19]
	v_mfma_f32_16x16x32_bf16 v[68:71], v[164:167], v[180:183], v[68:71]
	v_mfma_f32_16x16x32_bf16 v[64:67], v[172:175], v[180:183], v[64:67]
	v_mfma_f32_16x16x32_bf16 v[60:63], v[164:167], v[188:191], v[60:63]
	v_mfma_f32_16x16x32_bf16 v[56:59], v[172:175], v[188:191], v[56:59]
	v_mfma_f32_16x16x32_bf16 v[40:43], v[164:167], v[196:199], v[40:43]
	v_mfma_f32_16x16x32_bf16 v[36:39], v[172:175], v[196:199], v[36:39]
	v_mfma_f32_16x16x32_bf16 v[20:23], v[164:167], v[204:207], v[20:23]
	v_mfma_f32_16x16x32_bf16 v[16:19], v[172:175], v[204:207], v[16:19]
	s_setprio 1
	s_barrier
	s_andn2_b64 vcc, exec, s[8:9]
	s_mov_b64 s[10:11], -1
	s_mov_b64 s[8:9], 0
	s_mov_b64 s[12:13], 0x100
	s_cbranch_vccz .LBB0_1802
	s_cmpk_lt_u32 s18, 0x100
	s_cbranch_scc0 .LBB0_1805
	s_barrier

.LBB0_1958:
	s_add_u32 s44, s30, s38
	s_addc_u32 s45, s31, s39
	s_add_u32 s42, s44, 0x100
	s_addc_u32 s43, s45, 0
	s_and_b64 s[40:41], s[36:37], exec
	s_cselect_b32 s41, s11, s43
	s_cselect_b32 s40, s59, s42
	s_add_u32 s38, s28, s38
	s_addc_u32 s39, s29, s39
	s_add_u32 s38, s38, 0x100
	s_addc_u32 s39, s39, 0
	s_and_b64 s[36:37], s[36:37], exec
	s_cselect_b32 s43, s9, s39
	s_cselect_b32 s42, s60, s38
	s_add_u32 s46, s44, 0x10080
	ds_read_b128 v[148:151], v145
	ds_read_b128 v[152:155], v145 offset:1024
	ds_read_b128 v[156:159], v145 offset:2048
	ds_read_b128 v[160:163], v145 offset:3072
	ds_read_b128 v[164:167], v146
	ds_read_b128 v[168:171], v146 offset:1024
	ds_read_b128 v[172:175], v146 offset:2048
	ds_read_b128 v[176:179], v146 offset:3072
	s_addc_u32 s47, s45, 0
	s_add_i32 s70, s56, s21
	s_add_i32 m0, s15, 0xc000
	s_add_i32 s71, s15, 0xe000
	s_add_i32 s67, s70, 0x2000
	s_add_u32 s44, s42, 0x10000
	s_addc_u32 s45, s43, 0
	s_add_i32 s69, s57, s21
	s_add_i32 s68, s69, 0x2000
	s_add_i32 s66, 0, 0x18000
	s_add_i32 s65, 0, 0x1c000
	s_add_u32 s38, s40, 0x10000
	s_addc_u32 s39, s41, 0
	s_add_i32 s64, s66, s21
	s_add_i32 s62, s64, 0x2000
	s_add_u32 s36, s42, 0x10080
	s_addc_u32 s37, s43, 0
	s_add_i32 s63, s65, s21
	s_add_i32 s61, s63, 0x2000
	v_lshl_add_u64 v[140:141], s[46:47], 0, v[132:133]
	ds_read_b128 v[180:183], v147
	ds_read_b128 v[184:187], v147 offset:1024
	ds_read_b128 v[188:191], v147 offset:2048
	ds_read_b128 v[192:195], v147 offset:3072
	ds_read_b128 v[196:199], v147 offset:4096
	ds_read_b128 v[200:203], v147 offset:5120
	ds_read_b128 v[204:207], v147 offset:6144
	ds_read_b128 v[208:211], v147 offset:7168
	global_load_lds_dwordx4 v[140:141], off
	v_lshl_add_u64 v[140:141], s[46:47], 0, v[134:135]
	s_mov_b32 m0, s71
	s_nop 0
	global_load_lds_dwordx4 v[140:141], off
	s_waitcnt vmcnt(8)
	s_waitcnt lgkmcnt(0)
	s_barrier
	s_setprio 0
	s_waitcnt lgkmcnt(0)
	v_mfma_f32_16x16x32_bf16 v[124:127], v[148:151], v[180:183], v[124:127]
	v_mfma_f32_16x16x32_bf16 v[120:123], v[156:159], v[180:183], v[120:123]
	v_mfma_f32_16x16x32_bf16 v[116:119], v[148:151], v[188:191], v[116:119]
	v_mfma_f32_16x16x32_bf16 v[108:111], v[156:159], v[188:191], v[108:111]
	v_mfma_f32_16x16x32_bf16 v[100:103], v[148:151], v[196:199], v[100:103]
	v_mfma_f32_16x16x32_bf16 v[92:95], v[156:159], v[196:199], v[92:95]
	v_mfma_f32_16x16x32_bf16 v[84:87], v[148:151], v[204:207], v[84:87]
	v_mfma_f32_16x16x32_bf16 v[76:79], v[156:159], v[204:207], v[76:79]
	v_mfma_f32_16x16x32_bf16 v[124:127], v[152:155], v[184:187], v[124:127]
	v_mfma_f32_16x16x32_bf16 v[120:123], v[160:163], v[184:187], v[120:123]
	v_mfma_f32_16x16x32_bf16 v[116:119], v[152:155], v[192:195], v[116:119]
	v_mfma_f32_16x16x32_bf16 v[108:111], v[160:163], v[192:195], v[108:111]
	v_mfma_f32_16x16x32_bf16 v[100:103], v[152:155], v[200:203], v[100:103]
	v_mfma_f32_16x16x32_bf16 v[92:95], v[160:163], v[200:203], v[92:95]
	v_mfma_f32_16x16x32_bf16 v[84:87], v[152:155], v[208:211], v[84:87]
	v_mfma_f32_16x16x32_bf16 v[76:79], v[160:163], v[208:211], v[76:79]
	s_setprio 1
	s_setprio 0
	v_mfma_f32_16x16x32_bf16 v[112:115], v[164:167], v[180:183], v[112:115]
	v_mfma_f32_16x16x32_bf16 v[104:107], v[172:175], v[180:183], v[104:107]
	v_mfma_f32_16x16x32_bf16 v[96:99], v[164:167], v[188:191], v[96:99]
	v_mfma_f32_16x16x32_bf16 v[88:91], v[172:175], v[188:191], v[88:91]
	v_mfma_f32_16x16x32_bf16 v[80:83], v[164:167], v[196:199], v[80:83]
	v_mfma_f32_16x16x32_bf16 v[72:75], v[172:175], v[196:199], v[72:75]
	v_mfma_f32_16x16x32_bf16 v[52:55], v[164:167], v[204:207], v[52:55]
	v_mfma_f32_16x16x32_bf16 v[48:51], v[172:175], v[204:207], v[48:51]
	v_mfma_f32_16x16x32_bf16 v[112:115], v[168:171], v[184:187], v[112:115]
	v_mfma_f32_16x16x32_bf16 v[104:107], v[176:179], v[184:187], v[104:107]
	v_mfma_f32_16x16x32_bf16 v[96:99], v[168:171], v[192:195], v[96:99]
	v_mfma_f32_16x16x32_bf16 v[88:91], v[176:179], v[192:195], v[88:91]
	v_mfma_f32_16x16x32_bf16 v[80:83], v[168:171], v[200:203], v[80:83]
	v_mfma_f32_16x16x32_bf16 v[72:75], v[176:179], v[200:203], v[72:75]
	v_mfma_f32_16x16x32_bf16 v[52:55], v[168:171], v[208:211], v[52:55]
	v_mfma_f32_16x16x32_bf16 v[48:51], v[176:179], v[208:211], v[48:51]
	s_setprio 1
	s_barrier
	s_mov_b32 m0, s70
	v_lshl_add_u64 v[140:141], s[42:43], 0, v[128:129]
	ds_read_b128 v[180:183], v147 offset:16384
	ds_read_b128 v[184:187], v147 offset:17408
	ds_read_b128 v[188:191], v147 offset:18432
	ds_read_b128 v[192:195], v147 offset:19456
	ds_read_b128 v[196:199], v147 offset:20480
	ds_read_b128 v[200:203], v147 offset:21504
	ds_read_b128 v[204:207], v147 offset:22528
	ds_read_b128 v[208:211], v147 offset:23552
	global_load_lds_dwordx4 v[140:141], off
	v_lshl_add_u64 v[212:213], s[42:43], 0, v[130:131]
	s_mov_b32 m0, s67
	v_lshl_add_u64 v[214:215], s[44:45], 0, v[128:129]
	global_load_lds_dwordx4 v[212:213], off
	s_mov_b32 m0, s69
	v_lshl_add_u64 v[216:217], s[40:41], 0, v[134:135]
	global_load_lds_dwordx4 v[214:215], off
	v_lshl_add_u64 v[214:215], s[44:45], 0, v[130:131]
	s_mov_b32 m0, s68
	s_nop 0
	global_load_lds_dwordx4 v[214:215], off
	v_lshl_add_u64 v[214:215], s[40:41], 0, v[132:133]
	s_mov_b32 m0, s15
	s_nop 0
	global_load_lds_dwordx4 v[214:215], off
	s_mov_b32 m0, s49
	s_nop 0
	global_load_lds_dwordx4 v[216:217], off
	s_waitcnt vmcnt(8)
	s_waitcnt lgkmcnt(0)
	s_barrier
	s_setprio 0
	s_waitcnt lgkmcnt(0)
	v_mfma_f32_16x16x32_bf16 v[44:47], v[148:151], v[180:183], v[44:47]
	v_mfma_f32_16x16x32_bf16 v[32:35], v[156:159], v[180:183], v[32:35]
	v_mfma_f32_16x16x32_bf16 v[4:7], v[148:151], v[188:191], v[4:7]
	v_mfma_f32_16x16x32_bf16 v[0:3], v[156:159], v[188:191], v[0:3]
	v_mfma_f32_16x16x32_bf16 v[28:31], v[148:151], v[196:199], v[28:31]
	v_mfma_f32_16x16x32_bf16 v[24:27], v[156:159], v[196:199], v[24:27]
	v_mfma_f32_16x16x32_bf16 v[12:15], v[148:151], v[204:207], v[12:15]
	v_mfma_f32_16x16x32_bf16 v[8:11], v[156:159], v[204:207], v[8:11]
	v_mfma_f32_16x16x32_bf16 v[44:47], v[152:155], v[184:187], v[44:47]
	v_mfma_f32_16x16x32_bf16 v[32:35], v[160:163], v[184:187], v[32:35]
	v_mfma_f32_16x16x32_bf16 v[4:7], v[152:155], v[192:195], v[4:7]
	v_mfma_f32_16x16x32_bf16 v[0:3], v[160:163], v[192:195], v[0:3]
	v_mfma_f32_16x16x32_bf16 v[28:31], v[152:155], v[200:203], v[28:31]
	v_mfma_f32_16x16x32_bf16 v[24:27], v[160:163], v[200:203], v[24:27]
	v_mfma_f32_16x16x32_bf16 v[12:15], v[152:155], v[208:211], v[12:15]
	v_mfma_f32_16x16x32_bf16 v[8:11], v[160:163], v[208:211], v[8:11]
	s_setprio 1
	s_setprio 0
	v_mfma_f32_16x16x32_bf16 v[68:71], v[164:167], v[180:183], v[68:71]
	v_mfma_f32_16x16x32_bf16 v[64:67], v[172:175], v[180:183], v[64:67]
	v_mfma_f32_16x16x32_bf16 v[60:63], v[164:167], v[188:191], v[60:63]
	v_mfma_f32_16x16x32_bf16 v[56:59], v[172:175], v[188:191], v[56:59]
	v_mfma_f32_16x16x32_bf16 v[40:43], v[164:167], v[196:199], v[40:43]
	v_mfma_f32_16x16x32_bf16 v[36:39], v[172:175], v[196:199], v[36:39]
	v_mfma_f32_16x16x32_bf16 v[20:23], v[164:167], v[204:207], v[20:23]
	v_mfma_f32_16x16x32_bf16 v[16:19], v[172:175], v[204:207], v[16:19]
	v_mfma_f32_16x16x32_bf16 v[68:71], v[168:171], v[184:187], v[68:71]
	v_mfma_f32_16x16x32_bf16 v[64:67], v[176:179], v[184:187], v[64:67]
	v_mfma_f32_16x16x32_bf16 v[60:63], v[168:171], v[192:195], v[60:63]
	v_mfma_f32_16x16x32_bf16 v[56:59], v[176:179], v[192:195], v[56:59]
	v_mfma_f32_16x16x32_bf16 v[40:43], v[168:171], v[200:203], v[40:43]
	v_mfma_f32_16x16x32_bf16 v[36:39], v[176:179], v[200:203], v[36:39]
	v_mfma_f32_16x16x32_bf16 v[20:23], v[168:171], v[208:211], v[20:23]
	v_mfma_f32_16x16x32_bf16 v[16:19], v[176:179], v[208:211], v[16:19]
	s_setprio 1
	s_barrier
	v_add_u32_e32 v160, s66, v143
	v_add_u32_e32 v176, s65, v143
	ds_read_b128 v[148:151], v160
	ds_read_b128 v[152:155], v160 offset:1024
	ds_read_b128 v[156:159], v160 offset:2048
	ds_read_b128 v[160:163], v160 offset:3072
	ds_read_b128 v[164:167], v176
	ds_read_b128 v[168:171], v176 offset:1024
	ds_read_b128 v[172:175], v176 offset:2048
	ds_read_b128 v[176:179], v176 offset:3072
	s_mov_b32 m0, s50
	v_lshl_add_u64 v[218:219], s[38:39], 0, v[132:133]
	ds_read_b128 v[180:183], v147 offset:32768
	ds_read_b128 v[184:187], v147 offset:33792
	ds_read_b128 v[188:191], v147 offset:34816
	ds_read_b128 v[192:195], v147 offset:35840
	ds_read_b128 v[196:199], v147 offset:36864
	ds_read_b128 v[200:203], v147 offset:37888
	ds_read_b128 v[204:207], v147 offset:38912
	ds_read_b128 v[208:211], v147 offset:39936
	global_load_lds_dwordx4 v[218:219], off
	v_lshl_add_u64 v[218:219], s[38:39], 0, v[134:135]
	s_mov_b32 m0, s51
	s_nop 0
	global_load_lds_dwordx4 v[218:219], off
	s_waitcnt vmcnt(8)
	s_waitcnt lgkmcnt(0)
	s_barrier
	s_setprio 0
	s_waitcnt lgkmcnt(0)
	v_mfma_f32_16x16x32_bf16 v[124:127], v[148:151], v[180:183], v[124:127]
	v_mfma_f32_16x16x32_bf16 v[120:123], v[156:159], v[180:183], v[120:123]
	v_mfma_f32_16x16x32_bf16 v[116:119], v[148:151], v[188:191], v[116:119]
	v_mfma_f32_16x16x32_bf16 v[108:111], v[156:159], v[188:191], v[108:111]
	v_mfma_f32_16x16x32_bf16 v[100:103], v[148:151], v[196:199], v[100:103]
	v_mfma_f32_16x16x32_bf16 v[92:95], v[156:159], v[196:199], v[92:95]
	v_mfma_f32_16x16x32_bf16 v[84:87], v[148:151], v[204:207], v[84:87]
	v_mfma_f32_16x16x32_bf16 v[76:79], v[156:159], v[204:207], v[76:79]
	v_mfma_f32_16x16x32_bf16 v[124:127], v[152:155], v[184:187], v[124:127]
	v_mfma_f32_16x16x32_bf16 v[120:123], v[160:163], v[184:187], v[120:123]
	v_mfma_f32_16x16x32_bf16 v[116:119], v[152:155], v[192:195], v[116:119]
	v_mfma_f32_16x16x32_bf16 v[108:111], v[160:163], v[192:195], v[108:111]
	v_mfma_f32_16x16x32_bf16 v[100:103], v[152:155], v[200:203], v[100:103]
	v_mfma_f32_16x16x32_bf16 v[92:95], v[160:163], v[200:203], v[92:95]
	v_mfma_f32_16x16x32_bf16 v[84:87], v[152:155], v[208:211], v[84:87]
	v_mfma_f32_16x16x32_bf16 v[76:79], v[160:163], v[208:211], v[76:79]
	s_setprio 1
	s_setprio 0
	v_mfma_f32_16x16x32_bf16 v[112:115], v[164:167], v[180:183], v[112:115]
	v_mfma_f32_16x16x32_bf16 v[104:107], v[172:175], v[180:183], v[104:107]
	v_mfma_f32_16x16x32_bf16 v[96:99], v[164:167], v[188:191], v[96:99]
	v_mfma_f32_16x16x32_bf16 v[88:91], v[172:175], v[188:191], v[88:91]
	v_mfma_f32_16x16x32_bf16 v[80:83], v[164:167], v[196:199], v[80:83]
	v_mfma_f32_16x16x32_bf16 v[72:75], v[172:175], v[196:199], v[72:75]
	v_mfma_f32_16x16x32_bf16 v[52:55], v[164:167], v[204:207], v[52:55]
	v_mfma_f32_16x16x32_bf16 v[48:51], v[172:175], v[204:207], v[48:51]
	v_mfma_f32_16x16x32_bf16 v[112:115], v[168:171], v[184:187], v[112:115]
	v_mfma_f32_16x16x32_bf16 v[104:107], v[176:179], v[184:187], v[104:107]
	v_mfma_f32_16x16x32_bf16 v[96:99], v[168:171], v[192:195], v[96:99]
	v_mfma_f32_16x16x32_bf16 v[88:91], v[176:179], v[192:195], v[88:91]
	v_mfma_f32_16x16x32_bf16 v[80:83], v[168:171], v[200:203], v[80:83]
	v_mfma_f32_16x16x32_bf16 v[72:75], v[176:179], v[200:203], v[72:75]
	v_mfma_f32_16x16x32_bf16 v[52:55], v[168:171], v[208:211], v[52:55]
	v_mfma_f32_16x16x32_bf16 v[48:51], v[176:179], v[208:211], v[48:51]
	s_setprio 1
	s_barrier
	s_mov_b32 m0, s64
	v_lshl_add_u64 v[140:141], v[140:141], 0, s[4:5]
	ds_read_b128 v[180:183], v147 offset:49152
	ds_read_b128 v[184:187], v147 offset:50176
	ds_read_b128 v[188:191], v147 offset:51200
	ds_read_b128 v[192:195], v147 offset:52224
	ds_read_b128 v[196:199], v147 offset:53248
	ds_read_b128 v[200:203], v147 offset:54272
	ds_read_b128 v[204:207], v147 offset:55296
	ds_read_b128 v[208:211], v147 offset:56320
	global_load_lds_dwordx4 v[140:141], off
	v_lshl_add_u64 v[140:141], v[212:213], 0, s[4:5]
	s_mov_b32 m0, s62
	s_nop 0
	global_load_lds_dwordx4 v[140:141], off
	v_lshl_add_u64 v[140:141], s[36:37], 0, v[128:129]
	s_mov_b32 m0, s63
	s_nop 0
	global_load_lds_dwordx4 v[140:141], off
	v_lshl_add_u64 v[140:141], s[36:37], 0, v[130:131]
	s_mov_b32 m0, s61
	s_nop 0
	global_load_lds_dwordx4 v[140:141], off
	v_lshl_add_u64 v[140:141], v[214:215], 0, s[4:5]
	s_mov_b32 m0, s53
	s_nop 0
	global_load_lds_dwordx4 v[140:141], off
	v_lshl_add_u64 v[140:141], v[216:217], 0, s[4:5]
	s_mov_b32 m0, s54
	s_nop 0
	global_load_lds_dwordx4 v[140:141], off
	s_waitcnt vmcnt(8)
	s_waitcnt lgkmcnt(0)
	s_barrier
	s_setprio 0
	s_waitcnt lgkmcnt(0)
	v_mfma_f32_16x16x32_bf16 v[44:47], v[148:151], v[180:183], v[44:47]
	v_mfma_f32_16x16x32_bf16 v[32:35], v[156:159], v[180:183], v[32:35]
	v_mfma_f32_16x16x32_bf16 v[4:7], v[148:151], v[188:191], v[4:7]
	v_mfma_f32_16x16x32_bf16 v[0:3], v[156:159], v[188:191], v[0:3]
	v_mfma_f32_16x16x32_bf16 v[28:31], v[148:151], v[196:199], v[28:31]
	v_mfma_f32_16x16x32_bf16 v[24:27], v[156:159], v[196:199], v[24:27]
	v_mfma_f32_16x16x32_bf16 v[12:15], v[148:151], v[204:207], v[12:15]
	v_mfma_f32_16x16x32_bf16 v[8:11], v[156:159], v[204:207], v[8:11]
	v_mfma_f32_16x16x32_bf16 v[44:47], v[152:155], v[184:187], v[44:47]
	v_mfma_f32_16x16x32_bf16 v[32:35], v[160:163], v[184:187], v[32:35]
	v_mfma_f32_16x16x32_bf16 v[4:7], v[152:155], v[192:195], v[4:7]
	v_mfma_f32_16x16x32_bf16 v[0:3], v[160:163], v[192:195], v[0:3]
	v_mfma_f32_16x16x32_bf16 v[28:31], v[152:155], v[200:203], v[28:31]
	v_mfma_f32_16x16x32_bf16 v[24:27], v[160:163], v[200:203], v[24:27]
	v_mfma_f32_16x16x32_bf16 v[12:15], v[152:155], v[208:211], v[12:15]
	v_mfma_f32_16x16x32_bf16 v[8:11], v[160:163], v[208:211], v[8:11]
	s_setprio 1
	s_setprio 0
	v_mfma_f32_16x16x32_bf16 v[68:71], v[164:167], v[180:183], v[68:71]
	v_mfma_f32_16x16x32_bf16 v[64:67], v[172:175], v[180:183], v[64:67]
	v_mfma_f32_16x16x32_bf16 v[60:63], v[164:167], v[188:191], v[60:63]
	v_mfma_f32_16x16x32_bf16 v[56:59], v[172:175], v[188:191], v[56:59]
	v_mfma_f32_16x16x32_bf16 v[40:43], v[164:167], v[196:199], v[40:43]
	v_mfma_f32_16x16x32_bf16 v[36:39], v[172:175], v[196:199], v[36:39]
	v_mfma_f32_16x16x32_bf16 v[20:23], v[164:167], v[204:207], v[20:23]
	v_mfma_f32_16x16x32_bf16 v[16:19], v[172:175], v[204:207], v[16:19]
	v_mfma_f32_16x16x32_bf16 v[68:71], v[168:171], v[184:187], v[68:71]
	v_mfma_f32_16x16x32_bf16 v[64:67], v[176:179], v[184:187], v[64:67]
	v_mfma_f32_16x16x32_bf16 v[60:63], v[168:171], v[192:195], v[60:63]
	v_mfma_f32_16x16x32_bf16 v[56:59], v[176:179], v[192:195], v[56:59]
	v_mfma_f32_16x16x32_bf16 v[40:43], v[168:171], v[200:203], v[40:43]
	v_mfma_f32_16x16x32_bf16 v[36:39], v[176:179], v[200:203], v[36:39]
	v_mfma_f32_16x16x32_bf16 v[20:23], v[168:171], v[208:211], v[20:23]
	v_mfma_f32_16x16x32_bf16 v[16:19], v[176:179], v[208:211], v[16:19]
	s_setprio 1
	s_barrier
	s_andn2_b64 vcc, exec, s[34:35]
	s_mov_b64 s[36:37], -1
	s_mov_b64 s[34:35], 0
	s_mov_b64 s[38:39], 0x100
	s_cbranch_vccz .LBB0_1958
	s_and_b64 vcc, exec, s[6:7]
	s_cbranch_vccz .LBB0_1961
	s_barrier

.LBB0_1979:
	ds_read_b128 v[124:127], v221
	ds_read_b128 v[132:135], v221 offset:1024
	ds_read_b128 v[136:139], v221 offset:2048
	ds_read_b128 v[140:143], v221 offset:3072
	ds_read_b128 v[144:147], v222
	ds_read_b128 v[148:151], v222 offset:1024
	ds_read_b128 v[152:155], v222 offset:2048
	ds_read_b128 v[156:159], v222 offset:3072
	s_add_u32 s30, s28, 0xfffc0080
	s_addc_u32 s31, s29, -1
	s_cmp_eq_u32 s48, 12
	s_cselect_b32 s35, s9, s31
	s_cselect_b32 s34, s44, s30
	s_cselect_b32 s31, s7, s47
	s_cselect_b32 s30, s45, s46
	v_lshl_add_u64 v[206:207], s[28:29], 0, v[180:181]
	s_add_i32 m0, s17, 0xc000
	ds_read_b128 v[160:163], v223
	ds_read_b128 v[164:167], v223 offset:1024
	ds_read_b128 v[168:171], v223 offset:2048
	ds_read_b128 v[186:189], v223 offset:3072
	ds_read_b128 v[190:193], v223 offset:4096
	ds_read_b128 v[194:197], v223 offset:5120
	ds_read_b128 v[198:201], v223 offset:6144
	ds_read_b128 v[202:205], v223 offset:7168
	global_load_lds_dwordx4 v[206:207], off
	v_lshl_add_u64 v[206:207], s[28:29], 0, v[182:183]
	s_add_i32 m0, s17, 0xe000
	s_nop 0
	global_load_lds_dwordx4 v[206:207], off
	s_waitcnt vmcnt(8)
	s_waitcnt lgkmcnt(0)
	s_barrier
	s_setprio 0
	s_waitcnt lgkmcnt(0)
	v_mfma_f32_16x16x32_bf16 v[120:123], v[124:127], v[160:163], v[120:123]
	v_mfma_f32_16x16x32_bf16 v[128:131], v[136:139], v[160:163], v[128:131]
	v_mfma_f32_16x16x32_bf16 v[108:111], v[124:127], v[168:171], v[108:111]
	v_mfma_f32_16x16x32_bf16 v[104:107], v[136:139], v[168:171], v[104:107]
	v_mfma_f32_16x16x32_bf16 v[92:95], v[124:127], v[190:193], v[92:95]
	v_mfma_f32_16x16x32_bf16 v[88:91], v[136:139], v[190:193], v[88:91]
	v_mfma_f32_16x16x32_bf16 v[76:79], v[124:127], v[198:201], v[76:79]
	v_mfma_f32_16x16x32_bf16 v[72:75], v[136:139], v[198:201], v[72:75]
	v_mfma_f32_16x16x32_bf16 v[120:123], v[132:135], v[164:167], v[120:123]
	v_mfma_f32_16x16x32_bf16 v[128:131], v[140:143], v[164:167], v[128:131]
	v_mfma_f32_16x16x32_bf16 v[108:111], v[132:135], v[186:189], v[108:111]
	v_mfma_f32_16x16x32_bf16 v[104:107], v[140:143], v[186:189], v[104:107]
	v_mfma_f32_16x16x32_bf16 v[92:95], v[132:135], v[194:197], v[92:95]
	v_mfma_f32_16x16x32_bf16 v[88:91], v[140:143], v[194:197], v[88:91]
	v_mfma_f32_16x16x32_bf16 v[76:79], v[132:135], v[202:205], v[76:79]
	v_mfma_f32_16x16x32_bf16 v[72:75], v[140:143], v[202:205], v[72:75]
	s_setprio 1
	s_setprio 0
	v_mfma_f32_16x16x32_bf16 v[116:119], v[144:147], v[160:163], v[116:119]
	v_mfma_f32_16x16x32_bf16 v[112:115], v[152:155], v[160:163], v[112:115]
	v_mfma_f32_16x16x32_bf16 v[100:103], v[144:147], v[168:171], v[100:103]
	v_mfma_f32_16x16x32_bf16 v[96:99], v[152:155], v[168:171], v[96:99]
	v_mfma_f32_16x16x32_bf16 v[84:87], v[144:147], v[190:193], v[84:87]
	v_mfma_f32_16x16x32_bf16 v[80:83], v[152:155], v[190:193], v[80:83]
	v_mfma_f32_16x16x32_bf16 v[68:71], v[144:147], v[198:201], v[68:71]
	v_mfma_f32_16x16x32_bf16 v[64:67], v[152:155], v[198:201], v[64:67]
	v_mfma_f32_16x16x32_bf16 v[116:119], v[148:151], v[164:167], v[116:119]
	v_mfma_f32_16x16x32_bf16 v[112:115], v[156:159], v[164:167], v[112:115]
	v_mfma_f32_16x16x32_bf16 v[100:103], v[148:151], v[186:189], v[100:103]
	v_mfma_f32_16x16x32_bf16 v[96:99], v[156:159], v[186:189], v[96:99]
	v_mfma_f32_16x16x32_bf16 v[84:87], v[148:151], v[194:197], v[84:87]
	v_mfma_f32_16x16x32_bf16 v[80:83], v[156:159], v[194:197], v[80:83]
	v_mfma_f32_16x16x32_bf16 v[68:71], v[148:151], v[202:205], v[68:71]
	v_mfma_f32_16x16x32_bf16 v[64:67], v[156:159], v[202:205], v[64:67]
	s_setprio 1
	s_barrier
	s_add_i32 s49, s40, s20
	v_lshl_add_u64 v[206:207], s[30:31], 0, v[174:175]
	s_mov_b32 m0, s49
	ds_read_b128 v[160:163], v223 offset:16384
	ds_read_b128 v[164:167], v223 offset:17408
	ds_read_b128 v[168:171], v223 offset:18432
	ds_read_b128 v[186:189], v223 offset:19456
	ds_read_b128 v[190:193], v223 offset:20480
	ds_read_b128 v[194:197], v223 offset:21504
	ds_read_b128 v[198:201], v223 offset:22528
	ds_read_b128 v[202:205], v223 offset:23552
	global_load_lds_dwordx4 v[206:207], off
	s_add_i32 m0, s49, 0x2000
	s_add_u32 s50, s30, 0x40000
	v_lshl_add_u64 v[208:209], s[30:31], 0, v[172:173]
	s_addc_u32 s51, s31, 0
	s_add_i32 s49, s41, s20
	global_load_lds_dwordx4 v[208:209], off
	v_lshl_add_u64 v[210:211], s[50:51], 0, v[174:175]
	s_mov_b32 m0, s49
	v_lshl_add_u64 v[212:213], s[34:35], 0, v[178:179]
	global_load_lds_dwordx4 v[210:211], off
	v_lshl_add_u64 v[210:211], s[50:51], 0, v[172:173]
	s_add_i32 m0, s49, 0x2000
	s_nop 0
	global_load_lds_dwordx4 v[210:211], off
	v_lshl_add_u64 v[210:211], s[34:35], 0, v[176:177]
	s_mov_b32 m0, s17
	s_nop 0
	global_load_lds_dwordx4 v[210:211], off
	s_mov_b32 m0, s22
	s_nop 0
	global_load_lds_dwordx4 v[212:213], off
	s_waitcnt vmcnt(8)
	s_waitcnt lgkmcnt(0)
	s_barrier
	s_setprio 0
	s_waitcnt lgkmcnt(0)
	v_mfma_f32_16x16x32_bf16 v[60:63], v[124:127], v[160:163], v[60:63]
	v_mfma_f32_16x16x32_bf16 v[52:55], v[136:139], v[160:163], v[52:55]
	v_mfma_f32_16x16x32_bf16 v[44:47], v[124:127], v[168:171], v[44:47]
	v_mfma_f32_16x16x32_bf16 v[36:39], v[136:139], v[168:171], v[36:39]
	v_mfma_f32_16x16x32_bf16 v[28:31], v[124:127], v[190:193], v[28:31]
	v_mfma_f32_16x16x32_bf16 v[24:27], v[136:139], v[190:193], v[24:27]
	v_mfma_f32_16x16x32_bf16 v[12:15], v[124:127], v[198:201], v[12:15]
	v_mfma_f32_16x16x32_bf16 v[8:11], v[136:139], v[198:201], v[8:11]
	v_mfma_f32_16x16x32_bf16 v[60:63], v[132:135], v[164:167], v[60:63]
	v_mfma_f32_16x16x32_bf16 v[52:55], v[140:143], v[164:167], v[52:55]
	v_mfma_f32_16x16x32_bf16 v[44:47], v[132:135], v[186:189], v[44:47]
	v_mfma_f32_16x16x32_bf16 v[36:39], v[140:143], v[186:189], v[36:39]
	v_mfma_f32_16x16x32_bf16 v[28:31], v[132:135], v[194:197], v[28:31]
	v_mfma_f32_16x16x32_bf16 v[24:27], v[140:143], v[194:197], v[24:27]
	v_mfma_f32_16x16x32_bf16 v[12:15], v[132:135], v[202:205], v[12:15]
	v_mfma_f32_16x16x32_bf16 v[8:11], v[140:143], v[202:205], v[8:11]
	s_setprio 1
	s_setprio 0
	v_mfma_f32_16x16x32_bf16 v[56:59], v[144:147], v[160:163], v[56:59]
	v_mfma_f32_16x16x32_bf16 v[48:51], v[152:155], v[160:163], v[48:51]
	v_mfma_f32_16x16x32_bf16 v[40:43], v[144:147], v[168:171], v[40:43]
	v_mfma_f32_16x16x32_bf16 v[32:35], v[152:155], v[168:171], v[32:35]
	v_mfma_f32_16x16x32_bf16 v[20:23], v[144:147], v[190:193], v[20:23]
	v_mfma_f32_16x16x32_bf16 v[16:19], v[152:155], v[190:193], v[16:19]
	v_mfma_f32_16x16x32_bf16 v[4:7], v[144:147], v[198:201], v[4:7]
	v_mfma_f32_16x16x32_bf16 v[0:3], v[152:155], v[198:201], v[0:3]
	v_mfma_f32_16x16x32_bf16 v[56:59], v[148:151], v[164:167], v[56:59]
	v_mfma_f32_16x16x32_bf16 v[48:51], v[156:159], v[164:167], v[48:51]
	v_mfma_f32_16x16x32_bf16 v[40:43], v[148:151], v[186:189], v[40:43]
	v_mfma_f32_16x16x32_bf16 v[32:35], v[156:159], v[186:189], v[32:35]
	v_mfma_f32_16x16x32_bf16 v[20:23], v[148:151], v[194:197], v[20:23]
	v_mfma_f32_16x16x32_bf16 v[16:19], v[156:159], v[194:197], v[16:19]
	v_mfma_f32_16x16x32_bf16 v[4:7], v[148:151], v[202:205], v[4:7]
	v_mfma_f32_16x16x32_bf16 v[0:3], v[156:159], v[202:205], v[0:3]
	s_setprio 1
	s_barrier
	s_add_i32 s49, 0, 0x18000
	s_add_i32 s50, 0, 0x1c000
	v_add_u32_e32 v140, s49, v219
	v_add_u32_e32 v156, s50, v219
	ds_read_b128 v[124:127], v140
	ds_read_b128 v[132:135], v140 offset:1024
	ds_read_b128 v[136:139], v140 offset:2048
	ds_read_b128 v[140:143], v140 offset:3072
	ds_read_b128 v[144:147], v156
	ds_read_b128 v[148:151], v156 offset:1024
	ds_read_b128 v[152:155], v156 offset:2048
	ds_read_b128 v[156:159], v156 offset:3072
	s_add_u32 s34, s34, 0x40000
	s_addc_u32 s35, s35, 0
	s_mov_b32 m0, s23
	v_lshl_add_u64 v[214:215], s[34:35], 0, v[176:177]
	ds_read_b128 v[160:163], v223 offset:32768
	ds_read_b128 v[164:167], v223 offset:33792
	ds_read_b128 v[168:171], v223 offset:34816
	ds_read_b128 v[186:189], v223 offset:35840
	ds_read_b128 v[190:193], v223 offset:36864
	ds_read_b128 v[194:197], v223 offset:37888
	ds_read_b128 v[198:201], v223 offset:38912
	ds_read_b128 v[202:205], v223 offset:39936
	global_load_lds_dwordx4 v[214:215], off
	v_lshl_add_u64 v[214:215], s[34:35], 0, v[178:179]
	s_mov_b32 m0, s33
	s_nop 0
	global_load_lds_dwordx4 v[214:215], off
	s_waitcnt vmcnt(8)
	s_waitcnt lgkmcnt(0)
	s_barrier
	s_setprio 0
	s_waitcnt lgkmcnt(0)
	v_mfma_f32_16x16x32_bf16 v[120:123], v[124:127], v[160:163], v[120:123]
	v_mfma_f32_16x16x32_bf16 v[128:131], v[136:139], v[160:163], v[128:131]
	v_mfma_f32_16x16x32_bf16 v[108:111], v[124:127], v[168:171], v[108:111]
	v_mfma_f32_16x16x32_bf16 v[104:107], v[136:139], v[168:171], v[104:107]
	v_mfma_f32_16x16x32_bf16 v[92:95], v[124:127], v[190:193], v[92:95]
	v_mfma_f32_16x16x32_bf16 v[88:91], v[136:139], v[190:193], v[88:91]
	v_mfma_f32_16x16x32_bf16 v[76:79], v[124:127], v[198:201], v[76:79]
	v_mfma_f32_16x16x32_bf16 v[72:75], v[136:139], v[198:201], v[72:75]
	v_mfma_f32_16x16x32_bf16 v[120:123], v[132:135], v[164:167], v[120:123]
	v_mfma_f32_16x16x32_bf16 v[128:131], v[140:143], v[164:167], v[128:131]
	v_mfma_f32_16x16x32_bf16 v[108:111], v[132:135], v[186:189], v[108:111]
	v_mfma_f32_16x16x32_bf16 v[104:107], v[140:143], v[186:189], v[104:107]
	v_mfma_f32_16x16x32_bf16 v[92:95], v[132:135], v[194:197], v[92:95]
	v_mfma_f32_16x16x32_bf16 v[88:91], v[140:143], v[194:197], v[88:91]
	v_mfma_f32_16x16x32_bf16 v[76:79], v[132:135], v[202:205], v[76:79]
	v_mfma_f32_16x16x32_bf16 v[72:75], v[140:143], v[202:205], v[72:75]
	s_setprio 1
	s_setprio 0
	v_mfma_f32_16x16x32_bf16 v[116:119], v[144:147], v[160:163], v[116:119]
	v_mfma_f32_16x16x32_bf16 v[112:115], v[152:155], v[160:163], v[112:115]
	v_mfma_f32_16x16x32_bf16 v[100:103], v[144:147], v[168:171], v[100:103]
	v_mfma_f32_16x16x32_bf16 v[96:99], v[152:155], v[168:171], v[96:99]
	v_mfma_f32_16x16x32_bf16 v[84:87], v[144:147], v[190:193], v[84:87]
	v_mfma_f32_16x16x32_bf16 v[80:83], v[152:155], v[190:193], v[80:83]
	v_mfma_f32_16x16x32_bf16 v[68:71], v[144:147], v[198:201], v[68:71]
	v_mfma_f32_16x16x32_bf16 v[64:67], v[152:155], v[198:201], v[64:67]
	v_mfma_f32_16x16x32_bf16 v[116:119], v[148:151], v[164:167], v[116:119]
	v_mfma_f32_16x16x32_bf16 v[112:115], v[156:159], v[164:167], v[112:115]
	v_mfma_f32_16x16x32_bf16 v[100:103], v[148:151], v[186:189], v[100:103]
	v_mfma_f32_16x16x32_bf16 v[96:99], v[156:159], v[186:189], v[96:99]
	v_mfma_f32_16x16x32_bf16 v[84:87], v[148:151], v[194:197], v[84:87]
	v_mfma_f32_16x16x32_bf16 v[80:83], v[156:159], v[194:197], v[80:83]
	v_mfma_f32_16x16x32_bf16 v[68:71], v[148:151], v[202:205], v[68:71]
	v_mfma_f32_16x16x32_bf16 v[64:67], v[156:159], v[202:205], v[64:67]
	s_setprio 1
	s_barrier
	s_add_i32 s34, s49, s20
	v_lshl_add_u64 v[206:207], v[206:207], 0, s[2:3]
	s_mov_b32 m0, s34
	ds_read_b128 v[160:163], v223 offset:49152
	ds_read_b128 v[164:167], v223 offset:50176
	ds_read_b128 v[168:171], v223 offset:51200
	ds_read_b128 v[186:189], v223 offset:52224
	ds_read_b128 v[190:193], v223 offset:53248
	ds_read_b128 v[194:197], v223 offset:54272
	ds_read_b128 v[198:201], v223 offset:55296
	ds_read_b128 v[202:205], v223 offset:56320
	global_load_lds_dwordx4 v[206:207], off
	s_add_i32 m0, s34, 0x2000
	s_add_u32 s30, s30, 0x40080
	v_lshl_add_u64 v[206:207], v[208:209], 0, s[2:3]
	s_addc_u32 s31, s31, 0
	s_add_i32 s34, s50, s20
	global_load_lds_dwordx4 v[206:207], off
	v_lshl_add_u64 v[206:207], s[30:31], 0, v[174:175]
	s_mov_b32 m0, s34
	s_nop 0
	global_load_lds_dwordx4 v[206:207], off
	v_lshl_add_u64 v[206:207], s[30:31], 0, v[172:173]
	s_add_i32 m0, s34, 0x2000
	s_nop 0
	global_load_lds_dwordx4 v[206:207], off
	v_lshl_add_u64 v[206:207], v[210:211], 0, s[2:3]
	s_mov_b32 m0, s37
	s_nop 0
	global_load_lds_dwordx4 v[206:207], off
	v_lshl_add_u64 v[206:207], v[212:213], 0, s[2:3]
	s_mov_b32 m0, s38
	s_nop 0
	global_load_lds_dwordx4 v[206:207], off
	s_waitcnt vmcnt(8)
	s_waitcnt lgkmcnt(0)
	s_barrier
	s_setprio 0
	s_waitcnt lgkmcnt(0)
	v_mfma_f32_16x16x32_bf16 v[60:63], v[124:127], v[160:163], v[60:63]
	v_mfma_f32_16x16x32_bf16 v[52:55], v[136:139], v[160:163], v[52:55]
	v_mfma_f32_16x16x32_bf16 v[44:47], v[124:127], v[168:171], v[44:47]
	v_mfma_f32_16x16x32_bf16 v[36:39], v[136:139], v[168:171], v[36:39]
	v_mfma_f32_16x16x32_bf16 v[28:31], v[124:127], v[190:193], v[28:31]
	v_mfma_f32_16x16x32_bf16 v[24:27], v[136:139], v[190:193], v[24:27]
	v_mfma_f32_16x16x32_bf16 v[12:15], v[124:127], v[198:201], v[12:15]
	v_mfma_f32_16x16x32_bf16 v[8:11], v[136:139], v[198:201], v[8:11]
	v_mfma_f32_16x16x32_bf16 v[60:63], v[132:135], v[164:167], v[60:63]
	v_mfma_f32_16x16x32_bf16 v[52:55], v[140:143], v[164:167], v[52:55]
	v_mfma_f32_16x16x32_bf16 v[44:47], v[132:135], v[186:189], v[44:47]
	v_mfma_f32_16x16x32_bf16 v[36:39], v[140:143], v[186:189], v[36:39]
	v_mfma_f32_16x16x32_bf16 v[28:31], v[132:135], v[194:197], v[28:31]
	v_mfma_f32_16x16x32_bf16 v[24:27], v[140:143], v[194:197], v[24:27]
	v_mfma_f32_16x16x32_bf16 v[12:15], v[132:135], v[202:205], v[12:15]
	v_mfma_f32_16x16x32_bf16 v[8:11], v[140:143], v[202:205], v[8:11]
	s_setprio 1
	s_setprio 0
	v_mfma_f32_16x16x32_bf16 v[56:59], v[144:147], v[160:163], v[56:59]
	v_mfma_f32_16x16x32_bf16 v[48:51], v[152:155], v[160:163], v[48:51]
	v_mfma_f32_16x16x32_bf16 v[40:43], v[144:147], v[168:171], v[40:43]
	v_mfma_f32_16x16x32_bf16 v[32:35], v[152:155], v[168:171], v[32:35]
	v_mfma_f32_16x16x32_bf16 v[20:23], v[144:147], v[190:193], v[20:23]
	v_mfma_f32_16x16x32_bf16 v[16:19], v[152:155], v[190:193], v[16:19]
	v_mfma_f32_16x16x32_bf16 v[4:7], v[144:147], v[198:201], v[4:7]
	v_mfma_f32_16x16x32_bf16 v[0:3], v[152:155], v[198:201], v[0:3]
	v_mfma_f32_16x16x32_bf16 v[56:59], v[148:151], v[164:167], v[56:59]
	v_mfma_f32_16x16x32_bf16 v[48:51], v[156:159], v[164:167], v[48:51]
	v_mfma_f32_16x16x32_bf16 v[40:43], v[148:151], v[186:189], v[40:43]
	v_mfma_f32_16x16x32_bf16 v[32:35], v[156:159], v[186:189], v[32:35]
	v_mfma_f32_16x16x32_bf16 v[20:23], v[148:151], v[194:197], v[20:23]
	v_mfma_f32_16x16x32_bf16 v[16:19], v[156:159], v[194:197], v[16:19]
	v_mfma_f32_16x16x32_bf16 v[4:7], v[148:151], v[202:205], v[4:7]
	v_mfma_f32_16x16x32_bf16 v[0:3], v[156:159], v[202:205], v[0:3]
	s_setprio 1
	s_barrier
	s_add_i32 s48, s48, 2
	s_add_u32 s28, s28, 0x100
	s_addc_u32 s29, s29, 0
	s_add_u32 s46, s46, 0x100
	s_addc_u32 s47, s47, 0
	s_cmp_gt_u32 s48, 13
	s_cbranch_scc0 .LBB0_1979
	s_and_b64 vcc, exec, s[4:5]
	s_cbranch_vccz .LBB0_1982
	s_barrier

.LBB0_2052:
	ds_read_b128 v[20:23], v188
	ds_read_b128 v[24:27], v189
	ds_read_b128 v[16:19], v183
	ds_read_b128 v[0:3], v184
	ds_read_b128 v[28:31], v190
	ds_read_b128 v[4:7], v191
	ds_read_b128 v[8:11], v192
	ds_read_b128 v[12:15], v193
	s_add_u32 s26, s24, 0xfffe0080
	s_addc_u32 s27, s25, -1
	s_cmp_eq_u32 s50, 4
	s_cselect_b32 s29, s9, s27
	s_cselect_b32 s28, s46, s26
	s_cselect_b32 s27, s7, s49
	s_cselect_b32 s26, s47, s48
	v_lshl_add_u64 v[228:229], s[24:25], 0, v[168:169]
	s_add_i32 m0, s17, 0xc000
	ds_read_b128 v[174:177], v200
	ds_read_b128 v[178:181], v200 offset:1024
	ds_read_b128 v[204:207], v200 offset:2048
	ds_read_b128 v[208:211], v200 offset:3072
	ds_read_b128 v[212:215], v200 offset:4096
	ds_read_b128 v[216:219], v200 offset:5120
	ds_read_b128 v[220:223], v200 offset:6144
	ds_read_b128 v[224:227], v200 offset:7168
	global_load_lds_dwordx4 v[228:229], off
	v_lshl_add_u64 v[228:229], s[24:25], 0, v[170:171]
	s_add_i32 m0, s17, 0xe000
	s_nop 0
	global_load_lds_dwordx4 v[228:229], off
	s_waitcnt vmcnt(8)
	s_waitcnt lgkmcnt(0)
	s_barrier
	s_setprio 0
	s_waitcnt lgkmcnt(0)
	v_mfma_f32_16x16x128_f8f6f4 v[156:159], v[16:23], v[174:181], v[156:159]
	v_mfma_f32_16x16x128_f8f6f4 v[152:155], v[24:31], v[174:181], v[152:155]
	v_mfma_f32_16x16x128_f8f6f4 v[144:147], v[16:23], v[204:211], v[144:147]
	v_mfma_f32_16x16x128_f8f6f4 v[136:139], v[24:31], v[204:211], v[136:139]
	v_mfma_f32_16x16x128_f8f6f4 v[128:131], v[16:23], v[212:219], v[128:131]
	v_mfma_f32_16x16x128_f8f6f4 v[120:123], v[24:31], v[212:219], v[120:123]
	v_mfma_f32_16x16x128_f8f6f4 v[112:115], v[16:23], v[220:227], v[112:115]
	v_mfma_f32_16x16x128_f8f6f4 v[104:107], v[24:31], v[220:227], v[104:107]
	s_setprio 1
	s_setprio 0
	v_mfma_f32_16x16x128_f8f6f4 v[148:151], v[0:7], v[174:181], v[148:151]
	v_mfma_f32_16x16x128_f8f6f4 v[140:143], v[8:15], v[174:181], v[140:143]
	v_mfma_f32_16x16x128_f8f6f4 v[132:135], v[0:7], v[204:211], v[132:135]
	v_mfma_f32_16x16x128_f8f6f4 v[124:127], v[8:15], v[204:211], v[124:127]
	v_mfma_f32_16x16x128_f8f6f4 v[116:119], v[0:7], v[212:219], v[116:119]
	v_mfma_f32_16x16x128_f8f6f4 v[108:111], v[8:15], v[212:219], v[108:111]
	v_mfma_f32_16x16x128_f8f6f4 v[92:95], v[0:7], v[220:227], v[92:95]
	v_mfma_f32_16x16x128_f8f6f4 v[88:91], v[8:15], v[220:227], v[88:91]
	s_setprio 1
	s_barrier
	s_mov_b32 m0, s22
	v_lshl_add_u64 v[174:175], s[26:27], 0, v[162:163]
	s_add_u32 s52, s26, 0x20000
	ds_read_b128 v[204:207], v200 offset:16384
	ds_read_b128 v[208:211], v200 offset:17408
	ds_read_b128 v[212:215], v200 offset:18432
	ds_read_b128 v[216:219], v200 offset:19456
	ds_read_b128 v[220:223], v200 offset:20480
	ds_read_b128 v[224:227], v200 offset:21504
	ds_read_b128 v[228:231], v200 offset:22528
	ds_read_b128 v[232:235], v200 offset:23552
	global_load_lds_dwordx4 v[174:175], off
	v_lshl_add_u64 v[176:177], s[26:27], 0, v[160:161]
	s_mov_b32 m0, s23
	s_addc_u32 s53, s27, 0
	global_load_lds_dwordx4 v[176:177], off
	v_lshl_add_u64 v[178:179], s[52:53], 0, v[162:163]
	s_mov_b32 m0, s30
	v_lshl_add_u64 v[180:181], s[28:29], 0, v[166:167]
	global_load_lds_dwordx4 v[178:179], off
	v_lshl_add_u64 v[178:179], s[52:53], 0, v[160:161]
	s_mov_b32 m0, s31
	s_nop 0
	global_load_lds_dwordx4 v[178:179], off
	v_lshl_add_u64 v[178:179], s[28:29], 0, v[164:165]
	s_mov_b32 m0, s17
	s_nop 0
	global_load_lds_dwordx4 v[178:179], off
	s_mov_b32 m0, s33
	s_nop 0
	global_load_lds_dwordx4 v[180:181], off
	s_waitcnt vmcnt(8)
	s_waitcnt lgkmcnt(0)
	s_barrier
	s_setprio 0
	s_waitcnt lgkmcnt(0)
	v_mfma_f32_16x16x128_f8f6f4 v[76:79], v[16:23], v[204:211], v[76:79]
	v_mfma_f32_16x16x128_f8f6f4 v[72:75], v[24:31], v[204:211], v[72:75]
	v_mfma_f32_16x16x128_f8f6f4 v[52:55], v[16:23], v[212:219], v[52:55]
	v_mfma_f32_16x16x128_f8f6f4 v[48:51], v[24:31], v[212:219], v[48:51]
	v_mfma_f32_16x16x128_f8f6f4 v[60:63], v[16:23], v[220:227], v[60:63]
	v_mfma_f32_16x16x128_f8f6f4 v[56:59], v[24:31], v[220:227], v[56:59]
	v_mfma_f32_16x16x128_f8f6f4 v[36:39], v[16:23], v[228:235], v[36:39]
	v_mfma_f32_16x16x128_f8f6f4 v[32:35], v[24:31], v[228:235], v[32:35]
	s_setprio 1
	s_setprio 0
	v_mfma_f32_16x16x128_f8f6f4 v[100:103], v[0:7], v[204:211], v[100:103]
	v_mfma_f32_16x16x128_f8f6f4 v[96:99], v[8:15], v[204:211], v[96:99]
	v_mfma_f32_16x16x128_f8f6f4 v[84:87], v[0:7], v[212:219], v[84:87]
	v_mfma_f32_16x16x128_f8f6f4 v[80:83], v[8:15], v[212:219], v[80:83]
	v_mfma_f32_16x16x128_f8f6f4 v[68:71], v[0:7], v[220:227], v[68:71]
	v_mfma_f32_16x16x128_f8f6f4 v[64:67], v[8:15], v[220:227], v[64:67]
	v_mfma_f32_16x16x128_f8f6f4 v[44:47], v[0:7], v[228:235], v[44:47]
	v_mfma_f32_16x16x128_f8f6f4 v[40:43], v[8:15], v[228:235], v[40:43]
	s_setprio 1
	s_barrier
	ds_read_b128 v[4:7], v194
	ds_read_b128 v[8:11], v195
	ds_read_b128 v[0:3], v185
	ds_read_b128 v[16:19], v186
	ds_read_b128 v[12:15], v196
	ds_read_b128 v[20:23], v197
	ds_read_b128 v[24:27], v198
	ds_read_b128 v[28:31], v199
	s_add_u32 s28, s28, 0x20000
	s_addc_u32 s29, s29, 0
	s_mov_b32 m0, s34
	v_lshl_add_u64 v[236:237], s[28:29], 0, v[164:165]
	ds_read_b128 v[204:207], v200 offset:32768
	ds_read_b128 v[208:211], v200 offset:33792
	ds_read_b128 v[212:215], v200 offset:34816
	ds_read_b128 v[216:219], v200 offset:35840
	ds_read_b128 v[220:223], v200 offset:36864
	ds_read_b128 v[224:227], v200 offset:37888
	ds_read_b128 v[228:231], v200 offset:38912
	ds_read_b128 v[232:235], v200 offset:39936
	global_load_lds_dwordx4 v[236:237], off
	v_lshl_add_u64 v[236:237], s[28:29], 0, v[166:167]
	s_mov_b32 m0, s35
	s_nop 0
	global_load_lds_dwordx4 v[236:237], off
	s_waitcnt vmcnt(8)
	s_waitcnt lgkmcnt(0)
	s_barrier
	s_setprio 0
	s_waitcnt lgkmcnt(0)
	v_mfma_f32_16x16x128_f8f6f4 v[156:159], v[0:7], v[204:211], v[156:159]
	v_mfma_f32_16x16x128_f8f6f4 v[152:155], v[8:15], v[204:211], v[152:155]
	v_mfma_f32_16x16x128_f8f6f4 v[144:147], v[0:7], v[212:219], v[144:147]
	v_mfma_f32_16x16x128_f8f6f4 v[136:139], v[8:15], v[212:219], v[136:139]
	v_mfma_f32_16x16x128_f8f6f4 v[128:131], v[0:7], v[220:227], v[128:131]
	v_mfma_f32_16x16x128_f8f6f4 v[120:123], v[8:15], v[220:227], v[120:123]
	v_mfma_f32_16x16x128_f8f6f4 v[112:115], v[0:7], v[228:235], v[112:115]
	v_mfma_f32_16x16x128_f8f6f4 v[104:107], v[8:15], v[228:235], v[104:107]
	s_setprio 1
	s_setprio 0
	v_mfma_f32_16x16x128_f8f6f4 v[148:151], v[16:23], v[204:211], v[148:151]
	v_mfma_f32_16x16x128_f8f6f4 v[140:143], v[24:31], v[204:211], v[140:143]
	v_mfma_f32_16x16x128_f8f6f4 v[132:135], v[16:23], v[212:219], v[132:135]
	v_mfma_f32_16x16x128_f8f6f4 v[124:127], v[24:31], v[212:219], v[124:127]
	v_mfma_f32_16x16x128_f8f6f4 v[116:119], v[16:23], v[220:227], v[116:119]
	v_mfma_f32_16x16x128_f8f6f4 v[108:111], v[24:31], v[220:227], v[108:111]
	v_mfma_f32_16x16x128_f8f6f4 v[92:95], v[16:23], v[228:235], v[92:95]
	v_mfma_f32_16x16x128_f8f6f4 v[88:91], v[24:31], v[228:235], v[88:91]
	s_setprio 1
	s_barrier
	s_mov_b32 m0, s37
	v_lshl_add_u64 v[174:175], v[174:175], 0, s[2:3]
	s_add_u32 s26, s26, 0x20080
	ds_read_b128 v[204:207], v200 offset:49152
	ds_read_b128 v[208:211], v200 offset:50176
	ds_read_b128 v[212:215], v200 offset:51200
	ds_read_b128 v[216:219], v200 offset:52224
	ds_read_b128 v[220:223], v200 offset:53248
	ds_read_b128 v[224:227], v200 offset:54272
	ds_read_b128 v[228:231], v200 offset:55296
	ds_read_b128 v[232:235], v200 offset:56320
	global_load_lds_dwordx4 v[174:175], off
	v_lshl_add_u64 v[174:175], v[176:177], 0, s[2:3]
	s_mov_b32 m0, s38
	s_addc_u32 s27, s27, 0
	global_load_lds_dwordx4 v[174:175], off
	v_lshl_add_u64 v[174:175], s[26:27], 0, v[162:163]
	s_mov_b32 m0, s41
	s_nop 0
	global_load_lds_dwordx4 v[174:175], off
	v_lshl_add_u64 v[174:175], s[26:27], 0, v[160:161]
	s_mov_b32 m0, s42
	s_nop 0
	global_load_lds_dwordx4 v[174:175], off
	v_lshl_add_u64 v[174:175], v[178:179], 0, s[2:3]
	s_mov_b32 m0, s39
	s_nop 0
	global_load_lds_dwordx4 v[174:175], off
	v_lshl_add_u64 v[174:175], v[180:181], 0, s[2:3]
	s_mov_b32 m0, s40
	s_nop 0
	global_load_lds_dwordx4 v[174:175], off
	s_waitcnt vmcnt(8)
	s_waitcnt lgkmcnt(0)
	s_barrier
	s_setprio 0
	s_waitcnt lgkmcnt(0)
	v_mfma_f32_16x16x128_f8f6f4 v[76:79], v[0:7], v[204:211], v[76:79]
	v_mfma_f32_16x16x128_f8f6f4 v[72:75], v[8:15], v[204:211], v[72:75]
	v_mfma_f32_16x16x128_f8f6f4 v[52:55], v[0:7], v[212:219], v[52:55]
	v_mfma_f32_16x16x128_f8f6f4 v[48:51], v[8:15], v[212:219], v[48:51]
	v_mfma_f32_16x16x128_f8f6f4 v[60:63], v[0:7], v[220:227], v[60:63]
	v_mfma_f32_16x16x128_f8f6f4 v[56:59], v[8:15], v[220:227], v[56:59]
	v_mfma_f32_16x16x128_f8f6f4 v[36:39], v[0:7], v[228:235], v[36:39]
	v_mfma_f32_16x16x128_f8f6f4 v[32:35], v[8:15], v[228:235], v[32:35]
	s_setprio 1
	s_setprio 0
	v_mfma_f32_16x16x128_f8f6f4 v[100:103], v[16:23], v[204:211], v[100:103]
	v_mfma_f32_16x16x128_f8f6f4 v[96:99], v[24:31], v[204:211], v[96:99]
	v_mfma_f32_16x16x128_f8f6f4 v[84:87], v[16:23], v[212:219], v[84:87]
	v_mfma_f32_16x16x128_f8f6f4 v[80:83], v[24:31], v[212:219], v[80:83]
	v_mfma_f32_16x16x128_f8f6f4 v[68:71], v[16:23], v[220:227], v[68:71]
	v_mfma_f32_16x16x128_f8f6f4 v[64:67], v[24:31], v[220:227], v[64:67]
	v_mfma_f32_16x16x128_f8f6f4 v[44:47], v[16:23], v[228:235], v[44:47]
	v_mfma_f32_16x16x128_f8f6f4 v[40:43], v[24:31], v[228:235], v[40:43]
	s_setprio 1
	s_barrier
	s_add_i32 s50, s50, 2
	s_add_u32 s24, s24, 0x100
	s_addc_u32 s25, s25, 0
	s_add_u32 s48, s48, 0x100
	s_addc_u32 s49, s49, 0
	s_cmp_gt_u32 s50, 5
	s_cbranch_scc0 .LBB0_2052
	s_nop 15
	s_nop 7
	s_and_b64 vcc, exec, s[4:5]
	s_cbranch_vccz .LBB0_2055
	s_barrier

.LBB0_2380:
	ds_read_b128 v[20:23], v217
	ds_read_b128 v[24:27], v218
	ds_read_b128 v[16:19], v213
	ds_read_b128 v[0:3], v214
	ds_read_b128 v[28:31], v219
	ds_read_b128 v[4:7], v220
	ds_read_b128 v[8:11], v221
	ds_read_b128 v[12:15], v222
	s_add_u32 s6, s2, 0xfffe0080
	s_addc_u32 s7, s3, -1
	s_cmp_eq_u32 s49, 4
	s_cselect_b32 s47, s1, s7
	s_cselect_b32 s46, s5, s6
	s_cselect_b32 s7, s33, s48
	s_cselect_b32 s6, s37, s39
	v_lshl_add_u64 v[210:211], s[2:3], 0, v[194:195]
	s_add_i32 m0, s55, 0xc000
	ds_read_b128 v[160:163], v229
	ds_read_b128 v[164:167], v229 offset:1024
	ds_read_b128 v[168:171], v229 offset:2048
	ds_read_b128 v[172:175], v229 offset:3072
	ds_read_b128 v[176:179], v229 offset:4096
	ds_read_b128 v[180:183], v229 offset:5120
	ds_read_b128 v[202:205], v229 offset:6144
	ds_read_b128 v[206:209], v229 offset:7168
	global_load_lds_dwordx4 v[210:211], off
	v_lshl_add_u64 v[210:211], s[2:3], 0, v[196:197]
	s_add_i32 m0, s55, 0xe000
	s_nop 0
	global_load_lds_dwordx4 v[210:211], off
	s_waitcnt vmcnt(8)
	s_waitcnt lgkmcnt(0)
	s_barrier
	s_setprio 0
	s_waitcnt lgkmcnt(0)
	v_mfma_f32_16x16x128_f8f6f4 v[156:159], v[16:23], v[160:167], v[156:159]
	v_mfma_f32_16x16x128_f8f6f4 v[152:155], v[24:31], v[160:167], v[152:155]
	v_mfma_f32_16x16x128_f8f6f4 v[140:143], v[16:23], v[168:175], v[140:143]
	v_mfma_f32_16x16x128_f8f6f4 v[136:139], v[24:31], v[168:175], v[136:139]
	v_mfma_f32_16x16x128_f8f6f4 v[124:127], v[16:23], v[176:183], v[124:127]
	v_mfma_f32_16x16x128_f8f6f4 v[120:123], v[24:31], v[176:183], v[120:123]
	v_mfma_f32_16x16x128_f8f6f4 v[108:111], v[16:23], v[202:209], v[108:111]
	v_mfma_f32_16x16x128_f8f6f4 v[104:107], v[24:31], v[202:209], v[104:107]
	s_setprio 1
	s_setprio 0
	v_mfma_f32_16x16x128_f8f6f4 v[148:151], v[0:7], v[160:167], v[148:151]
	v_mfma_f32_16x16x128_f8f6f4 v[144:147], v[8:15], v[160:167], v[144:147]
	v_mfma_f32_16x16x128_f8f6f4 v[132:135], v[0:7], v[168:175], v[132:135]
	v_mfma_f32_16x16x128_f8f6f4 v[128:131], v[8:15], v[168:175], v[128:131]
	v_mfma_f32_16x16x128_f8f6f4 v[116:119], v[0:7], v[176:183], v[116:119]
	v_mfma_f32_16x16x128_f8f6f4 v[112:115], v[8:15], v[176:183], v[112:115]
	v_mfma_f32_16x16x128_f8f6f4 v[100:103], v[0:7], v[202:209], v[100:103]
	v_mfma_f32_16x16x128_f8f6f4 v[96:99], v[8:15], v[202:209], v[96:99]
	s_setprio 1
	s_barrier
	s_mov_b32 m0, s56
	v_lshl_add_u64 v[160:161], s[6:7], 0, v[184:185]
	s_add_u32 s50, s6, 0x20000
	ds_read_b128 v[168:171], v229 offset:16384
	ds_read_b128 v[172:175], v229 offset:17408
	ds_read_b128 v[176:179], v229 offset:18432
	ds_read_b128 v[180:183], v229 offset:19456
	ds_read_b128 v[202:205], v229 offset:20480
	ds_read_b128 v[206:209], v229 offset:21504
	ds_read_b128 v[236:239], v229 offset:22528
	ds_read_b128 v[240:243], v229 offset:23552
	global_load_lds_dwordx4 v[160:161], off
	v_lshl_add_u64 v[162:163], s[6:7], 0, v[186:187]
	s_mov_b32 m0, s57
	s_addc_u32 s51, s7, 0
	global_load_lds_dwordx4 v[162:163], off
	v_lshl_add_u64 v[164:165], s[50:51], 0, v[184:185]
	s_mov_b32 m0, s58
	v_lshl_add_u64 v[166:167], s[46:47], 0, v[190:191]
	global_load_lds_dwordx4 v[164:165], off
	v_lshl_add_u64 v[164:165], s[50:51], 0, v[186:187]
	s_mov_b32 m0, s59
	s_nop 0
	global_load_lds_dwordx4 v[164:165], off
	v_lshl_add_u64 v[164:165], s[46:47], 0, v[188:189]
	s_mov_b32 m0, s55
	s_nop 0
	global_load_lds_dwordx4 v[164:165], off
	s_mov_b32 m0, s60
	s_nop 0
	global_load_lds_dwordx4 v[166:167], off
	s_waitcnt vmcnt(8)
	s_waitcnt lgkmcnt(0)
	s_barrier
	s_setprio 0
	s_waitcnt lgkmcnt(0)
	v_mfma_f32_16x16x128_f8f6f4 v[84:87], v[16:23], v[168:175], v[84:87]
	v_mfma_f32_16x16x128_f8f6f4 v[80:83], v[24:31], v[168:175], v[80:83]
	v_mfma_f32_16x16x128_f8f6f4 v[68:71], v[16:23], v[176:183], v[68:71]
	v_mfma_f32_16x16x128_f8f6f4 v[64:67], v[24:31], v[176:183], v[64:67]
	v_mfma_f32_16x16x128_f8f6f4 v[56:59], v[16:23], v[202:209], v[56:59]
	v_mfma_f32_16x16x128_f8f6f4 v[48:51], v[24:31], v[202:209], v[48:51]
	v_mfma_f32_16x16x128_f8f6f4 v[40:43], v[16:23], v[236:243], v[40:43]
	v_mfma_f32_16x16x128_f8f6f4 v[32:35], v[24:31], v[236:243], v[32:35]
	s_setprio 1
	s_setprio 0
	v_mfma_f32_16x16x128_f8f6f4 v[92:95], v[0:7], v[168:175], v[92:95]
	v_mfma_f32_16x16x128_f8f6f4 v[88:91], v[8:15], v[168:175], v[88:91]
	v_mfma_f32_16x16x128_f8f6f4 v[76:79], v[0:7], v[176:183], v[76:79]
	v_mfma_f32_16x16x128_f8f6f4 v[72:75], v[8:15], v[176:183], v[72:75]
	v_mfma_f32_16x16x128_f8f6f4 v[60:63], v[0:7], v[202:209], v[60:63]
	v_mfma_f32_16x16x128_f8f6f4 v[52:55], v[8:15], v[202:209], v[52:55]
	v_mfma_f32_16x16x128_f8f6f4 v[44:47], v[0:7], v[236:243], v[44:47]
	v_mfma_f32_16x16x128_f8f6f4 v[36:39], v[8:15], v[236:243], v[36:39]
	s_setprio 1
	s_barrier
	ds_read_b128 v[4:7], v223
	ds_read_b128 v[8:11], v224
	ds_read_b128 v[0:3], v215
	ds_read_b128 v[16:19], v216
	ds_read_b128 v[12:15], v225
	ds_read_b128 v[20:23], v226
	ds_read_b128 v[24:27], v227
	ds_read_b128 v[28:31], v228
	s_add_u32 s46, s46, 0x20000
	s_addc_u32 s47, s47, 0
	s_mov_b32 m0, s61
	v_lshl_add_u64 v[210:211], s[46:47], 0, v[188:189]
	ds_read_b128 v[168:171], v229 offset:32768
	ds_read_b128 v[172:175], v229 offset:33792
	ds_read_b128 v[176:179], v229 offset:34816
	ds_read_b128 v[180:183], v229 offset:35840
	ds_read_b128 v[202:205], v229 offset:36864
	ds_read_b128 v[206:209], v229 offset:37888
	ds_read_b128 v[236:239], v229 offset:38912
	ds_read_b128 v[240:243], v229 offset:39936
	global_load_lds_dwordx4 v[210:211], off
	v_lshl_add_u64 v[210:211], s[46:47], 0, v[190:191]
	s_mov_b32 m0, s62
	s_nop 0
	global_load_lds_dwordx4 v[210:211], off
	s_waitcnt vmcnt(8)
	s_waitcnt lgkmcnt(0)
	s_barrier
	s_setprio 0
	s_waitcnt lgkmcnt(0)
	v_mfma_f32_16x16x128_f8f6f4 v[156:159], v[0:7], v[168:175], v[156:159]
	v_mfma_f32_16x16x128_f8f6f4 v[152:155], v[8:15], v[168:175], v[152:155]
	v_mfma_f32_16x16x128_f8f6f4 v[140:143], v[0:7], v[176:183], v[140:143]
	v_mfma_f32_16x16x128_f8f6f4 v[136:139], v[8:15], v[176:183], v[136:139]
	v_mfma_f32_16x16x128_f8f6f4 v[124:127], v[0:7], v[202:209], v[124:127]
	v_mfma_f32_16x16x128_f8f6f4 v[120:123], v[8:15], v[202:209], v[120:123]
	v_mfma_f32_16x16x128_f8f6f4 v[108:111], v[0:7], v[236:243], v[108:111]
	v_mfma_f32_16x16x128_f8f6f4 v[104:107], v[8:15], v[236:243], v[104:107]
	s_setprio 1
	s_setprio 0
	v_mfma_f32_16x16x128_f8f6f4 v[148:151], v[16:23], v[168:175], v[148:151]
	v_mfma_f32_16x16x128_f8f6f4 v[144:147], v[24:31], v[168:175], v[144:147]
	v_mfma_f32_16x16x128_f8f6f4 v[132:135], v[16:23], v[176:183], v[132:135]
	v_mfma_f32_16x16x128_f8f6f4 v[128:131], v[24:31], v[176:183], v[128:131]
	v_mfma_f32_16x16x128_f8f6f4 v[116:119], v[16:23], v[202:209], v[116:119]
	v_mfma_f32_16x16x128_f8f6f4 v[112:115], v[24:31], v[202:209], v[112:115]
	v_mfma_f32_16x16x128_f8f6f4 v[100:103], v[16:23], v[236:243], v[100:103]
	v_mfma_f32_16x16x128_f8f6f4 v[96:99], v[24:31], v[236:243], v[96:99]
	s_setprio 1
	s_barrier
	s_mov_b32 m0, s67
	v_lshl_add_u64 v[160:161], v[160:161], 0, s[24:25]
	s_add_u32 s6, s6, 0x20080
	ds_read_b128 v[168:171], v229 offset:49152
	ds_read_b128 v[172:175], v229 offset:50176
	ds_read_b128 v[176:179], v229 offset:51200
	ds_read_b128 v[180:183], v229 offset:52224
	ds_read_b128 v[202:205], v229 offset:53248
	ds_read_b128 v[206:209], v229 offset:54272
	ds_read_b128 v[236:239], v229 offset:55296
	ds_read_b128 v[240:243], v229 offset:56320
	global_load_lds_dwordx4 v[160:161], off
	v_lshl_add_u64 v[160:161], v[162:163], 0, s[24:25]
	s_mov_b32 m0, s68
	s_addc_u32 s7, s7, 0
	global_load_lds_dwordx4 v[160:161], off
	v_lshl_add_u64 v[160:161], s[6:7], 0, v[184:185]
	s_mov_b32 m0, s71
	s_nop 0
	global_load_lds_dwordx4 v[160:161], off
	v_lshl_add_u64 v[160:161], s[6:7], 0, v[186:187]
	s_mov_b32 m0, s78
	s_nop 0
	global_load_lds_dwordx4 v[160:161], off
	v_lshl_add_u64 v[160:161], v[164:165], 0, s[24:25]
	s_mov_b32 m0, s69
	s_nop 0
	global_load_lds_dwordx4 v[160:161], off
	v_lshl_add_u64 v[160:161], v[166:167], 0, s[24:25]
	s_mov_b32 m0, s70
	s_nop 0
	global_load_lds_dwordx4 v[160:161], off
	s_waitcnt vmcnt(8)
	s_waitcnt lgkmcnt(0)
	s_barrier
	s_setprio 0
	s_waitcnt lgkmcnt(0)
	v_mfma_f32_16x16x128_f8f6f4 v[84:87], v[0:7], v[168:175], v[84:87]
	v_mfma_f32_16x16x128_f8f6f4 v[80:83], v[8:15], v[168:175], v[80:83]
	v_mfma_f32_16x16x128_f8f6f4 v[68:71], v[0:7], v[176:183], v[68:71]
	v_mfma_f32_16x16x128_f8f6f4 v[64:67], v[8:15], v[176:183], v[64:67]
	v_mfma_f32_16x16x128_f8f6f4 v[56:59], v[0:7], v[202:209], v[56:59]
	v_mfma_f32_16x16x128_f8f6f4 v[48:51], v[8:15], v[202:209], v[48:51]
	v_mfma_f32_16x16x128_f8f6f4 v[40:43], v[0:7], v[236:243], v[40:43]
	v_mfma_f32_16x16x128_f8f6f4 v[32:35], v[8:15], v[236:243], v[32:35]
	s_setprio 1
	s_setprio 0
	v_mfma_f32_16x16x128_f8f6f4 v[92:95], v[16:23], v[168:175], v[92:95]
	v_mfma_f32_16x16x128_f8f6f4 v[88:91], v[24:31], v[168:175], v[88:91]
	v_mfma_f32_16x16x128_f8f6f4 v[76:79], v[16:23], v[176:183], v[76:79]
	v_mfma_f32_16x16x128_f8f6f4 v[72:75], v[24:31], v[176:183], v[72:75]
	v_mfma_f32_16x16x128_f8f6f4 v[60:63], v[16:23], v[202:209], v[60:63]
	v_mfma_f32_16x16x128_f8f6f4 v[52:55], v[24:31], v[202:209], v[52:55]
	v_mfma_f32_16x16x128_f8f6f4 v[44:47], v[16:23], v[236:243], v[44:47]
	v_mfma_f32_16x16x128_f8f6f4 v[36:39], v[24:31], v[236:243], v[36:39]
	s_setprio 1
	s_barrier
	s_add_i32 s49, s49, 2
	s_add_u32 s2, s2, 0x100
	s_addc_u32 s3, s3, 0
	s_add_u32 s39, s39, 0x100
	s_addc_u32 s48, s48, 0
	s_cmp_gt_u32 s49, 5
	s_cbranch_scc0 .LBB0_2380
	s_nop 15
	s_nop 7
	s_and_b64 vcc, exec, s[26:27]
	s_cbranch_vccz .LBB0_2383
	s_barrier

.LBB0_2571:
	s_add_u32 s36, s90, s4
	s_addc_u32 s37, s91, s5
	s_add_u32 s73, s36, 0x21c00100
	s_addc_u32 s74, s37, 0
	s_cmpk_eq_i32 s4, 0x300
	v_lshl_add_u64 v[0:1], v[180:181], 0, s[4:5]
	s_cselect_b64 vcc, -1, 0
	v_cndmask_b32_e32 v183, v1, v167, vcc
	v_cndmask_b32_e32 v182, v0, v220, vcc
	ds_read_b128 v[8:11], v194
	ds_read_b128 v[12:15], v198
	ds_read_b128 v[24:27], v199
	ds_read_b128 v[28:31], v200
	ds_read_b128 v[0:3], v195
	ds_read_b128 v[4:7], v201
	ds_read_b128 v[16:19], v202
	ds_read_b128 v[20:23], v203
	s_and_b64 s[36:37], vcc, exec
	s_cselect_b32 s37, s9, s74
	s_cselect_b32 s36, s8, s73
	v_cndmask_b32_e32 v160, v219, v215, vcc
	v_cndmask_b32_e32 v184, v170, v216, vcc
	v_cndmask_b32_e32 v175, v172, v217, vcc
	v_cndmask_b32_e32 v173, v174, v218, vcc
	v_lshl_add_u64 v[186:187], v[178:179], 0, s[4:5]
	s_add_i32 m0, s0, 0xc000
	ds_read_b128 v[222:225], v212
	ds_read_b128 v[226:229], v212 offset:1024
	ds_read_b128 v[230:233], v212 offset:2048
	ds_read_b128 v[234:237], v212 offset:3072
	ds_read_b128 v[238:241], v212 offset:4096
	ds_read_b128 v[242:245], v212 offset:5120
	ds_read_b128 v[246:249], v212 offset:6144
	ds_read_b128 v[250:253], v212 offset:7168
	global_load_lds_dwordx4 v[186:187], off
	v_lshl_add_u64 v[186:187], v[176:177], 0, s[4:5]
	s_add_i32 m0, s0, 0xe000
	s_nop 0
	global_load_lds_dwordx4 v[186:187], off
	s_waitcnt vmcnt(8)
	s_waitcnt lgkmcnt(0)
	s_barrier
	s_setprio 0
	s_waitcnt lgkmcnt(0)
	v_mfma_f32_16x16x128_f8f6f4 v[156:159], v[8:15], v[222:229], v[156:159]
	v_mfma_f32_16x16x128_f8f6f4 v[152:155], v[24:31], v[222:229], v[152:155]
	v_mfma_f32_16x16x128_f8f6f4 v[140:143], v[8:15], v[230:237], v[140:143]
	v_mfma_f32_16x16x128_f8f6f4 v[136:139], v[24:31], v[230:237], v[136:139]
	v_mfma_f32_16x16x128_f8f6f4 v[124:127], v[8:15], v[238:245], v[124:127]
	v_mfma_f32_16x16x128_f8f6f4 v[120:123], v[24:31], v[238:245], v[120:123]
	v_mfma_f32_16x16x128_f8f6f4 v[108:111], v[8:15], v[246:253], v[108:111]
	v_mfma_f32_16x16x128_f8f6f4 v[104:107], v[24:31], v[246:253], v[104:107]
	s_setprio 1
	s_setprio 0
	v_mfma_f32_16x16x128_f8f6f4 v[148:151], v[0:7], v[222:229], v[148:151]
	v_mfma_f32_16x16x128_f8f6f4 v[144:147], v[16:23], v[222:229], v[144:147]
	v_mfma_f32_16x16x128_f8f6f4 v[132:135], v[0:7], v[230:237], v[132:135]
	v_mfma_f32_16x16x128_f8f6f4 v[128:131], v[16:23], v[230:237], v[128:131]
	v_mfma_f32_16x16x128_f8f6f4 v[116:119], v[0:7], v[238:245], v[116:119]
	v_mfma_f32_16x16x128_f8f6f4 v[112:115], v[16:23], v[238:245], v[112:115]
	v_mfma_f32_16x16x128_f8f6f4 v[100:103], v[0:7], v[246:253], v[100:103]
	v_mfma_f32_16x16x128_f8f6f4 v[96:99], v[16:23], v[246:253], v[96:99]
	s_setprio 1
	s_barrier
	s_mov_b32 m0, s40
	v_lshl_add_u64 v[186:187], v[182:183], 0, v[164:165]
	ds_read_b128 v[222:225], v212 offset:16384
	ds_read_b128 v[226:229], v212 offset:17408
	ds_read_b128 v[230:233], v212 offset:18432
	ds_read_b128 v[234:237], v212 offset:19456
	ds_read_b128 v[238:241], v212 offset:20480
	ds_read_b128 v[242:245], v212 offset:21504
	ds_read_b128 v[246:249], v212 offset:22528
	ds_read_b128 v[250:253], v212 offset:23552
	global_load_lds_dwordx4 v[186:187], off
	v_lshl_add_u64 v[188:189], v[182:183], 0, v[162:163]
	s_mov_b32 m0, s41
	v_lshl_add_u64 v[190:191], v[182:183], 0, s[12:13]
	global_load_lds_dwordx4 v[188:189], off
	v_lshl_add_u64 v[192:193], v[190:191], 0, v[164:165]
	s_mov_b32 m0, s42
	v_lshl_add_u64 v[190:191], v[190:191], 0, v[162:163]
	global_load_lds_dwordx4 v[192:193], off
	s_mov_b32 m0, s43
	v_mov_b32_e32 v185, v161
	global_load_lds_dwordx4 v[190:191], off
	s_mov_b32 m0, s0
	v_lshl_add_u64 v[190:191], s[36:37], 0, v[160:161]
	global_load_lds_dwordx4 v160, s[36:37]
	s_mov_b32 m0, s44
	s_nop 0
	global_load_lds_dwordx4 v184, s[36:37]
	s_waitcnt vmcnt(8)
	s_waitcnt lgkmcnt(0)
	v_lshl_add_u64 v[184:185], s[36:37], 0, v[184:185]
	s_barrier
	s_setprio 0
	s_waitcnt lgkmcnt(0)
	v_mfma_f32_16x16x128_f8f6f4 v[84:87], v[8:15], v[222:229], v[84:87]
	v_mfma_f32_16x16x128_f8f6f4 v[80:83], v[24:31], v[222:229], v[80:83]
	v_mfma_f32_16x16x128_f8f6f4 v[68:71], v[8:15], v[230:237], v[68:71]
	v_mfma_f32_16x16x128_f8f6f4 v[64:67], v[24:31], v[230:237], v[64:67]
	v_mfma_f32_16x16x128_f8f6f4 v[52:55], v[8:15], v[238:245], v[52:55]
	v_mfma_f32_16x16x128_f8f6f4 v[48:51], v[24:31], v[238:245], v[48:51]
	v_mfma_f32_16x16x128_f8f6f4 v[36:39], v[8:15], v[246:253], v[36:39]
	v_mfma_f32_16x16x128_f8f6f4 v[32:35], v[24:31], v[246:253], v[32:35]
	s_setprio 1
	s_setprio 0
	v_mfma_f32_16x16x128_f8f6f4 v[92:95], v[0:7], v[222:229], v[92:95]
	v_mfma_f32_16x16x128_f8f6f4 v[88:91], v[16:23], v[222:229], v[88:91]
	v_mfma_f32_16x16x128_f8f6f4 v[76:79], v[0:7], v[230:237], v[76:79]
	v_mfma_f32_16x16x128_f8f6f4 v[72:75], v[16:23], v[230:237], v[72:75]
	v_mfma_f32_16x16x128_f8f6f4 v[60:63], v[0:7], v[238:245], v[60:63]
	v_mfma_f32_16x16x128_f8f6f4 v[56:59], v[16:23], v[238:245], v[56:59]
	v_mfma_f32_16x16x128_f8f6f4 v[44:47], v[0:7], v[246:253], v[44:47]
	v_mfma_f32_16x16x128_f8f6f4 v[40:43], v[16:23], v[246:253], v[40:43]
	s_setprio 1
	s_barrier
	ds_read_b128 v[4:7], v204
	ds_read_b128 v[8:11], v205
	ds_read_b128 v[0:3], v196
	ds_read_b128 v[16:19], v197
	ds_read_b128 v[12:15], v206
	ds_read_b128 v[20:23], v207
	ds_read_b128 v[24:27], v208
	ds_read_b128 v[28:31], v209
	s_mov_b32 m0, s45
	ds_read_b128 v[222:225], v212 offset:32768
	ds_read_b128 v[226:229], v212 offset:33792
	ds_read_b128 v[230:233], v212 offset:34816
	ds_read_b128 v[234:237], v212 offset:35840
	ds_read_b128 v[238:241], v212 offset:36864
	ds_read_b128 v[242:245], v212 offset:37888
	ds_read_b128 v[246:249], v212 offset:38912
	ds_read_b128 v[250:253], v212 offset:39936
	global_load_lds_dwordx4 v175, s[36:37]
	s_mov_b32 m0, s46
	s_nop 0
	global_load_lds_dwordx4 v173, s[36:37]
	s_waitcnt vmcnt(8)
	s_waitcnt lgkmcnt(0)
	s_barrier
	s_setprio 0
	s_waitcnt lgkmcnt(0)
	v_mfma_f32_16x16x128_f8f6f4 v[156:159], v[0:7], v[222:229], v[156:159]
	v_mfma_f32_16x16x128_f8f6f4 v[152:155], v[8:15], v[222:229], v[152:155]
	v_mfma_f32_16x16x128_f8f6f4 v[140:143], v[0:7], v[230:237], v[140:143]
	v_mfma_f32_16x16x128_f8f6f4 v[136:139], v[8:15], v[230:237], v[136:139]
	v_mfma_f32_16x16x128_f8f6f4 v[124:127], v[0:7], v[238:245], v[124:127]
	v_mfma_f32_16x16x128_f8f6f4 v[120:123], v[8:15], v[238:245], v[120:123]
	v_mfma_f32_16x16x128_f8f6f4 v[108:111], v[0:7], v[246:253], v[108:111]
	v_mfma_f32_16x16x128_f8f6f4 v[104:107], v[8:15], v[246:253], v[104:107]
	s_setprio 1
	s_setprio 0
	v_mfma_f32_16x16x128_f8f6f4 v[148:151], v[16:23], v[222:229], v[148:151]
	v_mfma_f32_16x16x128_f8f6f4 v[144:147], v[24:31], v[222:229], v[144:147]
	v_mfma_f32_16x16x128_f8f6f4 v[132:135], v[16:23], v[230:237], v[132:135]
	v_mfma_f32_16x16x128_f8f6f4 v[128:131], v[24:31], v[230:237], v[128:131]
	v_mfma_f32_16x16x128_f8f6f4 v[116:119], v[16:23], v[238:245], v[116:119]
	v_mfma_f32_16x16x128_f8f6f4 v[112:115], v[24:31], v[238:245], v[112:115]
	v_mfma_f32_16x16x128_f8f6f4 v[100:103], v[16:23], v[246:253], v[100:103]
	v_mfma_f32_16x16x128_f8f6f4 v[96:99], v[24:31], v[246:253], v[96:99]
	s_setprio 1
	s_barrier
	s_mov_b32 m0, s47
	v_lshl_add_u64 v[186:187], v[186:187], 0, s[16:17]
	ds_read_b128 v[222:225], v212 offset:49152
	ds_read_b128 v[226:229], v212 offset:50176
	ds_read_b128 v[230:233], v212 offset:51200
	ds_read_b128 v[234:237], v212 offset:52224
	ds_read_b128 v[238:241], v212 offset:53248
	ds_read_b128 v[242:245], v212 offset:54272
	ds_read_b128 v[246:249], v212 offset:55296
	ds_read_b128 v[250:253], v212 offset:56320
	global_load_lds_dwordx4 v[186:187], off
	v_lshl_add_u64 v[186:187], v[188:189], 0, s[16:17]
	s_mov_b32 m0, s48
	v_lshl_add_u64 v[182:183], v[182:183], 0, s[26:27]
	global_load_lds_dwordx4 v[186:187], off
	v_lshl_add_u64 v[186:187], v[182:183], 0, v[164:165]
	s_mov_b32 m0, s51
	v_lshl_add_u64 v[182:183], v[182:183], 0, v[162:163]
	global_load_lds_dwordx4 v[186:187], off
	s_mov_b32 m0, s52
	s_nop 0
	global_load_lds_dwordx4 v[182:183], off
	v_lshl_add_u64 v[182:183], v[190:191], 0, s[16:17]
	s_mov_b32 m0, s49
	s_nop 0
	global_load_lds_dwordx4 v[182:183], off
	v_lshl_add_u64 v[182:183], v[184:185], 0, s[16:17]
	s_mov_b32 m0, s50
	s_nop 0
	global_load_lds_dwordx4 v[182:183], off
	s_waitcnt vmcnt(8)
	s_waitcnt lgkmcnt(0)
	s_barrier
	s_setprio 0
	s_waitcnt lgkmcnt(0)
	v_mfma_f32_16x16x128_f8f6f4 v[84:87], v[0:7], v[222:229], v[84:87]
	v_mfma_f32_16x16x128_f8f6f4 v[80:83], v[8:15], v[222:229], v[80:83]
	v_mfma_f32_16x16x128_f8f6f4 v[68:71], v[0:7], v[230:237], v[68:71]
	v_mfma_f32_16x16x128_f8f6f4 v[64:67], v[8:15], v[230:237], v[64:67]
	v_mfma_f32_16x16x128_f8f6f4 v[52:55], v[0:7], v[238:245], v[52:55]
	v_mfma_f32_16x16x128_f8f6f4 v[48:51], v[8:15], v[238:245], v[48:51]
	v_mfma_f32_16x16x128_f8f6f4 v[36:39], v[0:7], v[246:253], v[36:39]
	v_mfma_f32_16x16x128_f8f6f4 v[32:35], v[8:15], v[246:253], v[32:35]
	s_setprio 1
	s_setprio 0
	v_mfma_f32_16x16x128_f8f6f4 v[92:95], v[16:23], v[222:229], v[92:95]
	v_mfma_f32_16x16x128_f8f6f4 v[88:91], v[24:31], v[222:229], v[88:91]
	v_mfma_f32_16x16x128_f8f6f4 v[76:79], v[16:23], v[230:237], v[76:79]
	v_mfma_f32_16x16x128_f8f6f4 v[72:75], v[24:31], v[230:237], v[72:75]
	v_mfma_f32_16x16x128_f8f6f4 v[60:63], v[16:23], v[238:245], v[60:63]
	v_mfma_f32_16x16x128_f8f6f4 v[56:59], v[24:31], v[238:245], v[56:59]
	v_mfma_f32_16x16x128_f8f6f4 v[44:47], v[16:23], v[246:253], v[44:47]
	v_mfma_f32_16x16x128_f8f6f4 v[40:43], v[24:31], v[246:253], v[40:43]
	s_setprio 1
	s_barrier
	s_add_i32 s35, s35, 2
	s_add_u32 s4, s4, 0x100
	s_addc_u32 s5, s5, 0
	s_cmp_gt_u32 s35, 5
	s_cbranch_scc0 .LBB0_2571
	s_nop 15
	s_nop 7
	s_and_b64 vcc, exec, s[28:29]
	s_cbranch_vccz .LBB0_2574
	s_barrier

.LBB0_2588:
	s_add_u32 s42, s28, s36
	s_addc_u32 s43, s29, s37
	s_add_u32 s40, s42, 0x100
	s_addc_u32 s41, s43, 0
	s_and_b64 s[38:39], s[34:35], exec
	s_cselect_b32 s39, s13, s41
	s_cselect_b32 s38, s61, s40
	s_add_u32 s36, s26, s36
	s_addc_u32 s37, s27, s37
	s_add_u32 s36, s36, 0x100
	s_addc_u32 s37, s37, 0
	s_and_b64 s[34:35], s[34:35], exec
	s_cselect_b32 s41, s15, s37
	s_cselect_b32 s40, s62, s36
	s_add_u32 s44, s42, 0x10080
	ds_read_b128 v[146:149], v143
	ds_read_b128 v[150:153], v143 offset:1024
	ds_read_b128 v[154:157], v143 offset:2048
	ds_read_b128 v[158:161], v143 offset:3072
	ds_read_b128 v[162:165], v144
	ds_read_b128 v[166:169], v144 offset:1024
	ds_read_b128 v[170:173], v144 offset:2048
	ds_read_b128 v[174:177], v144 offset:3072
	s_addc_u32 s45, s43, 0
	s_add_i32 s72, s0, s51
	s_add_i32 m0, s52, 0xc000
	s_add_i32 s73, s52, 0xe000
	s_add_i32 s69, s72, 0x2000
	s_add_u32 s42, s40, 0x10000
	s_addc_u32 s43, s41, 0
	s_add_i32 s71, s58, s51
	s_add_i32 s70, s71, 0x2000
	s_add_i32 s68, 0, 0x18000
	s_add_i32 s67, 0, 0x1c000
	s_add_u32 s36, s38, 0x10000
	s_addc_u32 s37, s39, 0
	s_add_i32 s66, s68, s51
	s_add_i32 s64, s66, 0x2000
	s_add_u32 s34, s40, 0x10080
	s_addc_u32 s35, s41, 0
	s_add_i32 s65, s67, s51
	s_add_i32 s63, s65, 0x2000
	v_lshl_add_u64 v[138:139], s[44:45], 0, v[132:133]
	ds_read_b128 v[178:181], v145
	ds_read_b128 v[182:185], v145 offset:1024
	ds_read_b128 v[186:189], v145 offset:2048
	ds_read_b128 v[190:193], v145 offset:3072
	ds_read_b128 v[194:197], v145 offset:4096
	ds_read_b128 v[198:201], v145 offset:5120
	ds_read_b128 v[202:205], v145 offset:6144
	ds_read_b128 v[206:209], v145 offset:7168
	global_load_lds_dwordx4 v[138:139], off
	v_lshl_add_u64 v[138:139], s[44:45], 0, v[134:135]
	s_mov_b32 m0, s73
	s_nop 0
	global_load_lds_dwordx4 v[138:139], off
	s_waitcnt vmcnt(8)
	s_waitcnt lgkmcnt(0)
	s_barrier
	s_setprio 0
	s_waitcnt lgkmcnt(0)
	v_mfma_f32_16x16x32_bf16 v[124:127], v[146:149], v[178:181], v[124:127]
	v_mfma_f32_16x16x32_bf16 v[120:123], v[154:157], v[178:181], v[120:123]
	v_mfma_f32_16x16x32_bf16 v[116:119], v[146:149], v[186:189], v[116:119]
	v_mfma_f32_16x16x32_bf16 v[108:111], v[154:157], v[186:189], v[108:111]
	v_mfma_f32_16x16x32_bf16 v[100:103], v[146:149], v[194:197], v[100:103]
	v_mfma_f32_16x16x32_bf16 v[92:95], v[154:157], v[194:197], v[92:95]
	v_mfma_f32_16x16x32_bf16 v[84:87], v[146:149], v[202:205], v[84:87]
	v_mfma_f32_16x16x32_bf16 v[76:79], v[154:157], v[202:205], v[76:79]
	v_mfma_f32_16x16x32_bf16 v[124:127], v[150:153], v[182:185], v[124:127]
	v_mfma_f32_16x16x32_bf16 v[120:123], v[158:161], v[182:185], v[120:123]
	v_mfma_f32_16x16x32_bf16 v[116:119], v[150:153], v[190:193], v[116:119]
	v_mfma_f32_16x16x32_bf16 v[108:111], v[158:161], v[190:193], v[108:111]
	v_mfma_f32_16x16x32_bf16 v[100:103], v[150:153], v[198:201], v[100:103]
	v_mfma_f32_16x16x32_bf16 v[92:95], v[158:161], v[198:201], v[92:95]
	v_mfma_f32_16x16x32_bf16 v[84:87], v[150:153], v[206:209], v[84:87]
	v_mfma_f32_16x16x32_bf16 v[76:79], v[158:161], v[206:209], v[76:79]
	s_setprio 1
	s_setprio 0
	v_mfma_f32_16x16x32_bf16 v[112:115], v[162:165], v[178:181], v[112:115]
	v_mfma_f32_16x16x32_bf16 v[104:107], v[170:173], v[178:181], v[104:107]
	v_mfma_f32_16x16x32_bf16 v[96:99], v[162:165], v[186:189], v[96:99]
	v_mfma_f32_16x16x32_bf16 v[88:91], v[170:173], v[186:189], v[88:91]
	v_mfma_f32_16x16x32_bf16 v[80:83], v[162:165], v[194:197], v[80:83]
	v_mfma_f32_16x16x32_bf16 v[72:75], v[170:173], v[194:197], v[72:75]
	v_mfma_f32_16x16x32_bf16 v[52:55], v[162:165], v[202:205], v[52:55]
	v_mfma_f32_16x16x32_bf16 v[48:51], v[170:173], v[202:205], v[48:51]
	v_mfma_f32_16x16x32_bf16 v[112:115], v[166:169], v[182:185], v[112:115]
	v_mfma_f32_16x16x32_bf16 v[104:107], v[174:177], v[182:185], v[104:107]
	v_mfma_f32_16x16x32_bf16 v[96:99], v[166:169], v[190:193], v[96:99]
	v_mfma_f32_16x16x32_bf16 v[88:91], v[174:177], v[190:193], v[88:91]
	v_mfma_f32_16x16x32_bf16 v[80:83], v[166:169], v[198:201], v[80:83]
	v_mfma_f32_16x16x32_bf16 v[72:75], v[174:177], v[198:201], v[72:75]
	v_mfma_f32_16x16x32_bf16 v[52:55], v[166:169], v[206:209], v[52:55]
	v_mfma_f32_16x16x32_bf16 v[48:51], v[174:177], v[206:209], v[48:51]
	s_setprio 1
	s_barrier
	s_mov_b32 m0, s72
	v_lshl_add_u64 v[138:139], s[40:41], 0, v[130:131]
	ds_read_b128 v[178:181], v145 offset:16384
	ds_read_b128 v[182:185], v145 offset:17408
	ds_read_b128 v[186:189], v145 offset:18432
	ds_read_b128 v[190:193], v145 offset:19456
	ds_read_b128 v[194:197], v145 offset:20480
	ds_read_b128 v[198:201], v145 offset:21504
	ds_read_b128 v[202:205], v145 offset:22528
	ds_read_b128 v[206:209], v145 offset:23552
	global_load_lds_dwordx4 v[138:139], off
	v_lshl_add_u64 v[210:211], s[40:41], 0, v[128:129]
	s_mov_b32 m0, s69
	v_lshl_add_u64 v[212:213], s[42:43], 0, v[130:131]
	global_load_lds_dwordx4 v[210:211], off
	s_mov_b32 m0, s71
	v_lshl_add_u64 v[214:215], s[38:39], 0, v[134:135]
	global_load_lds_dwordx4 v[212:213], off
	v_lshl_add_u64 v[212:213], s[42:43], 0, v[128:129]
	s_mov_b32 m0, s70
	s_nop 0
	global_load_lds_dwordx4 v[212:213], off
	v_lshl_add_u64 v[212:213], s[38:39], 0, v[132:133]
	s_mov_b32 m0, s52
	s_nop 0
	global_load_lds_dwordx4 v[212:213], off
	s_mov_b32 m0, s53
	s_nop 0
	global_load_lds_dwordx4 v[214:215], off
	s_waitcnt vmcnt(8)
	s_waitcnt lgkmcnt(0)
	s_barrier
	s_setprio 0
	s_waitcnt lgkmcnt(0)
	v_mfma_f32_16x16x32_bf16 v[44:47], v[146:149], v[178:181], v[44:47]
	v_mfma_f32_16x16x32_bf16 v[32:35], v[154:157], v[178:181], v[32:35]
	v_mfma_f32_16x16x32_bf16 v[4:7], v[146:149], v[186:189], v[4:7]
	v_mfma_f32_16x16x32_bf16 v[0:3], v[154:157], v[186:189], v[0:3]
	v_mfma_f32_16x16x32_bf16 v[28:31], v[146:149], v[194:197], v[28:31]
	v_mfma_f32_16x16x32_bf16 v[24:27], v[154:157], v[194:197], v[24:27]
	v_mfma_f32_16x16x32_bf16 v[12:15], v[146:149], v[202:205], v[12:15]
	v_mfma_f32_16x16x32_bf16 v[8:11], v[154:157], v[202:205], v[8:11]
	v_mfma_f32_16x16x32_bf16 v[44:47], v[150:153], v[182:185], v[44:47]
	v_mfma_f32_16x16x32_bf16 v[32:35], v[158:161], v[182:185], v[32:35]
	v_mfma_f32_16x16x32_bf16 v[4:7], v[150:153], v[190:193], v[4:7]
	v_mfma_f32_16x16x32_bf16 v[0:3], v[158:161], v[190:193], v[0:3]
	v_mfma_f32_16x16x32_bf16 v[28:31], v[150:153], v[198:201], v[28:31]
	v_mfma_f32_16x16x32_bf16 v[24:27], v[158:161], v[198:201], v[24:27]
	v_mfma_f32_16x16x32_bf16 v[12:15], v[150:153], v[206:209], v[12:15]
	v_mfma_f32_16x16x32_bf16 v[8:11], v[158:161], v[206:209], v[8:11]
	s_setprio 1
	s_setprio 0
	v_mfma_f32_16x16x32_bf16 v[68:71], v[162:165], v[178:181], v[68:71]
	v_mfma_f32_16x16x32_bf16 v[64:67], v[170:173], v[178:181], v[64:67]
	v_mfma_f32_16x16x32_bf16 v[60:63], v[162:165], v[186:189], v[60:63]
	v_mfma_f32_16x16x32_bf16 v[56:59], v[170:173], v[186:189], v[56:59]
	v_mfma_f32_16x16x32_bf16 v[40:43], v[162:165], v[194:197], v[40:43]
	v_mfma_f32_16x16x32_bf16 v[36:39], v[170:173], v[194:197], v[36:39]
	v_mfma_f32_16x16x32_bf16 v[20:23], v[162:165], v[202:205], v[20:23]
	v_mfma_f32_16x16x32_bf16 v[16:19], v[170:173], v[202:205], v[16:19]
	v_mfma_f32_16x16x32_bf16 v[68:71], v[166:169], v[182:185], v[68:71]
	v_mfma_f32_16x16x32_bf16 v[64:67], v[174:177], v[182:185], v[64:67]
	v_mfma_f32_16x16x32_bf16 v[60:63], v[166:169], v[190:193], v[60:63]
	v_mfma_f32_16x16x32_bf16 v[56:59], v[174:177], v[190:193], v[56:59]
	v_mfma_f32_16x16x32_bf16 v[40:43], v[166:169], v[198:201], v[40:43]
	v_mfma_f32_16x16x32_bf16 v[36:39], v[174:177], v[198:201], v[36:39]
	v_mfma_f32_16x16x32_bf16 v[20:23], v[166:169], v[206:209], v[20:23]
	v_mfma_f32_16x16x32_bf16 v[16:19], v[174:177], v[206:209], v[16:19]
	s_setprio 1
	s_barrier
	v_add_u32_e32 v158, s68, v141
	v_add_u32_e32 v174, s67, v141
	ds_read_b128 v[146:149], v158
	ds_read_b128 v[150:153], v158 offset:1024
	ds_read_b128 v[154:157], v158 offset:2048
	ds_read_b128 v[158:161], v158 offset:3072
	ds_read_b128 v[162:165], v174
	ds_read_b128 v[166:169], v174 offset:1024
	ds_read_b128 v[170:173], v174 offset:2048
	ds_read_b128 v[174:177], v174 offset:3072
	s_mov_b32 m0, s54
	v_lshl_add_u64 v[216:217], s[36:37], 0, v[132:133]
	ds_read_b128 v[178:181], v145 offset:32768
	ds_read_b128 v[182:185], v145 offset:33792
	ds_read_b128 v[186:189], v145 offset:34816
	ds_read_b128 v[190:193], v145 offset:35840
	ds_read_b128 v[194:197], v145 offset:36864
	ds_read_b128 v[198:201], v145 offset:37888
	ds_read_b128 v[202:205], v145 offset:38912
	ds_read_b128 v[206:209], v145 offset:39936
	global_load_lds_dwordx4 v[216:217], off
	v_lshl_add_u64 v[216:217], s[36:37], 0, v[134:135]
	s_mov_b32 m0, s55
	s_nop 0
	global_load_lds_dwordx4 v[216:217], off
	s_waitcnt vmcnt(8)
	s_waitcnt lgkmcnt(0)
	s_barrier
	s_setprio 0
	s_waitcnt lgkmcnt(0)
	v_mfma_f32_16x16x32_bf16 v[124:127], v[146:149], v[178:181], v[124:127]
	v_mfma_f32_16x16x32_bf16 v[120:123], v[154:157], v[178:181], v[120:123]
	v_mfma_f32_16x16x32_bf16 v[116:119], v[146:149], v[186:189], v[116:119]
	v_mfma_f32_16x16x32_bf16 v[108:111], v[154:157], v[186:189], v[108:111]
	v_mfma_f32_16x16x32_bf16 v[100:103], v[146:149], v[194:197], v[100:103]
	v_mfma_f32_16x16x32_bf16 v[92:95], v[154:157], v[194:197], v[92:95]
	v_mfma_f32_16x16x32_bf16 v[84:87], v[146:149], v[202:205], v[84:87]
	v_mfma_f32_16x16x32_bf16 v[76:79], v[154:157], v[202:205], v[76:79]
	v_mfma_f32_16x16x32_bf16 v[124:127], v[150:153], v[182:185], v[124:127]
	v_mfma_f32_16x16x32_bf16 v[120:123], v[158:161], v[182:185], v[120:123]
	v_mfma_f32_16x16x32_bf16 v[116:119], v[150:153], v[190:193], v[116:119]
	v_mfma_f32_16x16x32_bf16 v[108:111], v[158:161], v[190:193], v[108:111]
	v_mfma_f32_16x16x32_bf16 v[100:103], v[150:153], v[198:201], v[100:103]
	v_mfma_f32_16x16x32_bf16 v[92:95], v[158:161], v[198:201], v[92:95]
	v_mfma_f32_16x16x32_bf16 v[84:87], v[150:153], v[206:209], v[84:87]
	v_mfma_f32_16x16x32_bf16 v[76:79], v[158:161], v[206:209], v[76:79]
	s_setprio 1
	s_setprio 0
	v_mfma_f32_16x16x32_bf16 v[112:115], v[162:165], v[178:181], v[112:115]
	v_mfma_f32_16x16x32_bf16 v[104:107], v[170:173], v[178:181], v[104:107]
	v_mfma_f32_16x16x32_bf16 v[96:99], v[162:165], v[186:189], v[96:99]
	v_mfma_f32_16x16x32_bf16 v[88:91], v[170:173], v[186:189], v[88:91]
	v_mfma_f32_16x16x32_bf16 v[80:83], v[162:165], v[194:197], v[80:83]
	v_mfma_f32_16x16x32_bf16 v[72:75], v[170:173], v[194:197], v[72:75]
	v_mfma_f32_16x16x32_bf16 v[52:55], v[162:165], v[202:205], v[52:55]
	v_mfma_f32_16x16x32_bf16 v[48:51], v[170:173], v[202:205], v[48:51]
	v_mfma_f32_16x16x32_bf16 v[112:115], v[166:169], v[182:185], v[112:115]
	v_mfma_f32_16x16x32_bf16 v[104:107], v[174:177], v[182:185], v[104:107]
	v_mfma_f32_16x16x32_bf16 v[96:99], v[166:169], v[190:193], v[96:99]
	v_mfma_f32_16x16x32_bf16 v[88:91], v[174:177], v[190:193], v[88:91]
	v_mfma_f32_16x16x32_bf16 v[80:83], v[166:169], v[198:201], v[80:83]
	v_mfma_f32_16x16x32_bf16 v[72:75], v[174:177], v[198:201], v[72:75]
	v_mfma_f32_16x16x32_bf16 v[52:55], v[166:169], v[206:209], v[52:55]
	v_mfma_f32_16x16x32_bf16 v[48:51], v[174:177], v[206:209], v[48:51]
	s_setprio 1
	s_barrier
	s_mov_b32 m0, s66
	v_lshl_add_u64 v[138:139], v[138:139], 0, s[8:9]
	ds_read_b128 v[178:181], v145 offset:49152
	ds_read_b128 v[182:185], v145 offset:50176
	ds_read_b128 v[186:189], v145 offset:51200
	ds_read_b128 v[190:193], v145 offset:52224
	ds_read_b128 v[194:197], v145 offset:53248
	ds_read_b128 v[198:201], v145 offset:54272
	ds_read_b128 v[202:205], v145 offset:55296
	ds_read_b128 v[206:209], v145 offset:56320
	global_load_lds_dwordx4 v[138:139], off
	v_lshl_add_u64 v[138:139], v[210:211], 0, s[8:9]
	s_mov_b32 m0, s64
	s_nop 0
	global_load_lds_dwordx4 v[138:139], off
	v_lshl_add_u64 v[138:139], s[34:35], 0, v[130:131]
	s_mov_b32 m0, s65
	s_nop 0
	global_load_lds_dwordx4 v[138:139], off
	v_lshl_add_u64 v[138:139], s[34:35], 0, v[128:129]
	s_mov_b32 m0, s63
	s_nop 0
	global_load_lds_dwordx4 v[138:139], off
	v_lshl_add_u64 v[138:139], v[212:213], 0, s[8:9]
	s_mov_b32 m0, s56
	s_nop 0
	global_load_lds_dwordx4 v[138:139], off
	v_lshl_add_u64 v[138:139], v[214:215], 0, s[8:9]
	s_mov_b32 m0, s57
	s_nop 0
	global_load_lds_dwordx4 v[138:139], off
	s_waitcnt vmcnt(8)
	s_waitcnt lgkmcnt(0)
	s_barrier
	s_setprio 0
	s_waitcnt lgkmcnt(0)
	v_mfma_f32_16x16x32_bf16 v[44:47], v[146:149], v[178:181], v[44:47]
	v_mfma_f32_16x16x32_bf16 v[32:35], v[154:157], v[178:181], v[32:35]
	v_mfma_f32_16x16x32_bf16 v[4:7], v[146:149], v[186:189], v[4:7]
	v_mfma_f32_16x16x32_bf16 v[0:3], v[154:157], v[186:189], v[0:3]
	v_mfma_f32_16x16x32_bf16 v[28:31], v[146:149], v[194:197], v[28:31]
	v_mfma_f32_16x16x32_bf16 v[24:27], v[154:157], v[194:197], v[24:27]
	v_mfma_f32_16x16x32_bf16 v[12:15], v[146:149], v[202:205], v[12:15]
	v_mfma_f32_16x16x32_bf16 v[8:11], v[154:157], v[202:205], v[8:11]
	v_mfma_f32_16x16x32_bf16 v[44:47], v[150:153], v[182:185], v[44:47]
	v_mfma_f32_16x16x32_bf16 v[32:35], v[158:161], v[182:185], v[32:35]
	v_mfma_f32_16x16x32_bf16 v[4:7], v[150:153], v[190:193], v[4:7]
	v_mfma_f32_16x16x32_bf16 v[0:3], v[158:161], v[190:193], v[0:3]
	v_mfma_f32_16x16x32_bf16 v[28:31], v[150:153], v[198:201], v[28:31]
	v_mfma_f32_16x16x32_bf16 v[24:27], v[158:161], v[198:201], v[24:27]
	v_mfma_f32_16x16x32_bf16 v[12:15], v[150:153], v[206:209], v[12:15]
	v_mfma_f32_16x16x32_bf16 v[8:11], v[158:161], v[206:209], v[8:11]
	s_setprio 1
	s_setprio 0
	v_mfma_f32_16x16x32_bf16 v[68:71], v[162:165], v[178:181], v[68:71]
	v_mfma_f32_16x16x32_bf16 v[64:67], v[170:173], v[178:181], v[64:67]
	v_mfma_f32_16x16x32_bf16 v[60:63], v[162:165], v[186:189], v[60:63]
	v_mfma_f32_16x16x32_bf16 v[56:59], v[170:173], v[186:189], v[56:59]
	v_mfma_f32_16x16x32_bf16 v[40:43], v[162:165], v[194:197], v[40:43]
	v_mfma_f32_16x16x32_bf16 v[36:39], v[170:173], v[194:197], v[36:39]
	v_mfma_f32_16x16x32_bf16 v[20:23], v[162:165], v[202:205], v[20:23]
	v_mfma_f32_16x16x32_bf16 v[16:19], v[170:173], v[202:205], v[16:19]
	v_mfma_f32_16x16x32_bf16 v[68:71], v[166:169], v[182:185], v[68:71]
	v_mfma_f32_16x16x32_bf16 v[64:67], v[174:177], v[182:185], v[64:67]
	v_mfma_f32_16x16x32_bf16 v[60:63], v[166:169], v[190:193], v[60:63]
	v_mfma_f32_16x16x32_bf16 v[56:59], v[174:177], v[190:193], v[56:59]
	v_mfma_f32_16x16x32_bf16 v[40:43], v[166:169], v[198:201], v[40:43]
	v_mfma_f32_16x16x32_bf16 v[36:39], v[174:177], v[198:201], v[36:39]
	v_mfma_f32_16x16x32_bf16 v[20:23], v[166:169], v[206:209], v[20:23]
	v_mfma_f32_16x16x32_bf16 v[16:19], v[174:177], v[206:209], v[16:19]
	s_setprio 1
	s_barrier
	s_andn2_b64 vcc, exec, s[30:31]
	s_mov_b64 s[34:35], -1
	s_mov_b64 s[30:31], 0
	s_mov_b64 s[36:37], 0x100
	s_cbranch_vccz .LBB0_2588
	s_and_b64 vcc, exec, s[10:11]
	s_cbranch_vccz .LBB0_2591
	s_barrier

.LBB0_2669:
	s_mov_b64 s[80:81], 0x100
	v_lshl_add_u64 v[0:1], v[168:169], 0, s[36:37]
	v_lshl_add_u64 v[0:1], v[0:1], 0, s[80:81]
	v_cndmask_b32_e64 v179, v1, v171, s[34:35]
	v_cndmask_b32_e64 v178, v0, v205, s[34:35]
	ds_read_b128 v[8:11], v185
	ds_read_b128 v[12:15], v189
	ds_read_b128 v[24:27], v190
	ds_read_b128 v[28:31], v191
	ds_read_b128 v[0:3], v186
	ds_read_b128 v[4:7], v192
	ds_read_b128 v[16:19], v193
	ds_read_b128 v[20:23], v194
	s_add_u32 s15, s24, s36
	s_addc_u32 s79, s25, s37
	s_add_u32 s82, s15, 0x100
	s_addc_u32 s83, s79, 0
	s_and_b64 s[38:39], s[34:35], exec
	s_cselect_b32 s39, s27, s83
	s_cselect_b32 s38, s78, s82
	s_add_u32 s36, s15, 0x10080
	s_addc_u32 s37, s79, 0
	s_add_i32 m0, s43, 0xc000
	s_add_i32 s15, s43, 0xe000
	s_add_u32 s34, s38, 0x10000
	s_addc_u32 s35, s39, 0
	v_lshl_add_u64 v[180:181], v[178:179], 0, s[0:1]
	v_lshl_add_u64 v[174:175], v[178:179], 0, s[10:11]
	v_lshl_add_u64 v[176:177], s[36:37], 0, v[164:165]
	ds_read_b128 v[206:209], v203
	ds_read_b128 v[210:213], v203 offset:1024
	ds_read_b128 v[214:217], v203 offset:2048
	ds_read_b128 v[218:221], v203 offset:3072
	ds_read_b128 v[222:225], v203 offset:4096
	ds_read_b128 v[226:229], v203 offset:5120
	ds_read_b128 v[230:233], v203 offset:6144
	ds_read_b128 v[234:237], v203 offset:7168
	global_load_lds_dwordx4 v[176:177], off
	v_lshl_add_u64 v[176:177], s[36:37], 0, v[166:167]
	s_mov_b32 m0, s15
	s_nop 0
	global_load_lds_dwordx4 v[176:177], off
	s_waitcnt vmcnt(8)
	s_waitcnt lgkmcnt(0)
	s_barrier
	s_setprio 0
	s_waitcnt lgkmcnt(0)
	v_mfma_f32_16x16x128_f8f6f4 v[156:159], v[8:15], v[206:213], v[156:159]
	v_mfma_f32_16x16x128_f8f6f4 v[152:155], v[24:31], v[206:213], v[152:155]
	v_mfma_f32_16x16x128_f8f6f4 v[140:143], v[8:15], v[214:221], v[140:143]
	v_mfma_f32_16x16x128_f8f6f4 v[136:139], v[24:31], v[214:221], v[136:139]
	v_mfma_f32_16x16x128_f8f6f4 v[124:127], v[8:15], v[222:229], v[124:127]
	v_mfma_f32_16x16x128_f8f6f4 v[120:123], v[24:31], v[222:229], v[120:123]
	v_mfma_f32_16x16x128_f8f6f4 v[108:111], v[8:15], v[230:237], v[108:111]
	v_mfma_f32_16x16x128_f8f6f4 v[104:107], v[24:31], v[230:237], v[104:107]
	s_setprio 1
	s_setprio 0
	v_mfma_f32_16x16x128_f8f6f4 v[148:151], v[0:7], v[206:213], v[148:151]
	v_mfma_f32_16x16x128_f8f6f4 v[144:147], v[16:23], v[206:213], v[144:147]
	v_mfma_f32_16x16x128_f8f6f4 v[132:135], v[0:7], v[214:221], v[132:135]
	v_mfma_f32_16x16x128_f8f6f4 v[128:131], v[16:23], v[214:221], v[128:131]
	v_mfma_f32_16x16x128_f8f6f4 v[116:119], v[0:7], v[222:229], v[116:119]
	v_mfma_f32_16x16x128_f8f6f4 v[112:115], v[16:23], v[222:229], v[112:115]
	v_mfma_f32_16x16x128_f8f6f4 v[96:99], v[0:7], v[230:237], v[96:99]
	v_mfma_f32_16x16x128_f8f6f4 v[88:91], v[16:23], v[230:237], v[88:91]
	s_setprio 1
	s_barrier
	s_mov_b32 m0, s44
	v_lshl_add_u64 v[176:177], v[178:179], 0, v[162:163]
	ds_read_b128 v[206:209], v203 offset:16384
	ds_read_b128 v[210:213], v203 offset:17408
	ds_read_b128 v[214:217], v203 offset:18432
	ds_read_b128 v[218:221], v203 offset:19456
	ds_read_b128 v[222:225], v203 offset:20480
	ds_read_b128 v[226:229], v203 offset:21504
	ds_read_b128 v[230:233], v203 offset:22528
	ds_read_b128 v[234:237], v203 offset:23552
	global_load_lds_dwordx4 v[176:177], off
	v_lshl_add_u64 v[178:179], v[178:179], 0, v[160:161]
	s_mov_b32 m0, s45
	v_lshl_add_u64 v[182:183], v[180:181], 0, v[162:163]
	global_load_lds_dwordx4 v[178:179], off
	s_mov_b32 m0, s46
	v_lshl_add_u64 v[180:181], v[180:181], 0, v[160:161]
	global_load_lds_dwordx4 v[182:183], off
	s_mov_b32 m0, s47
	v_lshl_add_u64 v[182:183], s[38:39], 0, v[166:167]
	global_load_lds_dwordx4 v[180:181], off
	v_lshl_add_u64 v[180:181], s[38:39], 0, v[164:165]
	s_mov_b32 m0, s43
	s_nop 0
	global_load_lds_dwordx4 v[180:181], off
	s_mov_b32 m0, s48
	s_nop 0
	global_load_lds_dwordx4 v[182:183], off
	s_waitcnt vmcnt(8)
	s_waitcnt lgkmcnt(0)
	s_barrier
	s_setprio 0
	s_waitcnt lgkmcnt(0)
	v_mfma_f32_16x16x128_f8f6f4 v[84:87], v[8:15], v[206:213], v[84:87]
	v_mfma_f32_16x16x128_f8f6f4 v[76:79], v[24:31], v[206:213], v[76:79]
	v_mfma_f32_16x16x128_f8f6f4 v[60:63], v[8:15], v[214:221], v[60:63]
	v_mfma_f32_16x16x128_f8f6f4 v[48:51], v[24:31], v[214:221], v[48:51]
	v_mfma_f32_16x16x128_f8f6f4 v[68:71], v[8:15], v[222:229], v[68:71]
	v_mfma_f32_16x16x128_f8f6f4 v[56:59], v[24:31], v[222:229], v[56:59]
	v_mfma_f32_16x16x128_f8f6f4 v[44:47], v[8:15], v[230:237], v[44:47]
	v_mfma_f32_16x16x128_f8f6f4 v[36:39], v[24:31], v[230:237], v[36:39]
	s_setprio 1
	s_setprio 0
	v_mfma_f32_16x16x128_f8f6f4 v[100:103], v[0:7], v[206:213], v[100:103]
	v_mfma_f32_16x16x128_f8f6f4 v[92:95], v[16:23], v[206:213], v[92:95]
	v_mfma_f32_16x16x128_f8f6f4 v[80:83], v[0:7], v[214:221], v[80:83]
	v_mfma_f32_16x16x128_f8f6f4 v[72:75], v[16:23], v[214:221], v[72:75]
	v_mfma_f32_16x16x128_f8f6f4 v[64:67], v[0:7], v[222:229], v[64:67]
	v_mfma_f32_16x16x128_f8f6f4 v[52:55], v[16:23], v[222:229], v[52:55]
	v_mfma_f32_16x16x128_f8f6f4 v[40:43], v[0:7], v[230:237], v[40:43]
	v_mfma_f32_16x16x128_f8f6f4 v[32:35], v[16:23], v[230:237], v[32:35]
	s_setprio 1
	s_barrier
	ds_read_b128 v[4:7], v195
	ds_read_b128 v[8:11], v196
	ds_read_b128 v[0:3], v187
	ds_read_b128 v[16:19], v188
	ds_read_b128 v[12:15], v197
	ds_read_b128 v[20:23], v198
	ds_read_b128 v[24:27], v199
	ds_read_b128 v[28:31], v200
	s_mov_b32 m0, s49
	v_lshl_add_u64 v[238:239], s[34:35], 0, v[164:165]
	ds_read_b128 v[206:209], v203 offset:32768
	ds_read_b128 v[210:213], v203 offset:33792
	ds_read_b128 v[214:217], v203 offset:34816
	ds_read_b128 v[218:221], v203 offset:35840
	ds_read_b128 v[222:225], v203 offset:36864
	ds_read_b128 v[226:229], v203 offset:37888
	ds_read_b128 v[230:233], v203 offset:38912
	ds_read_b128 v[234:237], v203 offset:39936
	global_load_lds_dwordx4 v[238:239], off
	v_lshl_add_u64 v[238:239], s[34:35], 0, v[166:167]
	s_mov_b32 m0, s50
	s_nop 0
	global_load_lds_dwordx4 v[238:239], off
	s_waitcnt vmcnt(8)
	s_waitcnt lgkmcnt(0)
	s_barrier
	s_setprio 0
	s_waitcnt lgkmcnt(0)
	v_mfma_f32_16x16x128_f8f6f4 v[156:159], v[0:7], v[206:213], v[156:159]
	v_mfma_f32_16x16x128_f8f6f4 v[152:155], v[8:15], v[206:213], v[152:155]
	v_mfma_f32_16x16x128_f8f6f4 v[140:143], v[0:7], v[214:221], v[140:143]
	v_mfma_f32_16x16x128_f8f6f4 v[136:139], v[8:15], v[214:221], v[136:139]
	v_mfma_f32_16x16x128_f8f6f4 v[124:127], v[0:7], v[222:229], v[124:127]
	v_mfma_f32_16x16x128_f8f6f4 v[120:123], v[8:15], v[222:229], v[120:123]
	v_mfma_f32_16x16x128_f8f6f4 v[108:111], v[0:7], v[230:237], v[108:111]
	v_mfma_f32_16x16x128_f8f6f4 v[104:107], v[8:15], v[230:237], v[104:107]
	s_setprio 1
	s_setprio 0
	v_mfma_f32_16x16x128_f8f6f4 v[148:151], v[16:23], v[206:213], v[148:151]
	v_mfma_f32_16x16x128_f8f6f4 v[144:147], v[24:31], v[206:213], v[144:147]
	v_mfma_f32_16x16x128_f8f6f4 v[132:135], v[16:23], v[214:221], v[132:135]
	v_mfma_f32_16x16x128_f8f6f4 v[128:131], v[24:31], v[214:221], v[128:131]
	v_mfma_f32_16x16x128_f8f6f4 v[116:119], v[16:23], v[222:229], v[116:119]
	v_mfma_f32_16x16x128_f8f6f4 v[112:115], v[24:31], v[222:229], v[112:115]
	v_mfma_f32_16x16x128_f8f6f4 v[96:99], v[16:23], v[230:237], v[96:99]
	v_mfma_f32_16x16x128_f8f6f4 v[88:91], v[24:31], v[230:237], v[88:91]
	s_setprio 1
	s_barrier
	s_mov_b32 m0, s52
	v_lshl_add_u64 v[176:177], v[176:177], 0, s[8:9]
	ds_read_b128 v[206:209], v203 offset:49152
	ds_read_b128 v[210:213], v203 offset:50176
	ds_read_b128 v[214:217], v203 offset:51200
	ds_read_b128 v[218:221], v203 offset:52224
	ds_read_b128 v[222:225], v203 offset:53248
	ds_read_b128 v[226:229], v203 offset:54272
	ds_read_b128 v[230:233], v203 offset:55296
	ds_read_b128 v[234:237], v203 offset:56320
	global_load_lds_dwordx4 v[176:177], off
	v_lshl_add_u64 v[176:177], v[178:179], 0, s[8:9]
	s_mov_b32 m0, s53
	s_nop 0
	global_load_lds_dwordx4 v[176:177], off
	v_lshl_add_u64 v[176:177], v[174:175], 0, v[162:163]
	s_mov_b32 m0, s56
	v_lshl_add_u64 v[174:175], v[174:175], 0, v[160:161]
	global_load_lds_dwordx4 v[176:177], off
	s_mov_b32 m0, s57
	s_nop 0
	global_load_lds_dwordx4 v[174:175], off
	v_lshl_add_u64 v[174:175], v[180:181], 0, s[8:9]
	s_mov_b32 m0, s54
	s_nop 0
	global_load_lds_dwordx4 v[174:175], off
	v_lshl_add_u64 v[174:175], v[182:183], 0, s[8:9]
	s_mov_b32 m0, s55
	s_nop 0
	global_load_lds_dwordx4 v[174:175], off
	s_waitcnt vmcnt(8)
	s_waitcnt lgkmcnt(0)
	s_barrier
	s_setprio 0
	s_waitcnt lgkmcnt(0)
	v_mfma_f32_16x16x128_f8f6f4 v[84:87], v[0:7], v[206:213], v[84:87]
	v_mfma_f32_16x16x128_f8f6f4 v[76:79], v[8:15], v[206:213], v[76:79]
	v_mfma_f32_16x16x128_f8f6f4 v[60:63], v[0:7], v[214:221], v[60:63]
	v_mfma_f32_16x16x128_f8f6f4 v[48:51], v[8:15], v[214:221], v[48:51]
	v_mfma_f32_16x16x128_f8f6f4 v[68:71], v[0:7], v[222:229], v[68:71]
	v_mfma_f32_16x16x128_f8f6f4 v[56:59], v[8:15], v[222:229], v[56:59]
	v_mfma_f32_16x16x128_f8f6f4 v[44:47], v[0:7], v[230:237], v[44:47]
	v_mfma_f32_16x16x128_f8f6f4 v[36:39], v[8:15], v[230:237], v[36:39]
	s_setprio 1
	s_setprio 0
	v_mfma_f32_16x16x128_f8f6f4 v[100:103], v[16:23], v[206:213], v[100:103]
	v_mfma_f32_16x16x128_f8f6f4 v[92:95], v[24:31], v[206:213], v[92:95]
	v_mfma_f32_16x16x128_f8f6f4 v[80:83], v[16:23], v[214:221], v[80:83]
	v_mfma_f32_16x16x128_f8f6f4 v[72:75], v[24:31], v[214:221], v[72:75]
	v_mfma_f32_16x16x128_f8f6f4 v[64:67], v[16:23], v[222:229], v[64:67]
	v_mfma_f32_16x16x128_f8f6f4 v[52:55], v[24:31], v[222:229], v[52:55]
	v_mfma_f32_16x16x128_f8f6f4 v[40:43], v[16:23], v[230:237], v[40:43]
	v_mfma_f32_16x16x128_f8f6f4 v[32:35], v[24:31], v[230:237], v[32:35]
	s_setprio 1
	s_barrier
	s_andn2_b64 vcc, exec, s[30:31]
	s_mov_b64 s[34:35], -1
	s_mov_b64 s[30:31], 0
	s_mov_b64 s[36:37], 0x100
	s_cbranch_vccz .LBB0_2669
	s_nop 15
	s_nop 7
	s_and_b64 vcc, exec, s[12:13]
	s_cbranch_vccz .LBB0_2672
	s_barrier

.LBB0_2681:
	s_add_u32 s16, s4, s12
	s_addc_u32 s17, s5, s13
	s_add_u32 s24, s16, 0x100
	s_addc_u32 s25, s17, 0
	s_and_b64 s[14:15], s[10:11], exec
	s_cselect_b32 s15, s5, s25
	s_cselect_b32 s14, s4, s24
	s_add_u32 s12, s0, s12
	s_addc_u32 s13, s1, s13
	ds_read_b128 v[144:147], v138
	ds_read_b128 v[148:151], v138 offset:1024
	ds_read_b128 v[152:155], v138 offset:2048
	ds_read_b128 v[156:159], v138 offset:3072
	ds_read_b128 v[160:163], v139
	ds_read_b128 v[164:167], v139 offset:1024
	ds_read_b128 v[168:171], v139 offset:2048
	ds_read_b128 v[172:175], v139 offset:3072
	s_add_u32 s12, s12, 0x100
	s_addc_u32 s13, s13, 0
	s_and_b64 s[10:11], s[10:11], exec
	s_cselect_b32 s13, s1, s13
	s_cselect_b32 s12, s0, s12
	s_add_u32 s26, s16, 0x10080
	s_addc_u32 s27, s17, 0
	s_add_u32 s16, s12, 0x10000
	s_addc_u32 s17, s13, 0
	s_add_u32 s10, s14, 0x10000
	s_addc_u32 s11, s15, 0
	s_add_u32 s24, s12, 0x10080
	s_addc_u32 s25, s13, 0
	s_mov_b32 m0, s39
	v_lshl_add_u64 v[208:209], s[26:27], 0, v[132:133]
	ds_read_b128 v[176:179], v140
	ds_read_b128 v[180:183], v140 offset:1024
	ds_read_b128 v[184:187], v140 offset:2048
	ds_read_b128 v[188:191], v140 offset:3072
	ds_read_b128 v[192:195], v140 offset:4096
	ds_read_b128 v[196:199], v140 offset:5120
	ds_read_b128 v[200:203], v140 offset:6144
	ds_read_b128 v[204:207], v140 offset:7168
	global_load_lds_dwordx4 v[208:209], off
	v_lshl_add_u64 v[208:209], s[26:27], 0, v[134:135]
	s_mov_b32 m0, s40
	s_nop 0
	global_load_lds_dwordx4 v[208:209], off
	s_waitcnt vmcnt(8)
	s_waitcnt lgkmcnt(0)
	s_barrier
	s_setprio 0
	s_waitcnt lgkmcnt(0)
	v_mfma_f32_16x16x32_bf16 v[124:127], v[144:147], v[176:179], v[124:127]
	v_mfma_f32_16x16x32_bf16 v[120:123], v[152:155], v[176:179], v[120:123]
	v_mfma_f32_16x16x32_bf16 v[116:119], v[144:147], v[184:187], v[116:119]
	v_mfma_f32_16x16x32_bf16 v[108:111], v[152:155], v[184:187], v[108:111]
	v_mfma_f32_16x16x32_bf16 v[100:103], v[144:147], v[192:195], v[100:103]
	v_mfma_f32_16x16x32_bf16 v[92:95], v[152:155], v[192:195], v[92:95]
	v_mfma_f32_16x16x32_bf16 v[84:87], v[144:147], v[200:203], v[84:87]
	v_mfma_f32_16x16x32_bf16 v[76:79], v[152:155], v[200:203], v[76:79]
	v_mfma_f32_16x16x32_bf16 v[124:127], v[148:151], v[180:183], v[124:127]
	v_mfma_f32_16x16x32_bf16 v[120:123], v[156:159], v[180:183], v[120:123]
	v_mfma_f32_16x16x32_bf16 v[116:119], v[148:151], v[188:191], v[116:119]
	v_mfma_f32_16x16x32_bf16 v[108:111], v[156:159], v[188:191], v[108:111]
	v_mfma_f32_16x16x32_bf16 v[100:103], v[148:151], v[196:199], v[100:103]
	v_mfma_f32_16x16x32_bf16 v[92:95], v[156:159], v[196:199], v[92:95]
	v_mfma_f32_16x16x32_bf16 v[84:87], v[148:151], v[204:207], v[84:87]
	v_mfma_f32_16x16x32_bf16 v[76:79], v[156:159], v[204:207], v[76:79]
	s_setprio 1
	s_setprio 0
	v_mfma_f32_16x16x32_bf16 v[112:115], v[160:163], v[176:179], v[112:115]
	v_mfma_f32_16x16x32_bf16 v[104:107], v[168:171], v[176:179], v[104:107]
	v_mfma_f32_16x16x32_bf16 v[96:99], v[160:163], v[184:187], v[96:99]
	v_mfma_f32_16x16x32_bf16 v[88:91], v[168:171], v[184:187], v[88:91]
	v_mfma_f32_16x16x32_bf16 v[80:83], v[160:163], v[192:195], v[80:83]
	v_mfma_f32_16x16x32_bf16 v[72:75], v[168:171], v[192:195], v[72:75]
	v_mfma_f32_16x16x32_bf16 v[52:55], v[160:163], v[200:203], v[52:55]
	v_mfma_f32_16x16x32_bf16 v[48:51], v[168:171], v[200:203], v[48:51]
	v_mfma_f32_16x16x32_bf16 v[112:115], v[164:167], v[180:183], v[112:115]
	v_mfma_f32_16x16x32_bf16 v[104:107], v[172:175], v[180:183], v[104:107]
	v_mfma_f32_16x16x32_bf16 v[96:99], v[164:167], v[188:191], v[96:99]
	v_mfma_f32_16x16x32_bf16 v[88:91], v[172:175], v[188:191], v[88:91]
	v_mfma_f32_16x16x32_bf16 v[80:83], v[164:167], v[196:199], v[80:83]
	v_mfma_f32_16x16x32_bf16 v[72:75], v[172:175], v[196:199], v[72:75]
	v_mfma_f32_16x16x32_bf16 v[52:55], v[164:167], v[204:207], v[52:55]
	v_mfma_f32_16x16x32_bf16 v[48:51], v[172:175], v[204:207], v[48:51]
	s_setprio 1
	s_barrier
	s_mov_b32 m0, s41
	v_lshl_add_u64 v[208:209], s[12:13], 0, v[130:131]
	ds_read_b128 v[176:179], v140 offset:16384
	ds_read_b128 v[180:183], v140 offset:17408
	ds_read_b128 v[184:187], v140 offset:18432
	ds_read_b128 v[188:191], v140 offset:19456
	ds_read_b128 v[192:195], v140 offset:20480
	ds_read_b128 v[196:199], v140 offset:21504
	ds_read_b128 v[200:203], v140 offset:22528
	ds_read_b128 v[204:207], v140 offset:23552
	global_load_lds_dwordx4 v[208:209], off
	v_lshl_add_u64 v[210:211], s[12:13], 0, v[128:129]
	s_mov_b32 m0, s42
	v_lshl_add_u64 v[212:213], s[16:17], 0, v[130:131]
	global_load_lds_dwordx4 v[210:211], off
	s_mov_b32 m0, s43
	v_lshl_add_u64 v[214:215], s[14:15], 0, v[134:135]
	global_load_lds_dwordx4 v[212:213], off
	v_lshl_add_u64 v[212:213], s[16:17], 0, v[128:129]
	s_mov_b32 m0, s44
	s_nop 0
	global_load_lds_dwordx4 v[212:213], off
	v_lshl_add_u64 v[212:213], s[14:15], 0, v[132:133]
	s_mov_b32 m0, s31
	s_nop 0
	global_load_lds_dwordx4 v[212:213], off
	s_mov_b32 m0, s33
	s_nop 0
	global_load_lds_dwordx4 v[214:215], off
	s_waitcnt vmcnt(8)
	s_waitcnt lgkmcnt(0)
	s_barrier
	s_setprio 0
	s_waitcnt lgkmcnt(0)
	v_mfma_f32_16x16x32_bf16 v[44:47], v[144:147], v[176:179], v[44:47]
	v_mfma_f32_16x16x32_bf16 v[32:35], v[152:155], v[176:179], v[32:35]
	v_mfma_f32_16x16x32_bf16 v[4:7], v[144:147], v[184:187], v[4:7]
	v_mfma_f32_16x16x32_bf16 v[0:3], v[152:155], v[184:187], v[0:3]
	v_mfma_f32_16x16x32_bf16 v[28:31], v[144:147], v[192:195], v[28:31]
	v_mfma_f32_16x16x32_bf16 v[24:27], v[152:155], v[192:195], v[24:27]
	v_mfma_f32_16x16x32_bf16 v[12:15], v[144:147], v[200:203], v[12:15]
	v_mfma_f32_16x16x32_bf16 v[8:11], v[152:155], v[200:203], v[8:11]
	v_mfma_f32_16x16x32_bf16 v[44:47], v[148:151], v[180:183], v[44:47]
	v_mfma_f32_16x16x32_bf16 v[32:35], v[156:159], v[180:183], v[32:35]
	v_mfma_f32_16x16x32_bf16 v[4:7], v[148:151], v[188:191], v[4:7]
	v_mfma_f32_16x16x32_bf16 v[0:3], v[156:159], v[188:191], v[0:3]
	v_mfma_f32_16x16x32_bf16 v[28:31], v[148:151], v[196:199], v[28:31]
	v_mfma_f32_16x16x32_bf16 v[24:27], v[156:159], v[196:199], v[24:27]
	v_mfma_f32_16x16x32_bf16 v[12:15], v[148:151], v[204:207], v[12:15]
	v_mfma_f32_16x16x32_bf16 v[8:11], v[156:159], v[204:207], v[8:11]
	s_setprio 1
	s_setprio 0
	v_mfma_f32_16x16x32_bf16 v[68:71], v[160:163], v[176:179], v[68:71]
	v_mfma_f32_16x16x32_bf16 v[64:67], v[168:171], v[176:179], v[64:67]
	v_mfma_f32_16x16x32_bf16 v[60:63], v[160:163], v[184:187], v[60:63]
	v_mfma_f32_16x16x32_bf16 v[56:59], v[168:171], v[184:187], v[56:59]
	v_mfma_f32_16x16x32_bf16 v[40:43], v[160:163], v[192:195], v[40:43]
	v_mfma_f32_16x16x32_bf16 v[36:39], v[168:171], v[192:195], v[36:39]
	v_mfma_f32_16x16x32_bf16 v[20:23], v[160:163], v[200:203], v[20:23]
	v_mfma_f32_16x16x32_bf16 v[16:19], v[168:171], v[200:203], v[16:19]
	v_mfma_f32_16x16x32_bf16 v[68:71], v[164:167], v[180:183], v[68:71]
	v_mfma_f32_16x16x32_bf16 v[64:67], v[172:175], v[180:183], v[64:67]
	v_mfma_f32_16x16x32_bf16 v[60:63], v[164:167], v[188:191], v[60:63]
	v_mfma_f32_16x16x32_bf16 v[56:59], v[172:175], v[188:191], v[56:59]
	v_mfma_f32_16x16x32_bf16 v[40:43], v[164:167], v[196:199], v[40:43]
	v_mfma_f32_16x16x32_bf16 v[36:39], v[172:175], v[196:199], v[36:39]
	v_mfma_f32_16x16x32_bf16 v[20:23], v[164:167], v[204:207], v[20:23]
	v_mfma_f32_16x16x32_bf16 v[16:19], v[172:175], v[204:207], v[16:19]
	s_setprio 1
	s_barrier
	ds_read_b128 v[144:147], v141
	ds_read_b128 v[148:151], v141 offset:1024
	ds_read_b128 v[152:155], v141 offset:2048
	ds_read_b128 v[156:159], v141 offset:3072
	ds_read_b128 v[160:163], v142
	ds_read_b128 v[164:167], v142 offset:1024
	ds_read_b128 v[168:171], v142 offset:2048
	ds_read_b128 v[172:175], v142 offset:3072
	s_mov_b32 m0, s34
	v_lshl_add_u64 v[216:217], s[10:11], 0, v[132:133]
	ds_read_b128 v[176:179], v140 offset:32768
	ds_read_b128 v[180:183], v140 offset:33792
	ds_read_b128 v[184:187], v140 offset:34816
	ds_read_b128 v[188:191], v140 offset:35840
	ds_read_b128 v[192:195], v140 offset:36864
	ds_read_b128 v[196:199], v140 offset:37888
	ds_read_b128 v[200:203], v140 offset:38912
	ds_read_b128 v[204:207], v140 offset:39936
	global_load_lds_dwordx4 v[216:217], off
	v_lshl_add_u64 v[216:217], s[10:11], 0, v[134:135]
	s_mov_b32 m0, s35
	s_nop 0
	global_load_lds_dwordx4 v[216:217], off
	s_waitcnt vmcnt(8)
	s_waitcnt lgkmcnt(0)
	s_barrier
	s_setprio 0
	s_waitcnt lgkmcnt(0)
	v_mfma_f32_16x16x32_bf16 v[124:127], v[144:147], v[176:179], v[124:127]
	v_mfma_f32_16x16x32_bf16 v[120:123], v[152:155], v[176:179], v[120:123]
	v_mfma_f32_16x16x32_bf16 v[116:119], v[144:147], v[184:187], v[116:119]
	v_mfma_f32_16x16x32_bf16 v[108:111], v[152:155], v[184:187], v[108:111]
	v_mfma_f32_16x16x32_bf16 v[100:103], v[144:147], v[192:195], v[100:103]
	v_mfma_f32_16x16x32_bf16 v[92:95], v[152:155], v[192:195], v[92:95]
	v_mfma_f32_16x16x32_bf16 v[84:87], v[144:147], v[200:203], v[84:87]
	v_mfma_f32_16x16x32_bf16 v[76:79], v[152:155], v[200:203], v[76:79]
	v_mfma_f32_16x16x32_bf16 v[124:127], v[148:151], v[180:183], v[124:127]
	v_mfma_f32_16x16x32_bf16 v[120:123], v[156:159], v[180:183], v[120:123]
	v_mfma_f32_16x16x32_bf16 v[116:119], v[148:151], v[188:191], v[116:119]
	v_mfma_f32_16x16x32_bf16 v[108:111], v[156:159], v[188:191], v[108:111]
	v_mfma_f32_16x16x32_bf16 v[100:103], v[148:151], v[196:199], v[100:103]
	v_mfma_f32_16x16x32_bf16 v[92:95], v[156:159], v[196:199], v[92:95]
	v_mfma_f32_16x16x32_bf16 v[84:87], v[148:151], v[204:207], v[84:87]
	v_mfma_f32_16x16x32_bf16 v[76:79], v[156:159], v[204:207], v[76:79]
	s_setprio 1
	s_setprio 0
	v_mfma_f32_16x16x32_bf16 v[112:115], v[160:163], v[176:179], v[112:115]
	v_mfma_f32_16x16x32_bf16 v[104:107], v[168:171], v[176:179], v[104:107]
	v_mfma_f32_16x16x32_bf16 v[96:99], v[160:163], v[184:187], v[96:99]
	v_mfma_f32_16x16x32_bf16 v[88:91], v[168:171], v[184:187], v[88:91]
	v_mfma_f32_16x16x32_bf16 v[80:83], v[160:163], v[192:195], v[80:83]
	v_mfma_f32_16x16x32_bf16 v[72:75], v[168:171], v[192:195], v[72:75]
	v_mfma_f32_16x16x32_bf16 v[52:55], v[160:163], v[200:203], v[52:55]
	v_mfma_f32_16x16x32_bf16 v[48:51], v[168:171], v[200:203], v[48:51]
	v_mfma_f32_16x16x32_bf16 v[112:115], v[164:167], v[180:183], v[112:115]
	v_mfma_f32_16x16x32_bf16 v[104:107], v[172:175], v[180:183], v[104:107]
	v_mfma_f32_16x16x32_bf16 v[96:99], v[164:167], v[188:191], v[96:99]
	v_mfma_f32_16x16x32_bf16 v[88:91], v[172:175], v[188:191], v[88:91]
	v_mfma_f32_16x16x32_bf16 v[80:83], v[164:167], v[196:199], v[80:83]
	v_mfma_f32_16x16x32_bf16 v[72:75], v[172:175], v[196:199], v[72:75]
	v_mfma_f32_16x16x32_bf16 v[52:55], v[164:167], v[204:207], v[52:55]
	v_mfma_f32_16x16x32_bf16 v[48:51], v[172:175], v[204:207], v[48:51]
	s_setprio 1
	s_barrier
	s_mov_b32 m0, s45
	v_lshl_add_u64 v[208:209], v[208:209], 0, s[6:7]
	ds_read_b128 v[176:179], v140 offset:49152
	ds_read_b128 v[180:183], v140 offset:50176
	ds_read_b128 v[184:187], v140 offset:51200
	ds_read_b128 v[188:191], v140 offset:52224
	ds_read_b128 v[192:195], v140 offset:53248
	ds_read_b128 v[196:199], v140 offset:54272
	ds_read_b128 v[200:203], v140 offset:55296
	ds_read_b128 v[204:207], v140 offset:56320
	global_load_lds_dwordx4 v[208:209], off
	v_lshl_add_u64 v[208:209], v[210:211], 0, s[6:7]
	s_mov_b32 m0, s46
	s_nop 0
	global_load_lds_dwordx4 v[208:209], off
	v_lshl_add_u64 v[208:209], s[24:25], 0, v[130:131]
	s_mov_b32 m0, s47
	s_nop 0
	global_load_lds_dwordx4 v[208:209], off
	v_lshl_add_u64 v[208:209], s[24:25], 0, v[128:129]
	s_mov_b32 m0, s48
	s_nop 0
	global_load_lds_dwordx4 v[208:209], off
	v_lshl_add_u64 v[208:209], v[212:213], 0, s[6:7]
	s_mov_b32 m0, s37
	s_nop 0
	global_load_lds_dwordx4 v[208:209], off
	v_lshl_add_u64 v[208:209], v[214:215], 0, s[6:7]
	s_mov_b32 m0, s38
	s_nop 0
	global_load_lds_dwordx4 v[208:209], off
	s_waitcnt vmcnt(8)
	s_waitcnt lgkmcnt(0)
	s_barrier
	s_setprio 0
	s_waitcnt lgkmcnt(0)
	v_mfma_f32_16x16x32_bf16 v[44:47], v[144:147], v[176:179], v[44:47]
	v_mfma_f32_16x16x32_bf16 v[32:35], v[152:155], v[176:179], v[32:35]
	v_mfma_f32_16x16x32_bf16 v[4:7], v[144:147], v[184:187], v[4:7]
	v_mfma_f32_16x16x32_bf16 v[0:3], v[152:155], v[184:187], v[0:3]
	v_mfma_f32_16x16x32_bf16 v[28:31], v[144:147], v[192:195], v[28:31]
	v_mfma_f32_16x16x32_bf16 v[24:27], v[152:155], v[192:195], v[24:27]
	v_mfma_f32_16x16x32_bf16 v[12:15], v[144:147], v[200:203], v[12:15]
	v_mfma_f32_16x16x32_bf16 v[8:11], v[152:155], v[200:203], v[8:11]
	v_mfma_f32_16x16x32_bf16 v[44:47], v[148:151], v[180:183], v[44:47]
	v_mfma_f32_16x16x32_bf16 v[32:35], v[156:159], v[180:183], v[32:35]
	v_mfma_f32_16x16x32_bf16 v[4:7], v[148:151], v[188:191], v[4:7]
	v_mfma_f32_16x16x32_bf16 v[0:3], v[156:159], v[188:191], v[0:3]
	v_mfma_f32_16x16x32_bf16 v[28:31], v[148:151], v[196:199], v[28:31]
	v_mfma_f32_16x16x32_bf16 v[24:27], v[156:159], v[196:199], v[24:27]
	v_mfma_f32_16x16x32_bf16 v[12:15], v[148:151], v[204:207], v[12:15]
	v_mfma_f32_16x16x32_bf16 v[8:11], v[156:159], v[204:207], v[8:11]
	s_setprio 1
	s_setprio 0
	v_mfma_f32_16x16x32_bf16 v[68:71], v[160:163], v[176:179], v[68:71]
	v_mfma_f32_16x16x32_bf16 v[64:67], v[168:171], v[176:179], v[64:67]
	v_mfma_f32_16x16x32_bf16 v[60:63], v[160:163], v[184:187], v[60:63]
	v_mfma_f32_16x16x32_bf16 v[56:59], v[168:171], v[184:187], v[56:59]
	v_mfma_f32_16x16x32_bf16 v[40:43], v[160:163], v[192:195], v[40:43]
	v_mfma_f32_16x16x32_bf16 v[36:39], v[168:171], v[192:195], v[36:39]
	v_mfma_f32_16x16x32_bf16 v[20:23], v[160:163], v[200:203], v[20:23]
	v_mfma_f32_16x16x32_bf16 v[16:19], v[168:171], v[200:203], v[16:19]
	v_mfma_f32_16x16x32_bf16 v[68:71], v[164:167], v[180:183], v[68:71]
	v_mfma_f32_16x16x32_bf16 v[64:67], v[172:175], v[180:183], v[64:67]
	v_mfma_f32_16x16x32_bf16 v[60:63], v[164:167], v[188:191], v[60:63]
	v_mfma_f32_16x16x32_bf16 v[56:59], v[172:175], v[188:191], v[56:59]
	v_mfma_f32_16x16x32_bf16 v[40:43], v[164:167], v[196:199], v[40:43]
	v_mfma_f32_16x16x32_bf16 v[36:39], v[172:175], v[196:199], v[36:39]
	v_mfma_f32_16x16x32_bf16 v[20:23], v[164:167], v[204:207], v[20:23]
	v_mfma_f32_16x16x32_bf16 v[16:19], v[172:175], v[204:207], v[16:19]
	s_setprio 1
	s_barrier
	s_andn2_b64 vcc, exec, s[8:9]
	s_mov_b64 s[10:11], -1
	s_mov_b64 s[8:9], 0
	s_mov_b64 s[12:13], 0x100
	s_cbranch_vccz .LBB0_2681
	s_cmpk_lt_u32 s28, 0x100
	s_cbranch_scc0 .LBB0_2684
	s_barrier

.LBB0_2838:
	s_add_u32 s38, s24, s30
	s_addc_u32 s39, s25, s31
	s_add_u32 s36, s38, 0x100
	s_addc_u32 s37, s39, 0
	s_and_b64 s[34:35], s[28:29], exec
	s_cselect_b32 s35, s11, s37
	s_cselect_b32 s34, s59, s36
	s_add_u32 s30, s22, s30
	s_addc_u32 s31, s23, s31
	s_add_u32 s30, s30, 0x100
	s_addc_u32 s31, s31, 0
	s_and_b64 s[28:29], s[28:29], exec
	s_cselect_b32 s37, s9, s31
	s_cselect_b32 s36, s60, s30
	s_add_u32 s40, s38, 0x10080
	ds_read_b128 v[148:151], v145
	ds_read_b128 v[152:155], v145 offset:1024
	ds_read_b128 v[156:159], v145 offset:2048
	ds_read_b128 v[160:163], v145 offset:3072
	ds_read_b128 v[164:167], v146
	ds_read_b128 v[168:171], v146 offset:1024
	ds_read_b128 v[172:175], v146 offset:2048
	ds_read_b128 v[176:179], v146 offset:3072
	s_addc_u32 s41, s39, 0
	s_add_i32 s70, s56, s44
	s_add_i32 m0, s17, 0xc000
	s_add_i32 s71, s17, 0xe000
	s_add_i32 s67, s70, 0x2000
	s_add_u32 s38, s36, 0x10000
	s_addc_u32 s39, s37, 0
	s_add_i32 s69, s57, s44
	s_add_i32 s68, s69, 0x2000
	s_add_i32 s66, 0, 0x18000
	s_add_i32 s65, 0, 0x1c000
	s_add_u32 s30, s34, 0x10000
	s_addc_u32 s31, s35, 0
	s_add_i32 s64, s66, s44
	s_add_i32 s62, s64, 0x2000
	s_add_u32 s28, s36, 0x10080
	s_addc_u32 s29, s37, 0
	s_add_i32 s63, s65, s44
	s_add_i32 s61, s63, 0x2000
	v_lshl_add_u64 v[140:141], s[40:41], 0, v[132:133]
	ds_read_b128 v[180:183], v147
	ds_read_b128 v[184:187], v147 offset:1024
	ds_read_b128 v[188:191], v147 offset:2048
	ds_read_b128 v[192:195], v147 offset:3072
	ds_read_b128 v[196:199], v147 offset:4096
	ds_read_b128 v[200:203], v147 offset:5120
	ds_read_b128 v[204:207], v147 offset:6144
	ds_read_b128 v[208:211], v147 offset:7168
	global_load_lds_dwordx4 v[140:141], off
	v_lshl_add_u64 v[140:141], s[40:41], 0, v[134:135]
	s_mov_b32 m0, s71
	s_nop 0
	global_load_lds_dwordx4 v[140:141], off
	s_waitcnt vmcnt(8)
	s_waitcnt lgkmcnt(0)
	s_barrier
	s_setprio 0
	s_waitcnt lgkmcnt(0)
	v_mfma_f32_16x16x32_bf16 v[124:127], v[148:151], v[180:183], v[124:127]
	v_mfma_f32_16x16x32_bf16 v[120:123], v[156:159], v[180:183], v[120:123]
	v_mfma_f32_16x16x32_bf16 v[116:119], v[148:151], v[188:191], v[116:119]
	v_mfma_f32_16x16x32_bf16 v[108:111], v[156:159], v[188:191], v[108:111]
	v_mfma_f32_16x16x32_bf16 v[100:103], v[148:151], v[196:199], v[100:103]
	v_mfma_f32_16x16x32_bf16 v[92:95], v[156:159], v[196:199], v[92:95]
	v_mfma_f32_16x16x32_bf16 v[84:87], v[148:151], v[204:207], v[84:87]
	v_mfma_f32_16x16x32_bf16 v[76:79], v[156:159], v[204:207], v[76:79]
	v_mfma_f32_16x16x32_bf16 v[124:127], v[152:155], v[184:187], v[124:127]
	v_mfma_f32_16x16x32_bf16 v[120:123], v[160:163], v[184:187], v[120:123]
	v_mfma_f32_16x16x32_bf16 v[116:119], v[152:155], v[192:195], v[116:119]
	v_mfma_f32_16x16x32_bf16 v[108:111], v[160:163], v[192:195], v[108:111]
	v_mfma_f32_16x16x32_bf16 v[100:103], v[152:155], v[200:203], v[100:103]
	v_mfma_f32_16x16x32_bf16 v[92:95], v[160:163], v[200:203], v[92:95]
	v_mfma_f32_16x16x32_bf16 v[84:87], v[152:155], v[208:211], v[84:87]
	v_mfma_f32_16x16x32_bf16 v[76:79], v[160:163], v[208:211], v[76:79]
	s_setprio 1
	s_setprio 0
	v_mfma_f32_16x16x32_bf16 v[112:115], v[164:167], v[180:183], v[112:115]
	v_mfma_f32_16x16x32_bf16 v[104:107], v[172:175], v[180:183], v[104:107]
	v_mfma_f32_16x16x32_bf16 v[96:99], v[164:167], v[188:191], v[96:99]
	v_mfma_f32_16x16x32_bf16 v[88:91], v[172:175], v[188:191], v[88:91]
	v_mfma_f32_16x16x32_bf16 v[80:83], v[164:167], v[196:199], v[80:83]
	v_mfma_f32_16x16x32_bf16 v[72:75], v[172:175], v[196:199], v[72:75]
	v_mfma_f32_16x16x32_bf16 v[52:55], v[164:167], v[204:207], v[52:55]
	v_mfma_f32_16x16x32_bf16 v[48:51], v[172:175], v[204:207], v[48:51]
	v_mfma_f32_16x16x32_bf16 v[112:115], v[168:171], v[184:187], v[112:115]
	v_mfma_f32_16x16x32_bf16 v[104:107], v[176:179], v[184:187], v[104:107]
	v_mfma_f32_16x16x32_bf16 v[96:99], v[168:171], v[192:195], v[96:99]
	v_mfma_f32_16x16x32_bf16 v[88:91], v[176:179], v[192:195], v[88:91]
	v_mfma_f32_16x16x32_bf16 v[80:83], v[168:171], v[200:203], v[80:83]
	v_mfma_f32_16x16x32_bf16 v[72:75], v[176:179], v[200:203], v[72:75]
	v_mfma_f32_16x16x32_bf16 v[52:55], v[168:171], v[208:211], v[52:55]
	v_mfma_f32_16x16x32_bf16 v[48:51], v[176:179], v[208:211], v[48:51]
	s_setprio 1
	s_barrier
	s_mov_b32 m0, s70
	v_lshl_add_u64 v[140:141], s[36:37], 0, v[128:129]
	ds_read_b128 v[180:183], v147 offset:16384
	ds_read_b128 v[184:187], v147 offset:17408
	ds_read_b128 v[188:191], v147 offset:18432
	ds_read_b128 v[192:195], v147 offset:19456
	ds_read_b128 v[196:199], v147 offset:20480
	ds_read_b128 v[200:203], v147 offset:21504
	ds_read_b128 v[204:207], v147 offset:22528
	ds_read_b128 v[208:211], v147 offset:23552
	global_load_lds_dwordx4 v[140:141], off
	v_lshl_add_u64 v[212:213], s[36:37], 0, v[130:131]
	s_mov_b32 m0, s67
	v_lshl_add_u64 v[214:215], s[38:39], 0, v[128:129]
	global_load_lds_dwordx4 v[212:213], off
	s_mov_b32 m0, s69
	v_lshl_add_u64 v[216:217], s[34:35], 0, v[134:135]
	global_load_lds_dwordx4 v[214:215], off
	v_lshl_add_u64 v[214:215], s[38:39], 0, v[130:131]
	s_mov_b32 m0, s68
	s_nop 0
	global_load_lds_dwordx4 v[214:215], off
	v_lshl_add_u64 v[214:215], s[34:35], 0, v[132:133]
	s_mov_b32 m0, s17
	s_nop 0
	global_load_lds_dwordx4 v[214:215], off
	s_mov_b32 m0, s49
	s_nop 0
	global_load_lds_dwordx4 v[216:217], off
	s_waitcnt vmcnt(8)
	s_waitcnt lgkmcnt(0)
	s_barrier
	s_setprio 0
	s_waitcnt lgkmcnt(0)
	v_mfma_f32_16x16x32_bf16 v[44:47], v[148:151], v[180:183], v[44:47]
	v_mfma_f32_16x16x32_bf16 v[32:35], v[156:159], v[180:183], v[32:35]
	v_mfma_f32_16x16x32_bf16 v[4:7], v[148:151], v[188:191], v[4:7]
	v_mfma_f32_16x16x32_bf16 v[0:3], v[156:159], v[188:191], v[0:3]
	v_mfma_f32_16x16x32_bf16 v[28:31], v[148:151], v[196:199], v[28:31]
	v_mfma_f32_16x16x32_bf16 v[24:27], v[156:159], v[196:199], v[24:27]
	v_mfma_f32_16x16x32_bf16 v[12:15], v[148:151], v[204:207], v[12:15]
	v_mfma_f32_16x16x32_bf16 v[8:11], v[156:159], v[204:207], v[8:11]
	v_mfma_f32_16x16x32_bf16 v[44:47], v[152:155], v[184:187], v[44:47]
	v_mfma_f32_16x16x32_bf16 v[32:35], v[160:163], v[184:187], v[32:35]
	v_mfma_f32_16x16x32_bf16 v[4:7], v[152:155], v[192:195], v[4:7]
	v_mfma_f32_16x16x32_bf16 v[0:3], v[160:163], v[192:195], v[0:3]
	v_mfma_f32_16x16x32_bf16 v[28:31], v[152:155], v[200:203], v[28:31]
	v_mfma_f32_16x16x32_bf16 v[24:27], v[160:163], v[200:203], v[24:27]
	v_mfma_f32_16x16x32_bf16 v[12:15], v[152:155], v[208:211], v[12:15]
	v_mfma_f32_16x16x32_bf16 v[8:11], v[160:163], v[208:211], v[8:11]
	s_setprio 1
	s_setprio 0
	v_mfma_f32_16x16x32_bf16 v[68:71], v[164:167], v[180:183], v[68:71]
	v_mfma_f32_16x16x32_bf16 v[64:67], v[172:175], v[180:183], v[64:67]
	v_mfma_f32_16x16x32_bf16 v[60:63], v[164:167], v[188:191], v[60:63]
	v_mfma_f32_16x16x32_bf16 v[56:59], v[172:175], v[188:191], v[56:59]
	v_mfma_f32_16x16x32_bf16 v[40:43], v[164:167], v[196:199], v[40:43]
	v_mfma_f32_16x16x32_bf16 v[36:39], v[172:175], v[196:199], v[36:39]
	v_mfma_f32_16x16x32_bf16 v[20:23], v[164:167], v[204:207], v[20:23]
	v_mfma_f32_16x16x32_bf16 v[16:19], v[172:175], v[204:207], v[16:19]
	v_mfma_f32_16x16x32_bf16 v[68:71], v[168:171], v[184:187], v[68:71]
	v_mfma_f32_16x16x32_bf16 v[64:67], v[176:179], v[184:187], v[64:67]
	v_mfma_f32_16x16x32_bf16 v[60:63], v[168:171], v[192:195], v[60:63]
	v_mfma_f32_16x16x32_bf16 v[56:59], v[176:179], v[192:195], v[56:59]
	v_mfma_f32_16x16x32_bf16 v[40:43], v[168:171], v[200:203], v[40:43]
	v_mfma_f32_16x16x32_bf16 v[36:39], v[176:179], v[200:203], v[36:39]
	v_mfma_f32_16x16x32_bf16 v[20:23], v[168:171], v[208:211], v[20:23]
	v_mfma_f32_16x16x32_bf16 v[16:19], v[176:179], v[208:211], v[16:19]
	s_setprio 1
	s_barrier
	v_add_u32_e32 v160, s66, v143
	v_add_u32_e32 v176, s65, v143
	ds_read_b128 v[148:151], v160
	ds_read_b128 v[152:155], v160 offset:1024
	ds_read_b128 v[156:159], v160 offset:2048
	ds_read_b128 v[160:163], v160 offset:3072
	ds_read_b128 v[164:167], v176
	ds_read_b128 v[168:171], v176 offset:1024
	ds_read_b128 v[172:175], v176 offset:2048
	ds_read_b128 v[176:179], v176 offset:3072
	s_mov_b32 m0, s50
	v_lshl_add_u64 v[218:219], s[30:31], 0, v[132:133]
	ds_read_b128 v[180:183], v147 offset:32768
	ds_read_b128 v[184:187], v147 offset:33792
	ds_read_b128 v[188:191], v147 offset:34816
	ds_read_b128 v[192:195], v147 offset:35840
	ds_read_b128 v[196:199], v147 offset:36864
	ds_read_b128 v[200:203], v147 offset:37888
	ds_read_b128 v[204:207], v147 offset:38912
	ds_read_b128 v[208:211], v147 offset:39936
	global_load_lds_dwordx4 v[218:219], off
	v_lshl_add_u64 v[218:219], s[30:31], 0, v[134:135]
	s_mov_b32 m0, s51
	s_nop 0
	global_load_lds_dwordx4 v[218:219], off
	s_waitcnt vmcnt(8)
	s_waitcnt lgkmcnt(0)
	s_barrier
	s_setprio 0
	s_waitcnt lgkmcnt(0)
	v_mfma_f32_16x16x32_bf16 v[124:127], v[148:151], v[180:183], v[124:127]
	v_mfma_f32_16x16x32_bf16 v[120:123], v[156:159], v[180:183], v[120:123]
	v_mfma_f32_16x16x32_bf16 v[116:119], v[148:151], v[188:191], v[116:119]
	v_mfma_f32_16x16x32_bf16 v[108:111], v[156:159], v[188:191], v[108:111]
	v_mfma_f32_16x16x32_bf16 v[100:103], v[148:151], v[196:199], v[100:103]
	v_mfma_f32_16x16x32_bf16 v[92:95], v[156:159], v[196:199], v[92:95]
	v_mfma_f32_16x16x32_bf16 v[84:87], v[148:151], v[204:207], v[84:87]
	v_mfma_f32_16x16x32_bf16 v[76:79], v[156:159], v[204:207], v[76:79]
	v_mfma_f32_16x16x32_bf16 v[124:127], v[152:155], v[184:187], v[124:127]
	v_mfma_f32_16x16x32_bf16 v[120:123], v[160:163], v[184:187], v[120:123]
	v_mfma_f32_16x16x32_bf16 v[116:119], v[152:155], v[192:195], v[116:119]
	v_mfma_f32_16x16x32_bf16 v[108:111], v[160:163], v[192:195], v[108:111]
	v_mfma_f32_16x16x32_bf16 v[100:103], v[152:155], v[200:203], v[100:103]
	v_mfma_f32_16x16x32_bf16 v[92:95], v[160:163], v[200:203], v[92:95]
	v_mfma_f32_16x16x32_bf16 v[84:87], v[152:155], v[208:211], v[84:87]
	v_mfma_f32_16x16x32_bf16 v[76:79], v[160:163], v[208:211], v[76:79]
	s_setprio 1
	s_setprio 0
	v_mfma_f32_16x16x32_bf16 v[112:115], v[164:167], v[180:183], v[112:115]
	v_mfma_f32_16x16x32_bf16 v[104:107], v[172:175], v[180:183], v[104:107]
	v_mfma_f32_16x16x32_bf16 v[96:99], v[164:167], v[188:191], v[96:99]
	v_mfma_f32_16x16x32_bf16 v[88:91], v[172:175], v[188:191], v[88:91]
	v_mfma_f32_16x16x32_bf16 v[80:83], v[164:167], v[196:199], v[80:83]
	v_mfma_f32_16x16x32_bf16 v[72:75], v[172:175], v[196:199], v[72:75]
	v_mfma_f32_16x16x32_bf16 v[52:55], v[164:167], v[204:207], v[52:55]
	v_mfma_f32_16x16x32_bf16 v[48:51], v[172:175], v[204:207], v[48:51]
	v_mfma_f32_16x16x32_bf16 v[112:115], v[168:171], v[184:187], v[112:115]
	v_mfma_f32_16x16x32_bf16 v[104:107], v[176:179], v[184:187], v[104:107]
	v_mfma_f32_16x16x32_bf16 v[96:99], v[168:171], v[192:195], v[96:99]
	v_mfma_f32_16x16x32_bf16 v[88:91], v[176:179], v[192:195], v[88:91]
	v_mfma_f32_16x16x32_bf16 v[80:83], v[168:171], v[200:203], v[80:83]
	v_mfma_f32_16x16x32_bf16 v[72:75], v[176:179], v[200:203], v[72:75]
	v_mfma_f32_16x16x32_bf16 v[52:55], v[168:171], v[208:211], v[52:55]
	v_mfma_f32_16x16x32_bf16 v[48:51], v[176:179], v[208:211], v[48:51]
	s_setprio 1
	s_barrier
	s_mov_b32 m0, s64
	v_lshl_add_u64 v[140:141], v[140:141], 0, s[4:5]
	ds_read_b128 v[180:183], v147 offset:49152
	ds_read_b128 v[184:187], v147 offset:50176
	ds_read_b128 v[188:191], v147 offset:51200
	ds_read_b128 v[192:195], v147 offset:52224
	ds_read_b128 v[196:199], v147 offset:53248
	ds_read_b128 v[200:203], v147 offset:54272
	ds_read_b128 v[204:207], v147 offset:55296
	ds_read_b128 v[208:211], v147 offset:56320
	global_load_lds_dwordx4 v[140:141], off
	v_lshl_add_u64 v[140:141], v[212:213], 0, s[4:5]
	s_mov_b32 m0, s62
	s_nop 0
	global_load_lds_dwordx4 v[140:141], off
	v_lshl_add_u64 v[140:141], s[28:29], 0, v[128:129]
	s_mov_b32 m0, s63
	s_nop 0
	global_load_lds_dwordx4 v[140:141], off
	v_lshl_add_u64 v[140:141], s[28:29], 0, v[130:131]
	s_mov_b32 m0, s61
	s_nop 0
	global_load_lds_dwordx4 v[140:141], off
	v_lshl_add_u64 v[140:141], v[214:215], 0, s[4:5]
	s_mov_b32 m0, s53
	s_nop 0
	global_load_lds_dwordx4 v[140:141], off
	v_lshl_add_u64 v[140:141], v[216:217], 0, s[4:5]
	s_mov_b32 m0, s54
	s_nop 0
	global_load_lds_dwordx4 v[140:141], off
	s_waitcnt vmcnt(8)
	s_waitcnt lgkmcnt(0)
	s_barrier
	s_setprio 0
	s_waitcnt lgkmcnt(0)
	v_mfma_f32_16x16x32_bf16 v[44:47], v[148:151], v[180:183], v[44:47]
	v_mfma_f32_16x16x32_bf16 v[32:35], v[156:159], v[180:183], v[32:35]
	v_mfma_f32_16x16x32_bf16 v[4:7], v[148:151], v[188:191], v[4:7]
	v_mfma_f32_16x16x32_bf16 v[0:3], v[156:159], v[188:191], v[0:3]
	v_mfma_f32_16x16x32_bf16 v[28:31], v[148:151], v[196:199], v[28:31]
	v_mfma_f32_16x16x32_bf16 v[24:27], v[156:159], v[196:199], v[24:27]
	v_mfma_f32_16x16x32_bf16 v[12:15], v[148:151], v[204:207], v[12:15]
	v_mfma_f32_16x16x32_bf16 v[8:11], v[156:159], v[204:207], v[8:11]
	v_mfma_f32_16x16x32_bf16 v[44:47], v[152:155], v[184:187], v[44:47]
	v_mfma_f32_16x16x32_bf16 v[32:35], v[160:163], v[184:187], v[32:35]
	v_mfma_f32_16x16x32_bf16 v[4:7], v[152:155], v[192:195], v[4:7]
	v_mfma_f32_16x16x32_bf16 v[0:3], v[160:163], v[192:195], v[0:3]
	v_mfma_f32_16x16x32_bf16 v[28:31], v[152:155], v[200:203], v[28:31]
	v_mfma_f32_16x16x32_bf16 v[24:27], v[160:163], v[200:203], v[24:27]
	v_mfma_f32_16x16x32_bf16 v[12:15], v[152:155], v[208:211], v[12:15]
	v_mfma_f32_16x16x32_bf16 v[8:11], v[160:163], v[208:211], v[8:11]
	s_setprio 1
	s_setprio 0
	v_mfma_f32_16x16x32_bf16 v[68:71], v[164:167], v[180:183], v[68:71]
	v_mfma_f32_16x16x32_bf16 v[64:67], v[172:175], v[180:183], v[64:67]
	v_mfma_f32_16x16x32_bf16 v[60:63], v[164:167], v[188:191], v[60:63]
	v_mfma_f32_16x16x32_bf16 v[56:59], v[172:175], v[188:191], v[56:59]
	v_mfma_f32_16x16x32_bf16 v[40:43], v[164:167], v[196:199], v[40:43]
	v_mfma_f32_16x16x32_bf16 v[36:39], v[172:175], v[196:199], v[36:39]
	v_mfma_f32_16x16x32_bf16 v[20:23], v[164:167], v[204:207], v[20:23]
	v_mfma_f32_16x16x32_bf16 v[16:19], v[172:175], v[204:207], v[16:19]
	v_mfma_f32_16x16x32_bf16 v[68:71], v[168:171], v[184:187], v[68:71]
	v_mfma_f32_16x16x32_bf16 v[64:67], v[176:179], v[184:187], v[64:67]
	v_mfma_f32_16x16x32_bf16 v[60:63], v[168:171], v[192:195], v[60:63]
	v_mfma_f32_16x16x32_bf16 v[56:59], v[176:179], v[192:195], v[56:59]
	v_mfma_f32_16x16x32_bf16 v[40:43], v[168:171], v[200:203], v[40:43]
	v_mfma_f32_16x16x32_bf16 v[36:39], v[176:179], v[200:203], v[36:39]
	v_mfma_f32_16x16x32_bf16 v[20:23], v[168:171], v[208:211], v[20:23]
	v_mfma_f32_16x16x32_bf16 v[16:19], v[176:179], v[208:211], v[16:19]
	s_setprio 1
	s_barrier
	s_andn2_b64 vcc, exec, s[26:27]
	s_mov_b64 s[28:29], -1
	s_mov_b64 s[26:27], 0
	s_mov_b64 s[30:31], 0x100
	s_cbranch_vccz .LBB0_2838
	s_and_b64 vcc, exec, s[6:7]
	s_cbranch_vccz .LBB0_2841
	s_barrier

.LBB0_2859:
	ds_read_b128 v[124:127], v221
	ds_read_b128 v[132:135], v221 offset:1024
	ds_read_b128 v[136:139], v221 offset:2048
	ds_read_b128 v[140:143], v221 offset:3072
	ds_read_b128 v[144:147], v222
	ds_read_b128 v[148:151], v222 offset:1024
	ds_read_b128 v[152:155], v222 offset:2048
	ds_read_b128 v[156:159], v222 offset:3072
	s_add_u32 s30, s28, 0xfffc0080
	s_addc_u32 s31, s29, -1
	s_cmp_eq_u32 s54, 12
	s_cselect_b32 s35, s15, s31
	s_cselect_b32 s34, s50, s30
	s_cselect_b32 s31, s13, s53
	s_cselect_b32 s30, s51, s52
	v_lshl_add_u64 v[206:207], s[28:29], 0, v[180:181]
	s_add_i32 m0, s27, 0xc000
	ds_read_b128 v[160:163], v223
	ds_read_b128 v[164:167], v223 offset:1024
	ds_read_b128 v[168:171], v223 offset:2048
	ds_read_b128 v[186:189], v223 offset:3072
	ds_read_b128 v[190:193], v223 offset:4096
	ds_read_b128 v[194:197], v223 offset:5120
	ds_read_b128 v[198:201], v223 offset:6144
	ds_read_b128 v[202:205], v223 offset:7168
	global_load_lds_dwordx4 v[206:207], off
	v_lshl_add_u64 v[206:207], s[28:29], 0, v[182:183]
	s_add_i32 m0, s27, 0xe000
	s_nop 0
	global_load_lds_dwordx4 v[206:207], off
	s_waitcnt vmcnt(8)
	s_waitcnt lgkmcnt(0)
	s_barrier
	s_setprio 0
	s_waitcnt lgkmcnt(0)
	v_mfma_f32_16x16x32_bf16 v[120:123], v[124:127], v[160:163], v[120:123]
	v_mfma_f32_16x16x32_bf16 v[128:131], v[136:139], v[160:163], v[128:131]
	v_mfma_f32_16x16x32_bf16 v[108:111], v[124:127], v[168:171], v[108:111]
	v_mfma_f32_16x16x32_bf16 v[104:107], v[136:139], v[168:171], v[104:107]
	v_mfma_f32_16x16x32_bf16 v[92:95], v[124:127], v[190:193], v[92:95]
	v_mfma_f32_16x16x32_bf16 v[88:91], v[136:139], v[190:193], v[88:91]
	v_mfma_f32_16x16x32_bf16 v[76:79], v[124:127], v[198:201], v[76:79]
	v_mfma_f32_16x16x32_bf16 v[72:75], v[136:139], v[198:201], v[72:75]
	v_mfma_f32_16x16x32_bf16 v[120:123], v[132:135], v[164:167], v[120:123]
	v_mfma_f32_16x16x32_bf16 v[128:131], v[140:143], v[164:167], v[128:131]
	v_mfma_f32_16x16x32_bf16 v[108:111], v[132:135], v[186:189], v[108:111]
	v_mfma_f32_16x16x32_bf16 v[104:107], v[140:143], v[186:189], v[104:107]
	v_mfma_f32_16x16x32_bf16 v[92:95], v[132:135], v[194:197], v[92:95]
	v_mfma_f32_16x16x32_bf16 v[88:91], v[140:143], v[194:197], v[88:91]
	v_mfma_f32_16x16x32_bf16 v[76:79], v[132:135], v[202:205], v[76:79]
	v_mfma_f32_16x16x32_bf16 v[72:75], v[140:143], v[202:205], v[72:75]
	s_setprio 1
	s_setprio 0
	v_mfma_f32_16x16x32_bf16 v[116:119], v[144:147], v[160:163], v[116:119]
	v_mfma_f32_16x16x32_bf16 v[112:115], v[152:155], v[160:163], v[112:115]
	v_mfma_f32_16x16x32_bf16 v[100:103], v[144:147], v[168:171], v[100:103]
	v_mfma_f32_16x16x32_bf16 v[96:99], v[152:155], v[168:171], v[96:99]
	v_mfma_f32_16x16x32_bf16 v[84:87], v[144:147], v[190:193], v[84:87]
	v_mfma_f32_16x16x32_bf16 v[80:83], v[152:155], v[190:193], v[80:83]
	v_mfma_f32_16x16x32_bf16 v[68:71], v[144:147], v[198:201], v[68:71]
	v_mfma_f32_16x16x32_bf16 v[64:67], v[152:155], v[198:201], v[64:67]
	v_mfma_f32_16x16x32_bf16 v[116:119], v[148:151], v[164:167], v[116:119]
	v_mfma_f32_16x16x32_bf16 v[112:115], v[156:159], v[164:167], v[112:115]
	v_mfma_f32_16x16x32_bf16 v[100:103], v[148:151], v[186:189], v[100:103]
	v_mfma_f32_16x16x32_bf16 v[96:99], v[156:159], v[186:189], v[96:99]
	v_mfma_f32_16x16x32_bf16 v[84:87], v[148:151], v[194:197], v[84:87]
	v_mfma_f32_16x16x32_bf16 v[80:83], v[156:159], v[194:197], v[80:83]
	v_mfma_f32_16x16x32_bf16 v[68:71], v[148:151], v[202:205], v[68:71]
	v_mfma_f32_16x16x32_bf16 v[64:67], v[156:159], v[202:205], v[64:67]
	s_setprio 1
	s_barrier
	s_add_i32 s55, s46, s37
	v_lshl_add_u64 v[206:207], s[30:31], 0, v[174:175]
	s_mov_b32 m0, s55
	ds_read_b128 v[160:163], v223 offset:16384
	ds_read_b128 v[164:167], v223 offset:17408
	ds_read_b128 v[168:171], v223 offset:18432
	ds_read_b128 v[186:189], v223 offset:19456
	ds_read_b128 v[190:193], v223 offset:20480
	ds_read_b128 v[194:197], v223 offset:21504
	ds_read_b128 v[198:201], v223 offset:22528
	ds_read_b128 v[202:205], v223 offset:23552
	global_load_lds_dwordx4 v[206:207], off
	s_add_i32 m0, s55, 0x2000
	s_add_u32 s56, s30, 0x40000
	v_lshl_add_u64 v[208:209], s[30:31], 0, v[172:173]
	s_addc_u32 s57, s31, 0
	s_add_i32 s55, s47, s37
	global_load_lds_dwordx4 v[208:209], off
	v_lshl_add_u64 v[210:211], s[56:57], 0, v[174:175]
	s_mov_b32 m0, s55
	v_lshl_add_u64 v[212:213], s[34:35], 0, v[178:179]
	global_load_lds_dwordx4 v[210:211], off
	v_lshl_add_u64 v[210:211], s[56:57], 0, v[172:173]
	s_add_i32 m0, s55, 0x2000
	s_nop 0
	global_load_lds_dwordx4 v[210:211], off
	v_lshl_add_u64 v[210:211], s[34:35], 0, v[176:177]
	s_mov_b32 m0, s27
	s_nop 0
	global_load_lds_dwordx4 v[210:211], off
	s_mov_b32 m0, s39
	s_nop 0
	global_load_lds_dwordx4 v[212:213], off
	s_waitcnt vmcnt(8)
	s_waitcnt lgkmcnt(0)
	s_barrier
	s_setprio 0
	s_waitcnt lgkmcnt(0)
	v_mfma_f32_16x16x32_bf16 v[60:63], v[124:127], v[160:163], v[60:63]
	v_mfma_f32_16x16x32_bf16 v[52:55], v[136:139], v[160:163], v[52:55]
	v_mfma_f32_16x16x32_bf16 v[44:47], v[124:127], v[168:171], v[44:47]
	v_mfma_f32_16x16x32_bf16 v[36:39], v[136:139], v[168:171], v[36:39]
	v_mfma_f32_16x16x32_bf16 v[28:31], v[124:127], v[190:193], v[28:31]
	v_mfma_f32_16x16x32_bf16 v[24:27], v[136:139], v[190:193], v[24:27]
	v_mfma_f32_16x16x32_bf16 v[12:15], v[124:127], v[198:201], v[12:15]
	v_mfma_f32_16x16x32_bf16 v[8:11], v[136:139], v[198:201], v[8:11]
	v_mfma_f32_16x16x32_bf16 v[60:63], v[132:135], v[164:167], v[60:63]
	v_mfma_f32_16x16x32_bf16 v[52:55], v[140:143], v[164:167], v[52:55]
	v_mfma_f32_16x16x32_bf16 v[44:47], v[132:135], v[186:189], v[44:47]
	v_mfma_f32_16x16x32_bf16 v[36:39], v[140:143], v[186:189], v[36:39]
	v_mfma_f32_16x16x32_bf16 v[28:31], v[132:135], v[194:197], v[28:31]
	v_mfma_f32_16x16x32_bf16 v[24:27], v[140:143], v[194:197], v[24:27]
	v_mfma_f32_16x16x32_bf16 v[12:15], v[132:135], v[202:205], v[12:15]
	v_mfma_f32_16x16x32_bf16 v[8:11], v[140:143], v[202:205], v[8:11]
	s_setprio 1
	s_setprio 0
	v_mfma_f32_16x16x32_bf16 v[56:59], v[144:147], v[160:163], v[56:59]
	v_mfma_f32_16x16x32_bf16 v[48:51], v[152:155], v[160:163], v[48:51]
	v_mfma_f32_16x16x32_bf16 v[40:43], v[144:147], v[168:171], v[40:43]
	v_mfma_f32_16x16x32_bf16 v[32:35], v[152:155], v[168:171], v[32:35]
	v_mfma_f32_16x16x32_bf16 v[20:23], v[144:147], v[190:193], v[20:23]
	v_mfma_f32_16x16x32_bf16 v[16:19], v[152:155], v[190:193], v[16:19]
	v_mfma_f32_16x16x32_bf16 v[4:7], v[144:147], v[198:201], v[4:7]
	v_mfma_f32_16x16x32_bf16 v[0:3], v[152:155], v[198:201], v[0:3]
	v_mfma_f32_16x16x32_bf16 v[56:59], v[148:151], v[164:167], v[56:59]
	v_mfma_f32_16x16x32_bf16 v[48:51], v[156:159], v[164:167], v[48:51]
	v_mfma_f32_16x16x32_bf16 v[40:43], v[148:151], v[186:189], v[40:43]
	v_mfma_f32_16x16x32_bf16 v[32:35], v[156:159], v[186:189], v[32:35]
	v_mfma_f32_16x16x32_bf16 v[20:23], v[148:151], v[194:197], v[20:23]
	v_mfma_f32_16x16x32_bf16 v[16:19], v[156:159], v[194:197], v[16:19]
	v_mfma_f32_16x16x32_bf16 v[4:7], v[148:151], v[202:205], v[4:7]
	v_mfma_f32_16x16x32_bf16 v[0:3], v[156:159], v[202:205], v[0:3]
	s_setprio 1
	s_barrier
	s_add_i32 s55, 0, 0x18000
	s_add_i32 s56, 0, 0x1c000
	v_add_u32_e32 v140, s55, v219
	v_add_u32_e32 v156, s56, v219
	ds_read_b128 v[124:127], v140
	ds_read_b128 v[132:135], v140 offset:1024
	ds_read_b128 v[136:139], v140 offset:2048
	ds_read_b128 v[140:143], v140 offset:3072
	ds_read_b128 v[144:147], v156
	ds_read_b128 v[148:151], v156 offset:1024
	ds_read_b128 v[152:155], v156 offset:2048
	ds_read_b128 v[156:159], v156 offset:3072
	s_add_u32 s34, s34, 0x40000
	s_addc_u32 s35, s35, 0
	s_mov_b32 m0, s40
	v_lshl_add_u64 v[214:215], s[34:35], 0, v[176:177]
	ds_read_b128 v[160:163], v223 offset:32768
	ds_read_b128 v[164:167], v223 offset:33792
	ds_read_b128 v[168:171], v223 offset:34816
	ds_read_b128 v[186:189], v223 offset:35840
	ds_read_b128 v[190:193], v223 offset:36864
	ds_read_b128 v[194:197], v223 offset:37888
	ds_read_b128 v[198:201], v223 offset:38912
	ds_read_b128 v[202:205], v223 offset:39936
	global_load_lds_dwordx4 v[214:215], off
	v_lshl_add_u64 v[214:215], s[34:35], 0, v[178:179]
	s_mov_b32 m0, s41
	s_nop 0
	global_load_lds_dwordx4 v[214:215], off
	s_waitcnt vmcnt(8)
	s_waitcnt lgkmcnt(0)
	s_barrier
	s_setprio 0
	s_waitcnt lgkmcnt(0)
	v_mfma_f32_16x16x32_bf16 v[120:123], v[124:127], v[160:163], v[120:123]
	v_mfma_f32_16x16x32_bf16 v[128:131], v[136:139], v[160:163], v[128:131]
	v_mfma_f32_16x16x32_bf16 v[108:111], v[124:127], v[168:171], v[108:111]
	v_mfma_f32_16x16x32_bf16 v[104:107], v[136:139], v[168:171], v[104:107]
	v_mfma_f32_16x16x32_bf16 v[92:95], v[124:127], v[190:193], v[92:95]
	v_mfma_f32_16x16x32_bf16 v[88:91], v[136:139], v[190:193], v[88:91]
	v_mfma_f32_16x16x32_bf16 v[76:79], v[124:127], v[198:201], v[76:79]
	v_mfma_f32_16x16x32_bf16 v[72:75], v[136:139], v[198:201], v[72:75]
	v_mfma_f32_16x16x32_bf16 v[120:123], v[132:135], v[164:167], v[120:123]
	v_mfma_f32_16x16x32_bf16 v[128:131], v[140:143], v[164:167], v[128:131]
	v_mfma_f32_16x16x32_bf16 v[108:111], v[132:135], v[186:189], v[108:111]
	v_mfma_f32_16x16x32_bf16 v[104:107], v[140:143], v[186:189], v[104:107]
	v_mfma_f32_16x16x32_bf16 v[92:95], v[132:135], v[194:197], v[92:95]
	v_mfma_f32_16x16x32_bf16 v[88:91], v[140:143], v[194:197], v[88:91]
	v_mfma_f32_16x16x32_bf16 v[76:79], v[132:135], v[202:205], v[76:79]
	v_mfma_f32_16x16x32_bf16 v[72:75], v[140:143], v[202:205], v[72:75]
	s_setprio 1
	s_setprio 0
	v_mfma_f32_16x16x32_bf16 v[116:119], v[144:147], v[160:163], v[116:119]
	v_mfma_f32_16x16x32_bf16 v[112:115], v[152:155], v[160:163], v[112:115]
	v_mfma_f32_16x16x32_bf16 v[100:103], v[144:147], v[168:171], v[100:103]
	v_mfma_f32_16x16x32_bf16 v[96:99], v[152:155], v[168:171], v[96:99]
	v_mfma_f32_16x16x32_bf16 v[84:87], v[144:147], v[190:193], v[84:87]
	v_mfma_f32_16x16x32_bf16 v[80:83], v[152:155], v[190:193], v[80:83]
	v_mfma_f32_16x16x32_bf16 v[68:71], v[144:147], v[198:201], v[68:71]
	v_mfma_f32_16x16x32_bf16 v[64:67], v[152:155], v[198:201], v[64:67]
	v_mfma_f32_16x16x32_bf16 v[116:119], v[148:151], v[164:167], v[116:119]
	v_mfma_f32_16x16x32_bf16 v[112:115], v[156:159], v[164:167], v[112:115]
	v_mfma_f32_16x16x32_bf16 v[100:103], v[148:151], v[186:189], v[100:103]
	v_mfma_f32_16x16x32_bf16 v[96:99], v[156:159], v[186:189], v[96:99]
	v_mfma_f32_16x16x32_bf16 v[84:87], v[148:151], v[194:197], v[84:87]
	v_mfma_f32_16x16x32_bf16 v[80:83], v[156:159], v[194:197], v[80:83]
	v_mfma_f32_16x16x32_bf16 v[68:71], v[148:151], v[202:205], v[68:71]
	v_mfma_f32_16x16x32_bf16 v[64:67], v[156:159], v[202:205], v[64:67]
	s_setprio 1
	s_barrier
	s_add_i32 s34, s55, s37
	v_lshl_add_u64 v[206:207], v[206:207], 0, s[2:3]
	s_mov_b32 m0, s34
	ds_read_b128 v[160:163], v223 offset:49152
	ds_read_b128 v[164:167], v223 offset:50176
	ds_read_b128 v[168:171], v223 offset:51200
	ds_read_b128 v[186:189], v223 offset:52224
	ds_read_b128 v[190:193], v223 offset:53248
	ds_read_b128 v[194:197], v223 offset:54272
	ds_read_b128 v[198:201], v223 offset:55296
	ds_read_b128 v[202:205], v223 offset:56320
	global_load_lds_dwordx4 v[206:207], off
	s_add_i32 m0, s34, 0x2000
	s_add_u32 s30, s30, 0x40080
	v_lshl_add_u64 v[206:207], v[208:209], 0, s[2:3]
	s_addc_u32 s31, s31, 0
	s_add_i32 s34, s56, s37
	global_load_lds_dwordx4 v[206:207], off
	v_lshl_add_u64 v[206:207], s[30:31], 0, v[174:175]
	s_mov_b32 m0, s34
	s_nop 0
	global_load_lds_dwordx4 v[206:207], off
	v_lshl_add_u64 v[206:207], s[30:31], 0, v[172:173]
	s_add_i32 m0, s34, 0x2000
	s_nop 0
	global_load_lds_dwordx4 v[206:207], off
	v_lshl_add_u64 v[206:207], v[210:211], 0, s[2:3]
	s_mov_b32 m0, s43
	s_nop 0
	global_load_lds_dwordx4 v[206:207], off
	v_lshl_add_u64 v[206:207], v[212:213], 0, s[2:3]
	s_mov_b32 m0, s44
	s_nop 0
	global_load_lds_dwordx4 v[206:207], off
	s_waitcnt vmcnt(8)
	s_waitcnt lgkmcnt(0)
	s_barrier
	s_setprio 0
	s_waitcnt lgkmcnt(0)
	v_mfma_f32_16x16x32_bf16 v[60:63], v[124:127], v[160:163], v[60:63]
	v_mfma_f32_16x16x32_bf16 v[52:55], v[136:139], v[160:163], v[52:55]
	v_mfma_f32_16x16x32_bf16 v[44:47], v[124:127], v[168:171], v[44:47]
	v_mfma_f32_16x16x32_bf16 v[36:39], v[136:139], v[168:171], v[36:39]
	v_mfma_f32_16x16x32_bf16 v[28:31], v[124:127], v[190:193], v[28:31]
	v_mfma_f32_16x16x32_bf16 v[24:27], v[136:139], v[190:193], v[24:27]
	v_mfma_f32_16x16x32_bf16 v[12:15], v[124:127], v[198:201], v[12:15]
	v_mfma_f32_16x16x32_bf16 v[8:11], v[136:139], v[198:201], v[8:11]
	v_mfma_f32_16x16x32_bf16 v[60:63], v[132:135], v[164:167], v[60:63]
	v_mfma_f32_16x16x32_bf16 v[52:55], v[140:143], v[164:167], v[52:55]
	v_mfma_f32_16x16x32_bf16 v[44:47], v[132:135], v[186:189], v[44:47]
	v_mfma_f32_16x16x32_bf16 v[36:39], v[140:143], v[186:189], v[36:39]
	v_mfma_f32_16x16x32_bf16 v[28:31], v[132:135], v[194:197], v[28:31]
	v_mfma_f32_16x16x32_bf16 v[24:27], v[140:143], v[194:197], v[24:27]
	v_mfma_f32_16x16x32_bf16 v[12:15], v[132:135], v[202:205], v[12:15]
	v_mfma_f32_16x16x32_bf16 v[8:11], v[140:143], v[202:205], v[8:11]
	s_setprio 1
	s_setprio 0
	v_mfma_f32_16x16x32_bf16 v[56:59], v[144:147], v[160:163], v[56:59]
	v_mfma_f32_16x16x32_bf16 v[48:51], v[152:155], v[160:163], v[48:51]
	v_mfma_f32_16x16x32_bf16 v[40:43], v[144:147], v[168:171], v[40:43]
	v_mfma_f32_16x16x32_bf16 v[32:35], v[152:155], v[168:171], v[32:35]
	v_mfma_f32_16x16x32_bf16 v[20:23], v[144:147], v[190:193], v[20:23]
	v_mfma_f32_16x16x32_bf16 v[16:19], v[152:155], v[190:193], v[16:19]
	v_mfma_f32_16x16x32_bf16 v[4:7], v[144:147], v[198:201], v[4:7]
	v_mfma_f32_16x16x32_bf16 v[0:3], v[152:155], v[198:201], v[0:3]
	v_mfma_f32_16x16x32_bf16 v[56:59], v[148:151], v[164:167], v[56:59]
	v_mfma_f32_16x16x32_bf16 v[48:51], v[156:159], v[164:167], v[48:51]
	v_mfma_f32_16x16x32_bf16 v[40:43], v[148:151], v[186:189], v[40:43]
	v_mfma_f32_16x16x32_bf16 v[32:35], v[156:159], v[186:189], v[32:35]
	v_mfma_f32_16x16x32_bf16 v[20:23], v[148:151], v[194:197], v[20:23]
	v_mfma_f32_16x16x32_bf16 v[16:19], v[156:159], v[194:197], v[16:19]
	v_mfma_f32_16x16x32_bf16 v[4:7], v[148:151], v[202:205], v[4:7]
	v_mfma_f32_16x16x32_bf16 v[0:3], v[156:159], v[202:205], v[0:3]
	s_setprio 1
	s_barrier
	s_add_i32 s54, s54, 2
	s_add_u32 s28, s28, 0x100
	s_addc_u32 s29, s29, 0
	s_add_u32 s52, s52, 0x100
	s_addc_u32 s53, s53, 0
	s_cmp_gt_u32 s54, 13
	s_cbranch_scc0 .LBB0_2859
	s_and_b64 vcc, exec, s[4:5]
	s_cbranch_vccz .LBB0_2862
	s_barrier

.LBB0_2932:
	s_waitcnt lgkmcnt(0)
	ds_read_b128 v[20:23], v188
	ds_read_b128 v[24:27], v189
	ds_read_b128 v[16:19], v183
	ds_read_b128 v[0:3], v184
	ds_read_b128 v[28:31], v190
	ds_read_b128 v[4:7], v191
	ds_read_b128 v[8:11], v192
	ds_read_b128 v[12:15], v193
	s_add_u32 s24, s22, 0xfffe0080
	s_addc_u32 s25, s23, -1
	s_cmp_eq_u32 s58, 4
	s_cselect_b32 s27, s15, s25
	s_cselect_b32 s26, s54, s24
	s_cselect_b32 s25, s13, s57
	s_cselect_b32 s24, s55, s56
	v_lshl_add_u64 v[232:233], s[22:23], 0, v[168:169]
	s_add_i32 m0, s33, 0xc000
	ds_read_b128 v[174:177], v200
	ds_read_b128 v[178:181], v200 offset:1024
	ds_read_b128 v[208:211], v200 offset:2048
	ds_read_b128 v[212:215], v200 offset:3072
	ds_read_b128 v[216:219], v200 offset:4096
	ds_read_b128 v[220:223], v200 offset:5120
	ds_read_b128 v[224:227], v200 offset:6144
	ds_read_b128 v[228:231], v200 offset:7168
	global_load_lds_dwordx4 v[232:233], off
	v_lshl_add_u64 v[232:233], s[22:23], 0, v[170:171]
	s_add_i32 m0, s33, 0xe000
	s_nop 0
	global_load_lds_dwordx4 v[232:233], off
	s_waitcnt vmcnt(8)
	s_waitcnt lgkmcnt(0)
	s_barrier
	s_setprio 0
	s_waitcnt lgkmcnt(0)
	v_mfma_f32_16x16x128_f8f6f4 v[156:159], v[16:23], v[174:181], v[156:159]
	v_mfma_f32_16x16x128_f8f6f4 v[124:127], v[24:31], v[174:181], v[124:127]
	v_mfma_f32_16x16x128_f8f6f4 v[144:147], v[16:23], v[208:215], v[144:147]
	v_mfma_f32_16x16x128_f8f6f4 v[112:115], v[24:31], v[208:215], v[112:115]
	v_mfma_f32_16x16x128_f8f6f4 v[140:143], v[16:23], v[216:223], v[140:143]
	v_mfma_f32_16x16x128_f8f6f4 v[108:111], v[24:31], v[216:223], v[108:111]
	v_mfma_f32_16x16x128_f8f6f4 v[136:139], v[16:23], v[224:231], v[136:139]
	v_mfma_f32_16x16x128_f8f6f4 v[96:99], v[24:31], v[224:231], v[96:99]
	s_setprio 1
	s_setprio 0
	v_mfma_f32_16x16x128_f8f6f4 v[72:75], v[0:7], v[174:181], v[72:75]
	v_mfma_f32_16x16x128_f8f6f4 v[44:47], v[8:15], v[174:181], v[44:47]
	v_mfma_f32_16x16x128_f8f6f4 v[56:59], v[0:7], v[208:215], v[56:59]
	v_mfma_f32_16x16x128_f8f6f4 v[40:43], v[8:15], v[208:215], v[40:43]
	v_mfma_f32_16x16x128_f8f6f4 v[52:55], v[0:7], v[216:223], v[52:55]
	v_mfma_f32_16x16x128_f8f6f4 v[36:39], v[8:15], v[216:223], v[36:39]
	v_mfma_f32_16x16x128_f8f6f4 v[48:51], v[0:7], v[224:231], v[48:51]
	v_mfma_f32_16x16x128_f8f6f4 v[32:35], v[8:15], v[224:231], v[32:35]
	s_setprio 1
	s_barrier
	s_mov_b32 m0, s34
	v_lshl_add_u64 v[174:175], s[24:25], 0, v[162:163]
	s_add_u32 s60, s24, 0x20000
	ds_read_b128 v[208:211], v200 offset:16384
	ds_read_b128 v[212:215], v200 offset:17408
	ds_read_b128 v[216:219], v200 offset:18432
	ds_read_b128 v[220:223], v200 offset:19456
	ds_read_b128 v[224:227], v200 offset:20480
	ds_read_b128 v[228:231], v200 offset:21504
	ds_read_b128 v[232:235], v200 offset:22528
	ds_read_b128 v[236:239], v200 offset:23552
	global_load_lds_dwordx4 v[174:175], off
	v_lshl_add_u64 v[176:177], s[24:25], 0, v[160:161]
	s_mov_b32 m0, s35
	s_addc_u32 s61, s25, 0
	global_load_lds_dwordx4 v[176:177], off
	v_lshl_add_u64 v[178:179], s[60:61], 0, v[162:163]
	s_mov_b32 m0, s36
	v_lshl_add_u64 v[180:181], s[26:27], 0, v[166:167]
	global_load_lds_dwordx4 v[178:179], off
	v_lshl_add_u64 v[178:179], s[60:61], 0, v[160:161]
	s_mov_b32 m0, s37
	s_nop 0
	global_load_lds_dwordx4 v[178:179], off
	v_lshl_add_u64 v[178:179], s[26:27], 0, v[164:165]
	s_mov_b32 m0, s33
	s_nop 0
	global_load_lds_dwordx4 v[178:179], off
	s_mov_b32 m0, s38
	s_nop 0
	global_load_lds_dwordx4 v[180:181], off
	s_waitcnt vmcnt(8)
	s_waitcnt lgkmcnt(0)
	s_barrier
	s_setprio 0
	s_waitcnt lgkmcnt(0)
	v_mfma_f32_16x16x128_f8f6f4 v[128:131], v[16:23], v[208:215], v[128:131]
	v_mfma_f32_16x16x128_f8f6f4 v[84:87], v[24:31], v[208:215], v[84:87]
	v_mfma_f32_16x16x128_f8f6f4 v[116:119], v[16:23], v[216:223], v[116:119]
	v_mfma_f32_16x16x128_f8f6f4 v[64:67], v[24:31], v[216:223], v[64:67]
	v_mfma_f32_16x16x128_f8f6f4 v[148:151], v[16:23], v[224:231], v[148:151]
	v_mfma_f32_16x16x128_f8f6f4 v[120:123], v[24:31], v[224:231], v[120:123]
	v_mfma_f32_16x16x128_f8f6f4 v[152:155], v[16:23], v[232:239], v[152:155]
	v_mfma_f32_16x16x128_f8f6f4 v[132:135], v[24:31], v[232:239], v[132:135]
	s_setprio 1
	s_setprio 0
	v_mfma_f32_16x16x128_f8f6f4 v[88:91], v[0:7], v[208:215], v[88:91]
	v_mfma_f32_16x16x128_f8f6f4 v[60:63], v[8:15], v[208:215], v[60:63]
	v_mfma_f32_16x16x128_f8f6f4 v[92:95], v[0:7], v[216:223], v[92:95]
	v_mfma_f32_16x16x128_f8f6f4 v[68:71], v[8:15], v[216:223], v[68:71]
	v_mfma_f32_16x16x128_f8f6f4 v[100:103], v[0:7], v[224:231], v[100:103]
	v_mfma_f32_16x16x128_f8f6f4 v[76:79], v[8:15], v[224:231], v[76:79]
	v_mfma_f32_16x16x128_f8f6f4 v[104:107], v[0:7], v[232:239], v[104:107]
	v_mfma_f32_16x16x128_f8f6f4 v[80:83], v[8:15], v[232:239], v[80:83]
	s_setprio 1
	s_barrier
	ds_read_b128 v[4:7], v194
	ds_read_b128 v[8:11], v195
	ds_read_b128 v[0:3], v185
	ds_read_b128 v[16:19], v186
	ds_read_b128 v[12:15], v196
	ds_read_b128 v[20:23], v197
	ds_read_b128 v[24:27], v198
	ds_read_b128 v[28:31], v199
	s_add_u32 s26, s26, 0x20000
	s_addc_u32 s27, s27, 0
	s_mov_b32 m0, s39
	v_lshl_add_u64 v[240:241], s[26:27], 0, v[164:165]
	ds_read_b128 v[208:211], v200 offset:32768
	ds_read_b128 v[212:215], v200 offset:33792
	ds_read_b128 v[216:219], v200 offset:34816
	ds_read_b128 v[220:223], v200 offset:35840
	ds_read_b128 v[224:227], v200 offset:36864
	ds_read_b128 v[228:231], v200 offset:37888
	ds_read_b128 v[232:235], v200 offset:38912
	ds_read_b128 v[236:239], v200 offset:39936
	global_load_lds_dwordx4 v[240:241], off
	v_lshl_add_u64 v[240:241], s[26:27], 0, v[166:167]
	s_mov_b32 m0, s40
	s_nop 0
	global_load_lds_dwordx4 v[240:241], off
	s_waitcnt vmcnt(8)
	s_waitcnt lgkmcnt(0)
	s_barrier
	s_setprio 0
	s_waitcnt lgkmcnt(0)
	v_mfma_f32_16x16x128_f8f6f4 v[156:159], v[0:7], v[208:215], v[156:159]
	v_mfma_f32_16x16x128_f8f6f4 v[124:127], v[8:15], v[208:215], v[124:127]
	v_mfma_f32_16x16x128_f8f6f4 v[144:147], v[0:7], v[216:223], v[144:147]
	v_mfma_f32_16x16x128_f8f6f4 v[112:115], v[8:15], v[216:223], v[112:115]
	v_mfma_f32_16x16x128_f8f6f4 v[140:143], v[0:7], v[224:231], v[140:143]
	v_mfma_f32_16x16x128_f8f6f4 v[108:111], v[8:15], v[224:231], v[108:111]
	v_mfma_f32_16x16x128_f8f6f4 v[136:139], v[0:7], v[232:239], v[136:139]
	v_mfma_f32_16x16x128_f8f6f4 v[96:99], v[8:15], v[232:239], v[96:99]
	s_setprio 1
	s_setprio 0
	v_mfma_f32_16x16x128_f8f6f4 v[72:75], v[16:23], v[208:215], v[72:75]
	v_mfma_f32_16x16x128_f8f6f4 v[44:47], v[24:31], v[208:215], v[44:47]
	v_mfma_f32_16x16x128_f8f6f4 v[56:59], v[16:23], v[216:223], v[56:59]
	v_mfma_f32_16x16x128_f8f6f4 v[40:43], v[24:31], v[216:223], v[40:43]
	v_mfma_f32_16x16x128_f8f6f4 v[52:55], v[16:23], v[224:231], v[52:55]
	v_mfma_f32_16x16x128_f8f6f4 v[36:39], v[24:31], v[224:231], v[36:39]
	v_mfma_f32_16x16x128_f8f6f4 v[48:51], v[16:23], v[232:239], v[48:51]
	v_mfma_f32_16x16x128_f8f6f4 v[32:35], v[24:31], v[232:239], v[32:35]
	s_setprio 1
	s_barrier
	s_mov_b32 m0, s42
	v_lshl_add_u64 v[174:175], v[174:175], 0, s[8:9]
	s_add_u32 s24, s24, 0x20080
	ds_read_b128 v[208:211], v200 offset:49152
	ds_read_b128 v[212:215], v200 offset:50176
	ds_read_b128 v[216:219], v200 offset:51200
	ds_read_b128 v[220:223], v200 offset:52224
	ds_read_b128 v[224:227], v200 offset:53248
	ds_read_b128 v[228:231], v200 offset:54272
	ds_read_b128 v[232:235], v200 offset:55296
	ds_read_b128 v[236:239], v200 offset:56320
	global_load_lds_dwordx4 v[174:175], off
	v_lshl_add_u64 v[174:175], v[176:177], 0, s[8:9]
	s_mov_b32 m0, s43
	s_addc_u32 s25, s25, 0
	global_load_lds_dwordx4 v[174:175], off
	v_lshl_add_u64 v[174:175], s[24:25], 0, v[162:163]
	s_mov_b32 m0, s46
	s_nop 0
	global_load_lds_dwordx4 v[174:175], off
	v_lshl_add_u64 v[174:175], s[24:25], 0, v[160:161]
	s_mov_b32 m0, s47
	s_nop 0
	global_load_lds_dwordx4 v[174:175], off
	v_lshl_add_u64 v[174:175], v[178:179], 0, s[8:9]
	s_mov_b32 m0, s44
	s_nop 0
	global_load_lds_dwordx4 v[174:175], off
	v_lshl_add_u64 v[174:175], v[180:181], 0, s[8:9]
	s_mov_b32 m0, s45
	s_nop 0
	global_load_lds_dwordx4 v[174:175], off
	s_waitcnt vmcnt(8)
	s_waitcnt lgkmcnt(0)
	s_barrier
	s_setprio 0
	s_waitcnt lgkmcnt(0)
	v_mfma_f32_16x16x128_f8f6f4 v[128:131], v[0:7], v[208:215], v[128:131]
	v_mfma_f32_16x16x128_f8f6f4 v[84:87], v[8:15], v[208:215], v[84:87]
	v_mfma_f32_16x16x128_f8f6f4 v[116:119], v[0:7], v[216:223], v[116:119]
	v_mfma_f32_16x16x128_f8f6f4 v[64:67], v[8:15], v[216:223], v[64:67]
	v_mfma_f32_16x16x128_f8f6f4 v[148:151], v[0:7], v[224:231], v[148:151]
	v_mfma_f32_16x16x128_f8f6f4 v[120:123], v[8:15], v[224:231], v[120:123]
	v_mfma_f32_16x16x128_f8f6f4 v[152:155], v[0:7], v[232:239], v[152:155]
	v_mfma_f32_16x16x128_f8f6f4 v[132:135], v[8:15], v[232:239], v[132:135]
	s_setprio 1
	s_setprio 0
	v_mfma_f32_16x16x128_f8f6f4 v[88:91], v[16:23], v[208:215], v[88:91]
	v_mfma_f32_16x16x128_f8f6f4 v[60:63], v[24:31], v[208:215], v[60:63]
	v_mfma_f32_16x16x128_f8f6f4 v[92:95], v[16:23], v[216:223], v[92:95]
	v_mfma_f32_16x16x128_f8f6f4 v[68:71], v[24:31], v[216:223], v[68:71]
	v_mfma_f32_16x16x128_f8f6f4 v[100:103], v[16:23], v[224:231], v[100:103]
	v_mfma_f32_16x16x128_f8f6f4 v[76:79], v[24:31], v[224:231], v[76:79]
	v_mfma_f32_16x16x128_f8f6f4 v[104:107], v[16:23], v[232:239], v[104:107]
	v_mfma_f32_16x16x128_f8f6f4 v[80:83], v[24:31], v[232:239], v[80:83]
	s_setprio 1
	s_barrier
	s_add_i32 s58, s58, 2
	s_add_u32 s22, s22, 0x100
	s_addc_u32 s23, s23, 0
	s_add_u32 s56, s56, 0x100
	s_addc_u32 s57, s57, 0
	s_cmp_gt_u32 s58, 5
	s_cbranch_scc0 .LBB0_2932
	s_nop 15
	s_nop 7
	s_and_b64 vcc, exec, s[10:11]
	s_cbranch_vccz .LBB0_2935
	s_barrier

.LBB0_3128:
	ds_read_b128 v[20:23], v213
	ds_read_b128 v[24:27], v214
	ds_read_b128 v[16:19], v209
	ds_read_b128 v[0:3], v210
	ds_read_b128 v[28:31], v215
	ds_read_b128 v[4:7], v216
	ds_read_b128 v[8:11], v217
	ds_read_b128 v[12:15], v218
	s_add_u32 s6, s2, 0xfffe0080
	s_addc_u32 s7, s3, -1
	s_cmp_eq_u32 s49, 4
	s_cselect_b32 s47, s1, s7
	s_cselect_b32 s46, s5, s6
	s_cselect_b32 s7, s33, s48
	s_cselect_b32 s6, s37, s39
	v_lshl_add_u64 v[202:203], s[2:3], 0, v[194:195]
	s_add_i32 m0, s55, 0xc000
	ds_read_b128 v[160:163], v225
	ds_read_b128 v[164:167], v225 offset:1024
	ds_read_b128 v[168:171], v225 offset:2048
	ds_read_b128 v[172:175], v225 offset:3072
	ds_read_b128 v[176:179], v225 offset:4096
	ds_read_b128 v[180:183], v225 offset:5120
	ds_read_b128 v[232:235], v225 offset:6144
	ds_read_b128 v[236:239], v225 offset:7168
	global_load_lds_dwordx4 v[202:203], off
	v_lshl_add_u64 v[202:203], s[2:3], 0, v[196:197]
	s_add_i32 m0, s55, 0xe000
	s_nop 0
	global_load_lds_dwordx4 v[202:203], off
	s_waitcnt vmcnt(8)
	s_waitcnt lgkmcnt(0)
	s_barrier
	s_setprio 0
	s_waitcnt lgkmcnt(0)
	v_mfma_f32_16x16x128_f8f6f4 v[156:159], v[16:23], v[160:167], v[156:159]
	v_mfma_f32_16x16x128_f8f6f4 v[152:155], v[24:31], v[160:167], v[152:155]
	v_mfma_f32_16x16x128_f8f6f4 v[140:143], v[16:23], v[168:175], v[140:143]
	v_mfma_f32_16x16x128_f8f6f4 v[136:139], v[24:31], v[168:175], v[136:139]
	v_mfma_f32_16x16x128_f8f6f4 v[124:127], v[16:23], v[176:183], v[124:127]
	v_mfma_f32_16x16x128_f8f6f4 v[120:123], v[24:31], v[176:183], v[120:123]
	v_mfma_f32_16x16x128_f8f6f4 v[108:111], v[16:23], v[232:239], v[108:111]
	v_mfma_f32_16x16x128_f8f6f4 v[104:107], v[24:31], v[232:239], v[104:107]
	s_setprio 1
	s_setprio 0
	v_mfma_f32_16x16x128_f8f6f4 v[148:151], v[0:7], v[160:167], v[148:151]
	v_mfma_f32_16x16x128_f8f6f4 v[144:147], v[8:15], v[160:167], v[144:147]
	v_mfma_f32_16x16x128_f8f6f4 v[132:135], v[0:7], v[168:175], v[132:135]
	v_mfma_f32_16x16x128_f8f6f4 v[128:131], v[8:15], v[168:175], v[128:131]
	v_mfma_f32_16x16x128_f8f6f4 v[116:119], v[0:7], v[176:183], v[116:119]
	v_mfma_f32_16x16x128_f8f6f4 v[112:115], v[8:15], v[176:183], v[112:115]
	v_mfma_f32_16x16x128_f8f6f4 v[100:103], v[0:7], v[232:239], v[100:103]
	v_mfma_f32_16x16x128_f8f6f4 v[96:99], v[8:15], v[232:239], v[96:99]
	s_setprio 1
	s_barrier
	s_mov_b32 m0, s56
	v_lshl_add_u64 v[160:161], s[6:7], 0, v[184:185]
	s_add_u32 s50, s6, 0x20000
	ds_read_b128 v[168:171], v225 offset:16384
	ds_read_b128 v[172:175], v225 offset:17408
	ds_read_b128 v[176:179], v225 offset:18432
	ds_read_b128 v[180:183], v225 offset:19456
	ds_read_b128 v[232:235], v225 offset:20480
	ds_read_b128 v[236:239], v225 offset:21504
	ds_read_b128 v[240:243], v225 offset:22528
	ds_read_b128 v[244:247], v225 offset:23552
	global_load_lds_dwordx4 v[160:161], off
	v_lshl_add_u64 v[162:163], s[6:7], 0, v[186:187]
	s_mov_b32 m0, s57
	s_addc_u32 s51, s7, 0
	global_load_lds_dwordx4 v[162:163], off
	v_lshl_add_u64 v[164:165], s[50:51], 0, v[184:185]
	s_mov_b32 m0, s58
	v_lshl_add_u64 v[166:167], s[46:47], 0, v[190:191]
	global_load_lds_dwordx4 v[164:165], off
	v_lshl_add_u64 v[164:165], s[50:51], 0, v[186:187]
	s_mov_b32 m0, s59
	s_nop 0
	global_load_lds_dwordx4 v[164:165], off
	v_lshl_add_u64 v[164:165], s[46:47], 0, v[188:189]
	s_mov_b32 m0, s55
	s_nop 0
	global_load_lds_dwordx4 v[164:165], off
	s_mov_b32 m0, s60
	s_nop 0
	global_load_lds_dwordx4 v[166:167], off
	s_waitcnt vmcnt(8)
	s_waitcnt lgkmcnt(0)
	s_barrier
	s_setprio 0
	s_waitcnt lgkmcnt(0)
	v_mfma_f32_16x16x128_f8f6f4 v[84:87], v[16:23], v[168:175], v[84:87]
	v_mfma_f32_16x16x128_f8f6f4 v[80:83], v[24:31], v[168:175], v[80:83]
	v_mfma_f32_16x16x128_f8f6f4 v[68:71], v[16:23], v[176:183], v[68:71]
	v_mfma_f32_16x16x128_f8f6f4 v[64:67], v[24:31], v[176:183], v[64:67]
	v_mfma_f32_16x16x128_f8f6f4 v[56:59], v[16:23], v[232:239], v[56:59]
	v_mfma_f32_16x16x128_f8f6f4 v[48:51], v[24:31], v[232:239], v[48:51]
	v_mfma_f32_16x16x128_f8f6f4 v[40:43], v[16:23], v[240:247], v[40:43]
	v_mfma_f32_16x16x128_f8f6f4 v[32:35], v[24:31], v[240:247], v[32:35]
	s_setprio 1
	s_setprio 0
	v_mfma_f32_16x16x128_f8f6f4 v[92:95], v[0:7], v[168:175], v[92:95]
	v_mfma_f32_16x16x128_f8f6f4 v[88:91], v[8:15], v[168:175], v[88:91]
	v_mfma_f32_16x16x128_f8f6f4 v[76:79], v[0:7], v[176:183], v[76:79]
	v_mfma_f32_16x16x128_f8f6f4 v[72:75], v[8:15], v[176:183], v[72:75]
	v_mfma_f32_16x16x128_f8f6f4 v[60:63], v[0:7], v[232:239], v[60:63]
	v_mfma_f32_16x16x128_f8f6f4 v[52:55], v[8:15], v[232:239], v[52:55]
	v_mfma_f32_16x16x128_f8f6f4 v[44:47], v[0:7], v[240:247], v[44:47]
	v_mfma_f32_16x16x128_f8f6f4 v[36:39], v[8:15], v[240:247], v[36:39]
	s_setprio 1
	s_barrier
	ds_read_b128 v[4:7], v219
	ds_read_b128 v[8:11], v220
	ds_read_b128 v[0:3], v211
	ds_read_b128 v[16:19], v212
	ds_read_b128 v[12:15], v221
	ds_read_b128 v[20:23], v222
	ds_read_b128 v[24:27], v223
	ds_read_b128 v[28:31], v224
	s_add_u32 s46, s46, 0x20000
	s_addc_u32 s47, s47, 0
	s_mov_b32 m0, s61
	v_lshl_add_u64 v[202:203], s[46:47], 0, v[188:189]
	ds_read_b128 v[168:171], v225 offset:32768
	ds_read_b128 v[172:175], v225 offset:33792
	ds_read_b128 v[176:179], v225 offset:34816
	ds_read_b128 v[180:183], v225 offset:35840
	ds_read_b128 v[232:235], v225 offset:36864
	ds_read_b128 v[236:239], v225 offset:37888
	ds_read_b128 v[240:243], v225 offset:38912
	ds_read_b128 v[244:247], v225 offset:39936
	global_load_lds_dwordx4 v[202:203], off
	v_lshl_add_u64 v[202:203], s[46:47], 0, v[190:191]
	s_mov_b32 m0, s62
	s_nop 0
	global_load_lds_dwordx4 v[202:203], off
	s_waitcnt vmcnt(8)
	s_waitcnt lgkmcnt(0)
	s_barrier
	s_setprio 0
	s_waitcnt lgkmcnt(0)
	v_mfma_f32_16x16x128_f8f6f4 v[156:159], v[0:7], v[168:175], v[156:159]
	v_mfma_f32_16x16x128_f8f6f4 v[152:155], v[8:15], v[168:175], v[152:155]
	v_mfma_f32_16x16x128_f8f6f4 v[140:143], v[0:7], v[176:183], v[140:143]
	v_mfma_f32_16x16x128_f8f6f4 v[136:139], v[8:15], v[176:183], v[136:139]
	v_mfma_f32_16x16x128_f8f6f4 v[124:127], v[0:7], v[232:239], v[124:127]
	v_mfma_f32_16x16x128_f8f6f4 v[120:123], v[8:15], v[232:239], v[120:123]
	v_mfma_f32_16x16x128_f8f6f4 v[108:111], v[0:7], v[240:247], v[108:111]
	v_mfma_f32_16x16x128_f8f6f4 v[104:107], v[8:15], v[240:247], v[104:107]
	s_setprio 1
	s_setprio 0
	v_mfma_f32_16x16x128_f8f6f4 v[148:151], v[16:23], v[168:175], v[148:151]
	v_mfma_f32_16x16x128_f8f6f4 v[144:147], v[24:31], v[168:175], v[144:147]
	v_mfma_f32_16x16x128_f8f6f4 v[132:135], v[16:23], v[176:183], v[132:135]
	v_mfma_f32_16x16x128_f8f6f4 v[128:131], v[24:31], v[176:183], v[128:131]
	v_mfma_f32_16x16x128_f8f6f4 v[116:119], v[16:23], v[232:239], v[116:119]
	v_mfma_f32_16x16x128_f8f6f4 v[112:115], v[24:31], v[232:239], v[112:115]
	v_mfma_f32_16x16x128_f8f6f4 v[100:103], v[16:23], v[240:247], v[100:103]
	v_mfma_f32_16x16x128_f8f6f4 v[96:99], v[24:31], v[240:247], v[96:99]
	s_setprio 1
	s_barrier
	s_mov_b32 m0, s67
	v_lshl_add_u64 v[160:161], v[160:161], 0, s[24:25]
	s_add_u32 s6, s6, 0x20080
	ds_read_b128 v[168:171], v225 offset:49152
	ds_read_b128 v[172:175], v225 offset:50176
	ds_read_b128 v[176:179], v225 offset:51200
	ds_read_b128 v[180:183], v225 offset:52224
	ds_read_b128 v[232:235], v225 offset:53248
	ds_read_b128 v[236:239], v225 offset:54272
	ds_read_b128 v[240:243], v225 offset:55296
	ds_read_b128 v[244:247], v225 offset:56320
	global_load_lds_dwordx4 v[160:161], off
	v_lshl_add_u64 v[160:161], v[162:163], 0, s[24:25]
	s_mov_b32 m0, s68
	s_addc_u32 s7, s7, 0
	global_load_lds_dwordx4 v[160:161], off
	v_lshl_add_u64 v[160:161], s[6:7], 0, v[184:185]
	s_mov_b32 m0, s71
	s_nop 0
	global_load_lds_dwordx4 v[160:161], off
	v_lshl_add_u64 v[160:161], s[6:7], 0, v[186:187]
	s_mov_b32 m0, s78
	s_nop 0
	global_load_lds_dwordx4 v[160:161], off
	v_lshl_add_u64 v[160:161], v[164:165], 0, s[24:25]
	s_mov_b32 m0, s69
	s_nop 0
	global_load_lds_dwordx4 v[160:161], off
	v_lshl_add_u64 v[160:161], v[166:167], 0, s[24:25]
	s_mov_b32 m0, s70
	s_nop 0
	global_load_lds_dwordx4 v[160:161], off
	s_waitcnt vmcnt(8)
	s_waitcnt lgkmcnt(0)
	s_barrier
	s_setprio 0
	s_waitcnt lgkmcnt(0)
	v_mfma_f32_16x16x128_f8f6f4 v[84:87], v[0:7], v[168:175], v[84:87]
	v_mfma_f32_16x16x128_f8f6f4 v[80:83], v[8:15], v[168:175], v[80:83]
	v_mfma_f32_16x16x128_f8f6f4 v[68:71], v[0:7], v[176:183], v[68:71]
	v_mfma_f32_16x16x128_f8f6f4 v[64:67], v[8:15], v[176:183], v[64:67]
	v_mfma_f32_16x16x128_f8f6f4 v[56:59], v[0:7], v[232:239], v[56:59]
	v_mfma_f32_16x16x128_f8f6f4 v[48:51], v[8:15], v[232:239], v[48:51]
	v_mfma_f32_16x16x128_f8f6f4 v[40:43], v[0:7], v[240:247], v[40:43]
	v_mfma_f32_16x16x128_f8f6f4 v[32:35], v[8:15], v[240:247], v[32:35]
	s_setprio 1
	s_setprio 0
	v_mfma_f32_16x16x128_f8f6f4 v[92:95], v[16:23], v[168:175], v[92:95]
	v_mfma_f32_16x16x128_f8f6f4 v[88:91], v[24:31], v[168:175], v[88:91]
	v_mfma_f32_16x16x128_f8f6f4 v[76:79], v[16:23], v[176:183], v[76:79]
	v_mfma_f32_16x16x128_f8f6f4 v[72:75], v[24:31], v[176:183], v[72:75]
	v_mfma_f32_16x16x128_f8f6f4 v[60:63], v[16:23], v[232:239], v[60:63]
	v_mfma_f32_16x16x128_f8f6f4 v[52:55], v[24:31], v[232:239], v[52:55]
	v_mfma_f32_16x16x128_f8f6f4 v[44:47], v[16:23], v[240:247], v[44:47]
	v_mfma_f32_16x16x128_f8f6f4 v[36:39], v[24:31], v[240:247], v[36:39]
	s_setprio 1
	s_barrier
	s_add_i32 s49, s49, 2
	s_add_u32 s2, s2, 0x100
	s_addc_u32 s3, s3, 0
	s_add_u32 s39, s39, 0x100
	s_addc_u32 s48, s48, 0
	s_cmp_gt_u32 s49, 5
	s_cbranch_scc0 .LBB0_3128
	s_nop 15
	s_nop 7
	s_and_b64 vcc, exec, s[26:27]
	s_cbranch_vccz .LBB0_3131
	s_barrier

.LBB0_3319:
	s_add_u32 s34, s90, s4
	s_addc_u32 s35, s91, s5
	s_add_u32 s71, s34, 0x21c00100
	s_addc_u32 s72, s35, 0
	s_cmpk_eq_i32 s4, 0x300
	v_lshl_add_u64 v[0:1], v[180:181], 0, s[4:5]
	s_cselect_b64 vcc, -1, 0
	v_cndmask_b32_e32 v183, v1, v167, vcc
	v_cndmask_b32_e32 v182, v0, v220, vcc
	ds_read_b128 v[8:11], v194
	ds_read_b128 v[12:15], v198
	ds_read_b128 v[24:27], v199
	ds_read_b128 v[28:31], v200
	ds_read_b128 v[0:3], v195
	ds_read_b128 v[4:7], v201
	ds_read_b128 v[16:19], v202
	ds_read_b128 v[20:23], v203
	s_and_b64 s[34:35], vcc, exec
	s_cselect_b32 s35, s9, s72
	s_cselect_b32 s34, s8, s71
	v_cndmask_b32_e32 v160, v219, v215, vcc
	v_cndmask_b32_e32 v184, v170, v216, vcc
	v_cndmask_b32_e32 v175, v172, v217, vcc
	v_cndmask_b32_e32 v173, v174, v218, vcc
	v_lshl_add_u64 v[186:187], v[178:179], 0, s[4:5]
	s_add_i32 m0, s0, 0xc000
	ds_read_b128 v[222:225], v212
	ds_read_b128 v[226:229], v212 offset:1024
	ds_read_b128 v[230:233], v212 offset:2048
	ds_read_b128 v[234:237], v212 offset:3072
	ds_read_b128 v[238:241], v212 offset:4096
	ds_read_b128 v[242:245], v212 offset:5120
	ds_read_b128 v[246:249], v212 offset:6144
	ds_read_b128 v[250:253], v212 offset:7168
	global_load_lds_dwordx4 v[186:187], off
	v_lshl_add_u64 v[186:187], v[176:177], 0, s[4:5]
	s_add_i32 m0, s0, 0xe000
	s_nop 0
	global_load_lds_dwordx4 v[186:187], off
	s_waitcnt vmcnt(8)
	s_waitcnt lgkmcnt(0)
	s_barrier
	s_setprio 0
	s_waitcnt lgkmcnt(0)
	v_mfma_f32_16x16x128_f8f6f4 v[156:159], v[8:15], v[222:229], v[156:159]
	v_mfma_f32_16x16x128_f8f6f4 v[152:155], v[24:31], v[222:229], v[152:155]
	v_mfma_f32_16x16x128_f8f6f4 v[140:143], v[8:15], v[230:237], v[140:143]
	v_mfma_f32_16x16x128_f8f6f4 v[136:139], v[24:31], v[230:237], v[136:139]
	v_mfma_f32_16x16x128_f8f6f4 v[124:127], v[8:15], v[238:245], v[124:127]
	v_mfma_f32_16x16x128_f8f6f4 v[120:123], v[24:31], v[238:245], v[120:123]
	v_mfma_f32_16x16x128_f8f6f4 v[108:111], v[8:15], v[246:253], v[108:111]
	v_mfma_f32_16x16x128_f8f6f4 v[104:107], v[24:31], v[246:253], v[104:107]
	s_setprio 1
	s_setprio 0
	v_mfma_f32_16x16x128_f8f6f4 v[148:151], v[0:7], v[222:229], v[148:151]
	v_mfma_f32_16x16x128_f8f6f4 v[144:147], v[16:23], v[222:229], v[144:147]
	v_mfma_f32_16x16x128_f8f6f4 v[132:135], v[0:7], v[230:237], v[132:135]
	v_mfma_f32_16x16x128_f8f6f4 v[128:131], v[16:23], v[230:237], v[128:131]
	v_mfma_f32_16x16x128_f8f6f4 v[116:119], v[0:7], v[238:245], v[116:119]
	v_mfma_f32_16x16x128_f8f6f4 v[112:115], v[16:23], v[238:245], v[112:115]
	v_mfma_f32_16x16x128_f8f6f4 v[100:103], v[0:7], v[246:253], v[100:103]
	v_mfma_f32_16x16x128_f8f6f4 v[96:99], v[16:23], v[246:253], v[96:99]
	s_setprio 1
	s_barrier
	s_mov_b32 m0, s38
	v_lshl_add_u64 v[186:187], v[182:183], 0, v[164:165]
	ds_read_b128 v[222:225], v212 offset:16384
	ds_read_b128 v[226:229], v212 offset:17408
	ds_read_b128 v[230:233], v212 offset:18432
	ds_read_b128 v[234:237], v212 offset:19456
	ds_read_b128 v[238:241], v212 offset:20480
	ds_read_b128 v[242:245], v212 offset:21504
	ds_read_b128 v[246:249], v212 offset:22528
	ds_read_b128 v[250:253], v212 offset:23552
	global_load_lds_dwordx4 v[186:187], off
	v_lshl_add_u64 v[188:189], v[182:183], 0, v[162:163]
	s_mov_b32 m0, s39
	v_lshl_add_u64 v[190:191], v[182:183], 0, s[12:13]
	global_load_lds_dwordx4 v[188:189], off
	v_lshl_add_u64 v[192:193], v[190:191], 0, v[164:165]
	s_mov_b32 m0, s40
	v_lshl_add_u64 v[190:191], v[190:191], 0, v[162:163]
	global_load_lds_dwordx4 v[192:193], off
	s_mov_b32 m0, s41
	v_mov_b32_e32 v185, v161
	global_load_lds_dwordx4 v[190:191], off
	s_mov_b32 m0, s0
	v_lshl_add_u64 v[190:191], s[34:35], 0, v[160:161]
	global_load_lds_dwordx4 v160, s[34:35]
	s_mov_b32 m0, s42
	s_nop 0
	global_load_lds_dwordx4 v184, s[34:35]
	s_waitcnt vmcnt(8)
	s_waitcnt lgkmcnt(0)
	v_lshl_add_u64 v[184:185], s[34:35], 0, v[184:185]
	s_barrier
	s_setprio 0
	s_waitcnt lgkmcnt(0)
	v_mfma_f32_16x16x128_f8f6f4 v[84:87], v[8:15], v[222:229], v[84:87]
	v_mfma_f32_16x16x128_f8f6f4 v[80:83], v[24:31], v[222:229], v[80:83]
	v_mfma_f32_16x16x128_f8f6f4 v[68:71], v[8:15], v[230:237], v[68:71]
	v_mfma_f32_16x16x128_f8f6f4 v[64:67], v[24:31], v[230:237], v[64:67]
	v_mfma_f32_16x16x128_f8f6f4 v[52:55], v[8:15], v[238:245], v[52:55]
	v_mfma_f32_16x16x128_f8f6f4 v[48:51], v[24:31], v[238:245], v[48:51]
	v_mfma_f32_16x16x128_f8f6f4 v[36:39], v[8:15], v[246:253], v[36:39]
	v_mfma_f32_16x16x128_f8f6f4 v[32:35], v[24:31], v[246:253], v[32:35]
	s_setprio 1
	s_setprio 0
	v_mfma_f32_16x16x128_f8f6f4 v[92:95], v[0:7], v[222:229], v[92:95]
	v_mfma_f32_16x16x128_f8f6f4 v[88:91], v[16:23], v[222:229], v[88:91]
	v_mfma_f32_16x16x128_f8f6f4 v[76:79], v[0:7], v[230:237], v[76:79]
	v_mfma_f32_16x16x128_f8f6f4 v[72:75], v[16:23], v[230:237], v[72:75]
	v_mfma_f32_16x16x128_f8f6f4 v[60:63], v[0:7], v[238:245], v[60:63]
	v_mfma_f32_16x16x128_f8f6f4 v[56:59], v[16:23], v[238:245], v[56:59]
	v_mfma_f32_16x16x128_f8f6f4 v[44:47], v[0:7], v[246:253], v[44:47]
	v_mfma_f32_16x16x128_f8f6f4 v[40:43], v[16:23], v[246:253], v[40:43]
	s_setprio 1
	s_barrier
	ds_read_b128 v[4:7], v204
	ds_read_b128 v[8:11], v205
	ds_read_b128 v[0:3], v196
	ds_read_b128 v[16:19], v197
	ds_read_b128 v[12:15], v206
	ds_read_b128 v[20:23], v207
	ds_read_b128 v[24:27], v208
	ds_read_b128 v[28:31], v209
	s_mov_b32 m0, s43
	ds_read_b128 v[222:225], v212 offset:32768
	ds_read_b128 v[226:229], v212 offset:33792
	ds_read_b128 v[230:233], v212 offset:34816
	ds_read_b128 v[234:237], v212 offset:35840
	ds_read_b128 v[238:241], v212 offset:36864
	ds_read_b128 v[242:245], v212 offset:37888
	ds_read_b128 v[246:249], v212 offset:38912
	ds_read_b128 v[250:253], v212 offset:39936
	global_load_lds_dwordx4 v175, s[34:35]
	s_mov_b32 m0, s44
	s_nop 0
	global_load_lds_dwordx4 v173, s[34:35]
	s_waitcnt vmcnt(8)
	s_waitcnt lgkmcnt(0)
	s_barrier
	s_setprio 0
	s_waitcnt lgkmcnt(0)
	v_mfma_f32_16x16x128_f8f6f4 v[156:159], v[0:7], v[222:229], v[156:159]
	v_mfma_f32_16x16x128_f8f6f4 v[152:155], v[8:15], v[222:229], v[152:155]
	v_mfma_f32_16x16x128_f8f6f4 v[140:143], v[0:7], v[230:237], v[140:143]
	v_mfma_f32_16x16x128_f8f6f4 v[136:139], v[8:15], v[230:237], v[136:139]
	v_mfma_f32_16x16x128_f8f6f4 v[124:127], v[0:7], v[238:245], v[124:127]
	v_mfma_f32_16x16x128_f8f6f4 v[120:123], v[8:15], v[238:245], v[120:123]
	v_mfma_f32_16x16x128_f8f6f4 v[108:111], v[0:7], v[246:253], v[108:111]
	v_mfma_f32_16x16x128_f8f6f4 v[104:107], v[8:15], v[246:253], v[104:107]
	s_setprio 1
	s_setprio 0
	v_mfma_f32_16x16x128_f8f6f4 v[148:151], v[16:23], v[222:229], v[148:151]
	v_mfma_f32_16x16x128_f8f6f4 v[144:147], v[24:31], v[222:229], v[144:147]
	v_mfma_f32_16x16x128_f8f6f4 v[132:135], v[16:23], v[230:237], v[132:135]
	v_mfma_f32_16x16x128_f8f6f4 v[128:131], v[24:31], v[230:237], v[128:131]
	v_mfma_f32_16x16x128_f8f6f4 v[116:119], v[16:23], v[238:245], v[116:119]
	v_mfma_f32_16x16x128_f8f6f4 v[112:115], v[24:31], v[238:245], v[112:115]
	v_mfma_f32_16x16x128_f8f6f4 v[100:103], v[16:23], v[246:253], v[100:103]
	v_mfma_f32_16x16x128_f8f6f4 v[96:99], v[24:31], v[246:253], v[96:99]
	s_setprio 1
	s_barrier
	s_mov_b32 m0, s45
	v_lshl_add_u64 v[186:187], v[186:187], 0, s[16:17]
	ds_read_b128 v[222:225], v212 offset:49152
	ds_read_b128 v[226:229], v212 offset:50176
	ds_read_b128 v[230:233], v212 offset:51200
	ds_read_b128 v[234:237], v212 offset:52224
	ds_read_b128 v[238:241], v212 offset:53248
	ds_read_b128 v[242:245], v212 offset:54272
	ds_read_b128 v[246:249], v212 offset:55296
	ds_read_b128 v[250:253], v212 offset:56320
	global_load_lds_dwordx4 v[186:187], off
	v_lshl_add_u64 v[186:187], v[188:189], 0, s[16:17]
	s_mov_b32 m0, s46
	v_lshl_add_u64 v[182:183], v[182:183], 0, s[24:25]
	global_load_lds_dwordx4 v[186:187], off
	v_lshl_add_u64 v[186:187], v[182:183], 0, v[164:165]
	s_mov_b32 m0, s49
	v_lshl_add_u64 v[182:183], v[182:183], 0, v[162:163]
	global_load_lds_dwordx4 v[186:187], off
	s_mov_b32 m0, s50
	s_nop 0
	global_load_lds_dwordx4 v[182:183], off
	v_lshl_add_u64 v[182:183], v[190:191], 0, s[16:17]
	s_mov_b32 m0, s47
	s_nop 0
	global_load_lds_dwordx4 v[182:183], off
	v_lshl_add_u64 v[182:183], v[184:185], 0, s[16:17]
	s_mov_b32 m0, s48
	s_nop 0
	global_load_lds_dwordx4 v[182:183], off
	s_waitcnt vmcnt(8)
	s_waitcnt lgkmcnt(0)
	s_barrier
	s_setprio 0
	s_waitcnt lgkmcnt(0)
	v_mfma_f32_16x16x128_f8f6f4 v[84:87], v[0:7], v[222:229], v[84:87]
	v_mfma_f32_16x16x128_f8f6f4 v[80:83], v[8:15], v[222:229], v[80:83]
	v_mfma_f32_16x16x128_f8f6f4 v[68:71], v[0:7], v[230:237], v[68:71]
	v_mfma_f32_16x16x128_f8f6f4 v[64:67], v[8:15], v[230:237], v[64:67]
	v_mfma_f32_16x16x128_f8f6f4 v[52:55], v[0:7], v[238:245], v[52:55]
	v_mfma_f32_16x16x128_f8f6f4 v[48:51], v[8:15], v[238:245], v[48:51]
	v_mfma_f32_16x16x128_f8f6f4 v[36:39], v[0:7], v[246:253], v[36:39]
	v_mfma_f32_16x16x128_f8f6f4 v[32:35], v[8:15], v[246:253], v[32:35]
	s_setprio 1
	s_setprio 0
	v_mfma_f32_16x16x128_f8f6f4 v[92:95], v[16:23], v[222:229], v[92:95]
	v_mfma_f32_16x16x128_f8f6f4 v[88:91], v[24:31], v[222:229], v[88:91]
	v_mfma_f32_16x16x128_f8f6f4 v[76:79], v[16:23], v[230:237], v[76:79]
	v_mfma_f32_16x16x128_f8f6f4 v[72:75], v[24:31], v[230:237], v[72:75]
	v_mfma_f32_16x16x128_f8f6f4 v[60:63], v[16:23], v[238:245], v[60:63]
	v_mfma_f32_16x16x128_f8f6f4 v[56:59], v[24:31], v[238:245], v[56:59]
	v_mfma_f32_16x16x128_f8f6f4 v[44:47], v[16:23], v[246:253], v[44:47]
	v_mfma_f32_16x16x128_f8f6f4 v[40:43], v[24:31], v[246:253], v[40:43]
	s_setprio 1
	s_barrier
	s_add_i32 s31, s31, 2
	s_add_u32 s4, s4, 0x100
	s_addc_u32 s5, s5, 0
	s_cmp_gt_u32 s31, 5
	s_cbranch_scc0 .LBB0_3319
	s_nop 15
	s_nop 7
	s_and_b64 vcc, exec, s[26:27]
	s_cbranch_vccz .LBB0_3322
	s_barrier

.LBB0_3336:
	s_add_u32 s40, s26, s34
	s_addc_u32 s41, s27, s35
	s_add_u32 s38, s40, 0x100
	s_addc_u32 s39, s41, 0
	s_and_b64 s[36:37], s[30:31], exec
	s_cselect_b32 s37, s13, s39
	s_cselect_b32 s36, s60, s38
	s_add_u32 s34, s24, s34
	s_addc_u32 s35, s25, s35
	s_add_u32 s34, s34, 0x100
	s_addc_u32 s35, s35, 0
	s_and_b64 s[30:31], s[30:31], exec
	s_cselect_b32 s39, s15, s35
	s_cselect_b32 s38, s61, s34
	s_add_u32 s42, s40, 0x10080
	ds_read_b128 v[146:149], v143
	ds_read_b128 v[150:153], v143 offset:1024
	ds_read_b128 v[154:157], v143 offset:2048
	ds_read_b128 v[158:161], v143 offset:3072
	ds_read_b128 v[162:165], v144
	ds_read_b128 v[166:169], v144 offset:1024
	ds_read_b128 v[170:173], v144 offset:2048
	ds_read_b128 v[174:177], v144 offset:3072
	s_addc_u32 s43, s41, 0
	s_add_i32 s71, s0, s49
	s_add_i32 m0, s50, 0xc000
	s_add_i32 s72, s50, 0xe000
	s_add_i32 s68, s71, 0x2000
	s_add_u32 s40, s38, 0x10000
	s_addc_u32 s41, s39, 0
	s_add_i32 s70, s56, s49
	s_add_i32 s69, s70, 0x2000
	s_add_i32 s67, 0, 0x18000
	s_add_i32 s66, 0, 0x1c000
	s_add_u32 s34, s36, 0x10000
	s_addc_u32 s35, s37, 0
	s_add_i32 s65, s67, s49
	s_add_i32 s63, s65, 0x2000
	s_add_u32 s30, s38, 0x10080
	s_addc_u32 s31, s39, 0
	s_add_i32 s64, s66, s49
	s_add_i32 s62, s64, 0x2000
	v_lshl_add_u64 v[138:139], s[42:43], 0, v[132:133]
	ds_read_b128 v[178:181], v145
	ds_read_b128 v[182:185], v145 offset:1024
	ds_read_b128 v[186:189], v145 offset:2048
	ds_read_b128 v[190:193], v145 offset:3072
	ds_read_b128 v[194:197], v145 offset:4096
	ds_read_b128 v[198:201], v145 offset:5120
	ds_read_b128 v[202:205], v145 offset:6144
	ds_read_b128 v[206:209], v145 offset:7168
	global_load_lds_dwordx4 v[138:139], off
	v_lshl_add_u64 v[138:139], s[42:43], 0, v[134:135]
	s_mov_b32 m0, s72
	s_nop 0
	global_load_lds_dwordx4 v[138:139], off
	s_waitcnt vmcnt(8)
	s_waitcnt lgkmcnt(0)
	s_barrier
	s_setprio 0
	s_waitcnt lgkmcnt(0)
	v_mfma_f32_16x16x32_bf16 v[124:127], v[146:149], v[178:181], v[124:127]
	v_mfma_f32_16x16x32_bf16 v[120:123], v[154:157], v[178:181], v[120:123]
	v_mfma_f32_16x16x32_bf16 v[116:119], v[146:149], v[186:189], v[116:119]
	v_mfma_f32_16x16x32_bf16 v[108:111], v[154:157], v[186:189], v[108:111]
	v_mfma_f32_16x16x32_bf16 v[100:103], v[146:149], v[194:197], v[100:103]
	v_mfma_f32_16x16x32_bf16 v[92:95], v[154:157], v[194:197], v[92:95]
	v_mfma_f32_16x16x32_bf16 v[84:87], v[146:149], v[202:205], v[84:87]
	v_mfma_f32_16x16x32_bf16 v[76:79], v[154:157], v[202:205], v[76:79]
	v_mfma_f32_16x16x32_bf16 v[124:127], v[150:153], v[182:185], v[124:127]
	v_mfma_f32_16x16x32_bf16 v[120:123], v[158:161], v[182:185], v[120:123]
	v_mfma_f32_16x16x32_bf16 v[116:119], v[150:153], v[190:193], v[116:119]
	v_mfma_f32_16x16x32_bf16 v[108:111], v[158:161], v[190:193], v[108:111]
	v_mfma_f32_16x16x32_bf16 v[100:103], v[150:153], v[198:201], v[100:103]
	v_mfma_f32_16x16x32_bf16 v[92:95], v[158:161], v[198:201], v[92:95]
	v_mfma_f32_16x16x32_bf16 v[84:87], v[150:153], v[206:209], v[84:87]
	v_mfma_f32_16x16x32_bf16 v[76:79], v[158:161], v[206:209], v[76:79]
	s_setprio 1
	s_setprio 0
	v_mfma_f32_16x16x32_bf16 v[112:115], v[162:165], v[178:181], v[112:115]
	v_mfma_f32_16x16x32_bf16 v[104:107], v[170:173], v[178:181], v[104:107]
	v_mfma_f32_16x16x32_bf16 v[96:99], v[162:165], v[186:189], v[96:99]
	v_mfma_f32_16x16x32_bf16 v[88:91], v[170:173], v[186:189], v[88:91]
	v_mfma_f32_16x16x32_bf16 v[80:83], v[162:165], v[194:197], v[80:83]
	v_mfma_f32_16x16x32_bf16 v[72:75], v[170:173], v[194:197], v[72:75]
	v_mfma_f32_16x16x32_bf16 v[52:55], v[162:165], v[202:205], v[52:55]
	v_mfma_f32_16x16x32_bf16 v[48:51], v[170:173], v[202:205], v[48:51]
	v_mfma_f32_16x16x32_bf16 v[112:115], v[166:169], v[182:185], v[112:115]
	v_mfma_f32_16x16x32_bf16 v[104:107], v[174:177], v[182:185], v[104:107]
	v_mfma_f32_16x16x32_bf16 v[96:99], v[166:169], v[190:193], v[96:99]
	v_mfma_f32_16x16x32_bf16 v[88:91], v[174:177], v[190:193], v[88:91]
	v_mfma_f32_16x16x32_bf16 v[80:83], v[166:169], v[198:201], v[80:83]
	v_mfma_f32_16x16x32_bf16 v[72:75], v[174:177], v[198:201], v[72:75]
	v_mfma_f32_16x16x32_bf16 v[52:55], v[166:169], v[206:209], v[52:55]
	v_mfma_f32_16x16x32_bf16 v[48:51], v[174:177], v[206:209], v[48:51]
	s_setprio 1
	s_barrier
	s_mov_b32 m0, s71
	v_lshl_add_u64 v[138:139], s[38:39], 0, v[130:131]
	ds_read_b128 v[178:181], v145 offset:16384
	ds_read_b128 v[182:185], v145 offset:17408
	ds_read_b128 v[186:189], v145 offset:18432
	ds_read_b128 v[190:193], v145 offset:19456
	ds_read_b128 v[194:197], v145 offset:20480
	ds_read_b128 v[198:201], v145 offset:21504
	ds_read_b128 v[202:205], v145 offset:22528
	ds_read_b128 v[206:209], v145 offset:23552
	global_load_lds_dwordx4 v[138:139], off
	v_lshl_add_u64 v[210:211], s[38:39], 0, v[128:129]
	s_mov_b32 m0, s68
	v_lshl_add_u64 v[212:213], s[40:41], 0, v[130:131]
	global_load_lds_dwordx4 v[210:211], off
	s_mov_b32 m0, s70
	v_lshl_add_u64 v[214:215], s[36:37], 0, v[134:135]
	global_load_lds_dwordx4 v[212:213], off
	v_lshl_add_u64 v[212:213], s[40:41], 0, v[128:129]
	s_mov_b32 m0, s69
	s_nop 0
	global_load_lds_dwordx4 v[212:213], off
	v_lshl_add_u64 v[212:213], s[36:37], 0, v[132:133]
	s_mov_b32 m0, s50
	s_nop 0
	global_load_lds_dwordx4 v[212:213], off
	s_mov_b32 m0, s51
	s_nop 0
	global_load_lds_dwordx4 v[214:215], off
	s_waitcnt vmcnt(8)
	s_waitcnt lgkmcnt(0)
	s_barrier
	s_setprio 0
	s_waitcnt lgkmcnt(0)
	v_mfma_f32_16x16x32_bf16 v[44:47], v[146:149], v[178:181], v[44:47]
	v_mfma_f32_16x16x32_bf16 v[32:35], v[154:157], v[178:181], v[32:35]
	v_mfma_f32_16x16x32_bf16 v[4:7], v[146:149], v[186:189], v[4:7]
	v_mfma_f32_16x16x32_bf16 v[0:3], v[154:157], v[186:189], v[0:3]
	v_mfma_f32_16x16x32_bf16 v[28:31], v[146:149], v[194:197], v[28:31]
	v_mfma_f32_16x16x32_bf16 v[24:27], v[154:157], v[194:197], v[24:27]
	v_mfma_f32_16x16x32_bf16 v[12:15], v[146:149], v[202:205], v[12:15]
	v_mfma_f32_16x16x32_bf16 v[8:11], v[154:157], v[202:205], v[8:11]
	v_mfma_f32_16x16x32_bf16 v[44:47], v[150:153], v[182:185], v[44:47]
	v_mfma_f32_16x16x32_bf16 v[32:35], v[158:161], v[182:185], v[32:35]
	v_mfma_f32_16x16x32_bf16 v[4:7], v[150:153], v[190:193], v[4:7]
	v_mfma_f32_16x16x32_bf16 v[0:3], v[158:161], v[190:193], v[0:3]
	v_mfma_f32_16x16x32_bf16 v[28:31], v[150:153], v[198:201], v[28:31]
	v_mfma_f32_16x16x32_bf16 v[24:27], v[158:161], v[198:201], v[24:27]
	v_mfma_f32_16x16x32_bf16 v[12:15], v[150:153], v[206:209], v[12:15]
	v_mfma_f32_16x16x32_bf16 v[8:11], v[158:161], v[206:209], v[8:11]
	s_setprio 1
	s_setprio 0
	v_mfma_f32_16x16x32_bf16 v[68:71], v[162:165], v[178:181], v[68:71]
	v_mfma_f32_16x16x32_bf16 v[64:67], v[170:173], v[178:181], v[64:67]
	v_mfma_f32_16x16x32_bf16 v[60:63], v[162:165], v[186:189], v[60:63]
	v_mfma_f32_16x16x32_bf16 v[56:59], v[170:173], v[186:189], v[56:59]
	v_mfma_f32_16x16x32_bf16 v[40:43], v[162:165], v[194:197], v[40:43]
	v_mfma_f32_16x16x32_bf16 v[36:39], v[170:173], v[194:197], v[36:39]
	v_mfma_f32_16x16x32_bf16 v[20:23], v[162:165], v[202:205], v[20:23]
	v_mfma_f32_16x16x32_bf16 v[16:19], v[170:173], v[202:205], v[16:19]
	v_mfma_f32_16x16x32_bf16 v[68:71], v[166:169], v[182:185], v[68:71]
	v_mfma_f32_16x16x32_bf16 v[64:67], v[174:177], v[182:185], v[64:67]
	v_mfma_f32_16x16x32_bf16 v[60:63], v[166:169], v[190:193], v[60:63]
	v_mfma_f32_16x16x32_bf16 v[56:59], v[174:177], v[190:193], v[56:59]
	v_mfma_f32_16x16x32_bf16 v[40:43], v[166:169], v[198:201], v[40:43]
	v_mfma_f32_16x16x32_bf16 v[36:39], v[174:177], v[198:201], v[36:39]
	v_mfma_f32_16x16x32_bf16 v[20:23], v[166:169], v[206:209], v[20:23]
	v_mfma_f32_16x16x32_bf16 v[16:19], v[174:177], v[206:209], v[16:19]
	s_setprio 1
	s_barrier
	v_add_u32_e32 v158, s67, v141
	v_add_u32_e32 v174, s66, v141
	ds_read_b128 v[146:149], v158
	ds_read_b128 v[150:153], v158 offset:1024
	ds_read_b128 v[154:157], v158 offset:2048
	ds_read_b128 v[158:161], v158 offset:3072
	ds_read_b128 v[162:165], v174
	ds_read_b128 v[166:169], v174 offset:1024
	ds_read_b128 v[170:173], v174 offset:2048
	ds_read_b128 v[174:177], v174 offset:3072
	s_mov_b32 m0, s52
	v_lshl_add_u64 v[216:217], s[34:35], 0, v[132:133]
	ds_read_b128 v[178:181], v145 offset:32768
	ds_read_b128 v[182:185], v145 offset:33792
	ds_read_b128 v[186:189], v145 offset:34816
	ds_read_b128 v[190:193], v145 offset:35840
	ds_read_b128 v[194:197], v145 offset:36864
	ds_read_b128 v[198:201], v145 offset:37888
	ds_read_b128 v[202:205], v145 offset:38912
	ds_read_b128 v[206:209], v145 offset:39936
	global_load_lds_dwordx4 v[216:217], off
	v_lshl_add_u64 v[216:217], s[34:35], 0, v[134:135]
	s_mov_b32 m0, s53
	s_nop 0
	global_load_lds_dwordx4 v[216:217], off
	s_waitcnt vmcnt(8)
	s_waitcnt lgkmcnt(0)
	s_barrier
	s_setprio 0
	s_waitcnt lgkmcnt(0)
	v_mfma_f32_16x16x32_bf16 v[124:127], v[146:149], v[178:181], v[124:127]
	v_mfma_f32_16x16x32_bf16 v[120:123], v[154:157], v[178:181], v[120:123]
	v_mfma_f32_16x16x32_bf16 v[116:119], v[146:149], v[186:189], v[116:119]
	v_mfma_f32_16x16x32_bf16 v[108:111], v[154:157], v[186:189], v[108:111]
	v_mfma_f32_16x16x32_bf16 v[100:103], v[146:149], v[194:197], v[100:103]
	v_mfma_f32_16x16x32_bf16 v[92:95], v[154:157], v[194:197], v[92:95]
	v_mfma_f32_16x16x32_bf16 v[84:87], v[146:149], v[202:205], v[84:87]
	v_mfma_f32_16x16x32_bf16 v[76:79], v[154:157], v[202:205], v[76:79]
	v_mfma_f32_16x16x32_bf16 v[124:127], v[150:153], v[182:185], v[124:127]
	v_mfma_f32_16x16x32_bf16 v[120:123], v[158:161], v[182:185], v[120:123]
	v_mfma_f32_16x16x32_bf16 v[116:119], v[150:153], v[190:193], v[116:119]
	v_mfma_f32_16x16x32_bf16 v[108:111], v[158:161], v[190:193], v[108:111]
	v_mfma_f32_16x16x32_bf16 v[100:103], v[150:153], v[198:201], v[100:103]
	v_mfma_f32_16x16x32_bf16 v[92:95], v[158:161], v[198:201], v[92:95]
	v_mfma_f32_16x16x32_bf16 v[84:87], v[150:153], v[206:209], v[84:87]
	v_mfma_f32_16x16x32_bf16 v[76:79], v[158:161], v[206:209], v[76:79]
	s_setprio 1
	s_setprio 0
	v_mfma_f32_16x16x32_bf16 v[112:115], v[162:165], v[178:181], v[112:115]
	v_mfma_f32_16x16x32_bf16 v[104:107], v[170:173], v[178:181], v[104:107]
	v_mfma_f32_16x16x32_bf16 v[96:99], v[162:165], v[186:189], v[96:99]
	v_mfma_f32_16x16x32_bf16 v[88:91], v[170:173], v[186:189], v[88:91]
	v_mfma_f32_16x16x32_bf16 v[80:83], v[162:165], v[194:197], v[80:83]
	v_mfma_f32_16x16x32_bf16 v[72:75], v[170:173], v[194:197], v[72:75]
	v_mfma_f32_16x16x32_bf16 v[52:55], v[162:165], v[202:205], v[52:55]
	v_mfma_f32_16x16x32_bf16 v[48:51], v[170:173], v[202:205], v[48:51]
	v_mfma_f32_16x16x32_bf16 v[112:115], v[166:169], v[182:185], v[112:115]
	v_mfma_f32_16x16x32_bf16 v[104:107], v[174:177], v[182:185], v[104:107]
	v_mfma_f32_16x16x32_bf16 v[96:99], v[166:169], v[190:193], v[96:99]
	v_mfma_f32_16x16x32_bf16 v[88:91], v[174:177], v[190:193], v[88:91]
	v_mfma_f32_16x16x32_bf16 v[80:83], v[166:169], v[198:201], v[80:83]
	v_mfma_f32_16x16x32_bf16 v[72:75], v[174:177], v[198:201], v[72:75]
	v_mfma_f32_16x16x32_bf16 v[52:55], v[166:169], v[206:209], v[52:55]
	v_mfma_f32_16x16x32_bf16 v[48:51], v[174:177], v[206:209], v[48:51]
	s_setprio 1
	s_barrier
	s_mov_b32 m0, s65
	v_lshl_add_u64 v[138:139], v[138:139], 0, s[8:9]
	ds_read_b128 v[178:181], v145 offset:49152
	ds_read_b128 v[182:185], v145 offset:50176
	ds_read_b128 v[186:189], v145 offset:51200
	ds_read_b128 v[190:193], v145 offset:52224
	ds_read_b128 v[194:197], v145 offset:53248
	ds_read_b128 v[198:201], v145 offset:54272
	ds_read_b128 v[202:205], v145 offset:55296
	ds_read_b128 v[206:209], v145 offset:56320
	global_load_lds_dwordx4 v[138:139], off
	v_lshl_add_u64 v[138:139], v[210:211], 0, s[8:9]
	s_mov_b32 m0, s63
	s_nop 0
	global_load_lds_dwordx4 v[138:139], off
	v_lshl_add_u64 v[138:139], s[30:31], 0, v[130:131]
	s_mov_b32 m0, s64
	s_nop 0
	global_load_lds_dwordx4 v[138:139], off
	v_lshl_add_u64 v[138:139], s[30:31], 0, v[128:129]
	s_mov_b32 m0, s62
	s_nop 0
	global_load_lds_dwordx4 v[138:139], off
	v_lshl_add_u64 v[138:139], v[212:213], 0, s[8:9]
	s_mov_b32 m0, s54
	s_nop 0
	global_load_lds_dwordx4 v[138:139], off
	v_lshl_add_u64 v[138:139], v[214:215], 0, s[8:9]
	s_mov_b32 m0, s55
	s_nop 0
	global_load_lds_dwordx4 v[138:139], off
	s_waitcnt vmcnt(8)
	s_waitcnt lgkmcnt(0)
	s_barrier
	s_setprio 0
	s_waitcnt lgkmcnt(0)
	v_mfma_f32_16x16x32_bf16 v[44:47], v[146:149], v[178:181], v[44:47]
	v_mfma_f32_16x16x32_bf16 v[32:35], v[154:157], v[178:181], v[32:35]
	v_mfma_f32_16x16x32_bf16 v[4:7], v[146:149], v[186:189], v[4:7]
	v_mfma_f32_16x16x32_bf16 v[0:3], v[154:157], v[186:189], v[0:3]
	v_mfma_f32_16x16x32_bf16 v[28:31], v[146:149], v[194:197], v[28:31]
	v_mfma_f32_16x16x32_bf16 v[24:27], v[154:157], v[194:197], v[24:27]
	v_mfma_f32_16x16x32_bf16 v[12:15], v[146:149], v[202:205], v[12:15]
	v_mfma_f32_16x16x32_bf16 v[8:11], v[154:157], v[202:205], v[8:11]
	v_mfma_f32_16x16x32_bf16 v[44:47], v[150:153], v[182:185], v[44:47]
	v_mfma_f32_16x16x32_bf16 v[32:35], v[158:161], v[182:185], v[32:35]
	v_mfma_f32_16x16x32_bf16 v[4:7], v[150:153], v[190:193], v[4:7]
	v_mfma_f32_16x16x32_bf16 v[0:3], v[158:161], v[190:193], v[0:3]
	v_mfma_f32_16x16x32_bf16 v[28:31], v[150:153], v[198:201], v[28:31]
	v_mfma_f32_16x16x32_bf16 v[24:27], v[158:161], v[198:201], v[24:27]
	v_mfma_f32_16x16x32_bf16 v[12:15], v[150:153], v[206:209], v[12:15]
	v_mfma_f32_16x16x32_bf16 v[8:11], v[158:161], v[206:209], v[8:11]
	s_setprio 1
	s_setprio 0
	v_mfma_f32_16x16x32_bf16 v[68:71], v[162:165], v[178:181], v[68:71]
	v_mfma_f32_16x16x32_bf16 v[64:67], v[170:173], v[178:181], v[64:67]
	v_mfma_f32_16x16x32_bf16 v[60:63], v[162:165], v[186:189], v[60:63]
	v_mfma_f32_16x16x32_bf16 v[56:59], v[170:173], v[186:189], v[56:59]
	v_mfma_f32_16x16x32_bf16 v[40:43], v[162:165], v[194:197], v[40:43]
	v_mfma_f32_16x16x32_bf16 v[36:39], v[170:173], v[194:197], v[36:39]
	v_mfma_f32_16x16x32_bf16 v[20:23], v[162:165], v[202:205], v[20:23]
	v_mfma_f32_16x16x32_bf16 v[16:19], v[170:173], v[202:205], v[16:19]
	v_mfma_f32_16x16x32_bf16 v[68:71], v[166:169], v[182:185], v[68:71]
	v_mfma_f32_16x16x32_bf16 v[64:67], v[174:177], v[182:185], v[64:67]
	v_mfma_f32_16x16x32_bf16 v[60:63], v[166:169], v[190:193], v[60:63]
	v_mfma_f32_16x16x32_bf16 v[56:59], v[174:177], v[190:193], v[56:59]
	v_mfma_f32_16x16x32_bf16 v[40:43], v[166:169], v[198:201], v[40:43]
	v_mfma_f32_16x16x32_bf16 v[36:39], v[174:177], v[198:201], v[36:39]
	v_mfma_f32_16x16x32_bf16 v[20:23], v[166:169], v[206:209], v[20:23]
	v_mfma_f32_16x16x32_bf16 v[16:19], v[174:177], v[206:209], v[16:19]
	s_setprio 1
	s_barrier
	s_andn2_b64 vcc, exec, s[28:29]
	s_mov_b64 s[30:31], -1
	s_mov_b64 s[28:29], 0
	s_mov_b64 s[34:35], 0x100
	s_cbranch_vccz .LBB0_3336
	s_and_b64 vcc, exec, s[10:11]
	s_cbranch_vccz .LBB0_3339
	s_barrier

.LBB0_3417:
	s_mov_b64 s[76:77], 0x100
	v_lshl_add_u64 v[0:1], v[168:169], 0, s[34:35]
	v_lshl_add_u64 v[0:1], v[0:1], 0, s[76:77]
	v_cndmask_b32_e64 v179, v1, v171, s[30:31]
	v_cndmask_b32_e64 v178, v0, v205, s[30:31]
	ds_read_b128 v[8:11], v185
	ds_read_b128 v[12:15], v189
	ds_read_b128 v[24:27], v190
	ds_read_b128 v[28:31], v191
	ds_read_b128 v[0:3], v186
	ds_read_b128 v[4:7], v192
	ds_read_b128 v[16:19], v193
	ds_read_b128 v[20:23], v194
	s_add_u32 s15, s22, s34
	s_addc_u32 s75, s23, s35
	s_add_u32 s78, s15, 0x100
	s_addc_u32 s79, s75, 0
	s_and_b64 s[36:37], s[30:31], exec
	s_cselect_b32 s37, s25, s79
	s_cselect_b32 s36, s74, s78
	s_add_u32 s34, s15, 0x10080
	s_addc_u32 s35, s75, 0
	s_add_i32 m0, s41, 0xc000
	s_add_i32 s15, s41, 0xe000
	s_add_u32 s30, s36, 0x10000
	s_addc_u32 s31, s37, 0
	v_lshl_add_u64 v[180:181], v[178:179], 0, s[0:1]
	v_lshl_add_u64 v[174:175], v[178:179], 0, s[10:11]
	v_lshl_add_u64 v[176:177], s[34:35], 0, v[164:165]
	ds_read_b128 v[206:209], v203
	ds_read_b128 v[210:213], v203 offset:1024
	ds_read_b128 v[214:217], v203 offset:2048
	ds_read_b128 v[218:221], v203 offset:3072
	ds_read_b128 v[222:225], v203 offset:4096
	ds_read_b128 v[226:229], v203 offset:5120
	ds_read_b128 v[230:233], v203 offset:6144
	ds_read_b128 v[234:237], v203 offset:7168
	global_load_lds_dwordx4 v[176:177], off
	v_lshl_add_u64 v[176:177], s[34:35], 0, v[166:167]
	s_mov_b32 m0, s15
	s_nop 0
	global_load_lds_dwordx4 v[176:177], off
	s_waitcnt vmcnt(8)
	s_waitcnt lgkmcnt(0)
	s_barrier
	s_setprio 0
	s_waitcnt lgkmcnt(0)
	v_mfma_f32_16x16x128_f8f6f4 v[156:159], v[8:15], v[206:213], v[156:159]
	v_mfma_f32_16x16x128_f8f6f4 v[152:155], v[24:31], v[206:213], v[152:155]
	v_mfma_f32_16x16x128_f8f6f4 v[140:143], v[8:15], v[214:221], v[140:143]
	v_mfma_f32_16x16x128_f8f6f4 v[136:139], v[24:31], v[214:221], v[136:139]
	v_mfma_f32_16x16x128_f8f6f4 v[124:127], v[8:15], v[222:229], v[124:127]
	v_mfma_f32_16x16x128_f8f6f4 v[120:123], v[24:31], v[222:229], v[120:123]
	v_mfma_f32_16x16x128_f8f6f4 v[108:111], v[8:15], v[230:237], v[108:111]
	v_mfma_f32_16x16x128_f8f6f4 v[104:107], v[24:31], v[230:237], v[104:107]
	s_setprio 1
	s_setprio 0
	v_mfma_f32_16x16x128_f8f6f4 v[148:151], v[0:7], v[206:213], v[148:151]
	v_mfma_f32_16x16x128_f8f6f4 v[144:147], v[16:23], v[206:213], v[144:147]
	v_mfma_f32_16x16x128_f8f6f4 v[132:135], v[0:7], v[214:221], v[132:135]
	v_mfma_f32_16x16x128_f8f6f4 v[128:131], v[16:23], v[214:221], v[128:131]
	v_mfma_f32_16x16x128_f8f6f4 v[116:119], v[0:7], v[222:229], v[116:119]
	v_mfma_f32_16x16x128_f8f6f4 v[112:115], v[16:23], v[222:229], v[112:115]
	v_mfma_f32_16x16x128_f8f6f4 v[92:95], v[0:7], v[230:237], v[92:95]
	v_mfma_f32_16x16x128_f8f6f4 v[88:91], v[16:23], v[230:237], v[88:91]
	s_setprio 1
	s_barrier
	s_mov_b32 m0, s42
	v_lshl_add_u64 v[176:177], v[178:179], 0, v[162:163]
	ds_read_b128 v[206:209], v203 offset:16384
	ds_read_b128 v[210:213], v203 offset:17408
	ds_read_b128 v[214:217], v203 offset:18432
	ds_read_b128 v[218:221], v203 offset:19456
	ds_read_b128 v[222:225], v203 offset:20480
	ds_read_b128 v[226:229], v203 offset:21504
	ds_read_b128 v[230:233], v203 offset:22528
	ds_read_b128 v[234:237], v203 offset:23552
	global_load_lds_dwordx4 v[176:177], off
	v_lshl_add_u64 v[178:179], v[178:179], 0, v[160:161]
	s_mov_b32 m0, s43
	v_lshl_add_u64 v[182:183], v[180:181], 0, v[162:163]
	global_load_lds_dwordx4 v[178:179], off
	s_mov_b32 m0, s44
	v_lshl_add_u64 v[180:181], v[180:181], 0, v[160:161]
	global_load_lds_dwordx4 v[182:183], off
	s_mov_b32 m0, s45
	v_lshl_add_u64 v[182:183], s[36:37], 0, v[166:167]
	global_load_lds_dwordx4 v[180:181], off
	v_lshl_add_u64 v[180:181], s[36:37], 0, v[164:165]
	s_mov_b32 m0, s41
	s_nop 0
	global_load_lds_dwordx4 v[180:181], off
	s_mov_b32 m0, s46
	s_nop 0
	global_load_lds_dwordx4 v[182:183], off
	s_waitcnt vmcnt(8)
	s_waitcnt lgkmcnt(0)
	s_barrier
	s_setprio 0
	s_waitcnt lgkmcnt(0)
	v_mfma_f32_16x16x128_f8f6f4 v[84:87], v[8:15], v[206:213], v[84:87]
	v_mfma_f32_16x16x128_f8f6f4 v[76:79], v[24:31], v[206:213], v[76:79]
	v_mfma_f32_16x16x128_f8f6f4 v[60:63], v[8:15], v[214:221], v[60:63]
	v_mfma_f32_16x16x128_f8f6f4 v[48:51], v[24:31], v[214:221], v[48:51]
	v_mfma_f32_16x16x128_f8f6f4 v[68:71], v[8:15], v[222:229], v[68:71]
	v_mfma_f32_16x16x128_f8f6f4 v[56:59], v[24:31], v[222:229], v[56:59]
	v_mfma_f32_16x16x128_f8f6f4 v[44:47], v[8:15], v[230:237], v[44:47]
	v_mfma_f32_16x16x128_f8f6f4 v[36:39], v[24:31], v[230:237], v[36:39]
	s_setprio 1
	s_setprio 0
	v_mfma_f32_16x16x128_f8f6f4 v[100:103], v[0:7], v[206:213], v[100:103]
	v_mfma_f32_16x16x128_f8f6f4 v[96:99], v[16:23], v[206:213], v[96:99]
	v_mfma_f32_16x16x128_f8f6f4 v[80:83], v[0:7], v[214:221], v[80:83]
	v_mfma_f32_16x16x128_f8f6f4 v[72:75], v[16:23], v[214:221], v[72:75]
	v_mfma_f32_16x16x128_f8f6f4 v[64:67], v[0:7], v[222:229], v[64:67]
	v_mfma_f32_16x16x128_f8f6f4 v[52:55], v[16:23], v[222:229], v[52:55]
	v_mfma_f32_16x16x128_f8f6f4 v[40:43], v[0:7], v[230:237], v[40:43]
	v_mfma_f32_16x16x128_f8f6f4 v[32:35], v[16:23], v[230:237], v[32:35]
	s_setprio 1
	s_barrier
	ds_read_b128 v[4:7], v195
	ds_read_b128 v[8:11], v196
	ds_read_b128 v[0:3], v187
	ds_read_b128 v[16:19], v188
	ds_read_b128 v[12:15], v197
	ds_read_b128 v[20:23], v198
	ds_read_b128 v[24:27], v199
	ds_read_b128 v[28:31], v200
	s_mov_b32 m0, s47
	v_lshl_add_u64 v[238:239], s[30:31], 0, v[164:165]
	ds_read_b128 v[206:209], v203 offset:32768
	ds_read_b128 v[210:213], v203 offset:33792
	ds_read_b128 v[214:217], v203 offset:34816
	ds_read_b128 v[218:221], v203 offset:35840
	ds_read_b128 v[222:225], v203 offset:36864
	ds_read_b128 v[226:229], v203 offset:37888
	ds_read_b128 v[230:233], v203 offset:38912
	ds_read_b128 v[234:237], v203 offset:39936
	global_load_lds_dwordx4 v[238:239], off
	v_lshl_add_u64 v[238:239], s[30:31], 0, v[166:167]
	s_mov_b32 m0, s48
	s_nop 0
	global_load_lds_dwordx4 v[238:239], off
	s_waitcnt vmcnt(8)
	s_waitcnt lgkmcnt(0)
	s_barrier
	s_setprio 0
	s_waitcnt lgkmcnt(0)
	v_mfma_f32_16x16x128_f8f6f4 v[156:159], v[0:7], v[206:213], v[156:159]
	v_mfma_f32_16x16x128_f8f6f4 v[152:155], v[8:15], v[206:213], v[152:155]
	v_mfma_f32_16x16x128_f8f6f4 v[140:143], v[0:7], v[214:221], v[140:143]
	v_mfma_f32_16x16x128_f8f6f4 v[136:139], v[8:15], v[214:221], v[136:139]
	v_mfma_f32_16x16x128_f8f6f4 v[124:127], v[0:7], v[222:229], v[124:127]
	v_mfma_f32_16x16x128_f8f6f4 v[120:123], v[8:15], v[222:229], v[120:123]
	v_mfma_f32_16x16x128_f8f6f4 v[108:111], v[0:7], v[230:237], v[108:111]
	v_mfma_f32_16x16x128_f8f6f4 v[104:107], v[8:15], v[230:237], v[104:107]
	s_setprio 1
	s_setprio 0
	v_mfma_f32_16x16x128_f8f6f4 v[148:151], v[16:23], v[206:213], v[148:151]
	v_mfma_f32_16x16x128_f8f6f4 v[144:147], v[24:31], v[206:213], v[144:147]
	v_mfma_f32_16x16x128_f8f6f4 v[132:135], v[16:23], v[214:221], v[132:135]
	v_mfma_f32_16x16x128_f8f6f4 v[128:131], v[24:31], v[214:221], v[128:131]
	v_mfma_f32_16x16x128_f8f6f4 v[116:119], v[16:23], v[222:229], v[116:119]
	v_mfma_f32_16x16x128_f8f6f4 v[112:115], v[24:31], v[222:229], v[112:115]
	v_mfma_f32_16x16x128_f8f6f4 v[92:95], v[16:23], v[230:237], v[92:95]
	v_mfma_f32_16x16x128_f8f6f4 v[88:91], v[24:31], v[230:237], v[88:91]
	s_setprio 1
	s_barrier
	s_mov_b32 m0, s50
	v_lshl_add_u64 v[176:177], v[176:177], 0, s[8:9]
	ds_read_b128 v[206:209], v203 offset:49152
	ds_read_b128 v[210:213], v203 offset:50176
	ds_read_b128 v[214:217], v203 offset:51200
	ds_read_b128 v[218:221], v203 offset:52224
	ds_read_b128 v[222:225], v203 offset:53248
	ds_read_b128 v[226:229], v203 offset:54272
	ds_read_b128 v[230:233], v203 offset:55296
	ds_read_b128 v[234:237], v203 offset:56320
	global_load_lds_dwordx4 v[176:177], off
	v_lshl_add_u64 v[176:177], v[178:179], 0, s[8:9]
	s_mov_b32 m0, s51
	s_nop 0
	global_load_lds_dwordx4 v[176:177], off
	v_lshl_add_u64 v[176:177], v[174:175], 0, v[162:163]
	s_mov_b32 m0, s54
	v_lshl_add_u64 v[174:175], v[174:175], 0, v[160:161]
	global_load_lds_dwordx4 v[176:177], off
	s_mov_b32 m0, s55
	s_nop 0
	global_load_lds_dwordx4 v[174:175], off
	v_lshl_add_u64 v[174:175], v[180:181], 0, s[8:9]
	s_mov_b32 m0, s52
	s_nop 0
	global_load_lds_dwordx4 v[174:175], off
	v_lshl_add_u64 v[174:175], v[182:183], 0, s[8:9]
	s_mov_b32 m0, s53
	s_nop 0
	global_load_lds_dwordx4 v[174:175], off
	s_waitcnt vmcnt(8)
	s_waitcnt lgkmcnt(0)
	s_barrier
	s_setprio 0
	s_waitcnt lgkmcnt(0)
	v_mfma_f32_16x16x128_f8f6f4 v[84:87], v[0:7], v[206:213], v[84:87]
	v_mfma_f32_16x16x128_f8f6f4 v[76:79], v[8:15], v[206:213], v[76:79]
	v_mfma_f32_16x16x128_f8f6f4 v[60:63], v[0:7], v[214:221], v[60:63]
	v_mfma_f32_16x16x128_f8f6f4 v[48:51], v[8:15], v[214:221], v[48:51]
	v_mfma_f32_16x16x128_f8f6f4 v[68:71], v[0:7], v[222:229], v[68:71]
	v_mfma_f32_16x16x128_f8f6f4 v[56:59], v[8:15], v[222:229], v[56:59]
	v_mfma_f32_16x16x128_f8f6f4 v[44:47], v[0:7], v[230:237], v[44:47]
	v_mfma_f32_16x16x128_f8f6f4 v[36:39], v[8:15], v[230:237], v[36:39]
	s_setprio 1
	s_setprio 0
	v_mfma_f32_16x16x128_f8f6f4 v[100:103], v[16:23], v[206:213], v[100:103]
	v_mfma_f32_16x16x128_f8f6f4 v[96:99], v[24:31], v[206:213], v[96:99]
	v_mfma_f32_16x16x128_f8f6f4 v[80:83], v[16:23], v[214:221], v[80:83]
	v_mfma_f32_16x16x128_f8f6f4 v[72:75], v[24:31], v[214:221], v[72:75]
	v_mfma_f32_16x16x128_f8f6f4 v[64:67], v[16:23], v[222:229], v[64:67]
	v_mfma_f32_16x16x128_f8f6f4 v[52:55], v[24:31], v[222:229], v[52:55]
	v_mfma_f32_16x16x128_f8f6f4 v[40:43], v[16:23], v[230:237], v[40:43]
	v_mfma_f32_16x16x128_f8f6f4 v[32:35], v[24:31], v[230:237], v[32:35]
	s_setprio 1
	s_barrier
	s_andn2_b64 vcc, exec, s[28:29]
	s_mov_b64 s[30:31], -1
	s_mov_b64 s[28:29], 0
	s_mov_b64 s[34:35], 0x100
	s_cbranch_vccz .LBB0_3417
	s_nop 15
	s_nop 7
	s_and_b64 vcc, exec, s[12:13]
	s_cbranch_vccz .LBB0_3420
	s_barrier

.LBB0_3429:
	s_add_u32 s16, s4, s12
	s_addc_u32 s17, s5, s13
	s_add_u32 s22, s16, 0x100
	s_addc_u32 s23, s17, 0
	s_and_b64 s[14:15], s[10:11], exec
	s_cselect_b32 s15, s5, s23
	s_cselect_b32 s14, s4, s22
	s_add_u32 s12, s0, s12
	s_addc_u32 s13, s1, s13
	ds_read_b128 v[144:147], v138
	ds_read_b128 v[148:151], v138 offset:1024
	ds_read_b128 v[152:155], v138 offset:2048
	ds_read_b128 v[156:159], v138 offset:3072
	ds_read_b128 v[160:163], v139
	ds_read_b128 v[164:167], v139 offset:1024
	ds_read_b128 v[168:171], v139 offset:2048
	ds_read_b128 v[172:175], v139 offset:3072
	s_add_u32 s12, s12, 0x100
	s_addc_u32 s13, s13, 0
	s_and_b64 s[10:11], s[10:11], exec
	s_cselect_b32 s13, s1, s13
	s_cselect_b32 s12, s0, s12
	s_add_u32 s24, s16, 0x10080
	s_addc_u32 s25, s17, 0
	s_add_u32 s16, s12, 0x10000
	s_addc_u32 s17, s13, 0
	s_add_u32 s10, s14, 0x10000
	s_addc_u32 s11, s15, 0
	s_add_u32 s22, s12, 0x10080
	s_addc_u32 s23, s13, 0
	s_mov_b32 m0, s37
	v_lshl_add_u64 v[208:209], s[24:25], 0, v[132:133]
	ds_read_b128 v[176:179], v140
	ds_read_b128 v[180:183], v140 offset:1024
	ds_read_b128 v[184:187], v140 offset:2048
	ds_read_b128 v[188:191], v140 offset:3072
	ds_read_b128 v[192:195], v140 offset:4096
	ds_read_b128 v[196:199], v140 offset:5120
	ds_read_b128 v[200:203], v140 offset:6144
	ds_read_b128 v[204:207], v140 offset:7168
	global_load_lds_dwordx4 v[208:209], off
	v_lshl_add_u64 v[208:209], s[24:25], 0, v[134:135]
	s_mov_b32 m0, s38
	s_nop 0
	global_load_lds_dwordx4 v[208:209], off
	s_waitcnt vmcnt(8)
	s_waitcnt lgkmcnt(0)
	s_barrier
	s_setprio 0
	s_waitcnt lgkmcnt(0)
	v_mfma_f32_16x16x32_bf16 v[124:127], v[144:147], v[176:179], v[124:127]
	v_mfma_f32_16x16x32_bf16 v[120:123], v[152:155], v[176:179], v[120:123]
	v_mfma_f32_16x16x32_bf16 v[116:119], v[144:147], v[184:187], v[116:119]
	v_mfma_f32_16x16x32_bf16 v[108:111], v[152:155], v[184:187], v[108:111]
	v_mfma_f32_16x16x32_bf16 v[100:103], v[144:147], v[192:195], v[100:103]
	v_mfma_f32_16x16x32_bf16 v[92:95], v[152:155], v[192:195], v[92:95]
	v_mfma_f32_16x16x32_bf16 v[84:87], v[144:147], v[200:203], v[84:87]
	v_mfma_f32_16x16x32_bf16 v[76:79], v[152:155], v[200:203], v[76:79]
	v_mfma_f32_16x16x32_bf16 v[124:127], v[148:151], v[180:183], v[124:127]
	v_mfma_f32_16x16x32_bf16 v[120:123], v[156:159], v[180:183], v[120:123]
	v_mfma_f32_16x16x32_bf16 v[116:119], v[148:151], v[188:191], v[116:119]
	v_mfma_f32_16x16x32_bf16 v[108:111], v[156:159], v[188:191], v[108:111]
	v_mfma_f32_16x16x32_bf16 v[100:103], v[148:151], v[196:199], v[100:103]
	v_mfma_f32_16x16x32_bf16 v[92:95], v[156:159], v[196:199], v[92:95]
	v_mfma_f32_16x16x32_bf16 v[84:87], v[148:151], v[204:207], v[84:87]
	v_mfma_f32_16x16x32_bf16 v[76:79], v[156:159], v[204:207], v[76:79]
	s_setprio 1
	s_setprio 0
	v_mfma_f32_16x16x32_bf16 v[112:115], v[160:163], v[176:179], v[112:115]
	v_mfma_f32_16x16x32_bf16 v[104:107], v[168:171], v[176:179], v[104:107]
	v_mfma_f32_16x16x32_bf16 v[96:99], v[160:163], v[184:187], v[96:99]
	v_mfma_f32_16x16x32_bf16 v[88:91], v[168:171], v[184:187], v[88:91]
	v_mfma_f32_16x16x32_bf16 v[80:83], v[160:163], v[192:195], v[80:83]
	v_mfma_f32_16x16x32_bf16 v[72:75], v[168:171], v[192:195], v[72:75]
	v_mfma_f32_16x16x32_bf16 v[52:55], v[160:163], v[200:203], v[52:55]
	v_mfma_f32_16x16x32_bf16 v[48:51], v[168:171], v[200:203], v[48:51]
	v_mfma_f32_16x16x32_bf16 v[112:115], v[164:167], v[180:183], v[112:115]
	v_mfma_f32_16x16x32_bf16 v[104:107], v[172:175], v[180:183], v[104:107]
	v_mfma_f32_16x16x32_bf16 v[96:99], v[164:167], v[188:191], v[96:99]
	v_mfma_f32_16x16x32_bf16 v[88:91], v[172:175], v[188:191], v[88:91]
	v_mfma_f32_16x16x32_bf16 v[80:83], v[164:167], v[196:199], v[80:83]
	v_mfma_f32_16x16x32_bf16 v[72:75], v[172:175], v[196:199], v[72:75]
	v_mfma_f32_16x16x32_bf16 v[52:55], v[164:167], v[204:207], v[52:55]
	v_mfma_f32_16x16x32_bf16 v[48:51], v[172:175], v[204:207], v[48:51]
	s_setprio 1
	s_barrier
	s_mov_b32 m0, s39
	v_lshl_add_u64 v[208:209], s[12:13], 0, v[130:131]
	ds_read_b128 v[176:179], v140 offset:16384
	ds_read_b128 v[180:183], v140 offset:17408
	ds_read_b128 v[184:187], v140 offset:18432
	ds_read_b128 v[188:191], v140 offset:19456
	ds_read_b128 v[192:195], v140 offset:20480
	ds_read_b128 v[196:199], v140 offset:21504
	ds_read_b128 v[200:203], v140 offset:22528
	ds_read_b128 v[204:207], v140 offset:23552
	global_load_lds_dwordx4 v[208:209], off
	v_lshl_add_u64 v[210:211], s[12:13], 0, v[128:129]
	s_mov_b32 m0, s40
	v_lshl_add_u64 v[212:213], s[16:17], 0, v[130:131]
	global_load_lds_dwordx4 v[210:211], off
	s_mov_b32 m0, s41
	v_lshl_add_u64 v[214:215], s[14:15], 0, v[134:135]
	global_load_lds_dwordx4 v[212:213], off
	v_lshl_add_u64 v[212:213], s[16:17], 0, v[128:129]
	s_mov_b32 m0, s42
	s_nop 0
	global_load_lds_dwordx4 v[212:213], off
	v_lshl_add_u64 v[212:213], s[14:15], 0, v[132:133]
	s_mov_b32 m0, s29
	s_nop 0
	global_load_lds_dwordx4 v[212:213], off
	s_mov_b32 m0, s30
	s_nop 0
	global_load_lds_dwordx4 v[214:215], off
	s_waitcnt vmcnt(8)
	s_waitcnt lgkmcnt(0)
	s_barrier
	s_setprio 0
	s_waitcnt lgkmcnt(0)
	v_mfma_f32_16x16x32_bf16 v[44:47], v[144:147], v[176:179], v[44:47]
	v_mfma_f32_16x16x32_bf16 v[32:35], v[152:155], v[176:179], v[32:35]
	v_mfma_f32_16x16x32_bf16 v[4:7], v[144:147], v[184:187], v[4:7]
	v_mfma_f32_16x16x32_bf16 v[0:3], v[152:155], v[184:187], v[0:3]
	v_mfma_f32_16x16x32_bf16 v[28:31], v[144:147], v[192:195], v[28:31]
	v_mfma_f32_16x16x32_bf16 v[24:27], v[152:155], v[192:195], v[24:27]
	v_mfma_f32_16x16x32_bf16 v[12:15], v[144:147], v[200:203], v[12:15]
	v_mfma_f32_16x16x32_bf16 v[8:11], v[152:155], v[200:203], v[8:11]
	v_mfma_f32_16x16x32_bf16 v[44:47], v[148:151], v[180:183], v[44:47]
	v_mfma_f32_16x16x32_bf16 v[32:35], v[156:159], v[180:183], v[32:35]
	v_mfma_f32_16x16x32_bf16 v[4:7], v[148:151], v[188:191], v[4:7]
	v_mfma_f32_16x16x32_bf16 v[0:3], v[156:159], v[188:191], v[0:3]
	v_mfma_f32_16x16x32_bf16 v[28:31], v[148:151], v[196:199], v[28:31]
	v_mfma_f32_16x16x32_bf16 v[24:27], v[156:159], v[196:199], v[24:27]
	v_mfma_f32_16x16x32_bf16 v[12:15], v[148:151], v[204:207], v[12:15]
	v_mfma_f32_16x16x32_bf16 v[8:11], v[156:159], v[204:207], v[8:11]
	s_setprio 1
	s_setprio 0
	v_mfma_f32_16x16x32_bf16 v[68:71], v[160:163], v[176:179], v[68:71]
	v_mfma_f32_16x16x32_bf16 v[64:67], v[168:171], v[176:179], v[64:67]
	v_mfma_f32_16x16x32_bf16 v[60:63], v[160:163], v[184:187], v[60:63]
	v_mfma_f32_16x16x32_bf16 v[56:59], v[168:171], v[184:187], v[56:59]
	v_mfma_f32_16x16x32_bf16 v[40:43], v[160:163], v[192:195], v[40:43]
	v_mfma_f32_16x16x32_bf16 v[36:39], v[168:171], v[192:195], v[36:39]
	v_mfma_f32_16x16x32_bf16 v[20:23], v[160:163], v[200:203], v[20:23]
	v_mfma_f32_16x16x32_bf16 v[16:19], v[168:171], v[200:203], v[16:19]
	v_mfma_f32_16x16x32_bf16 v[68:71], v[164:167], v[180:183], v[68:71]
	v_mfma_f32_16x16x32_bf16 v[64:67], v[172:175], v[180:183], v[64:67]
	v_mfma_f32_16x16x32_bf16 v[60:63], v[164:167], v[188:191], v[60:63]
	v_mfma_f32_16x16x32_bf16 v[56:59], v[172:175], v[188:191], v[56:59]
	v_mfma_f32_16x16x32_bf16 v[40:43], v[164:167], v[196:199], v[40:43]
	v_mfma_f32_16x16x32_bf16 v[36:39], v[172:175], v[196:199], v[36:39]
	v_mfma_f32_16x16x32_bf16 v[20:23], v[164:167], v[204:207], v[20:23]
	v_mfma_f32_16x16x32_bf16 v[16:19], v[172:175], v[204:207], v[16:19]
	s_setprio 1
	s_barrier
	ds_read_b128 v[144:147], v141
	ds_read_b128 v[148:151], v141 offset:1024
	ds_read_b128 v[152:155], v141 offset:2048
	ds_read_b128 v[156:159], v141 offset:3072
	ds_read_b128 v[160:163], v142
	ds_read_b128 v[164:167], v142 offset:1024
	ds_read_b128 v[168:171], v142 offset:2048
	ds_read_b128 v[172:175], v142 offset:3072
	s_mov_b32 m0, s31
	v_lshl_add_u64 v[216:217], s[10:11], 0, v[132:133]
	ds_read_b128 v[176:179], v140 offset:32768
	ds_read_b128 v[180:183], v140 offset:33792
	ds_read_b128 v[184:187], v140 offset:34816
	ds_read_b128 v[188:191], v140 offset:35840
	ds_read_b128 v[192:195], v140 offset:36864
	ds_read_b128 v[196:199], v140 offset:37888
	ds_read_b128 v[200:203], v140 offset:38912
	ds_read_b128 v[204:207], v140 offset:39936
	global_load_lds_dwordx4 v[216:217], off
	v_lshl_add_u64 v[216:217], s[10:11], 0, v[134:135]
	s_mov_b32 m0, s33
	s_nop 0
	global_load_lds_dwordx4 v[216:217], off
	s_waitcnt vmcnt(8)
	s_waitcnt lgkmcnt(0)
	s_barrier
	s_setprio 0
	s_waitcnt lgkmcnt(0)
	v_mfma_f32_16x16x32_bf16 v[124:127], v[144:147], v[176:179], v[124:127]
	v_mfma_f32_16x16x32_bf16 v[120:123], v[152:155], v[176:179], v[120:123]
	v_mfma_f32_16x16x32_bf16 v[116:119], v[144:147], v[184:187], v[116:119]
	v_mfma_f32_16x16x32_bf16 v[108:111], v[152:155], v[184:187], v[108:111]
	v_mfma_f32_16x16x32_bf16 v[100:103], v[144:147], v[192:195], v[100:103]
	v_mfma_f32_16x16x32_bf16 v[92:95], v[152:155], v[192:195], v[92:95]
	v_mfma_f32_16x16x32_bf16 v[84:87], v[144:147], v[200:203], v[84:87]
	v_mfma_f32_16x16x32_bf16 v[76:79], v[152:155], v[200:203], v[76:79]
	v_mfma_f32_16x16x32_bf16 v[124:127], v[148:151], v[180:183], v[124:127]
	v_mfma_f32_16x16x32_bf16 v[120:123], v[156:159], v[180:183], v[120:123]
	v_mfma_f32_16x16x32_bf16 v[116:119], v[148:151], v[188:191], v[116:119]
	v_mfma_f32_16x16x32_bf16 v[108:111], v[156:159], v[188:191], v[108:111]
	v_mfma_f32_16x16x32_bf16 v[100:103], v[148:151], v[196:199], v[100:103]
	v_mfma_f32_16x16x32_bf16 v[92:95], v[156:159], v[196:199], v[92:95]
	v_mfma_f32_16x16x32_bf16 v[84:87], v[148:151], v[204:207], v[84:87]
	v_mfma_f32_16x16x32_bf16 v[76:79], v[156:159], v[204:207], v[76:79]
	s_setprio 1
	s_setprio 0
	v_mfma_f32_16x16x32_bf16 v[112:115], v[160:163], v[176:179], v[112:115]
	v_mfma_f32_16x16x32_bf16 v[104:107], v[168:171], v[176:179], v[104:107]
	v_mfma_f32_16x16x32_bf16 v[96:99], v[160:163], v[184:187], v[96:99]
	v_mfma_f32_16x16x32_bf16 v[88:91], v[168:171], v[184:187], v[88:91]
	v_mfma_f32_16x16x32_bf16 v[80:83], v[160:163], v[192:195], v[80:83]
	v_mfma_f32_16x16x32_bf16 v[72:75], v[168:171], v[192:195], v[72:75]
	v_mfma_f32_16x16x32_bf16 v[52:55], v[160:163], v[200:203], v[52:55]
	v_mfma_f32_16x16x32_bf16 v[48:51], v[168:171], v[200:203], v[48:51]
	v_mfma_f32_16x16x32_bf16 v[112:115], v[164:167], v[180:183], v[112:115]
	v_mfma_f32_16x16x32_bf16 v[104:107], v[172:175], v[180:183], v[104:107]
	v_mfma_f32_16x16x32_bf16 v[96:99], v[164:167], v[188:191], v[96:99]
	v_mfma_f32_16x16x32_bf16 v[88:91], v[172:175], v[188:191], v[88:91]
	v_mfma_f32_16x16x32_bf16 v[80:83], v[164:167], v[196:199], v[80:83]
	v_mfma_f32_16x16x32_bf16 v[72:75], v[172:175], v[196:199], v[72:75]
	v_mfma_f32_16x16x32_bf16 v[52:55], v[164:167], v[204:207], v[52:55]
	v_mfma_f32_16x16x32_bf16 v[48:51], v[172:175], v[204:207], v[48:51]
	s_setprio 1
	s_barrier
	s_mov_b32 m0, s43
	v_lshl_add_u64 v[208:209], v[208:209], 0, s[6:7]
	ds_read_b128 v[176:179], v140 offset:49152
	ds_read_b128 v[180:183], v140 offset:50176
	ds_read_b128 v[184:187], v140 offset:51200
	ds_read_b128 v[188:191], v140 offset:52224
	ds_read_b128 v[192:195], v140 offset:53248
	ds_read_b128 v[196:199], v140 offset:54272
	ds_read_b128 v[200:203], v140 offset:55296
	ds_read_b128 v[204:207], v140 offset:56320
	global_load_lds_dwordx4 v[208:209], off
	v_lshl_add_u64 v[208:209], v[210:211], 0, s[6:7]
	s_mov_b32 m0, s44
	s_nop 0
	global_load_lds_dwordx4 v[208:209], off
	v_lshl_add_u64 v[208:209], s[22:23], 0, v[130:131]
	s_mov_b32 m0, s45
	s_nop 0
	global_load_lds_dwordx4 v[208:209], off
	v_lshl_add_u64 v[208:209], s[22:23], 0, v[128:129]
	s_mov_b32 m0, s46
	s_nop 0
	global_load_lds_dwordx4 v[208:209], off
	v_lshl_add_u64 v[208:209], v[212:213], 0, s[6:7]
	s_mov_b32 m0, s35
	s_nop 0
	global_load_lds_dwordx4 v[208:209], off
	v_lshl_add_u64 v[208:209], v[214:215], 0, s[6:7]
	s_mov_b32 m0, s36
	s_nop 0
	global_load_lds_dwordx4 v[208:209], off
	s_waitcnt vmcnt(8)
	s_waitcnt lgkmcnt(0)
	s_barrier
	s_setprio 0
	s_waitcnt lgkmcnt(0)
	v_mfma_f32_16x16x32_bf16 v[44:47], v[144:147], v[176:179], v[44:47]
	v_mfma_f32_16x16x32_bf16 v[32:35], v[152:155], v[176:179], v[32:35]
	v_mfma_f32_16x16x32_bf16 v[4:7], v[144:147], v[184:187], v[4:7]
	v_mfma_f32_16x16x32_bf16 v[0:3], v[152:155], v[184:187], v[0:3]
	v_mfma_f32_16x16x32_bf16 v[28:31], v[144:147], v[192:195], v[28:31]
	v_mfma_f32_16x16x32_bf16 v[24:27], v[152:155], v[192:195], v[24:27]
	v_mfma_f32_16x16x32_bf16 v[12:15], v[144:147], v[200:203], v[12:15]
	v_mfma_f32_16x16x32_bf16 v[8:11], v[152:155], v[200:203], v[8:11]
	v_mfma_f32_16x16x32_bf16 v[44:47], v[148:151], v[180:183], v[44:47]
	v_mfma_f32_16x16x32_bf16 v[32:35], v[156:159], v[180:183], v[32:35]
	v_mfma_f32_16x16x32_bf16 v[4:7], v[148:151], v[188:191], v[4:7]
	v_mfma_f32_16x16x32_bf16 v[0:3], v[156:159], v[188:191], v[0:3]
	v_mfma_f32_16x16x32_bf16 v[28:31], v[148:151], v[196:199], v[28:31]
	v_mfma_f32_16x16x32_bf16 v[24:27], v[156:159], v[196:199], v[24:27]
	v_mfma_f32_16x16x32_bf16 v[12:15], v[148:151], v[204:207], v[12:15]
	v_mfma_f32_16x16x32_bf16 v[8:11], v[156:159], v[204:207], v[8:11]
	s_setprio 1
	s_setprio 0
	v_mfma_f32_16x16x32_bf16 v[68:71], v[160:163], v[176:179], v[68:71]
	v_mfma_f32_16x16x32_bf16 v[64:67], v[168:171], v[176:179], v[64:67]
	v_mfma_f32_16x16x32_bf16 v[60:63], v[160:163], v[184:187], v[60:63]
	v_mfma_f32_16x16x32_bf16 v[56:59], v[168:171], v[184:187], v[56:59]
	v_mfma_f32_16x16x32_bf16 v[40:43], v[160:163], v[192:195], v[40:43]
	v_mfma_f32_16x16x32_bf16 v[36:39], v[168:171], v[192:195], v[36:39]
	v_mfma_f32_16x16x32_bf16 v[20:23], v[160:163], v[200:203], v[20:23]
	v_mfma_f32_16x16x32_bf16 v[16:19], v[168:171], v[200:203], v[16:19]
	v_mfma_f32_16x16x32_bf16 v[68:71], v[164:167], v[180:183], v[68:71]
	v_mfma_f32_16x16x32_bf16 v[64:67], v[172:175], v[180:183], v[64:67]
	v_mfma_f32_16x16x32_bf16 v[60:63], v[164:167], v[188:191], v[60:63]
	v_mfma_f32_16x16x32_bf16 v[56:59], v[172:175], v[188:191], v[56:59]
	v_mfma_f32_16x16x32_bf16 v[40:43], v[164:167], v[196:199], v[40:43]
	v_mfma_f32_16x16x32_bf16 v[36:39], v[172:175], v[196:199], v[36:39]
	v_mfma_f32_16x16x32_bf16 v[20:23], v[164:167], v[204:207], v[20:23]
	v_mfma_f32_16x16x32_bf16 v[16:19], v[172:175], v[204:207], v[16:19]
	s_setprio 1
	s_barrier
	s_andn2_b64 vcc, exec, s[8:9]
	s_mov_b64 s[10:11], -1
	s_mov_b64 s[8:9], 0
	s_mov_b64 s[12:13], 0x100
	s_cbranch_vccz .LBB0_3429
	s_cmpk_lt_u32 s26, 0x100
	s_cbranch_scc0 .LBB0_3432
	s_barrier

.LBB0_3585:
	s_add_u32 s44, s30, s38
	s_addc_u32 s45, s31, s39
	s_add_u32 s42, s44, 0x100
	s_addc_u32 s43, s45, 0
	s_and_b64 s[40:41], s[36:37], exec
	s_cselect_b32 s41, s21, s43
	s_cselect_b32 s40, s69, s42
	s_add_u32 s38, s28, s38
	s_addc_u32 s39, s29, s39
	s_add_u32 s38, s38, 0x100
	s_addc_u32 s39, s39, 0
	s_and_b64 s[36:37], s[36:37], exec
	s_cselect_b32 s43, s17, s39
	s_cselect_b32 s42, s70, s38
	s_add_u32 s46, s44, 0x10080
	ds_read_b128 v[148:151], v145
	ds_read_b128 v[152:155], v145 offset:1024
	ds_read_b128 v[156:159], v145 offset:2048
	ds_read_b128 v[160:163], v145 offset:3072
	ds_read_b128 v[164:167], v146
	ds_read_b128 v[168:171], v146 offset:1024
	ds_read_b128 v[172:175], v146 offset:2048
	ds_read_b128 v[176:179], v146 offset:3072
	s_addc_u32 s47, s45, 0
	s_add_i32 s78, s62, s50
	s_add_i32 m0, s27, 0xc000
	s_add_i32 s81, s27, 0xe000
	s_add_i32 s75, s78, 0x2000
	s_add_u32 s44, s42, 0x10000
	s_addc_u32 s45, s43, 0
	s_add_i32 s77, s63, s50
	s_add_i32 s76, s77, 0x2000
	s_add_i32 s74, 0, 0x18000
	s_add_i32 s73, 0, 0x1c000
	s_add_u32 s38, s40, 0x10000
	s_addc_u32 s39, s41, 0
	s_add_i32 s72, s74, s50
	s_add_i32 s71, s72, 0x2000
	s_add_u32 s36, s42, 0x10080
	s_addc_u32 s37, s43, 0
	s_add_i32 s80, s73, s50
	s_add_i32 s79, s80, 0x2000
	v_lshl_add_u64 v[140:141], s[46:47], 0, v[132:133]
	ds_read_b128 v[180:183], v147
	ds_read_b128 v[184:187], v147 offset:1024
	ds_read_b128 v[188:191], v147 offset:2048
	ds_read_b128 v[192:195], v147 offset:3072
	ds_read_b128 v[196:199], v147 offset:4096
	ds_read_b128 v[200:203], v147 offset:5120
	ds_read_b128 v[204:207], v147 offset:6144
	ds_read_b128 v[208:211], v147 offset:7168
	global_load_lds_dwordx4 v[140:141], off
	v_lshl_add_u64 v[140:141], s[46:47], 0, v[134:135]
	s_mov_b32 m0, s81
	s_nop 0
	global_load_lds_dwordx4 v[140:141], off
	s_waitcnt vmcnt(8)
	s_waitcnt lgkmcnt(0)
	s_barrier
	s_setprio 0
	s_waitcnt lgkmcnt(0)
	v_mfma_f32_16x16x32_bf16 v[124:127], v[148:151], v[180:183], v[124:127]
	v_mfma_f32_16x16x32_bf16 v[120:123], v[156:159], v[180:183], v[120:123]
	v_mfma_f32_16x16x32_bf16 v[116:119], v[148:151], v[188:191], v[116:119]
	v_mfma_f32_16x16x32_bf16 v[108:111], v[156:159], v[188:191], v[108:111]
	v_mfma_f32_16x16x32_bf16 v[100:103], v[148:151], v[196:199], v[100:103]
	v_mfma_f32_16x16x32_bf16 v[92:95], v[156:159], v[196:199], v[92:95]
	v_mfma_f32_16x16x32_bf16 v[84:87], v[148:151], v[204:207], v[84:87]
	v_mfma_f32_16x16x32_bf16 v[76:79], v[156:159], v[204:207], v[76:79]
	v_mfma_f32_16x16x32_bf16 v[124:127], v[152:155], v[184:187], v[124:127]
	v_mfma_f32_16x16x32_bf16 v[120:123], v[160:163], v[184:187], v[120:123]
	v_mfma_f32_16x16x32_bf16 v[116:119], v[152:155], v[192:195], v[116:119]
	v_mfma_f32_16x16x32_bf16 v[108:111], v[160:163], v[192:195], v[108:111]
	v_mfma_f32_16x16x32_bf16 v[100:103], v[152:155], v[200:203], v[100:103]
	v_mfma_f32_16x16x32_bf16 v[92:95], v[160:163], v[200:203], v[92:95]
	v_mfma_f32_16x16x32_bf16 v[84:87], v[152:155], v[208:211], v[84:87]
	v_mfma_f32_16x16x32_bf16 v[76:79], v[160:163], v[208:211], v[76:79]
	s_setprio 1
	s_setprio 0
	v_mfma_f32_16x16x32_bf16 v[112:115], v[164:167], v[180:183], v[112:115]
	v_mfma_f32_16x16x32_bf16 v[104:107], v[172:175], v[180:183], v[104:107]
	v_mfma_f32_16x16x32_bf16 v[96:99], v[164:167], v[188:191], v[96:99]
	v_mfma_f32_16x16x32_bf16 v[88:91], v[172:175], v[188:191], v[88:91]
	v_mfma_f32_16x16x32_bf16 v[80:83], v[164:167], v[196:199], v[80:83]
	v_mfma_f32_16x16x32_bf16 v[72:75], v[172:175], v[196:199], v[72:75]
	v_mfma_f32_16x16x32_bf16 v[52:55], v[164:167], v[204:207], v[52:55]
	v_mfma_f32_16x16x32_bf16 v[48:51], v[172:175], v[204:207], v[48:51]
	v_mfma_f32_16x16x32_bf16 v[112:115], v[168:171], v[184:187], v[112:115]
	v_mfma_f32_16x16x32_bf16 v[104:107], v[176:179], v[184:187], v[104:107]
	v_mfma_f32_16x16x32_bf16 v[96:99], v[168:171], v[192:195], v[96:99]
	v_mfma_f32_16x16x32_bf16 v[88:91], v[176:179], v[192:195], v[88:91]
	v_mfma_f32_16x16x32_bf16 v[80:83], v[168:171], v[200:203], v[80:83]
	v_mfma_f32_16x16x32_bf16 v[72:75], v[176:179], v[200:203], v[72:75]
	v_mfma_f32_16x16x32_bf16 v[52:55], v[168:171], v[208:211], v[52:55]
	v_mfma_f32_16x16x32_bf16 v[48:51], v[176:179], v[208:211], v[48:51]
	s_setprio 1
	s_barrier
	s_mov_b32 m0, s78
	v_lshl_add_u64 v[140:141], s[42:43], 0, v[128:129]
	ds_read_b128 v[180:183], v147 offset:16384
	ds_read_b128 v[184:187], v147 offset:17408
	ds_read_b128 v[188:191], v147 offset:18432
	ds_read_b128 v[192:195], v147 offset:19456
	ds_read_b128 v[196:199], v147 offset:20480
	ds_read_b128 v[200:203], v147 offset:21504
	ds_read_b128 v[204:207], v147 offset:22528
	ds_read_b128 v[208:211], v147 offset:23552
	global_load_lds_dwordx4 v[140:141], off
	v_lshl_add_u64 v[212:213], s[42:43], 0, v[130:131]
	s_mov_b32 m0, s75
	v_lshl_add_u64 v[214:215], s[44:45], 0, v[128:129]
	global_load_lds_dwordx4 v[212:213], off
	s_mov_b32 m0, s77
	v_lshl_add_u64 v[216:217], s[40:41], 0, v[134:135]
	global_load_lds_dwordx4 v[214:215], off
	v_lshl_add_u64 v[214:215], s[44:45], 0, v[130:131]
	s_mov_b32 m0, s76
	s_nop 0
	global_load_lds_dwordx4 v[214:215], off
	v_lshl_add_u64 v[214:215], s[40:41], 0, v[132:133]
	s_mov_b32 m0, s27
	s_nop 0
	global_load_lds_dwordx4 v[214:215], off
	s_mov_b32 m0, s55
	s_nop 0
	global_load_lds_dwordx4 v[216:217], off
	s_waitcnt vmcnt(8)
	s_waitcnt lgkmcnt(0)
	s_barrier
	s_setprio 0
	s_waitcnt lgkmcnt(0)
	v_mfma_f32_16x16x32_bf16 v[40:43], v[148:151], v[180:183], v[40:43]
	v_mfma_f32_16x16x32_bf16 v[28:31], v[156:159], v[180:183], v[28:31]
	v_mfma_f32_16x16x32_bf16 v[4:7], v[148:151], v[188:191], v[4:7]
	v_mfma_f32_16x16x32_bf16 v[0:3], v[156:159], v[188:191], v[0:3]
	v_mfma_f32_16x16x32_bf16 v[32:35], v[148:151], v[196:199], v[32:35]
	v_mfma_f32_16x16x32_bf16 v[24:27], v[156:159], v[196:199], v[24:27]
	v_mfma_f32_16x16x32_bf16 v[12:15], v[148:151], v[204:207], v[12:15]
	v_mfma_f32_16x16x32_bf16 v[8:11], v[156:159], v[204:207], v[8:11]
	v_mfma_f32_16x16x32_bf16 v[40:43], v[152:155], v[184:187], v[40:43]
	v_mfma_f32_16x16x32_bf16 v[28:31], v[160:163], v[184:187], v[28:31]
	v_mfma_f32_16x16x32_bf16 v[4:7], v[152:155], v[192:195], v[4:7]
	v_mfma_f32_16x16x32_bf16 v[0:3], v[160:163], v[192:195], v[0:3]
	v_mfma_f32_16x16x32_bf16 v[32:35], v[152:155], v[200:203], v[32:35]
	v_mfma_f32_16x16x32_bf16 v[24:27], v[160:163], v[200:203], v[24:27]
	v_mfma_f32_16x16x32_bf16 v[12:15], v[152:155], v[208:211], v[12:15]
	v_mfma_f32_16x16x32_bf16 v[8:11], v[160:163], v[208:211], v[8:11]
	s_setprio 1
	s_setprio 0
	v_mfma_f32_16x16x32_bf16 v[68:71], v[164:167], v[180:183], v[68:71]
	v_mfma_f32_16x16x32_bf16 v[64:67], v[172:175], v[180:183], v[64:67]
	v_mfma_f32_16x16x32_bf16 v[60:63], v[164:167], v[188:191], v[60:63]
	v_mfma_f32_16x16x32_bf16 v[56:59], v[172:175], v[188:191], v[56:59]
	v_mfma_f32_16x16x32_bf16 v[44:47], v[164:167], v[196:199], v[44:47]
	v_mfma_f32_16x16x32_bf16 v[36:39], v[172:175], v[196:199], v[36:39]
	v_mfma_f32_16x16x32_bf16 v[20:23], v[164:167], v[204:207], v[20:23]
	v_mfma_f32_16x16x32_bf16 v[16:19], v[172:175], v[204:207], v[16:19]
	v_mfma_f32_16x16x32_bf16 v[68:71], v[168:171], v[184:187], v[68:71]
	v_mfma_f32_16x16x32_bf16 v[64:67], v[176:179], v[184:187], v[64:67]
	v_mfma_f32_16x16x32_bf16 v[60:63], v[168:171], v[192:195], v[60:63]
	v_mfma_f32_16x16x32_bf16 v[56:59], v[176:179], v[192:195], v[56:59]
	v_mfma_f32_16x16x32_bf16 v[44:47], v[168:171], v[200:203], v[44:47]
	v_mfma_f32_16x16x32_bf16 v[36:39], v[176:179], v[200:203], v[36:39]
	v_mfma_f32_16x16x32_bf16 v[20:23], v[168:171], v[208:211], v[20:23]
	v_mfma_f32_16x16x32_bf16 v[16:19], v[176:179], v[208:211], v[16:19]
	s_setprio 1
	s_barrier
	v_add_u32_e32 v160, s74, v143
	v_add_u32_e32 v176, s73, v143
	ds_read_b128 v[148:151], v160
	ds_read_b128 v[152:155], v160 offset:1024
	ds_read_b128 v[156:159], v160 offset:2048
	ds_read_b128 v[160:163], v160 offset:3072
	ds_read_b128 v[164:167], v176
	ds_read_b128 v[168:171], v176 offset:1024
	ds_read_b128 v[172:175], v176 offset:2048
	ds_read_b128 v[176:179], v176 offset:3072
	s_mov_b32 m0, s56
	v_lshl_add_u64 v[218:219], s[38:39], 0, v[132:133]
	ds_read_b128 v[180:183], v147 offset:32768
	ds_read_b128 v[184:187], v147 offset:33792
	ds_read_b128 v[188:191], v147 offset:34816
	ds_read_b128 v[192:195], v147 offset:35840
	ds_read_b128 v[196:199], v147 offset:36864
	ds_read_b128 v[200:203], v147 offset:37888
	ds_read_b128 v[204:207], v147 offset:38912
	ds_read_b128 v[208:211], v147 offset:39936
	global_load_lds_dwordx4 v[218:219], off
	v_lshl_add_u64 v[218:219], s[38:39], 0, v[134:135]
	s_mov_b32 m0, s57
	s_nop 0
	global_load_lds_dwordx4 v[218:219], off
	s_waitcnt vmcnt(8)
	s_waitcnt lgkmcnt(0)
	s_barrier
	s_setprio 0
	s_waitcnt lgkmcnt(0)
	v_mfma_f32_16x16x32_bf16 v[124:127], v[148:151], v[180:183], v[124:127]
	v_mfma_f32_16x16x32_bf16 v[120:123], v[156:159], v[180:183], v[120:123]
	v_mfma_f32_16x16x32_bf16 v[116:119], v[148:151], v[188:191], v[116:119]
	v_mfma_f32_16x16x32_bf16 v[108:111], v[156:159], v[188:191], v[108:111]
	v_mfma_f32_16x16x32_bf16 v[100:103], v[148:151], v[196:199], v[100:103]
	v_mfma_f32_16x16x32_bf16 v[92:95], v[156:159], v[196:199], v[92:95]
	v_mfma_f32_16x16x32_bf16 v[84:87], v[148:151], v[204:207], v[84:87]
	v_mfma_f32_16x16x32_bf16 v[76:79], v[156:159], v[204:207], v[76:79]
	v_mfma_f32_16x16x32_bf16 v[124:127], v[152:155], v[184:187], v[124:127]
	v_mfma_f32_16x16x32_bf16 v[120:123], v[160:163], v[184:187], v[120:123]
	v_mfma_f32_16x16x32_bf16 v[116:119], v[152:155], v[192:195], v[116:119]
	v_mfma_f32_16x16x32_bf16 v[108:111], v[160:163], v[192:195], v[108:111]
	v_mfma_f32_16x16x32_bf16 v[100:103], v[152:155], v[200:203], v[100:103]
	v_mfma_f32_16x16x32_bf16 v[92:95], v[160:163], v[200:203], v[92:95]
	v_mfma_f32_16x16x32_bf16 v[84:87], v[152:155], v[208:211], v[84:87]
	v_mfma_f32_16x16x32_bf16 v[76:79], v[160:163], v[208:211], v[76:79]
	s_setprio 1
	s_setprio 0
	v_mfma_f32_16x16x32_bf16 v[112:115], v[164:167], v[180:183], v[112:115]
	v_mfma_f32_16x16x32_bf16 v[104:107], v[172:175], v[180:183], v[104:107]
	v_mfma_f32_16x16x32_bf16 v[96:99], v[164:167], v[188:191], v[96:99]
	v_mfma_f32_16x16x32_bf16 v[88:91], v[172:175], v[188:191], v[88:91]
	v_mfma_f32_16x16x32_bf16 v[80:83], v[164:167], v[196:199], v[80:83]
	v_mfma_f32_16x16x32_bf16 v[72:75], v[172:175], v[196:199], v[72:75]
	v_mfma_f32_16x16x32_bf16 v[52:55], v[164:167], v[204:207], v[52:55]
	v_mfma_f32_16x16x32_bf16 v[48:51], v[172:175], v[204:207], v[48:51]
	v_mfma_f32_16x16x32_bf16 v[112:115], v[168:171], v[184:187], v[112:115]
	v_mfma_f32_16x16x32_bf16 v[104:107], v[176:179], v[184:187], v[104:107]
	v_mfma_f32_16x16x32_bf16 v[96:99], v[168:171], v[192:195], v[96:99]
	v_mfma_f32_16x16x32_bf16 v[88:91], v[176:179], v[192:195], v[88:91]
	v_mfma_f32_16x16x32_bf16 v[80:83], v[168:171], v[200:203], v[80:83]
	v_mfma_f32_16x16x32_bf16 v[72:75], v[176:179], v[200:203], v[72:75]
	v_mfma_f32_16x16x32_bf16 v[52:55], v[168:171], v[208:211], v[52:55]
	v_mfma_f32_16x16x32_bf16 v[48:51], v[176:179], v[208:211], v[48:51]
	s_setprio 1
	s_barrier
	s_mov_b32 m0, s72
	v_lshl_add_u64 v[140:141], v[140:141], 0, s[4:5]
	ds_read_b128 v[180:183], v147 offset:49152
	ds_read_b128 v[184:187], v147 offset:50176
	ds_read_b128 v[188:191], v147 offset:51200
	ds_read_b128 v[192:195], v147 offset:52224
	ds_read_b128 v[196:199], v147 offset:53248
	ds_read_b128 v[200:203], v147 offset:54272
	ds_read_b128 v[204:207], v147 offset:55296
	ds_read_b128 v[208:211], v147 offset:56320
	global_load_lds_dwordx4 v[140:141], off
	v_lshl_add_u64 v[140:141], v[212:213], 0, s[4:5]
	s_mov_b32 m0, s71
	s_nop 0
	global_load_lds_dwordx4 v[140:141], off
	v_lshl_add_u64 v[140:141], s[36:37], 0, v[128:129]
	s_mov_b32 m0, s80
	s_nop 0
	global_load_lds_dwordx4 v[140:141], off
	v_lshl_add_u64 v[140:141], s[36:37], 0, v[130:131]
	s_mov_b32 m0, s79
	s_nop 0
	global_load_lds_dwordx4 v[140:141], off
	v_lshl_add_u64 v[140:141], v[214:215], 0, s[4:5]
	s_mov_b32 m0, s59
	s_nop 0
	global_load_lds_dwordx4 v[140:141], off
	v_lshl_add_u64 v[140:141], v[216:217], 0, s[4:5]
	s_mov_b32 m0, s60
	s_nop 0
	global_load_lds_dwordx4 v[140:141], off
	s_waitcnt vmcnt(8)
	s_waitcnt lgkmcnt(0)
	s_barrier
	s_setprio 0
	s_waitcnt lgkmcnt(0)
	v_mfma_f32_16x16x32_bf16 v[40:43], v[148:151], v[180:183], v[40:43]
	v_mfma_f32_16x16x32_bf16 v[28:31], v[156:159], v[180:183], v[28:31]
	v_mfma_f32_16x16x32_bf16 v[4:7], v[148:151], v[188:191], v[4:7]
	v_mfma_f32_16x16x32_bf16 v[0:3], v[156:159], v[188:191], v[0:3]
	v_mfma_f32_16x16x32_bf16 v[32:35], v[148:151], v[196:199], v[32:35]
	v_mfma_f32_16x16x32_bf16 v[24:27], v[156:159], v[196:199], v[24:27]
	v_mfma_f32_16x16x32_bf16 v[12:15], v[148:151], v[204:207], v[12:15]
	v_mfma_f32_16x16x32_bf16 v[8:11], v[156:159], v[204:207], v[8:11]
	v_mfma_f32_16x16x32_bf16 v[40:43], v[152:155], v[184:187], v[40:43]
	v_mfma_f32_16x16x32_bf16 v[28:31], v[160:163], v[184:187], v[28:31]
	v_mfma_f32_16x16x32_bf16 v[4:7], v[152:155], v[192:195], v[4:7]
	v_mfma_f32_16x16x32_bf16 v[0:3], v[160:163], v[192:195], v[0:3]
	v_mfma_f32_16x16x32_bf16 v[32:35], v[152:155], v[200:203], v[32:35]
	v_mfma_f32_16x16x32_bf16 v[24:27], v[160:163], v[200:203], v[24:27]
	v_mfma_f32_16x16x32_bf16 v[12:15], v[152:155], v[208:211], v[12:15]
	v_mfma_f32_16x16x32_bf16 v[8:11], v[160:163], v[208:211], v[8:11]
	s_setprio 1
	s_setprio 0
	v_mfma_f32_16x16x32_bf16 v[68:71], v[164:167], v[180:183], v[68:71]
	v_mfma_f32_16x16x32_bf16 v[64:67], v[172:175], v[180:183], v[64:67]
	v_mfma_f32_16x16x32_bf16 v[60:63], v[164:167], v[188:191], v[60:63]
	v_mfma_f32_16x16x32_bf16 v[56:59], v[172:175], v[188:191], v[56:59]
	v_mfma_f32_16x16x32_bf16 v[44:47], v[164:167], v[196:199], v[44:47]
	v_mfma_f32_16x16x32_bf16 v[36:39], v[172:175], v[196:199], v[36:39]
	v_mfma_f32_16x16x32_bf16 v[20:23], v[164:167], v[204:207], v[20:23]
	v_mfma_f32_16x16x32_bf16 v[16:19], v[172:175], v[204:207], v[16:19]
	v_mfma_f32_16x16x32_bf16 v[68:71], v[168:171], v[184:187], v[68:71]
	v_mfma_f32_16x16x32_bf16 v[64:67], v[176:179], v[184:187], v[64:67]
	v_mfma_f32_16x16x32_bf16 v[60:63], v[168:171], v[192:195], v[60:63]
	v_mfma_f32_16x16x32_bf16 v[56:59], v[176:179], v[192:195], v[56:59]
	v_mfma_f32_16x16x32_bf16 v[44:47], v[168:171], v[200:203], v[44:47]
	v_mfma_f32_16x16x32_bf16 v[36:39], v[176:179], v[200:203], v[36:39]
	v_mfma_f32_16x16x32_bf16 v[20:23], v[168:171], v[208:211], v[20:23]
	v_mfma_f32_16x16x32_bf16 v[16:19], v[176:179], v[208:211], v[16:19]
	s_setprio 1
	s_barrier
	s_andn2_b64 vcc, exec, s[34:35]
	s_mov_b64 s[36:37], -1
	s_mov_b64 s[34:35], 0
	s_mov_b64 s[38:39], 0x100
	s_cbranch_vccz .LBB0_3585
	s_and_b64 vcc, exec, s[6:7]
	s_cbranch_vccz .LBB0_3588
	s_barrier

.LBB0_3621:
	ds_read_b128 v[124:127], v213
	ds_read_b128 v[128:131], v213 offset:1024
	ds_read_b128 v[136:139], v213 offset:2048
	ds_read_b128 v[140:143], v213 offset:3072
	ds_read_b128 v[144:147], v214
	ds_read_b128 v[148:151], v214 offset:1024
	ds_read_b128 v[152:155], v214 offset:2048
	ds_read_b128 v[156:159], v214 offset:3072
	s_add_u32 s36, s34, 0xfffc0080
	s_addc_u32 s37, s35, -1
	s_cmp_eq_u32 s55, 12
	s_cselect_b32 s39, s3, s37
	s_cselect_b32 s38, s23, s36
	s_cselect_b32 s37, s21, s54
	s_cselect_b32 s36, s52, s53
	v_lshl_add_u64 v[206:207], s[34:35], 0, v[192:193]
	s_add_i32 m0, s31, 0xc000
	ds_read_b128 v[160:163], v215
	ds_read_b128 v[164:167], v215 offset:1024
	ds_read_b128 v[168:171], v215 offset:2048
	ds_read_b128 v[172:175], v215 offset:3072
	ds_read_b128 v[176:179], v215 offset:4096
	ds_read_b128 v[180:183], v215 offset:5120
	ds_read_b128 v[198:201], v215 offset:6144
	ds_read_b128 v[202:205], v215 offset:7168
	global_load_lds_dwordx4 v[206:207], off
	v_lshl_add_u64 v[206:207], s[34:35], 0, v[194:195]
	s_add_i32 m0, s31, 0xe000
	s_nop 0
	global_load_lds_dwordx4 v[206:207], off
	s_waitcnt vmcnt(8)
	s_waitcnt lgkmcnt(0)
	s_barrier
	s_setprio 0
	s_waitcnt lgkmcnt(0)
	v_mfma_f32_16x16x32_bf16 v[132:135], v[124:127], v[160:163], v[132:135]
	v_mfma_f32_16x16x32_bf16 v[120:123], v[136:139], v[160:163], v[120:123]
	v_mfma_f32_16x16x32_bf16 v[108:111], v[124:127], v[168:171], v[108:111]
	v_mfma_f32_16x16x32_bf16 v[104:107], v[136:139], v[168:171], v[104:107]
	v_mfma_f32_16x16x32_bf16 v[92:95], v[124:127], v[176:179], v[92:95]
	v_mfma_f32_16x16x32_bf16 v[88:91], v[136:139], v[176:179], v[88:91]
	v_mfma_f32_16x16x32_bf16 v[76:79], v[124:127], v[198:201], v[76:79]
	v_mfma_f32_16x16x32_bf16 v[72:75], v[136:139], v[198:201], v[72:75]
	v_mfma_f32_16x16x32_bf16 v[132:135], v[128:131], v[164:167], v[132:135]
	v_mfma_f32_16x16x32_bf16 v[120:123], v[140:143], v[164:167], v[120:123]
	v_mfma_f32_16x16x32_bf16 v[108:111], v[128:131], v[172:175], v[108:111]
	v_mfma_f32_16x16x32_bf16 v[104:107], v[140:143], v[172:175], v[104:107]
	v_mfma_f32_16x16x32_bf16 v[92:95], v[128:131], v[180:183], v[92:95]
	v_mfma_f32_16x16x32_bf16 v[88:91], v[140:143], v[180:183], v[88:91]
	v_mfma_f32_16x16x32_bf16 v[76:79], v[128:131], v[202:205], v[76:79]
	v_mfma_f32_16x16x32_bf16 v[72:75], v[140:143], v[202:205], v[72:75]
	s_setprio 1
	s_setprio 0
	v_mfma_f32_16x16x32_bf16 v[116:119], v[144:147], v[160:163], v[116:119]
	v_mfma_f32_16x16x32_bf16 v[112:115], v[152:155], v[160:163], v[112:115]
	v_mfma_f32_16x16x32_bf16 v[100:103], v[144:147], v[168:171], v[100:103]
	v_mfma_f32_16x16x32_bf16 v[96:99], v[152:155], v[168:171], v[96:99]
	v_mfma_f32_16x16x32_bf16 v[84:87], v[144:147], v[176:179], v[84:87]
	v_mfma_f32_16x16x32_bf16 v[80:83], v[152:155], v[176:179], v[80:83]
	v_mfma_f32_16x16x32_bf16 v[68:71], v[144:147], v[198:201], v[68:71]
	v_mfma_f32_16x16x32_bf16 v[64:67], v[152:155], v[198:201], v[64:67]
	v_mfma_f32_16x16x32_bf16 v[116:119], v[148:151], v[164:167], v[116:119]
	v_mfma_f32_16x16x32_bf16 v[112:115], v[156:159], v[164:167], v[112:115]
	v_mfma_f32_16x16x32_bf16 v[100:103], v[148:151], v[172:175], v[100:103]
	v_mfma_f32_16x16x32_bf16 v[96:99], v[156:159], v[172:175], v[96:99]
	v_mfma_f32_16x16x32_bf16 v[84:87], v[148:151], v[180:183], v[84:87]
	v_mfma_f32_16x16x32_bf16 v[80:83], v[156:159], v[180:183], v[80:83]
	v_mfma_f32_16x16x32_bf16 v[68:71], v[148:151], v[202:205], v[68:71]
	v_mfma_f32_16x16x32_bf16 v[64:67], v[156:159], v[202:205], v[64:67]
	s_setprio 1
	s_barrier
	s_add_i32 s56, s50, s41
	v_lshl_add_u64 v[206:207], s[36:37], 0, v[184:185]
	s_mov_b32 m0, s56
	ds_read_b128 v[160:163], v215 offset:16384
	ds_read_b128 v[164:167], v215 offset:17408
	ds_read_b128 v[168:171], v215 offset:18432
	ds_read_b128 v[172:175], v215 offset:19456
	ds_read_b128 v[176:179], v215 offset:20480
	ds_read_b128 v[180:183], v215 offset:21504
	ds_read_b128 v[198:201], v215 offset:22528
	ds_read_b128 v[202:205], v215 offset:23552
	global_load_lds_dwordx4 v[206:207], off
	s_add_i32 m0, s56, 0x2000
	s_add_u32 s56, s36, 0x40000
	v_lshl_add_u64 v[208:209], s[36:37], 0, v[186:187]
	s_addc_u32 s57, s37, 0
	s_add_i32 s58, s51, s41
	global_load_lds_dwordx4 v[208:209], off
	v_lshl_add_u64 v[216:217], s[56:57], 0, v[184:185]
	s_mov_b32 m0, s58
	v_lshl_add_u64 v[218:219], s[38:39], 0, v[190:191]
	global_load_lds_dwordx4 v[216:217], off
	v_lshl_add_u64 v[216:217], s[56:57], 0, v[186:187]
	s_add_i32 m0, s58, 0x2000
	s_nop 0
	global_load_lds_dwordx4 v[216:217], off
	v_lshl_add_u64 v[216:217], s[38:39], 0, v[188:189]
	s_mov_b32 m0, s31
	s_nop 0
	global_load_lds_dwordx4 v[216:217], off
	s_mov_b32 m0, s42
	s_nop 0
	global_load_lds_dwordx4 v[218:219], off
	s_waitcnt vmcnt(8)
	s_waitcnt lgkmcnt(0)
	s_barrier
	s_setprio 0
	s_waitcnt lgkmcnt(0)
	v_mfma_f32_16x16x32_bf16 v[60:63], v[124:127], v[160:163], v[60:63]
	v_mfma_f32_16x16x32_bf16 v[52:55], v[136:139], v[160:163], v[52:55]
	v_mfma_f32_16x16x32_bf16 v[44:47], v[124:127], v[168:171], v[44:47]
	v_mfma_f32_16x16x32_bf16 v[36:39], v[136:139], v[168:171], v[36:39]
	v_mfma_f32_16x16x32_bf16 v[28:31], v[124:127], v[176:179], v[28:31]
	v_mfma_f32_16x16x32_bf16 v[24:27], v[136:139], v[176:179], v[24:27]
	v_mfma_f32_16x16x32_bf16 v[12:15], v[124:127], v[198:201], v[12:15]
	v_mfma_f32_16x16x32_bf16 v[8:11], v[136:139], v[198:201], v[8:11]
	v_mfma_f32_16x16x32_bf16 v[60:63], v[128:131], v[164:167], v[60:63]
	v_mfma_f32_16x16x32_bf16 v[52:55], v[140:143], v[164:167], v[52:55]
	v_mfma_f32_16x16x32_bf16 v[44:47], v[128:131], v[172:175], v[44:47]
	v_mfma_f32_16x16x32_bf16 v[36:39], v[140:143], v[172:175], v[36:39]
	v_mfma_f32_16x16x32_bf16 v[28:31], v[128:131], v[180:183], v[28:31]
	v_mfma_f32_16x16x32_bf16 v[24:27], v[140:143], v[180:183], v[24:27]
	v_mfma_f32_16x16x32_bf16 v[12:15], v[128:131], v[202:205], v[12:15]
	v_mfma_f32_16x16x32_bf16 v[8:11], v[140:143], v[202:205], v[8:11]
	s_setprio 1
	s_setprio 0
	v_mfma_f32_16x16x32_bf16 v[56:59], v[144:147], v[160:163], v[56:59]
	v_mfma_f32_16x16x32_bf16 v[48:51], v[152:155], v[160:163], v[48:51]
	v_mfma_f32_16x16x32_bf16 v[40:43], v[144:147], v[168:171], v[40:43]
	v_mfma_f32_16x16x32_bf16 v[32:35], v[152:155], v[168:171], v[32:35]
	v_mfma_f32_16x16x32_bf16 v[20:23], v[144:147], v[176:179], v[20:23]
	v_mfma_f32_16x16x32_bf16 v[16:19], v[152:155], v[176:179], v[16:19]
	v_mfma_f32_16x16x32_bf16 v[4:7], v[144:147], v[198:201], v[4:7]
	v_mfma_f32_16x16x32_bf16 v[0:3], v[152:155], v[198:201], v[0:3]
	v_mfma_f32_16x16x32_bf16 v[56:59], v[148:151], v[164:167], v[56:59]
	v_mfma_f32_16x16x32_bf16 v[48:51], v[156:159], v[164:167], v[48:51]
	v_mfma_f32_16x16x32_bf16 v[40:43], v[148:151], v[172:175], v[40:43]
	v_mfma_f32_16x16x32_bf16 v[32:35], v[156:159], v[172:175], v[32:35]
	v_mfma_f32_16x16x32_bf16 v[20:23], v[148:151], v[180:183], v[20:23]
	v_mfma_f32_16x16x32_bf16 v[16:19], v[156:159], v[180:183], v[16:19]
	v_mfma_f32_16x16x32_bf16 v[4:7], v[148:151], v[202:205], v[4:7]
	v_mfma_f32_16x16x32_bf16 v[0:3], v[156:159], v[202:205], v[0:3]
	s_setprio 1
	s_barrier
	s_add_i32 s56, 0, 0x18000
	s_add_i32 s57, 0, 0x1c000
	v_add_u32_e32 v140, s56, v211
	v_add_u32_e32 v156, s57, v211
	ds_read_b128 v[124:127], v140
	ds_read_b128 v[128:131], v140 offset:1024
	ds_read_b128 v[136:139], v140 offset:2048
	ds_read_b128 v[140:143], v140 offset:3072
	ds_read_b128 v[144:147], v156
	ds_read_b128 v[148:151], v156 offset:1024
	ds_read_b128 v[152:155], v156 offset:2048
	ds_read_b128 v[156:159], v156 offset:3072
	s_add_u32 s38, s38, 0x40000
	s_addc_u32 s39, s39, 0
	s_mov_b32 m0, s43
	v_lshl_add_u64 v[220:221], s[38:39], 0, v[188:189]
	ds_read_b128 v[160:163], v215 offset:32768
	ds_read_b128 v[164:167], v215 offset:33792
	ds_read_b128 v[168:171], v215 offset:34816
	ds_read_b128 v[172:175], v215 offset:35840
	ds_read_b128 v[176:179], v215 offset:36864
	ds_read_b128 v[180:183], v215 offset:37888
	ds_read_b128 v[198:201], v215 offset:38912
	ds_read_b128 v[202:205], v215 offset:39936
	global_load_lds_dwordx4 v[220:221], off
	v_lshl_add_u64 v[220:221], s[38:39], 0, v[190:191]
	s_mov_b32 m0, s44
	s_nop 0
	global_load_lds_dwordx4 v[220:221], off
	s_waitcnt vmcnt(8)
	s_waitcnt lgkmcnt(0)
	s_barrier
	s_setprio 0
	s_waitcnt lgkmcnt(0)
	v_mfma_f32_16x16x32_bf16 v[132:135], v[124:127], v[160:163], v[132:135]
	v_mfma_f32_16x16x32_bf16 v[120:123], v[136:139], v[160:163], v[120:123]
	v_mfma_f32_16x16x32_bf16 v[108:111], v[124:127], v[168:171], v[108:111]
	v_mfma_f32_16x16x32_bf16 v[104:107], v[136:139], v[168:171], v[104:107]
	v_mfma_f32_16x16x32_bf16 v[92:95], v[124:127], v[176:179], v[92:95]
	v_mfma_f32_16x16x32_bf16 v[88:91], v[136:139], v[176:179], v[88:91]
	v_mfma_f32_16x16x32_bf16 v[76:79], v[124:127], v[198:201], v[76:79]
	v_mfma_f32_16x16x32_bf16 v[72:75], v[136:139], v[198:201], v[72:75]
	v_mfma_f32_16x16x32_bf16 v[132:135], v[128:131], v[164:167], v[132:135]
	v_mfma_f32_16x16x32_bf16 v[120:123], v[140:143], v[164:167], v[120:123]
	v_mfma_f32_16x16x32_bf16 v[108:111], v[128:131], v[172:175], v[108:111]
	v_mfma_f32_16x16x32_bf16 v[104:107], v[140:143], v[172:175], v[104:107]
	v_mfma_f32_16x16x32_bf16 v[92:95], v[128:131], v[180:183], v[92:95]
	v_mfma_f32_16x16x32_bf16 v[88:91], v[140:143], v[180:183], v[88:91]
	v_mfma_f32_16x16x32_bf16 v[76:79], v[128:131], v[202:205], v[76:79]
	v_mfma_f32_16x16x32_bf16 v[72:75], v[140:143], v[202:205], v[72:75]
	s_setprio 1
	s_setprio 0
	v_mfma_f32_16x16x32_bf16 v[116:119], v[144:147], v[160:163], v[116:119]
	v_mfma_f32_16x16x32_bf16 v[112:115], v[152:155], v[160:163], v[112:115]
	v_mfma_f32_16x16x32_bf16 v[100:103], v[144:147], v[168:171], v[100:103]
	v_mfma_f32_16x16x32_bf16 v[96:99], v[152:155], v[168:171], v[96:99]
	v_mfma_f32_16x16x32_bf16 v[84:87], v[144:147], v[176:179], v[84:87]
	v_mfma_f32_16x16x32_bf16 v[80:83], v[152:155], v[176:179], v[80:83]
	v_mfma_f32_16x16x32_bf16 v[68:71], v[144:147], v[198:201], v[68:71]
	v_mfma_f32_16x16x32_bf16 v[64:67], v[152:155], v[198:201], v[64:67]
	v_mfma_f32_16x16x32_bf16 v[116:119], v[148:151], v[164:167], v[116:119]
	v_mfma_f32_16x16x32_bf16 v[112:115], v[156:159], v[164:167], v[112:115]
	v_mfma_f32_16x16x32_bf16 v[100:103], v[148:151], v[172:175], v[100:103]
	v_mfma_f32_16x16x32_bf16 v[96:99], v[156:159], v[172:175], v[96:99]
	v_mfma_f32_16x16x32_bf16 v[84:87], v[148:151], v[180:183], v[84:87]
	v_mfma_f32_16x16x32_bf16 v[80:83], v[156:159], v[180:183], v[80:83]
	v_mfma_f32_16x16x32_bf16 v[68:71], v[148:151], v[202:205], v[68:71]
	v_mfma_f32_16x16x32_bf16 v[64:67], v[156:159], v[202:205], v[64:67]
	s_setprio 1
	s_barrier
	s_add_i32 s38, s56, s41
	v_lshl_add_u64 v[206:207], v[206:207], 0, s[6:7]
	s_mov_b32 m0, s38
	ds_read_b128 v[160:163], v215 offset:49152
	ds_read_b128 v[164:167], v215 offset:50176
	ds_read_b128 v[168:171], v215 offset:51200
	ds_read_b128 v[172:175], v215 offset:52224
	ds_read_b128 v[176:179], v215 offset:53248
	ds_read_b128 v[180:183], v215 offset:54272
	ds_read_b128 v[198:201], v215 offset:55296
	ds_read_b128 v[202:205], v215 offset:56320
	global_load_lds_dwordx4 v[206:207], off
	s_add_i32 m0, s38, 0x2000
	s_add_u32 s36, s36, 0x40080
	v_lshl_add_u64 v[206:207], v[208:209], 0, s[6:7]
	s_addc_u32 s37, s37, 0
	s_add_i32 s38, s57, s41
	global_load_lds_dwordx4 v[206:207], off
	v_lshl_add_u64 v[206:207], s[36:37], 0, v[184:185]
	s_mov_b32 m0, s38
	s_nop 0
	global_load_lds_dwordx4 v[206:207], off
	v_lshl_add_u64 v[206:207], s[36:37], 0, v[186:187]
	s_add_i32 m0, s38, 0x2000
	s_nop 0
	global_load_lds_dwordx4 v[206:207], off
	v_lshl_add_u64 v[206:207], v[216:217], 0, s[6:7]
	s_mov_b32 m0, s48
	s_nop 0
	global_load_lds_dwordx4 v[206:207], off
	v_lshl_add_u64 v[206:207], v[218:219], 0, s[6:7]
	s_mov_b32 m0, s49
	s_nop 0
	global_load_lds_dwordx4 v[206:207], off
	s_waitcnt vmcnt(8)
	s_waitcnt lgkmcnt(0)
	s_barrier
	s_setprio 0
	s_waitcnt lgkmcnt(0)
	v_mfma_f32_16x16x32_bf16 v[60:63], v[124:127], v[160:163], v[60:63]
	v_mfma_f32_16x16x32_bf16 v[52:55], v[136:139], v[160:163], v[52:55]
	v_mfma_f32_16x16x32_bf16 v[44:47], v[124:127], v[168:171], v[44:47]
	v_mfma_f32_16x16x32_bf16 v[36:39], v[136:139], v[168:171], v[36:39]
	v_mfma_f32_16x16x32_bf16 v[28:31], v[124:127], v[176:179], v[28:31]
	v_mfma_f32_16x16x32_bf16 v[24:27], v[136:139], v[176:179], v[24:27]
	v_mfma_f32_16x16x32_bf16 v[12:15], v[124:127], v[198:201], v[12:15]
	v_mfma_f32_16x16x32_bf16 v[8:11], v[136:139], v[198:201], v[8:11]
	v_mfma_f32_16x16x32_bf16 v[60:63], v[128:131], v[164:167], v[60:63]
	v_mfma_f32_16x16x32_bf16 v[52:55], v[140:143], v[164:167], v[52:55]
	v_mfma_f32_16x16x32_bf16 v[44:47], v[128:131], v[172:175], v[44:47]
	v_mfma_f32_16x16x32_bf16 v[36:39], v[140:143], v[172:175], v[36:39]
	v_mfma_f32_16x16x32_bf16 v[28:31], v[128:131], v[180:183], v[28:31]
	v_mfma_f32_16x16x32_bf16 v[24:27], v[140:143], v[180:183], v[24:27]
	v_mfma_f32_16x16x32_bf16 v[12:15], v[128:131], v[202:205], v[12:15]
	v_mfma_f32_16x16x32_bf16 v[8:11], v[140:143], v[202:205], v[8:11]
	s_setprio 1
	s_setprio 0
	v_mfma_f32_16x16x32_bf16 v[56:59], v[144:147], v[160:163], v[56:59]
	v_mfma_f32_16x16x32_bf16 v[48:51], v[152:155], v[160:163], v[48:51]
	v_mfma_f32_16x16x32_bf16 v[40:43], v[144:147], v[168:171], v[40:43]
	v_mfma_f32_16x16x32_bf16 v[32:35], v[152:155], v[168:171], v[32:35]
	v_mfma_f32_16x16x32_bf16 v[20:23], v[144:147], v[176:179], v[20:23]
	v_mfma_f32_16x16x32_bf16 v[16:19], v[152:155], v[176:179], v[16:19]
	v_mfma_f32_16x16x32_bf16 v[4:7], v[144:147], v[198:201], v[4:7]
	v_mfma_f32_16x16x32_bf16 v[0:3], v[152:155], v[198:201], v[0:3]
	v_mfma_f32_16x16x32_bf16 v[56:59], v[148:151], v[164:167], v[56:59]
	v_mfma_f32_16x16x32_bf16 v[48:51], v[156:159], v[164:167], v[48:51]
	v_mfma_f32_16x16x32_bf16 v[40:43], v[148:151], v[172:175], v[40:43]
	v_mfma_f32_16x16x32_bf16 v[32:35], v[156:159], v[172:175], v[32:35]
	v_mfma_f32_16x16x32_bf16 v[20:23], v[148:151], v[180:183], v[20:23]
	v_mfma_f32_16x16x32_bf16 v[16:19], v[156:159], v[180:183], v[16:19]
	v_mfma_f32_16x16x32_bf16 v[4:7], v[148:151], v[202:205], v[4:7]
	v_mfma_f32_16x16x32_bf16 v[0:3], v[156:159], v[202:205], v[0:3]
	s_setprio 1
	s_barrier
	s_add_i32 s55, s55, 2
	s_add_u32 s34, s34, 0x100
	s_addc_u32 s35, s35, 0
	s_add_u32 s53, s53, 0x100
	s_addc_u32 s54, s54, 0
	s_cmp_gt_u32 s55, 13
	s_cbranch_scc0 .LBB0_3621
	s_and_b64 vcc, exec, s[8:9]
	s_cbranch_vccz .LBB0_3624
	s_barrier
